# hand-written router row loop: loads de-serialised (next row's x and modulation prefetched), DPP reduce-scatter for the 16 logits, fallback bodies removed
# speedup vs baseline: 1.0394x; 1.0159x over previous
.LBB0_6295:
	s_andn2_b64 vcc, exec, s[0:1]
	s_cbranch_vccnz .LBB0_6363
	v_readlane_b32 s4, v251, 59
	v_readlane_b32 s5, v251, 60
	v_readlane_b32 s8, v255, 20
	v_readlane_b32 s10, v251, 61
	v_readfirstlane_b32 s0, v0
	v_readlane_b32 s70, v251, 11
	v_readlane_b32 s71, v251, 12
	v_readlane_b32 s72, v251, 13
	v_readlane_b32 s73, v251, 14
	v_readlane_b32 s74, v251, 15
	v_readlane_b32 s75, v251, 16
	v_readlane_b32 s76, v251, 17
	v_readlane_b32 s77, v251, 18
	v_readlane_b32 s78, v251, 7
	v_readlane_b32 s79, v251, 8
	s_nop 3
	s_lshr_b32 s0, s0, 6
	s_add_i32 s10, s10, s0
	s_lshl_b32 s1, s8, 9
	s_add_u32 s70, s70, s1
	s_addc_u32 s71, s71, 0
	s_add_u32 s72, s72, s1
	s_addc_u32 s73, s73, 0
	s_lshl_b32 s1, s8, 11
	s_add_u32 s74, s74, s1
	s_addc_u32 s75, s75, 0
	s_lshl_b32 s1, s8, 10
	s_add_u32 s76, s76, s1
	s_addc_u32 s77, s77, 0
	s_lshl_b32 s1, s8, 6
	s_add_u32 s78, s78, s1
	s_addc_u32 s79, s79, 0
	s_add_u32 s48, s4, 0x41491000
	s_addc_u32 s49, s5, 0
	s_add_u32 s50, s4, 0x4b690000
	s_addc_u32 s51, s5, 0
	s_add_u32 s52, s4, 0xe8000
	s_addc_u32 s53, s5, 0
	s_add_u32 s54, s4, 0x168000
	s_addc_u32 s55, s5, 0
	s_add_u32 s56, s4, 0x4bf90000
	s_addc_u32 s57, s5, 0
	s_add_u32 s58, s4, 0x4e390000
	s_addc_u32 s59, s5, 0
	s_add_u32 s62, s4, 0x4fe8fe00
	s_addc_u32 s63, s5, 0
	s_add_u32 s64, s4, 0x4ec90000
	s_addc_u32 s65, s5, 0
	s_mov_b32 s66, 0
	s_mov_b32 s67, -1
	s_mov_b32 s68, 0xf0f0f0f0
	s_mov_b32 s69, 0xf0f0f0f0
	s_mov_b32 s47, 0xbfb8aa3b
	v_and_b32_e32 v1, 63, v0
	v_and_b32_e32 v2, 15, v1
	v_lshlrev_b32_e32 v4, 4, v1
	v_mov_b32_e32 v176, 0x800
	v_mov_b32_e32 v177, 0xe00
	v_cndmask_b32_e64 v5, v176, v177, s[66:67]
	v_add_u32_e32 v5, v5, v4
	v_lshlrev_b32_e32 v6, 2, v2
	v_and_b32_e32 v7, 7, v1
	v_lshlrev_b32_e32 v7, 5, v7
	v_bfe_u32 v176, v1, 3, 1
	v_lshlrev_b32_e32 v176, 5, v176
	v_and_b32_e32 v177, 3, v1
	v_or_b32_e32 v176, v176, v177
	s_movk_i32 s0, 0x2400
	v_mul_u32_u24_e32 v176, s0, v176
	v_mov_b32_e32 v177, 0x268000
	v_mov_b32_e32 v178, 0x2f8000
	v_cndmask_b32_e64 v177, v177, v178, s[68:69]
	v_add_u32_e32 v8, v176, v177
	v_and_b32_e32 v9, 8, v1
	v_lshlrev_b32_e32 v9, 28, v9
	v_xor_b32_e32 v9, 0x80000000, v9
	v_mov_b32_e32 v176, 0x413504f3
	v_mov_b32_e32 v177, 0x41800000
	v_cndmask_b32_e64 v10, v176, v177, s[66:67]
	v_lshlrev_b32_e32 v176, 5, v2
	v_lshlrev_b32_e32 v177, 5, v1
	v_add_u32_e32 v178, 0xfffffc00, v177
	global_load_dwordx4 v[12:15], v176, s[70:71]
	global_load_dwordx4 v[16:19], v176, s[70:71] offset:16
	global_load_dwordx4 v[28:31], v177, s[74:75]
	global_load_dwordx4 v[32:35], v177, s[74:75] offset:16
	global_load_dword v11, v6, s[78:79]
	s_mov_b64 exec, 0xffffffff
	global_load_dwordx4 v[20:23], v176, s[72:73]
	global_load_dwordx4 v[24:27], v176, s[72:73] offset:16
	s_mov_b64 exec, s[66:67]
	global_load_dwordx4 v[20:23], v178, s[76:77]
	global_load_dwordx4 v[24:27], v178, s[76:77] offset:16
	s_mov_b64 exec, -1
	s_add_i32 s11, s10, 0x0
	s_lshr_b32 s0, s11, 8
	s_mul_i32 s0, s0, 57
	s_lshr_b32 s0, s0, 9
	s_mul_i32 s1, s0, 0x900
	s_sub_i32 s43, s11, s1
	s_sub_i32 s0, s43, 0x100
	s_max_i32 s0, s0, 0
	s_mul_i32 s1, s11, 0x2400
	s_add_u32 s12, s48, s1
	s_addc_u32 s13, s49, 0
	s_lshl_b32 s1, s11, 9
	s_add_u32 s14, s50, s1
	s_addc_u32 s15, s51, 0
	s_lshl_b32 s1, s0, 8
	s_add_u32 s16, s52, s1
	s_addc_u32 s17, s53, 0
	s_add_u32 s18, s54, s1
	s_addc_u32 s19, s55, 0
	global_load_dwordx4 v[36:39], v4, s[12:13]
	global_load_dwordx4 v[40:43], v4, s[12:13] offset:1024
	global_load_dwordx4 v[44:47], v5, s[12:13]
	global_load_dwordx4 v[48:51], v4, s[12:13] offset:3072
	global_load_dword v68, v6, s[14:15]
	global_load_dwordx4 v[52:55], v7, s[16:17]
	global_load_dwordx4 v[56:59], v7, s[16:17] offset:16
	global_load_dwordx4 v[60:63], v7, s[18:19]
	global_load_dwordx4 v[64:67], v7, s[18:19] offset:16
	s_add_i32 s11, s10, 0x800
	s_lshr_b32 s0, s11, 8
	s_mul_i32 s0, s0, 57
	s_lshr_b32 s0, s0, 9
	s_mul_i32 s1, s0, 0x900
	s_sub_i32 s43, s11, s1
	s_sub_i32 s0, s43, 0x100
	s_max_i32 s0, s0, 0
	s_mul_i32 s1, s11, 0x2400
	s_add_u32 s12, s48, s1
	s_addc_u32 s13, s49, 0
	s_lshl_b32 s1, s11, 9
	s_add_u32 s14, s50, s1
	s_addc_u32 s15, s51, 0
	s_lshl_b32 s1, s0, 8
	s_add_u32 s16, s52, s1
	s_addc_u32 s17, s53, 0
	s_add_u32 s18, s54, s1
	s_addc_u32 s19, s55, 0
	global_load_dwordx4 v[70:73], v4, s[12:13]
	global_load_dwordx4 v[74:77], v4, s[12:13] offset:1024
	global_load_dwordx4 v[78:81], v5, s[12:13]
	global_load_dwordx4 v[82:85], v4, s[12:13] offset:3072
	global_load_dword v102, v6, s[14:15]
	global_load_dwordx4 v[86:89], v7, s[16:17]
	global_load_dwordx4 v[90:93], v7, s[16:17] offset:16
	global_load_dwordx4 v[94:97], v7, s[18:19]
	global_load_dwordx4 v[98:101], v7, s[18:19] offset:16
	s_add_i32 s11, s10, 0x1000
	s_lshr_b32 s0, s11, 8
	s_mul_i32 s0, s0, 57
	s_lshr_b32 s0, s0, 9
	s_mul_i32 s1, s0, 0x900
	s_sub_i32 s43, s11, s1
	s_sub_i32 s0, s43, 0x100
	s_max_i32 s0, s0, 0
	s_mul_i32 s1, s11, 0x2400
	s_add_u32 s12, s48, s1
	s_addc_u32 s13, s49, 0
	s_lshl_b32 s1, s11, 9
	s_add_u32 s14, s50, s1
	s_addc_u32 s15, s51, 0
	s_lshl_b32 s1, s0, 8
	s_add_u32 s16, s52, s1
	s_addc_u32 s17, s53, 0
	s_add_u32 s18, s54, s1
	s_addc_u32 s19, s55, 0
	global_load_dwordx4 v[104:107], v4, s[12:13]
	global_load_dwordx4 v[108:111], v4, s[12:13] offset:1024
	global_load_dwordx4 v[112:115], v5, s[12:13]
	global_load_dwordx4 v[116:119], v4, s[12:13] offset:3072
	global_load_dword v136, v6, s[14:15]
	global_load_dwordx4 v[120:123], v7, s[16:17]
	global_load_dwordx4 v[124:127], v7, s[16:17] offset:16
	global_load_dwordx4 v[128:131], v7, s[18:19]
	global_load_dwordx4 v[132:135], v7, s[18:19] offset:16
	s_waitcnt vmcnt(27)
	v_mul_f32_e32 v12, 0x3fb8aa3b, v12
	v_mul_f32_e32 v13, 0x3fb8aa3b, v13
	v_mul_f32_e32 v14, 0x3fb8aa3b, v14
	v_mul_f32_e32 v15, 0x3fb8aa3b, v15
	v_mul_f32_e32 v16, 0x3fb8aa3b, v16
	v_mul_f32_e32 v17, 0x3fb8aa3b, v17
	v_mul_f32_e32 v18, 0x3fb8aa3b, v18
	v_mul_f32_e32 v19, 0x3fb8aa3b, v19
	v_mul_f32_e32 v20, v10, v20
	v_mul_f32_e32 v21, v10, v21
	v_mul_f32_e32 v22, v10, v22
	v_mul_f32_e32 v23, v10, v23
	v_mul_f32_e32 v24, v10, v24
	v_mul_f32_e32 v25, v10, v25
	v_mul_f32_e32 v26, v10, v26
	v_mul_f32_e32 v27, v10, v27
	v_mul_f32_e32 v28, 0x41b504f3, v28
	v_mul_f32_e32 v29, 0x41b504f3, v29
	v_mul_f32_e32 v30, 0x41b504f3, v30
	v_mul_f32_e32 v31, 0x41b504f3, v31
	v_mul_f32_e32 v32, 0x41b504f3, v32
	v_mul_f32_e32 v33, 0x41b504f3, v33
	v_mul_f32_e32 v34, 0x41b504f3, v34
	v_mul_f32_e32 v35, 0x41b504f3, v35
	s_waitcnt vmcnt(18)
	s_add_i32 s11, s10, 0x0
	s_lshr_b32 s0, s11, 8
	s_mul_i32 s0, s0, 57
	s_lshr_b32 s0, s0, 9
	s_mul_i32 s1, s0, 0x900
	s_sub_i32 s43, s11, s1
	s_mul_i32 s1, s0, 0x9000
	s_lshl_b32 s2, s43, 2
	s_add_i32 s1, s1, s2
	s_add_u32 s44, s4, s1
	s_addc_u32 s45, s5, 0
	s_lshl_b32 s1, s11, 11
	s_add_u32 s22, s56, s1
	s_addc_u32 s23, s57, 0
	s_lshl_b32 s1, s11, 9
	s_add_u32 s28, s58, s1
	s_addc_u32 s29, s59, 0
	s_add_u32 s30, s62, s1
	s_addc_u32 s31, s63, 0
	s_lshl_b32 s1, s11, 10
	s_add_u32 s34, s64, s1
	s_addc_u32 s35, s65, 0
	v_xor_b32_e32 v168, v9, v60
	v_xor_b32_e32 v169, v9, v61
	v_xor_b32_e32 v170, v9, v62
	v_xor_b32_e32 v171, v9, v63
	v_xor_b32_e32 v172, v9, v64
	v_xor_b32_e32 v173, v9, v65
	v_xor_b32_e32 v174, v9, v66
	v_xor_b32_e32 v175, v9, v67
	s_cmpk_ge_u32 s43, 0x100
	v_lshlrev_b32_e32 v148, 16, v36
	v_and_b32_e32 v149, 0xffff0000, v36
	v_lshlrev_b32_e32 v150, 16, v37
	v_and_b32_e32 v151, 0xffff0000, v37
	v_lshlrev_b32_e32 v152, 16, v38
	v_and_b32_e32 v153, 0xffff0000, v38
	v_lshlrev_b32_e32 v154, 16, v39
	v_and_b32_e32 v155, 0xffff0000, v39
	v_mul_f32_e32 v164, v148, v148
	v_fmac_f32_e32 v164, v149, v149
	v_fmac_f32_e32 v164, v150, v150
	v_fmac_f32_e32 v164, v151, v151
	v_fmac_f32_e32 v164, v152, v152
	v_fmac_f32_e32 v164, v153, v153
	v_fmac_f32_e32 v164, v154, v154
	v_fmac_f32_e32 v164, v155, v155
	v_mul_f32_e32 v148, v148, v12
	v_mul_f32_e32 v149, v149, v13
	v_add_f32_dpp v164, v164, v164 quad_perm:[1,0,3,2] row_mask:0xf bank_mask:0xf
	v_mul_f32_e32 v150, v150, v14
	v_mul_f32_e32 v151, v151, v15
	v_add_f32_dpp v164, v164, v164 quad_perm:[2,3,0,1] row_mask:0xf bank_mask:0xf
	v_mul_f32_e32 v152, v152, v16
	v_mul_f32_e32 v153, v153, v17
	v_add_f32_dpp v164, v164, v164 row_half_mirror row_mask:0xf bank_mask:0xf
	v_mul_f32_e32 v154, v154, v18
	v_mul_f32_e32 v155, v155, v19
	v_add_f32_dpp v164, v164, v164 row_mirror row_mask:0xf bank_mask:0xf
	v_add_f32_e32 v164, 0x390637bd, v164
	v_rsq_f32_e32 v165, v164
	s_nop 0
	v_mul_f32_e32 v148, v148, v165
	v_mul_f32_e32 v149, v149, v165
	v_mul_f32_e32 v150, v150, v165
	v_mul_f32_e32 v151, v151, v165
	v_mul_f32_e32 v152, v152, v165
	v_mul_f32_e32 v153, v153, v165
	v_mul_f32_e32 v154, v154, v165
	v_mul_f32_e32 v155, v155, v165
	s_cbranch_scc0 .Lpp_norope_q0_0
	v_mul_f32_dpp v156, v148, v168 row_ror:8 row_mask:0xf bank_mask:0xf
	v_mul_f32_dpp v157, v149, v169 row_ror:8 row_mask:0xf bank_mask:0xf
	v_mul_f32_dpp v158, v150, v170 row_ror:8 row_mask:0xf bank_mask:0xf
	v_mul_f32_dpp v159, v151, v171 row_ror:8 row_mask:0xf bank_mask:0xf
	v_mul_f32_dpp v160, v152, v172 row_ror:8 row_mask:0xf bank_mask:0xf
	v_mul_f32_dpp v161, v153, v173 row_ror:8 row_mask:0xf bank_mask:0xf
	v_mul_f32_dpp v162, v154, v174 row_ror:8 row_mask:0xf bank_mask:0xf
	v_mul_f32_dpp v163, v155, v175 row_ror:8 row_mask:0xf bank_mask:0xf
	v_fmac_f32_e32 v156, v148, v52
	v_fmac_f32_e32 v157, v149, v53
	v_fmac_f32_e32 v158, v150, v54
	v_fmac_f32_e32 v159, v151, v55
	v_fmac_f32_e32 v160, v152, v56
	v_fmac_f32_e32 v161, v153, v57
	v_fmac_f32_e32 v162, v154, v58
	v_fmac_f32_e32 v163, v155, v59
	s_branch .Lpp_ropedone_q0_0

.Lpp_ropedone_kk_8:
	v_cvt_pk_bf16_f32 v156, v156, v157
	v_cvt_pk_bf16_f32 v157, v158, v159
	v_cvt_pk_bf16_f32 v158, v160, v161
	v_cvt_pk_bf16_f32 v159, v162, v163
	s_mov_b64 exec, 0xffffffff
	global_store_dwordx4 v4, v[156:159], s[28:29]
	s_mov_b64 exec, s[66:67]
	global_store_dwordx4 v4, v[156:159], s[30:31]
	s_mov_b64 exec, -1
	v_lshlrev_b32_e32 v148, 16, v116
	v_and_b32_e32 v149, 0xffff0000, v116
	v_lshlrev_b32_e32 v150, 16, v117
	v_and_b32_e32 v151, 0xffff0000, v117
	v_lshlrev_b32_e32 v152, 16, v118
	v_and_b32_e32 v153, 0xffff0000, v118
	v_lshlrev_b32_e32 v154, 16, v119
	v_and_b32_e32 v155, 0xffff0000, v119
	v_mul_f32_e32 v164, v148, v148
	v_fmac_f32_e32 v164, v149, v149
	v_fmac_f32_e32 v164, v150, v150
	v_fmac_f32_e32 v164, v151, v151
	v_fmac_f32_e32 v164, v152, v152
	v_fmac_f32_e32 v164, v153, v153
	v_fmac_f32_e32 v164, v154, v154
	v_fmac_f32_e32 v164, v155, v155
	v_mul_f32_e32 v148, v148, v28
	v_mul_f32_e32 v149, v149, v29
	v_add_f32_dpp v164, v164, v164 quad_perm:[1,0,3,2] row_mask:0xf bank_mask:0xf
	v_mul_f32_e32 v150, v150, v30
	v_mul_f32_e32 v151, v151, v31
	v_add_f32_dpp v164, v164, v164 quad_perm:[2,3,0,1] row_mask:0xf bank_mask:0xf
	v_mul_f32_e32 v152, v152, v32
	v_mul_f32_e32 v153, v153, v33
	v_add_f32_dpp v164, v164, v164 row_half_mirror row_mask:0xf bank_mask:0xf
	v_mul_f32_e32 v154, v154, v34
	v_mul_f32_e32 v155, v155, v35
	v_add_f32_dpp v164, v164, v164 row_mirror row_mask:0xf bank_mask:0xf
	s_nop 0
	v_readlane_b32 s0, v164, 0
	v_readlane_b32 s1, v164, 16
	v_readlane_b32 s2, v164, 32
	v_readlane_b32 s3, v164, 48
	s_nop 1
	v_mov_b32_e32 v166, s0
	v_add_f32_e32 v166, s1, v166
	v_add_f32_e32 v166, s2, v166
	v_add_f32_e32 v166, s3, v166
	v_add_f32_e32 v166, 0x3a0637bd, v166
	v_rsq_f32_e32 v165, v166
	s_nop 0
	v_mul_f32_e32 v148, v148, v165
	v_mul_f32_e32 v149, v149, v165
	v_mul_f32_e32 v150, v150, v165
	v_mul_f32_e32 v151, v151, v165
	v_mul_f32_e32 v152, v152, v165
	v_mul_f32_e32 v153, v153, v165
	v_mul_f32_e32 v154, v154, v165
	v_mul_f32_e32 v155, v155, v165
	v_cvt_pk_bf16_f32 v156, v148, v149
	v_cvt_pk_bf16_f32 v157, v150, v151
	v_cvt_pk_bf16_f32 v158, v152, v153
	v_cvt_pk_bf16_f32 v159, v154, v155
	global_store_dwordx4 v4, v[156:159], s[34:35]
	v_add_f32_e32 v176, v136, v11
	v_mul_f32_e64 v177, |v176|, s47
	v_exp_f32_e32 v177, v177
	s_nop 0
	v_add_f32_e32 v178, 1.0, v177
	v_add_f32_e32 v179, -1.0, v178
	v_log_f32_e32 v180, v178
	v_rcp_f32_e32 v181, v179
	v_cmp_eq_f32_e32 vcc, 0, v179
	s_nop 0
	v_mul_f32_e32 v181, v177, v181
	s_nop 0
	v_cndmask_b32_e64 v181, v181, 1.0, vcc
	v_mul_f32_e32 v180, 0x3f317218, v180
	v_mul_f32_e32 v180, v180, v181
	v_min_f32_e32 v177, 0, v176
	v_sub_f32_e32 v177, v177, v180
	v_cndmask_b32_e64 v177, v176, v177, s[68:69]
	s_mov_b64 exec, 0xffff
	global_store_dword v8, v177, s[44:45]
	s_mov_b64 exec, -1
.LBB0_6309:
	v_readlane_b32 s0, v255, 22
	s_add_i32 s2, s0, 4
	v_readlane_b32 s0, v251, 39
	v_readlane_b32 s1, v251, 40
	s_cmp_ge_i32 s2, s1
	s_cbranch_scc1 .LBB0_6363
	s_waitcnt vmcnt(0)
	s_barrier
	s_mov_b64 s[0:1], exec
	v_readlane_b32 s4, v251, 37
	v_readlane_b32 s5, v251, 38
	s_and_b64 s[4:5], s[0:1], s[4:5]
	s_mov_b64 exec, s[4:5]
	s_cbranch_execz .LBB0_6362
	v_readlane_b32 s3, v255, 11
	s_waitcnt vmcnt(0) expcnt(0) lgkmcnt(0)
	s_nop 0
	v_mov_b32_e32 v1, s3
	ds_read_b32 v4, v1
	v_readlane_b32 s3, v255, 12
	s_waitcnt lgkmcnt(0)
	v_cmp_ne_u32_e32 vcc, 0, v4
	v_mov_b32_e32 v1, s3
	ds_read_b32 v2, v1
	s_cbranch_vccnz .LBB0_6326
	v_readlane_b32 s20, v251, 0
	v_readlane_b32 s21, v251, 1
	s_load_dwordx2 s[4:5], s[20:21], 0x4
	v_readlane_b32 s3, v251, 2
	s_mov_b32 s6, 1
	s_waitcnt lgkmcnt(0)
	s_mul_i32 s3, s4, s3
	s_mul_i32 s3, s3, s5
	s_branch .LBB0_6314

.LBB0_6454:
	s_andn2_b64 vcc, exec, s[0:1]
	s_cbranch_vccnz .LBB0_6626
	v_readlane_b32 s4, v251, 59
	v_readlane_b32 s5, v251, 60
	v_readlane_b32 s8, v255, 20
	v_readlane_b32 s10, v251, 61
	v_readfirstlane_b32 s0, v0
	v_readlane_b32 s62, v251, 23
	v_readlane_b32 s63, v251, 24
	v_readlane_b32 s64, v251, 25
	v_readlane_b32 s65, v251, 26
	s_nop 3
	s_lshr_b32 s0, s0, 6
	s_add_i32 s10, s10, s0
	s_mul_i32 s1, s8, 0x300
	s_add_u32 s62, s62, s1
	s_addc_u32 s63, s63, 0
	s_add_u32 s64, s64, s1
	s_addc_u32 s65, s65, 0
	s_add_u32 s48, s4, 0x50790000
	s_addc_u32 s49, s5, 0
	s_add_u32 s50, s4, 0x52290000
	s_addc_u32 s51, s5, 0
	s_add_u32 s52, s4, 0x4b690000
	s_addc_u32 s53, s5, 0
	s_add_u32 s54, s4, 0x1e8000
	s_addc_u32 s55, s5, 0
	s_add_u32 s56, s4, 0x228000
	s_addc_u32 s57, s5, 0
	s_add_u32 s58, s4, 0x54690000
	s_addc_u32 s59, s5, 0
	s_add_u32 s44, s4, 0x56190000
	s_addc_u32 s45, s5, 0
	v_and_b32_e32 v1, 63, v0
	v_and_b32_e32 v2, 15, v1
	v_lshrrev_b32_e32 v100, 4, v1
	s_movk_i32 s0, 0x180
	v_lshlrev_b32_e32 v4, 4, v2
	v_mad_u32_u24 v4, v100, s0, v4
	v_lshlrev_b32_e32 v5, 3, v2
	v_mad_u32_u24 v5, v100, s0, v5
	v_add_u32_e32 v5, 0x100, v5
	v_lshlrev_b32_e32 v6, 9, v100
	v_lshl_add_u32 v6, v2, 4, v6
	v_lshlrev_b32_e32 v7, 4, v2
	v_add_u32_e32 v7, 64, v7
	v_and_b32_e32 v8, 7, v2
	v_lshlrev_b32_e32 v8, 4, v8
	v_and_b32_e32 v9, 8, v2
	v_lshlrev_b32_e32 v9, 28, v9
	v_xor_b32_e32 v9, 0x80000000, v9
	v_lshlrev_b32_e32 v101, 5, v2
	v_lshlrev_b32_e32 v102, 4, v2
	global_load_dwordx4 v[10:13], v101, s[62:63]
	global_load_dwordx4 v[14:17], v101, s[62:63] offset:16
	global_load_dwordx4 v[18:21], v102, s[62:63] offset:512
	global_load_dwordx4 v[22:25], v101, s[64:65]
	global_load_dwordx4 v[26:29], v101, s[64:65] offset:16
	global_load_dwordx4 v[30:33], v102, s[64:65] offset:512
	s_add_i32 s11, s10, 0x0
	s_lshr_b32 s0, s11, 8
	s_mul_i32 s0, s0, 57
	s_lshr_b32 s0, s0, 9
	s_mul_i32 s0, s0, 0x900
	s_sub_i32 s0, s11, s0
	s_sub_i32 s0, s0, 0x100
	s_max_i32 s0, s0, 0
	s_mul_i32 s1, s11, 0x600
	s_add_u32 s12, s48, s1
	s_addc_u32 s13, s49, 0
	s_lshl_b32 s1, s11, 11
	s_add_u32 s14, s50, s1
	s_addc_u32 s15, s51, 0
	s_lshl_b32 s1, s11, 9
	s_add_u32 s16, s52, s1
	s_addc_u32 s17, s53, 0
	s_lshl_b32 s1, s0, 7
	s_add_u32 s18, s54, s1
	s_addc_u32 s19, s55, 0
	s_add_u32 s22, s56, s1
	s_addc_u32 s23, s57, 0
	global_load_dwordx4 v[34:37], v4, s[12:13]
	global_load_dwordx2 v[38:39], v5, s[12:13]
	global_load_dwordx4 v[40:43], v6, s[14:15]
	global_load_dwordx4 v[44:47], v7, s[16:17]
	global_load_dwordx4 v[48:51], v8, s[18:19]
	global_load_dwordx4 v[52:55], v8, s[22:23]
	s_add_i32 s11, s10, 0x800
	s_lshr_b32 s0, s11, 8
	s_mul_i32 s0, s0, 57
	s_lshr_b32 s0, s0, 9
	s_mul_i32 s0, s0, 0x900
	s_sub_i32 s0, s11, s0
	s_sub_i32 s0, s0, 0x100
	s_max_i32 s0, s0, 0
	s_mul_i32 s1, s11, 0x600
	s_add_u32 s12, s48, s1
	s_addc_u32 s13, s49, 0
	s_lshl_b32 s1, s11, 11
	s_add_u32 s14, s50, s1
	s_addc_u32 s15, s51, 0
	s_lshl_b32 s1, s11, 9
	s_add_u32 s16, s52, s1
	s_addc_u32 s17, s53, 0
	s_lshl_b32 s1, s0, 7
	s_add_u32 s18, s54, s1
	s_addc_u32 s19, s55, 0
	s_add_u32 s22, s56, s1
	s_addc_u32 s23, s57, 0
	global_load_dwordx4 v[56:59], v4, s[12:13]
	global_load_dwordx2 v[60:61], v5, s[12:13]
	global_load_dwordx4 v[62:65], v6, s[14:15]
	global_load_dwordx4 v[66:69], v7, s[16:17]
	global_load_dwordx4 v[70:73], v8, s[18:19]
	global_load_dwordx4 v[74:77], v8, s[22:23]
	s_add_i32 s11, s10, 0x1000
	s_lshr_b32 s0, s11, 8
	s_mul_i32 s0, s0, 57
	s_lshr_b32 s0, s0, 9
	s_mul_i32 s0, s0, 0x900
	s_sub_i32 s0, s11, s0
	s_sub_i32 s0, s0, 0x100
	s_max_i32 s0, s0, 0
	s_mul_i32 s1, s11, 0x600
	s_add_u32 s12, s48, s1
	s_addc_u32 s13, s49, 0
	s_lshl_b32 s1, s11, 11
	s_add_u32 s14, s50, s1
	s_addc_u32 s15, s51, 0
	s_lshl_b32 s1, s11, 9
	s_add_u32 s16, s52, s1
	s_addc_u32 s17, s53, 0
	s_lshl_b32 s1, s0, 7
	s_add_u32 s18, s54, s1
	s_addc_u32 s19, s55, 0
	s_add_u32 s22, s56, s1
	s_addc_u32 s23, s57, 0
	global_load_dwordx4 v[78:81], v4, s[12:13]
	global_load_dwordx2 v[82:83], v5, s[12:13]
	global_load_dwordx4 v[84:87], v6, s[14:15]
	global_load_dwordx4 v[88:91], v7, s[16:17]
	global_load_dwordx4 v[92:95], v8, s[18:19]
	global_load_dwordx4 v[96:99], v8, s[22:23]
	s_waitcnt vmcnt(18)
	v_mul_f32_e32 v10, 0x3fb8aa3b, v10
	v_mul_f32_e32 v11, 0x3fb8aa3b, v11
	v_mul_f32_e32 v12, 0x3fb8aa3b, v12
	v_mul_f32_e32 v13, 0x3fb8aa3b, v13
	v_mul_f32_e32 v14, 0x3fb8aa3b, v14
	v_mul_f32_e32 v15, 0x3fb8aa3b, v15
	v_mul_f32_e32 v16, 0x3fb8aa3b, v16
	v_mul_f32_e32 v17, 0x3fb8aa3b, v17
	v_mul_f32_e32 v18, 0x3fb8aa3b, v18
	v_mul_f32_e32 v19, 0x3fb8aa3b, v19
	v_mul_f32_e32 v20, 0x3fb8aa3b, v20
	v_mul_f32_e32 v21, 0x3fb8aa3b, v21
	v_mul_f32_e32 v22, 0x415db3d7, v22
	v_mul_f32_e32 v23, 0x415db3d7, v23
	v_mul_f32_e32 v24, 0x415db3d7, v24
	v_mul_f32_e32 v25, 0x415db3d7, v25
	v_mul_f32_e32 v26, 0x415db3d7, v26
	v_mul_f32_e32 v27, 0x415db3d7, v27
	v_mul_f32_e32 v28, 0x415db3d7, v28
	v_mul_f32_e32 v29, 0x415db3d7, v29
	v_mul_f32_e32 v30, 0x415db3d7, v30
	v_mul_f32_e32 v31, 0x415db3d7, v31
	v_mul_f32_e32 v32, 0x415db3d7, v32
	v_mul_f32_e32 v33, 0x415db3d7, v33
	s_waitcnt vmcnt(12)
	s_add_i32 s11, s10, 0x0
	s_lshr_b32 s0, s11, 8
	s_mul_i32 s0, s0, 57
	s_lshr_b32 s0, s0, 9
	s_mul_i32 s0, s0, 0x900
	s_sub_i32 s0, s11, s0
	s_mul_i32 s1, s11, 0x600
	s_add_u32 s28, s58, s1
	s_addc_u32 s29, s59, 0
	s_add_u32 s30, s44, s1
	s_addc_u32 s31, s45, 0
	v_xor_b32_e32 v114, v9, v52
	v_xor_b32_e32 v115, v9, v53
	v_xor_b32_e32 v116, v9, v54
	v_xor_b32_e32 v117, v9, v55
	s_cmpk_ge_u32 s0, 0x100
	v_lshlrev_b32_e32 v100, 16, v34
	v_and_b32_e32 v101, 0xffff0000, v34
	v_lshlrev_b32_e32 v102, 16, v35
	v_and_b32_e32 v103, 0xffff0000, v35
	v_lshlrev_b32_e32 v104, 16, v36
	v_and_b32_e32 v105, 0xffff0000, v36
	v_lshlrev_b32_e32 v106, 16, v37
	v_and_b32_e32 v107, 0xffff0000, v37
	v_lshlrev_b32_e32 v108, 16, v38
	v_and_b32_e32 v109, 0xffff0000, v38
	v_lshlrev_b32_e32 v110, 16, v39
	v_and_b32_e32 v111, 0xffff0000, v39
	v_mul_f32_e32 v112, v100, v100
	v_fmac_f32_e32 v112, v101, v101
	v_fmac_f32_e32 v112, v102, v102
	v_fmac_f32_e32 v112, v103, v103
	v_fmac_f32_e32 v112, v104, v104
	v_fmac_f32_e32 v112, v105, v105
	v_fmac_f32_e32 v112, v106, v106
	v_fmac_f32_e32 v112, v107, v107
	v_fmac_f32_e32 v112, v108, v108
	v_fmac_f32_e32 v112, v109, v109
	v_fmac_f32_e32 v112, v110, v110
	v_fmac_f32_e32 v112, v111, v111
	v_mul_f32_e32 v100, v100, v10
	v_mul_f32_e32 v101, v101, v11
	v_add_f32_dpp v112, v112, v112 quad_perm:[1,0,3,2] row_mask:0xf bank_mask:0xf
	v_mul_f32_e32 v102, v102, v12
	v_mul_f32_e32 v103, v103, v13
	v_add_f32_dpp v112, v112, v112 quad_perm:[2,3,0,1] row_mask:0xf bank_mask:0xf
	v_mul_f32_e32 v104, v104, v14
	v_mul_f32_e32 v105, v105, v15
	v_add_f32_dpp v112, v112, v112 row_half_mirror row_mask:0xf bank_mask:0xf
	v_mul_f32_e32 v106, v106, v16
	v_mul_f32_e32 v107, v107, v17
	v_add_f32_dpp v112, v112, v112 row_mirror row_mask:0xf bank_mask:0xf
	v_mul_f32_e32 v108, v108, v18
	v_mul_f32_e32 v109, v109, v19
	v_mul_f32_e32 v110, v110, v20
	v_mul_f32_e32 v111, v111, v21
	v_add_f32_e32 v112, 0x3949539c, v112
	v_rsq_f32_e32 v113, v112
	s_nop 0
	v_mul_f32_e32 v108, v108, v113
	v_mul_f32_e32 v109, v109, v113
	v_mul_f32_e32 v110, v110, v113
	v_mul_f32_e32 v111, v111, v113
	v_mul_f32_e32 v100, v100, v113
	v_mul_f32_e32 v101, v101, v113
	v_mul_f32_e32 v102, v102, v113
	v_mul_f32_e32 v103, v103, v113
	v_mul_f32_e32 v104, v104, v113
	v_mul_f32_e32 v105, v105, v113
	v_mul_f32_e32 v106, v106, v113
	v_mul_f32_e32 v107, v107, v113
	s_cbranch_scc0 .Lmp_norope_q0
	v_mul_f32_dpp v118, v108, v114 row_ror:8 row_mask:0xf bank_mask:0xf
	v_mul_f32_dpp v119, v109, v115 row_ror:8 row_mask:0xf bank_mask:0xf
	v_mul_f32_dpp v120, v110, v116 row_ror:8 row_mask:0xf bank_mask:0xf
	v_mul_f32_dpp v121, v111, v117 row_ror:8 row_mask:0xf bank_mask:0xf
	v_fmac_f32_e32 v118, v108, v48
	v_fmac_f32_e32 v119, v109, v49
	v_fmac_f32_e32 v120, v110, v50
	v_fmac_f32_e32 v121, v111, v51
	s_branch .Lmp_ropedone_q0

.Lmp_ropedone_k8:
	v_cvt_pk_bf16_f32 v100, v100, v101
	v_cvt_pk_bf16_f32 v101, v102, v103
	v_cvt_pk_bf16_f32 v102, v104, v105
	v_cvt_pk_bf16_f32 v103, v106, v107
	v_cvt_pk_bf16_f32 v118, v118, v119
	v_cvt_pk_bf16_f32 v119, v120, v121
	global_store_dwordx4 v4, v[100:103], s[30:31]
	global_store_dwordx2 v5, v[118:119], s[30:31]
	s_nop 1
.LBB0_6572:
	v_readlane_b32 s0, v255, 22
	s_add_i32 s2, s0, 6
	v_readlane_b32 s0, v251, 39
	v_readlane_b32 s1, v251, 40
	s_cmp_ge_i32 s2, s1
	s_cbranch_scc1 .LBB0_6626
	s_waitcnt vmcnt(0)
	s_waitcnt lgkmcnt(0)
	s_barrier
	s_mov_b64 s[0:1], exec
	v_readlane_b32 s4, v251, 37
	v_readlane_b32 s5, v251, 38
	s_and_b64 s[4:5], s[0:1], s[4:5]
	s_mov_b64 exec, s[4:5]
	s_cbranch_execz .LBB0_6625
	v_readlane_b32 s3, v255, 11
	s_waitcnt vmcnt(0) expcnt(0) lgkmcnt(0)
	s_nop 0
	v_mov_b32_e32 v1, s3
	ds_read_b32 v4, v1
	v_readlane_b32 s3, v255, 12
	s_waitcnt lgkmcnt(0)
	v_cmp_ne_u32_e32 vcc, 0, v4
	v_mov_b32_e32 v1, s3
	ds_read_b32 v2, v1
	s_cbranch_vccnz .LBB0_6589
	v_readlane_b32 s20, v251, 0
	v_readlane_b32 s21, v251, 1
	s_load_dwordx2 s[4:5], s[20:21], 0x4
	v_readlane_b32 s3, v251, 2
	s_mov_b32 s6, 1
	s_waitcnt lgkmcnt(0)
	s_mul_i32 s3, s4, s3
	s_mul_i32 s3, s3, s5
	s_branch .LBB0_6577

.LBB0_8841:
	s_andn2_b64 vcc, exec, s[0:1]
	s_cbranch_vccnz .LBB0_8937
	v_readlane_b32 s0, v255, 20
	v_readlane_b32 s1, v255, 21
	s_lshl_b32 s6, s0, 15
	v_readlane_b32 s40, v251, 21
	s_lshl_b64 s[0:1], s[6:7], 2
	v_readlane_b32 s48, v251, 29
	v_readlane_b32 s49, v251, 30
	s_add_u32 s2, s48, s0
	s_waitcnt vmcnt(0)
	v_mov_b32_e32 v4, v0
	s_addc_u32 s3, s49, s1
	v_readlane_b32 s8, v251, 57
	v_ashrrev_i32_e32 v5, 31, v4
	v_lshl_add_u64 v[62:63], v[4:5], 4, s[2:3]
	s_movk_i32 s2, 0x2000
	v_add_co_u32_e32 v10, vcc, s2, v62
	v_readlane_b32 s10, v251, 59
	v_readlane_b32 s11, v251, 60
	v_addc_co_u32_e32 v11, vcc, 0, v63, vcc
	s_movk_i32 s2, 0x4000
	s_mov_b64 s[0:1], s[10:11]
	v_add_co_u32_e32 v14, vcc, s2, v62
	s_waitcnt lgkmcnt(0)
	s_barrier
	global_load_dwordx4 v[6:9], v[62:63], off
	s_nop 0
	global_load_dwordx4 v[10:13], v[10:11], off
	v_addc_co_u32_e32 v15, vcc, 0, v63, vcc
	s_movk_i32 s2, 0x6000
	v_add_co_u32_e32 v18, vcc, s2, v62
	s_mov_b32 s2, 0x8000
	s_nop 0
	v_addc_co_u32_e32 v19, vcc, 0, v63, vcc
	global_load_dwordx4 v[14:17], v[14:15], off
	s_nop 0
	global_load_dwordx4 v[18:21], v[18:19], off
	v_add_co_u32_e32 v22, vcc, s2, v62
	s_mov_b32 s2, 0xa000
	s_nop 0
	v_addc_co_u32_e32 v23, vcc, 0, v63, vcc
	v_add_co_u32_e32 v26, vcc, s2, v62
	s_mov_b32 s2, 0xc000
	s_nop 0
	v_addc_co_u32_e32 v27, vcc, 0, v63, vcc
	global_load_dwordx4 v[22:25], v[22:23], off
	s_nop 0
	global_load_dwordx4 v[26:29], v[26:27], off
	v_add_co_u32_e32 v30, vcc, s2, v62
	s_mov_b32 s2, 0xe000
	s_nop 0
	v_addc_co_u32_e32 v31, vcc, 0, v63, vcc
	v_add_co_u32_e32 v34, vcc, s2, v62
	s_mov_b32 s2, 0x10000
	s_nop 0
	v_addc_co_u32_e32 v35, vcc, 0, v63, vcc
	global_load_dwordx4 v[30:33], v[30:31], off
	s_nop 0
	global_load_dwordx4 v[34:37], v[34:35], off
	v_add_co_u32_e32 v38, vcc, s2, v62
	s_mov_b32 s2, 0x12000
	s_nop 0
	v_addc_co_u32_e32 v39, vcc, 0, v63, vcc
	v_add_co_u32_e32 v42, vcc, s2, v62
	s_mov_b32 s2, 0x14000
	s_nop 0
	v_addc_co_u32_e32 v43, vcc, 0, v63, vcc
	global_load_dwordx4 v[38:41], v[38:39], off
	s_nop 0
	global_load_dwordx4 v[42:45], v[42:43], off
	v_add_co_u32_e32 v46, vcc, s2, v62
	s_mov_b32 s2, 0x16000
	s_nop 0
	v_addc_co_u32_e32 v47, vcc, 0, v63, vcc
	v_add_co_u32_e32 v50, vcc, s2, v62
	s_mov_b32 s2, 0x18000
	s_nop 0
	v_addc_co_u32_e32 v51, vcc, 0, v63, vcc
	global_load_dwordx4 v[46:49], v[46:47], off
	s_nop 0
	global_load_dwordx4 v[50:53], v[50:51], off
	v_add_co_u32_e32 v54, vcc, s2, v62
	s_mov_b32 s2, 0x1a000
	s_nop 0
	v_addc_co_u32_e32 v55, vcc, 0, v63, vcc
	v_add_co_u32_e32 v58, vcc, s2, v62
	s_mov_b32 s2, 0x1c000
	s_nop 0
	v_addc_co_u32_e32 v59, vcc, 0, v63, vcc
	global_load_dwordx4 v[54:57], v[54:55], off
	s_nop 0
	global_load_dwordx4 v[58:61], v[58:59], off
	v_add_co_u32_e32 v64, vcc, s2, v62
	s_mov_b32 s2, 0x1e000
	s_nop 0
	v_addc_co_u32_e32 v65, vcc, 0, v63, vcc
	v_add_co_u32_e32 v66, vcc, s2, v62
	v_lshlrev_b32_e32 v1, 2, v4
	s_nop 0
	v_addc_co_u32_e32 v67, vcc, 0, v63, vcc
	global_load_dwordx4 v[62:65], v[64:65], off
	s_nop 0
	global_load_dwordx4 v[66:69], v[66:67], off
	v_add_u32_e32 v2, 0x200, v4
	v_and_b32_e32 v1, 12, v1
	v_and_b32_e32 v83, -4, v4
	v_mul_u32_u24_e32 v1, 0x2010, v1
	v_and_b32_e32 v2, -4, v2
	v_add_u32_e32 v5, 0x400, v4
	v_add3_u32 v83, 0, v83, v1
	v_add3_u32 v2, 0, v2, v1
	s_waitcnt vmcnt(15)
	ds_write_b32 v83, v6
	ds_write_b32 v83, v7 offset:8208
	ds_write_b32 v83, v8 offset:16416
	ds_write_b32 v83, v9 offset:24624
	s_waitcnt vmcnt(14)
	ds_write_b32 v2, v10
	ds_write_b32 v2, v11 offset:8208
	ds_write_b32 v2, v12 offset:16416
	ds_write_b32 v2, v13 offset:24624
	v_and_b32_e32 v2, -4, v5
	v_add_u32_e32 v70, 0x600, v4
	v_add3_u32 v2, 0, v2, v1
	s_waitcnt vmcnt(13)
	ds_write_b32 v2, v14
	ds_write_b32 v2, v15 offset:8208
	ds_write_b32 v2, v16 offset:16416
	ds_write_b32 v2, v17 offset:24624
	v_and_b32_e32 v2, -4, v70
	v_add_u32_e32 v71, 0x800, v4
	v_add3_u32 v2, 0, v2, v1
	s_waitcnt vmcnt(12)
	ds_write_b32 v2, v18
	ds_write_b32 v2, v19 offset:8208
	ds_write_b32 v2, v20 offset:16416
	ds_write_b32 v2, v21 offset:24624
	v_and_b32_e32 v2, -4, v71
	v_add_u32_e32 v72, 0xa00, v4
	v_add3_u32 v2, 0, v2, v1
	s_waitcnt vmcnt(11)
	ds_write_b32 v2, v22
	ds_write_b32 v2, v23 offset:8208
	ds_write_b32 v2, v24 offset:16416
	ds_write_b32 v2, v25 offset:24624
	v_and_b32_e32 v2, -4, v72
	v_add_u32_e32 v73, 0xc00, v4
	v_add3_u32 v2, 0, v2, v1
	s_waitcnt vmcnt(10)
	ds_write_b32 v2, v26
	ds_write_b32 v2, v27 offset:8208
	ds_write_b32 v2, v28 offset:16416
	ds_write_b32 v2, v29 offset:24624
	v_and_b32_e32 v2, -4, v73
	v_add_u32_e32 v74, 0xe00, v4
	v_add3_u32 v2, 0, v2, v1
	s_waitcnt vmcnt(9)
	ds_write_b32 v2, v30
	ds_write_b32 v2, v31 offset:8208
	ds_write_b32 v2, v32 offset:16416
	ds_write_b32 v2, v33 offset:24624
	v_and_b32_e32 v2, -4, v74
	v_add_u32_e32 v75, 0x1000, v4
	v_add3_u32 v2, 0, v2, v1
	s_waitcnt vmcnt(8)
	ds_write_b32 v2, v34
	ds_write_b32 v2, v35 offset:8208
	ds_write_b32 v2, v36 offset:16416
	ds_write_b32 v2, v37 offset:24624
	v_and_b32_e32 v2, -4, v75
	v_add_u32_e32 v76, 0x1200, v4
	v_add3_u32 v2, 0, v2, v1
	s_waitcnt vmcnt(7)
	ds_write_b32 v2, v38
	ds_write_b32 v2, v39 offset:8208
	ds_write_b32 v2, v40 offset:16416
	ds_write_b32 v2, v41 offset:24624
	v_and_b32_e32 v2, -4, v76
	v_add_u32_e32 v77, 0x1400, v4
	v_add3_u32 v2, 0, v2, v1
	s_waitcnt vmcnt(6)
	ds_write_b32 v2, v42
	ds_write_b32 v2, v43 offset:8208
	ds_write_b32 v2, v44 offset:16416
	ds_write_b32 v2, v45 offset:24624
	v_and_b32_e32 v2, -4, v77
	v_add_u32_e32 v78, 0x1600, v4
	v_add3_u32 v2, 0, v2, v1
	s_waitcnt vmcnt(5)
	ds_write_b32 v2, v46
	ds_write_b32 v2, v47 offset:8208
	ds_write_b32 v2, v48 offset:16416
	ds_write_b32 v2, v49 offset:24624
	v_and_b32_e32 v2, -4, v78
	v_add_u32_e32 v79, 0x1800, v4
	v_add3_u32 v2, 0, v2, v1
	s_waitcnt vmcnt(4)
	ds_write_b32 v2, v50
	ds_write_b32 v2, v51 offset:8208
	ds_write_b32 v2, v52 offset:16416
	ds_write_b32 v2, v53 offset:24624
	v_and_b32_e32 v2, -4, v79
	v_add_u32_e32 v80, 0x1a00, v4
	v_add3_u32 v2, 0, v2, v1
	s_waitcnt vmcnt(3)
	ds_write_b32 v2, v54
	ds_write_b32 v2, v55 offset:8208
	ds_write_b32 v2, v56 offset:16416
	ds_write_b32 v2, v57 offset:24624
	v_and_b32_e32 v2, -4, v80
	v_add_u32_e32 v81, 0x1c00, v4
	v_add3_u32 v2, 0, v2, v1
	v_readfirstlane_b32 s4, v4
	s_waitcnt vmcnt(2)
	ds_write_b32 v2, v58
	ds_write_b32 v2, v59 offset:8208
	ds_write_b32 v2, v60 offset:16416
	ds_write_b32 v2, v61 offset:24624
	v_and_b32_e32 v2, -4, v81
	v_add_u32_e32 v82, 0x1e00, v4
	s_ashr_i32 s2, s4, 6
	v_add3_u32 v2, 0, v2, v1
	v_readlane_b32 s3, v251, 61
	s_waitcnt vmcnt(1)
	ds_write_b32 v2, v62
	ds_write_b32 v2, v63 offset:8208
	ds_write_b32 v2, v64 offset:16416
	ds_write_b32 v2, v65 offset:24624
	v_and_b32_e32 v2, -4, v82
	s_add_i32 s20, s2, s3
	v_add3_u32 v1, 0, v2, v1
	s_cmpk_gt_i32 s20, 0x47ff
	v_readlane_b32 s41, v251, 22
	v_readlane_b32 s42, v251, 23
	v_readlane_b32 s43, v251, 24
	v_readlane_b32 s44, v251, 25
	v_readlane_b32 s45, v251, 26
	v_readlane_b32 s46, v251, 27
	v_readlane_b32 s47, v251, 28
	v_readlane_b32 s50, v251, 31
	v_readlane_b32 s51, v251, 32
	v_readlane_b32 s52, v251, 33
	v_readlane_b32 s53, v251, 34
	v_readlane_b32 s54, v251, 35
	v_readlane_b32 s55, v251, 36
	v_readlane_b32 s9, v251, 58
	s_waitcnt vmcnt(0)
	ds_write_b32 v1, v66
	ds_write_b32 v1, v67 offset:8208
	ds_write_b32 v1, v68 offset:16416
	ds_write_b32 v1, v69 offset:24624
	s_waitcnt lgkmcnt(0)
	s_barrier
	s_cbranch_scc1 .LBB0_8883
	v_readlane_b32 s4, v251, 59
	v_readlane_b32 s5, v251, 60
	v_readlane_b32 s8, v255, 20
	v_readlane_b32 s10, v251, 61
	v_readfirstlane_b32 s0, v0
	v_readlane_b32 s56, v251, 55
	v_readlane_b32 s57, v251, 56
	s_nop 3
	s_lshr_b32 s0, s0, 6
	s_add_i32 s10, s10, s0
	s_lshl_b32 s1, s8, 13
	s_add_u32 s56, s56, s1
	s_addc_u32 s57, s57, 0
	s_add_u32 s58, s56, 0x1000
	s_addc_u32 s59, s57, 0
	s_add_u32 s48, s4, 0x33c90000
	s_addc_u32 s49, s5, 0
	s_add_u32 s50, s4, 0x3cc90000
	s_addc_u32 s51, s5, 0
	s_add_u32 s54, s4, 0x388000
	s_addc_u32 s55, s5, 0
	s_mul_i32 s1, s8, 0x6c000
	s_add_i32 s1, s1, 0x10000
	s_add_u32 s52, s4, s1
	s_addc_u32 s53, s5, 0
	s_mov_b32 s62, 0xaaaaaaaa
	s_mov_b32 s63, 0xaaaaaaaa
	s_mov_b32 s64, 0xcccccccc
	s_mov_b32 s65, 0xcccccccc
	s_mov_b32 s66, 0xf0f0f0f0
	s_mov_b32 s67, 0xf0f0f0f0
	s_mov_b32 s68, 0xff00ff00
	s_mov_b32 s69, 0xff00ff00
	v_and_b32_e32 v191, 63, v0
	v_lshlrev_b32_e32 v1, 4, v191
	v_lshlrev_b32_e32 v2, 3, v191
	v_mov_b32_e32 v152, v1
	v_add_u32_e32 v153, 0x10080, v1
	v_and_b32_e32 v164, 15, v191
	s_movk_i32 s0, 0x2400
	v_mul_u32_u24_e32 v164, s0, v164
	v_xor_b32_e32 v165, 16, v191
	v_lshlrev_b32_e32 v165, 2, v165
	v_xor_b32_e32 v166, 32, v191
	v_lshlrev_b32_e32 v166, 2, v166
	s_add_i32 s11, s10, 0x0
	s_lshr_b32 s0, s11, 8
	s_mul_i32 s0, s0, 57
	s_lshr_b32 s0, s0, 9
	s_mul_i32 s1, s0, 0x900
	s_sub_i32 s43, s11, s1
	s_lshl_b32 s1, s11, 13
	s_add_u32 s12, s48, s1
	s_addc_u32 s13, s49, 0
	s_add_u32 s14, s12, 0x1000
	s_addc_u32 s15, s13, 0
	global_load_dwordx4 v[100:103], v1, s[12:13]
	global_load_dwordx4 v[104:107], v1, s[12:13] offset:1024
	global_load_dwordx4 v[108:111], v1, s[12:13] offset:2048
	global_load_dwordx4 v[112:115], v1, s[12:13] offset:3072
	global_load_dwordx4 v[116:119], v1, s[14:15]
	global_load_dwordx4 v[120:123], v1, s[14:15] offset:1024
	global_load_dwordx4 v[124:127], v1, s[14:15] offset:2048
	global_load_dwordx4 v[128:131], v1, s[14:15] offset:3072
	s_add_i32 s11, s10, 0x0
	s_lshr_b32 s0, s11, 8
	s_mul_i32 s0, s0, 57
	s_lshr_b32 s0, s0, 9
	s_mul_i32 s1, s0, 0x900
	s_sub_i32 s43, s11, s1
	s_cmpk_lt_u32 s43, 0x100
	s_cselect_b32 s0, 8, s0
	s_mul_i32 s1, s0, 0xc000
	s_add_u32 s18, s52, s1
	s_addc_u32 s19, s53, 0
	s_add_u32 s18, s18, 0x6000
	s_addc_u32 s19, s19, 0
	s_add_u32 s22, s18, 0x1000
	s_addc_u32 s23, s19, 0
	s_add_u32 s28, s18, 0x2000
	s_addc_u32 s29, s19, 0
	s_add_u32 s30, s18, 0x3000
	s_addc_u32 s31, s19, 0
	global_load_dwordx4 v[4:7], v1, s[56:57]
	global_load_dwordx4 v[36:39], v1, s[28:29]
	global_load_dwordx4 v[68:71], v1, s[18:19]
	global_load_dwordx4 v[8:11], v1, s[56:57] offset:1024
	global_load_dwordx4 v[40:43], v1, s[28:29] offset:1024
	global_load_dwordx4 v[72:75], v1, s[18:19] offset:1024
	global_load_dwordx4 v[12:15], v1, s[56:57] offset:2048
	global_load_dwordx4 v[44:47], v1, s[28:29] offset:2048
	global_load_dwordx4 v[76:79], v1, s[18:19] offset:2048
	global_load_dwordx4 v[16:19], v1, s[56:57] offset:3072
	global_load_dwordx4 v[48:51], v1, s[28:29] offset:3072
	global_load_dwordx4 v[80:83], v1, s[18:19] offset:3072
	global_load_dwordx4 v[20:23], v1, s[58:59]
	global_load_dwordx4 v[52:55], v1, s[30:31]
	global_load_dwordx4 v[84:87], v1, s[22:23]
	global_load_dwordx4 v[24:27], v1, s[58:59] offset:1024
	global_load_dwordx4 v[56:59], v1, s[30:31] offset:1024
	global_load_dwordx4 v[88:91], v1, s[22:23] offset:1024
	global_load_dwordx4 v[28:31], v1, s[58:59] offset:2048
	global_load_dwordx4 v[60:63], v1, s[30:31] offset:2048
	global_load_dwordx4 v[92:95], v1, s[22:23] offset:2048
	global_load_dwordx4 v[32:35], v1, s[58:59] offset:3072
	global_load_dwordx4 v[64:67], v1, s[30:31] offset:3072
	global_load_dwordx4 v[96:99], v1, s[22:23] offset:3072
	s_add_i32 s11, s10, 0x800
	s_lshr_b32 s0, s11, 8
	s_mul_i32 s0, s0, 57
	s_lshr_b32 s0, s0, 9
	s_mul_i32 s1, s0, 0x900
	s_sub_i32 s43, s11, s1
	s_lshl_b32 s1, s11, 13
	s_add_u32 s12, s48, s1
	s_addc_u32 s13, s49, 0
	s_add_u32 s14, s12, 0x1000
	s_addc_u32 s15, s13, 0
	global_load_dwordx4 v[204:207], v1, s[12:13]
	global_load_dwordx4 v[208:211], v1, s[12:13] offset:1024
	global_load_dwordx4 v[212:215], v1, s[12:13] offset:2048
	global_load_dwordx4 v[216:219], v1, s[12:13] offset:3072
	global_load_dwordx4 v[226:229], v1, s[14:15]
	global_load_dwordx4 v[230:233], v1, s[14:15] offset:1024
	global_load_dwordx4 v[234:237], v1, s[14:15] offset:2048
	global_load_dwordx4 v[238:241], v1, s[14:15] offset:3072
	s_waitcnt vmcnt(8)
	s_add_i32 s11, s10, 0x0
	s_lshr_b32 s0, s11, 8
	s_mul_i32 s0, s0, 57
	s_lshr_b32 s0, s0, 9
	s_mul_i32 s1, s0, 0x900
	s_sub_i32 s43, s11, s1
	s_lshl_b32 s1, s11, 12
	s_add_u32 s16, s50, s1
	s_addc_u32 s17, s51, 0
	s_mul_i32 s1, s0, 0x24000
	s_lshl_b32 s2, s43, 2
	s_add_i32 s1, s1, s2
	s_add_u32 s34, s54, s1
	s_addc_u32 s35, s55, 0
	v_mul_f32_e32 v184, v100, v100
	v_fmac_f32_e32 v184, v101, v101
	v_fmac_f32_e32 v184, v102, v102
	v_fmac_f32_e32 v184, v103, v103
	v_fmac_f32_e32 v184, v104, v104
	v_fmac_f32_e32 v184, v105, v105
	v_fmac_f32_e32 v184, v106, v106
	v_fmac_f32_e32 v184, v107, v107
	v_fmac_f32_e32 v184, v108, v108
	v_fmac_f32_e32 v184, v109, v109
	v_fmac_f32_e32 v184, v110, v110
	v_fmac_f32_e32 v184, v111, v111
	v_fmac_f32_e32 v184, v112, v112
	v_fmac_f32_e32 v184, v113, v113
	v_fmac_f32_e32 v184, v114, v114
	v_fmac_f32_e32 v184, v115, v115
	v_fmac_f32_e32 v184, v116, v116
	v_fmac_f32_e32 v184, v117, v117
	v_fmac_f32_e32 v184, v118, v118
	v_fmac_f32_e32 v184, v119, v119
	v_fmac_f32_e32 v184, v120, v120
	v_fmac_f32_e32 v184, v121, v121
	v_fmac_f32_e32 v184, v122, v122
	v_fmac_f32_e32 v184, v123, v123
	v_fmac_f32_e32 v184, v124, v124
	v_fmac_f32_e32 v184, v125, v125
	v_fmac_f32_e32 v184, v126, v126
	v_fmac_f32_e32 v184, v127, v127
	v_fmac_f32_e32 v184, v128, v128
	v_fmac_f32_e32 v184, v129, v129
	v_fmac_f32_e32 v184, v130, v130
	v_fmac_f32_e32 v184, v131, v131
	ds_read_b128 v[168:171], v152 offset:0
	ds_read_b128 v[172:175], v152 offset:8208
	ds_read_b128 v[176:179], v152 offset:16416
	ds_read_b128 v[180:183], v152 offset:24624
	s_nop 0
	v_add_f32_dpp v184, v184, v184 quad_perm:[1,0,3,2] row_mask:0xf bank_mask:0xf
	s_nop 1
	v_add_f32_dpp v184, v184, v184 quad_perm:[2,3,0,1] row_mask:0xf bank_mask:0xf
	s_nop 1
	v_add_f32_dpp v184, v184, v184 row_half_mirror row_mask:0xf bank_mask:0xf
	s_nop 1
	v_add_f32_dpp v184, v184, v184 row_mirror row_mask:0xf bank_mask:0xf
	s_nop 1
	v_readlane_b32 s0, v184, 0
	v_readlane_b32 s1, v184, 16
	v_readlane_b32 s2, v184, 32
	v_readlane_b32 s3, v184, 48
	v_fma_f32 v4, v4, v36, v4
	v_fma_f32 v5, v5, v37, v5
	v_fma_f32 v6, v6, v38, v6
	v_fma_f32 v7, v7, v39, v7
	v_fma_f32 v8, v8, v40, v8
	v_fma_f32 v9, v9, v41, v9
	v_fma_f32 v10, v10, v42, v10
	v_fma_f32 v11, v11, v43, v11
	v_fma_f32 v12, v12, v44, v12
	v_fma_f32 v13, v13, v45, v13
	v_fma_f32 v14, v14, v46, v14
	v_fma_f32 v15, v15, v47, v15
	v_fma_f32 v16, v16, v48, v16
	v_fma_f32 v17, v17, v49, v17
	v_fma_f32 v18, v18, v50, v18
	v_fma_f32 v19, v19, v51, v19
	v_fma_f32 v20, v20, v52, v20
	v_fma_f32 v21, v21, v53, v21
	v_fma_f32 v22, v22, v54, v22
	v_fma_f32 v23, v23, v55, v23
	v_fma_f32 v24, v24, v56, v24
	v_fma_f32 v25, v25, v57, v25
	v_fma_f32 v26, v26, v58, v26
	v_fma_f32 v27, v27, v59, v27
	v_fma_f32 v28, v28, v60, v28
	v_fma_f32 v29, v29, v61, v29
	v_fma_f32 v30, v30, v62, v30
	v_fma_f32 v31, v31, v63, v31
	v_fma_f32 v32, v32, v64, v32
	v_fma_f32 v33, v33, v65, v33
	v_fma_f32 v34, v34, v66, v34
	v_fma_f32 v35, v35, v67, v35
	v_mov_b32_e32 v190, s0
	v_add_f32_e32 v190, s1, v190
	v_add_f32_e32 v190, s2, v190
	v_add_f32_e32 v190, s3, v190
	v_mul_f32_e32 v190, 0x3a000000, v190
	v_add_f32_e32 v190, 0x358637bd, v190
	v_rsq_f32_e32 v190, v190
	s_nop 0
	v_mul_f32_e32 v4, v4, v190
	v_mul_f32_e32 v5, v5, v190
	v_mul_f32_e32 v6, v6, v190
	v_mul_f32_e32 v7, v7, v190
	v_mul_f32_e32 v8, v8, v190
	v_mul_f32_e32 v9, v9, v190
	v_mul_f32_e32 v10, v10, v190
	v_mul_f32_e32 v11, v11, v190
	v_mul_f32_e32 v12, v12, v190
	v_mul_f32_e32 v13, v13, v190
	v_mul_f32_e32 v14, v14, v190
	v_mul_f32_e32 v15, v15, v190
	v_mul_f32_e32 v16, v16, v190
	v_mul_f32_e32 v17, v17, v190
	v_mul_f32_e32 v18, v18, v190
	v_mul_f32_e32 v19, v19, v190
	v_mul_f32_e32 v20, v20, v190
	v_mul_f32_e32 v21, v21, v190
	v_mul_f32_e32 v22, v22, v190
	v_mul_f32_e32 v23, v23, v190
	v_mul_f32_e32 v24, v24, v190
	v_mul_f32_e32 v25, v25, v190
	v_mul_f32_e32 v26, v26, v190
	v_mul_f32_e32 v27, v27, v190
	v_mul_f32_e32 v28, v28, v190
	v_mul_f32_e32 v29, v29, v190
	v_mul_f32_e32 v30, v30, v190
	v_mul_f32_e32 v31, v31, v190
	v_mul_f32_e32 v32, v32, v190
	v_mul_f32_e32 v33, v33, v190
	v_mul_f32_e32 v34, v34, v190
	v_mul_f32_e32 v35, v35, v190
	v_fma_f32 v100, v100, v4, v68
	v_fma_f32 v101, v101, v5, v69
	v_fma_f32 v102, v102, v6, v70
	v_fma_f32 v103, v103, v7, v71
	v_fma_f32 v104, v104, v8, v72
	v_fma_f32 v105, v105, v9, v73
	v_fma_f32 v106, v106, v10, v74
	v_fma_f32 v107, v107, v11, v75
	v_fma_f32 v108, v108, v12, v76
	v_fma_f32 v109, v109, v13, v77
	v_fma_f32 v110, v110, v14, v78
	v_fma_f32 v111, v111, v15, v79
	v_fma_f32 v112, v112, v16, v80
	v_fma_f32 v113, v113, v17, v81
	v_fma_f32 v114, v114, v18, v82
	v_fma_f32 v115, v115, v19, v83
	v_fma_f32 v116, v116, v20, v84
	v_fma_f32 v117, v117, v21, v85
	v_fma_f32 v118, v118, v22, v86
	v_fma_f32 v119, v119, v23, v87
	v_fma_f32 v120, v120, v24, v88
	v_fma_f32 v121, v121, v25, v89
	v_fma_f32 v122, v122, v26, v90
	v_fma_f32 v123, v123, v27, v91
	v_fma_f32 v124, v124, v28, v92
	v_fma_f32 v125, v125, v29, v93
	v_fma_f32 v126, v126, v30, v94
	v_fma_f32 v127, v127, v31, v95
	v_fma_f32 v128, v128, v32, v96
	v_fma_f32 v129, v129, v33, v97
	v_fma_f32 v130, v130, v34, v98
	v_fma_f32 v131, v131, v35, v99
	v_cvt_pk_bf16_f32 v242, v100, v101
	v_cvt_pk_bf16_f32 v243, v102, v103
	global_store_dwordx2 v2, v[242:243], s[16:17]
	v_cvt_pk_bf16_f32 v244, v104, v105
	v_cvt_pk_bf16_f32 v245, v106, v107
	global_store_dwordx2 v2, v[244:245], s[16:17] offset:512
	v_cvt_pk_bf16_f32 v242, v108, v109
	v_cvt_pk_bf16_f32 v243, v110, v111
	global_store_dwordx2 v2, v[242:243], s[16:17] offset:1024
	v_cvt_pk_bf16_f32 v244, v112, v113
	v_cvt_pk_bf16_f32 v245, v114, v115
	global_store_dwordx2 v2, v[244:245], s[16:17] offset:1536
	v_cvt_pk_bf16_f32 v242, v116, v117
	v_cvt_pk_bf16_f32 v243, v118, v119
	global_store_dwordx2 v2, v[242:243], s[16:17] offset:2048
	v_cvt_pk_bf16_f32 v244, v120, v121
	v_cvt_pk_bf16_f32 v245, v122, v123
	global_store_dwordx2 v2, v[244:245], s[16:17] offset:2560
	v_cvt_pk_bf16_f32 v242, v124, v125
	v_cvt_pk_bf16_f32 v243, v126, v127
	global_store_dwordx2 v2, v[242:243], s[16:17] offset:3072
	v_cvt_pk_bf16_f32 v244, v128, v129
	v_cvt_pk_bf16_f32 v245, v130, v131
	global_store_dwordx2 v2, v[244:245], s[16:17] offset:3584
	s_add_i32 s11, s10, 0x800
	s_lshr_b32 s0, s11, 8
	s_mul_i32 s0, s0, 57
	s_lshr_b32 s0, s0, 9
	s_mul_i32 s1, s0, 0x900
	s_sub_i32 s43, s11, s1
	s_cmpk_lt_u32 s43, 0x100
	s_cselect_b32 s0, 8, s0
	s_mul_i32 s1, s0, 0xc000
	s_add_u32 s18, s52, s1
	s_addc_u32 s19, s53, 0
	s_add_u32 s18, s18, 0x6000
	s_addc_u32 s19, s19, 0
	s_add_u32 s22, s18, 0x1000
	s_addc_u32 s23, s19, 0
	s_add_u32 s28, s18, 0x2000
	s_addc_u32 s29, s19, 0
	s_add_u32 s30, s18, 0x3000
	s_addc_u32 s31, s19, 0
	global_load_dwordx4 v[4:7], v1, s[56:57]
	global_load_dwordx4 v[36:39], v1, s[28:29]
	global_load_dwordx4 v[68:71], v1, s[18:19]
	global_load_dwordx4 v[8:11], v1, s[56:57] offset:1024
	global_load_dwordx4 v[40:43], v1, s[28:29] offset:1024
	global_load_dwordx4 v[72:75], v1, s[18:19] offset:1024
	global_load_dwordx4 v[12:15], v1, s[56:57] offset:2048
	global_load_dwordx4 v[44:47], v1, s[28:29] offset:2048
	global_load_dwordx4 v[76:79], v1, s[18:19] offset:2048
	global_load_dwordx4 v[16:19], v1, s[56:57] offset:3072
	global_load_dwordx4 v[48:51], v1, s[28:29] offset:3072
	global_load_dwordx4 v[80:83], v1, s[18:19] offset:3072
	global_load_dwordx4 v[20:23], v1, s[58:59]
	global_load_dwordx4 v[52:55], v1, s[30:31]
	global_load_dwordx4 v[84:87], v1, s[22:23]
	global_load_dwordx4 v[24:27], v1, s[58:59] offset:1024
	global_load_dwordx4 v[56:59], v1, s[30:31] offset:1024
	global_load_dwordx4 v[88:91], v1, s[22:23] offset:1024
	global_load_dwordx4 v[28:31], v1, s[58:59] offset:2048
	global_load_dwordx4 v[60:63], v1, s[30:31] offset:2048
	global_load_dwordx4 v[92:95], v1, s[22:23] offset:2048
	global_load_dwordx4 v[32:35], v1, s[58:59] offset:3072
	global_load_dwordx4 v[64:67], v1, s[30:31] offset:3072
	global_load_dwordx4 v[96:99], v1, s[22:23] offset:3072
	v_mov_b32_e32 v132, 0
	v_mov_b32_e32 v133, 0
	v_mov_b32_e32 v134, 0
	v_mov_b32_e32 v135, 0
	v_mov_b32_e32 v136, 0
	v_mov_b32_e32 v137, 0
	v_mov_b32_e32 v138, 0
	v_mov_b32_e32 v139, 0
	v_mov_b32_e32 v140, 0
	v_mov_b32_e32 v141, 0
	v_mov_b32_e32 v142, 0
	v_mov_b32_e32 v143, 0
	v_mov_b32_e32 v144, 0
	v_mov_b32_e32 v145, 0
	v_mov_b32_e32 v146, 0
	v_mov_b32_e32 v147, 0
	ds_read_b128 v[148:151], v152 offset:32832
	ds_read_b128 v[186:189], v152 offset:41040
	ds_read_b128 v[194:197], v152 offset:49248
	ds_read_b128 v[198:201], v152 offset:57456
	s_waitcnt lgkmcnt(4)
	v_fmac_f32_e32 v132, v100, v168
	v_fmac_f32_e32 v132, v101, v169
	v_fmac_f32_e32 v132, v102, v170
	v_fmac_f32_e32 v132, v103, v171
	v_fmac_f32_e32 v133, v100, v172
	v_fmac_f32_e32 v133, v101, v173
	v_fmac_f32_e32 v133, v102, v174
	v_fmac_f32_e32 v133, v103, v175
	v_fmac_f32_e32 v134, v100, v176
	v_fmac_f32_e32 v134, v101, v177
	v_fmac_f32_e32 v134, v102, v178
	v_fmac_f32_e32 v134, v103, v179
	v_fmac_f32_e32 v135, v100, v180
	v_fmac_f32_e32 v135, v101, v181
	v_fmac_f32_e32 v135, v102, v182
	v_fmac_f32_e32 v135, v103, v183
	ds_read_b128 v[168:171], v153 offset:0
	ds_read_b128 v[172:175], v153 offset:8208
	ds_read_b128 v[176:179], v153 offset:16416
	ds_read_b128 v[180:183], v153 offset:24624
	s_waitcnt lgkmcnt(4)
	v_fmac_f32_e32 v136, v100, v148
	v_fmac_f32_e32 v136, v101, v149
	v_fmac_f32_e32 v136, v102, v150
	v_fmac_f32_e32 v136, v103, v151
	v_fmac_f32_e32 v137, v100, v186
	v_fmac_f32_e32 v137, v101, v187
	v_fmac_f32_e32 v137, v102, v188
	v_fmac_f32_e32 v137, v103, v189
	v_fmac_f32_e32 v138, v100, v194
	v_fmac_f32_e32 v138, v101, v195
	v_fmac_f32_e32 v138, v102, v196
	v_fmac_f32_e32 v138, v103, v197
	v_fmac_f32_e32 v139, v100, v198
	v_fmac_f32_e32 v139, v101, v199
	v_fmac_f32_e32 v139, v102, v200
	v_fmac_f32_e32 v139, v103, v201
	ds_read_b128 v[148:151], v153 offset:32832
	ds_read_b128 v[186:189], v153 offset:41040
	ds_read_b128 v[194:197], v153 offset:49248
	ds_read_b128 v[198:201], v153 offset:57456
	s_waitcnt lgkmcnt(4)
	v_fmac_f32_e32 v140, v100, v168
	v_fmac_f32_e32 v140, v101, v169
	v_fmac_f32_e32 v140, v102, v170
	v_fmac_f32_e32 v140, v103, v171
	v_fmac_f32_e32 v141, v100, v172
	v_fmac_f32_e32 v141, v101, v173
	v_fmac_f32_e32 v141, v102, v174
	v_fmac_f32_e32 v141, v103, v175
	v_fmac_f32_e32 v142, v100, v176
	v_fmac_f32_e32 v142, v101, v177
	v_fmac_f32_e32 v142, v102, v178
	v_fmac_f32_e32 v142, v103, v179
	v_fmac_f32_e32 v143, v100, v180
	v_fmac_f32_e32 v143, v101, v181
	v_fmac_f32_e32 v143, v102, v182
	v_fmac_f32_e32 v143, v103, v183
	ds_read_b128 v[168:171], v152 offset:1024
	ds_read_b128 v[172:175], v152 offset:9232
	ds_read_b128 v[176:179], v152 offset:17440
	ds_read_b128 v[180:183], v152 offset:25648
	s_waitcnt lgkmcnt(4)
	v_fmac_f32_e32 v144, v100, v148
	v_fmac_f32_e32 v144, v101, v149
	v_fmac_f32_e32 v144, v102, v150
	v_fmac_f32_e32 v144, v103, v151
	v_fmac_f32_e32 v145, v100, v186
	v_fmac_f32_e32 v145, v101, v187
	v_fmac_f32_e32 v145, v102, v188
	v_fmac_f32_e32 v145, v103, v189
	v_fmac_f32_e32 v146, v100, v194
	v_fmac_f32_e32 v146, v101, v195
	v_fmac_f32_e32 v146, v102, v196
	v_fmac_f32_e32 v146, v103, v197
	v_fmac_f32_e32 v147, v100, v198
	v_fmac_f32_e32 v147, v101, v199
	v_fmac_f32_e32 v147, v102, v200
	v_fmac_f32_e32 v147, v103, v201
	ds_read_b128 v[148:151], v152 offset:33856
	ds_read_b128 v[186:189], v152 offset:42064
	ds_read_b128 v[194:197], v152 offset:50272
	ds_read_b128 v[198:201], v152 offset:58480
	s_waitcnt lgkmcnt(4)
	v_fmac_f32_e32 v132, v104, v168
	v_fmac_f32_e32 v132, v105, v169
	v_fmac_f32_e32 v132, v106, v170
	v_fmac_f32_e32 v132, v107, v171
	v_fmac_f32_e32 v133, v104, v172
	v_fmac_f32_e32 v133, v105, v173
	v_fmac_f32_e32 v133, v106, v174
	v_fmac_f32_e32 v133, v107, v175
	v_fmac_f32_e32 v134, v104, v176
	v_fmac_f32_e32 v134, v105, v177
	v_fmac_f32_e32 v134, v106, v178
	v_fmac_f32_e32 v134, v107, v179
	v_fmac_f32_e32 v135, v104, v180
	v_fmac_f32_e32 v135, v105, v181
	v_fmac_f32_e32 v135, v106, v182
	v_fmac_f32_e32 v135, v107, v183
	ds_read_b128 v[168:171], v153 offset:1024
	ds_read_b128 v[172:175], v153 offset:9232
	ds_read_b128 v[176:179], v153 offset:17440
	ds_read_b128 v[180:183], v153 offset:25648
	s_waitcnt lgkmcnt(4)
	v_fmac_f32_e32 v136, v104, v148
	v_fmac_f32_e32 v136, v105, v149
	v_fmac_f32_e32 v136, v106, v150
	v_fmac_f32_e32 v136, v107, v151
	v_fmac_f32_e32 v137, v104, v186
	v_fmac_f32_e32 v137, v105, v187
	v_fmac_f32_e32 v137, v106, v188
	v_fmac_f32_e32 v137, v107, v189
	v_fmac_f32_e32 v138, v104, v194
	v_fmac_f32_e32 v138, v105, v195
	v_fmac_f32_e32 v138, v106, v196
	v_fmac_f32_e32 v138, v107, v197
	v_fmac_f32_e32 v139, v104, v198
	v_fmac_f32_e32 v139, v105, v199
	v_fmac_f32_e32 v139, v106, v200
	v_fmac_f32_e32 v139, v107, v201
	ds_read_b128 v[148:151], v153 offset:33856
	ds_read_b128 v[186:189], v153 offset:42064
	ds_read_b128 v[194:197], v153 offset:50272
	ds_read_b128 v[198:201], v153 offset:58480
	s_waitcnt lgkmcnt(4)
	v_fmac_f32_e32 v140, v104, v168
	v_fmac_f32_e32 v140, v105, v169
	v_fmac_f32_e32 v140, v106, v170
	v_fmac_f32_e32 v140, v107, v171
	v_fmac_f32_e32 v141, v104, v172
	v_fmac_f32_e32 v141, v105, v173
	v_fmac_f32_e32 v141, v106, v174
	v_fmac_f32_e32 v141, v107, v175
	v_fmac_f32_e32 v142, v104, v176
	v_fmac_f32_e32 v142, v105, v177
	v_fmac_f32_e32 v142, v106, v178
	v_fmac_f32_e32 v142, v107, v179
	v_fmac_f32_e32 v143, v104, v180
	v_fmac_f32_e32 v143, v105, v181
	v_fmac_f32_e32 v143, v106, v182
	v_fmac_f32_e32 v143, v107, v183
	ds_read_b128 v[168:171], v152 offset:2048
	ds_read_b128 v[172:175], v152 offset:10256
	ds_read_b128 v[176:179], v152 offset:18464
	ds_read_b128 v[180:183], v152 offset:26672
	s_waitcnt lgkmcnt(4)
	v_fmac_f32_e32 v144, v104, v148
	v_fmac_f32_e32 v144, v105, v149
	v_fmac_f32_e32 v144, v106, v150
	v_fmac_f32_e32 v144, v107, v151
	v_fmac_f32_e32 v145, v104, v186
	v_fmac_f32_e32 v145, v105, v187
	v_fmac_f32_e32 v145, v106, v188
	v_fmac_f32_e32 v145, v107, v189
	v_fmac_f32_e32 v146, v104, v194
	v_fmac_f32_e32 v146, v105, v195
	v_fmac_f32_e32 v146, v106, v196
	v_fmac_f32_e32 v146, v107, v197
	v_fmac_f32_e32 v147, v104, v198
	v_fmac_f32_e32 v147, v105, v199
	v_fmac_f32_e32 v147, v106, v200
	v_fmac_f32_e32 v147, v107, v201
	ds_read_b128 v[148:151], v152 offset:34880
	ds_read_b128 v[186:189], v152 offset:43088
	ds_read_b128 v[194:197], v152 offset:51296
	ds_read_b128 v[198:201], v152 offset:59504
	s_waitcnt lgkmcnt(4)
	v_fmac_f32_e32 v132, v108, v168
	v_fmac_f32_e32 v132, v109, v169
	v_fmac_f32_e32 v132, v110, v170
	v_fmac_f32_e32 v132, v111, v171
	v_fmac_f32_e32 v133, v108, v172
	v_fmac_f32_e32 v133, v109, v173
	v_fmac_f32_e32 v133, v110, v174
	v_fmac_f32_e32 v133, v111, v175
	v_fmac_f32_e32 v134, v108, v176
	v_fmac_f32_e32 v134, v109, v177
	v_fmac_f32_e32 v134, v110, v178
	v_fmac_f32_e32 v134, v111, v179
	v_fmac_f32_e32 v135, v108, v180
	v_fmac_f32_e32 v135, v109, v181
	v_fmac_f32_e32 v135, v110, v182
	v_fmac_f32_e32 v135, v111, v183
	ds_read_b128 v[168:171], v153 offset:2048
	ds_read_b128 v[172:175], v153 offset:10256
	ds_read_b128 v[176:179], v153 offset:18464
	ds_read_b128 v[180:183], v153 offset:26672
	s_waitcnt lgkmcnt(4)
	v_fmac_f32_e32 v136, v108, v148
	v_fmac_f32_e32 v136, v109, v149
	v_fmac_f32_e32 v136, v110, v150
	v_fmac_f32_e32 v136, v111, v151
	v_fmac_f32_e32 v137, v108, v186
	v_fmac_f32_e32 v137, v109, v187
	v_fmac_f32_e32 v137, v110, v188
	v_fmac_f32_e32 v137, v111, v189
	v_fmac_f32_e32 v138, v108, v194
	v_fmac_f32_e32 v138, v109, v195
	v_fmac_f32_e32 v138, v110, v196
	v_fmac_f32_e32 v138, v111, v197
	v_fmac_f32_e32 v139, v108, v198
	v_fmac_f32_e32 v139, v109, v199
	v_fmac_f32_e32 v139, v110, v200
	v_fmac_f32_e32 v139, v111, v201
	ds_read_b128 v[148:151], v153 offset:34880
	ds_read_b128 v[186:189], v153 offset:43088
	ds_read_b128 v[194:197], v153 offset:51296
	ds_read_b128 v[198:201], v153 offset:59504
	s_waitcnt lgkmcnt(4)
	v_fmac_f32_e32 v140, v108, v168
	v_fmac_f32_e32 v140, v109, v169
	v_fmac_f32_e32 v140, v110, v170
	v_fmac_f32_e32 v140, v111, v171
	v_fmac_f32_e32 v141, v108, v172
	v_fmac_f32_e32 v141, v109, v173
	v_fmac_f32_e32 v141, v110, v174
	v_fmac_f32_e32 v141, v111, v175
	v_fmac_f32_e32 v142, v108, v176
	v_fmac_f32_e32 v142, v109, v177
	v_fmac_f32_e32 v142, v110, v178
	v_fmac_f32_e32 v142, v111, v179
	v_fmac_f32_e32 v143, v108, v180
	v_fmac_f32_e32 v143, v109, v181
	v_fmac_f32_e32 v143, v110, v182
	v_fmac_f32_e32 v143, v111, v183
	ds_read_b128 v[168:171], v152 offset:3072
	ds_read_b128 v[172:175], v152 offset:11280
	ds_read_b128 v[176:179], v152 offset:19488
	ds_read_b128 v[180:183], v152 offset:27696
	s_waitcnt lgkmcnt(4)
	v_fmac_f32_e32 v144, v108, v148
	v_fmac_f32_e32 v144, v109, v149
	v_fmac_f32_e32 v144, v110, v150
	v_fmac_f32_e32 v144, v111, v151
	v_fmac_f32_e32 v145, v108, v186
	v_fmac_f32_e32 v145, v109, v187
	v_fmac_f32_e32 v145, v110, v188
	v_fmac_f32_e32 v145, v111, v189
	v_fmac_f32_e32 v146, v108, v194
	v_fmac_f32_e32 v146, v109, v195
	v_fmac_f32_e32 v146, v110, v196
	v_fmac_f32_e32 v146, v111, v197
	v_fmac_f32_e32 v147, v108, v198
	v_fmac_f32_e32 v147, v109, v199
	v_fmac_f32_e32 v147, v110, v200
	v_fmac_f32_e32 v147, v111, v201
	ds_read_b128 v[148:151], v152 offset:35904
	ds_read_b128 v[186:189], v152 offset:44112
	ds_read_b128 v[194:197], v152 offset:52320
	ds_read_b128 v[198:201], v152 offset:60528
	s_waitcnt lgkmcnt(4)
	v_fmac_f32_e32 v132, v112, v168
	v_fmac_f32_e32 v132, v113, v169
	v_fmac_f32_e32 v132, v114, v170
	v_fmac_f32_e32 v132, v115, v171
	v_fmac_f32_e32 v133, v112, v172
	v_fmac_f32_e32 v133, v113, v173
	v_fmac_f32_e32 v133, v114, v174
	v_fmac_f32_e32 v133, v115, v175
	v_fmac_f32_e32 v134, v112, v176
	v_fmac_f32_e32 v134, v113, v177
	v_fmac_f32_e32 v134, v114, v178
	v_fmac_f32_e32 v134, v115, v179
	v_fmac_f32_e32 v135, v112, v180
	v_fmac_f32_e32 v135, v113, v181
	v_fmac_f32_e32 v135, v114, v182
	v_fmac_f32_e32 v135, v115, v183
	ds_read_b128 v[168:171], v153 offset:3072
	ds_read_b128 v[172:175], v153 offset:11280
	ds_read_b128 v[176:179], v153 offset:19488
	ds_read_b128 v[180:183], v153 offset:27696
	s_waitcnt lgkmcnt(4)
	v_fmac_f32_e32 v136, v112, v148
	v_fmac_f32_e32 v136, v113, v149
	v_fmac_f32_e32 v136, v114, v150
	v_fmac_f32_e32 v136, v115, v151
	v_fmac_f32_e32 v137, v112, v186
	v_fmac_f32_e32 v137, v113, v187
	v_fmac_f32_e32 v137, v114, v188
	v_fmac_f32_e32 v137, v115, v189
	v_fmac_f32_e32 v138, v112, v194
	v_fmac_f32_e32 v138, v113, v195
	v_fmac_f32_e32 v138, v114, v196
	v_fmac_f32_e32 v138, v115, v197
	v_fmac_f32_e32 v139, v112, v198
	v_fmac_f32_e32 v139, v113, v199
	v_fmac_f32_e32 v139, v114, v200
	v_fmac_f32_e32 v139, v115, v201
	ds_read_b128 v[148:151], v153 offset:35904
	ds_read_b128 v[186:189], v153 offset:44112
	ds_read_b128 v[194:197], v153 offset:52320
	ds_read_b128 v[198:201], v153 offset:60528
	s_waitcnt lgkmcnt(4)
	v_fmac_f32_e32 v140, v112, v168
	v_fmac_f32_e32 v140, v113, v169
	v_fmac_f32_e32 v140, v114, v170
	v_fmac_f32_e32 v140, v115, v171
	v_fmac_f32_e32 v141, v112, v172
	v_fmac_f32_e32 v141, v113, v173
	v_fmac_f32_e32 v141, v114, v174
	v_fmac_f32_e32 v141, v115, v175
	v_fmac_f32_e32 v142, v112, v176
	v_fmac_f32_e32 v142, v113, v177
	v_fmac_f32_e32 v142, v114, v178
	v_fmac_f32_e32 v142, v115, v179
	v_fmac_f32_e32 v143, v112, v180
	v_fmac_f32_e32 v143, v113, v181
	v_fmac_f32_e32 v143, v114, v182
	v_fmac_f32_e32 v143, v115, v183
	ds_read_b128 v[168:171], v152 offset:4096
	ds_read_b128 v[172:175], v152 offset:12304
	ds_read_b128 v[176:179], v152 offset:20512
	ds_read_b128 v[180:183], v152 offset:28720
	s_waitcnt lgkmcnt(4)
	v_fmac_f32_e32 v144, v112, v148
	v_fmac_f32_e32 v144, v113, v149
	v_fmac_f32_e32 v144, v114, v150
	v_fmac_f32_e32 v144, v115, v151
	v_fmac_f32_e32 v145, v112, v186
	v_fmac_f32_e32 v145, v113, v187
	v_fmac_f32_e32 v145, v114, v188
	v_fmac_f32_e32 v145, v115, v189
	v_fmac_f32_e32 v146, v112, v194
	v_fmac_f32_e32 v146, v113, v195
	v_fmac_f32_e32 v146, v114, v196
	v_fmac_f32_e32 v146, v115, v197
	v_fmac_f32_e32 v147, v112, v198
	v_fmac_f32_e32 v147, v113, v199
	v_fmac_f32_e32 v147, v114, v200
	v_fmac_f32_e32 v147, v115, v201
	ds_read_b128 v[148:151], v152 offset:36928
	ds_read_b128 v[186:189], v152 offset:45136
	ds_read_b128 v[194:197], v152 offset:53344
	ds_read_b128 v[198:201], v152 offset:61552
	s_waitcnt lgkmcnt(4)
	v_fmac_f32_e32 v132, v116, v168
	v_fmac_f32_e32 v132, v117, v169
	v_fmac_f32_e32 v132, v118, v170
	v_fmac_f32_e32 v132, v119, v171
	v_fmac_f32_e32 v133, v116, v172
	v_fmac_f32_e32 v133, v117, v173
	v_fmac_f32_e32 v133, v118, v174
	v_fmac_f32_e32 v133, v119, v175
	v_fmac_f32_e32 v134, v116, v176
	v_fmac_f32_e32 v134, v117, v177
	v_fmac_f32_e32 v134, v118, v178
	v_fmac_f32_e32 v134, v119, v179
	v_fmac_f32_e32 v135, v116, v180
	v_fmac_f32_e32 v135, v117, v181
	v_fmac_f32_e32 v135, v118, v182
	v_fmac_f32_e32 v135, v119, v183
	ds_read_b128 v[168:171], v153 offset:4096
	ds_read_b128 v[172:175], v153 offset:12304
	ds_read_b128 v[176:179], v153 offset:20512
	ds_read_b128 v[180:183], v153 offset:28720
	s_waitcnt lgkmcnt(4)
	v_fmac_f32_e32 v136, v116, v148
	v_fmac_f32_e32 v136, v117, v149
	v_fmac_f32_e32 v136, v118, v150
	v_fmac_f32_e32 v136, v119, v151
	v_fmac_f32_e32 v137, v116, v186
	v_fmac_f32_e32 v137, v117, v187
	v_fmac_f32_e32 v137, v118, v188
	v_fmac_f32_e32 v137, v119, v189
	v_fmac_f32_e32 v138, v116, v194
	v_fmac_f32_e32 v138, v117, v195
	v_fmac_f32_e32 v138, v118, v196
	v_fmac_f32_e32 v138, v119, v197
	v_fmac_f32_e32 v139, v116, v198
	v_fmac_f32_e32 v139, v117, v199
	v_fmac_f32_e32 v139, v118, v200
	v_fmac_f32_e32 v139, v119, v201
	ds_read_b128 v[148:151], v153 offset:36928
	ds_read_b128 v[186:189], v153 offset:45136
	ds_read_b128 v[194:197], v153 offset:53344
	ds_read_b128 v[198:201], v153 offset:61552
	s_waitcnt lgkmcnt(4)
	v_fmac_f32_e32 v140, v116, v168
	v_fmac_f32_e32 v140, v117, v169
	v_fmac_f32_e32 v140, v118, v170
	v_fmac_f32_e32 v140, v119, v171
	v_fmac_f32_e32 v141, v116, v172
	v_fmac_f32_e32 v141, v117, v173
	v_fmac_f32_e32 v141, v118, v174
	v_fmac_f32_e32 v141, v119, v175
	v_fmac_f32_e32 v142, v116, v176
	v_fmac_f32_e32 v142, v117, v177
	v_fmac_f32_e32 v142, v118, v178
	v_fmac_f32_e32 v142, v119, v179
	v_fmac_f32_e32 v143, v116, v180
	v_fmac_f32_e32 v143, v117, v181
	v_fmac_f32_e32 v143, v118, v182
	v_fmac_f32_e32 v143, v119, v183
	ds_read_b128 v[168:171], v152 offset:5120
	ds_read_b128 v[172:175], v152 offset:13328
	ds_read_b128 v[176:179], v152 offset:21536
	ds_read_b128 v[180:183], v152 offset:29744
	s_waitcnt lgkmcnt(4)
	v_fmac_f32_e32 v144, v116, v148
	v_fmac_f32_e32 v144, v117, v149
	v_fmac_f32_e32 v144, v118, v150
	v_fmac_f32_e32 v144, v119, v151
	v_fmac_f32_e32 v145, v116, v186
	v_fmac_f32_e32 v145, v117, v187
	v_fmac_f32_e32 v145, v118, v188
	v_fmac_f32_e32 v145, v119, v189
	v_fmac_f32_e32 v146, v116, v194
	v_fmac_f32_e32 v146, v117, v195
	v_fmac_f32_e32 v146, v118, v196
	v_fmac_f32_e32 v146, v119, v197
	v_fmac_f32_e32 v147, v116, v198
	v_fmac_f32_e32 v147, v117, v199
	v_fmac_f32_e32 v147, v118, v200
	v_fmac_f32_e32 v147, v119, v201
	ds_read_b128 v[148:151], v152 offset:37952
	ds_read_b128 v[186:189], v152 offset:46160
	ds_read_b128 v[194:197], v152 offset:54368
	ds_read_b128 v[198:201], v152 offset:62576
	s_waitcnt lgkmcnt(4)
	v_fmac_f32_e32 v132, v120, v168
	v_fmac_f32_e32 v132, v121, v169
	v_fmac_f32_e32 v132, v122, v170
	v_fmac_f32_e32 v132, v123, v171
	v_fmac_f32_e32 v133, v120, v172
	v_fmac_f32_e32 v133, v121, v173
	v_fmac_f32_e32 v133, v122, v174
	v_fmac_f32_e32 v133, v123, v175
	v_fmac_f32_e32 v134, v120, v176
	v_fmac_f32_e32 v134, v121, v177
	v_fmac_f32_e32 v134, v122, v178
	v_fmac_f32_e32 v134, v123, v179
	v_fmac_f32_e32 v135, v120, v180
	v_fmac_f32_e32 v135, v121, v181
	v_fmac_f32_e32 v135, v122, v182
	v_fmac_f32_e32 v135, v123, v183
	ds_read_b128 v[168:171], v153 offset:5120
	ds_read_b128 v[172:175], v153 offset:13328
	ds_read_b128 v[176:179], v153 offset:21536
	ds_read_b128 v[180:183], v153 offset:29744
	s_waitcnt lgkmcnt(4)
	v_fmac_f32_e32 v136, v120, v148
	v_fmac_f32_e32 v136, v121, v149
	v_fmac_f32_e32 v136, v122, v150
	v_fmac_f32_e32 v136, v123, v151
	v_fmac_f32_e32 v137, v120, v186
	v_fmac_f32_e32 v137, v121, v187
	v_fmac_f32_e32 v137, v122, v188
	v_fmac_f32_e32 v137, v123, v189
	v_fmac_f32_e32 v138, v120, v194
	v_fmac_f32_e32 v138, v121, v195
	v_fmac_f32_e32 v138, v122, v196
	v_fmac_f32_e32 v138, v123, v197
	v_fmac_f32_e32 v139, v120, v198
	v_fmac_f32_e32 v139, v121, v199
	v_fmac_f32_e32 v139, v122, v200
	v_fmac_f32_e32 v139, v123, v201
	ds_read_b128 v[148:151], v153 offset:37952
	ds_read_b128 v[186:189], v153 offset:46160
	ds_read_b128 v[194:197], v153 offset:54368
	ds_read_b128 v[198:201], v153 offset:62576
	s_waitcnt lgkmcnt(4)
	v_fmac_f32_e32 v140, v120, v168
	v_fmac_f32_e32 v140, v121, v169
	v_fmac_f32_e32 v140, v122, v170
	v_fmac_f32_e32 v140, v123, v171
	v_fmac_f32_e32 v141, v120, v172
	v_fmac_f32_e32 v141, v121, v173
	v_fmac_f32_e32 v141, v122, v174
	v_fmac_f32_e32 v141, v123, v175
	v_fmac_f32_e32 v142, v120, v176
	v_fmac_f32_e32 v142, v121, v177
	v_fmac_f32_e32 v142, v122, v178
	v_fmac_f32_e32 v142, v123, v179
	v_fmac_f32_e32 v143, v120, v180
	v_fmac_f32_e32 v143, v121, v181
	v_fmac_f32_e32 v143, v122, v182
	v_fmac_f32_e32 v143, v123, v183
	ds_read_b128 v[168:171], v152 offset:6144
	ds_read_b128 v[172:175], v152 offset:14352
	ds_read_b128 v[176:179], v152 offset:22560
	ds_read_b128 v[180:183], v152 offset:30768
	s_waitcnt lgkmcnt(4)
	v_fmac_f32_e32 v144, v120, v148
	v_fmac_f32_e32 v144, v121, v149
	v_fmac_f32_e32 v144, v122, v150
	v_fmac_f32_e32 v144, v123, v151
	v_fmac_f32_e32 v145, v120, v186
	v_fmac_f32_e32 v145, v121, v187
	v_fmac_f32_e32 v145, v122, v188
	v_fmac_f32_e32 v145, v123, v189
	v_fmac_f32_e32 v146, v120, v194
	v_fmac_f32_e32 v146, v121, v195
	v_fmac_f32_e32 v146, v122, v196
	v_fmac_f32_e32 v146, v123, v197
	v_fmac_f32_e32 v147, v120, v198
	v_fmac_f32_e32 v147, v121, v199
	v_fmac_f32_e32 v147, v122, v200
	v_fmac_f32_e32 v147, v123, v201
	ds_read_b128 v[148:151], v152 offset:38976
	ds_read_b128 v[186:189], v152 offset:47184
	ds_read_b128 v[194:197], v152 offset:55392
	ds_read_b128 v[198:201], v152 offset:63600
	s_waitcnt lgkmcnt(4)
	v_fmac_f32_e32 v132, v124, v168
	v_fmac_f32_e32 v132, v125, v169
	v_fmac_f32_e32 v132, v126, v170
	v_fmac_f32_e32 v132, v127, v171
	v_fmac_f32_e32 v133, v124, v172
	v_fmac_f32_e32 v133, v125, v173
	v_fmac_f32_e32 v133, v126, v174
	v_fmac_f32_e32 v133, v127, v175
	v_fmac_f32_e32 v134, v124, v176
	v_fmac_f32_e32 v134, v125, v177
	v_fmac_f32_e32 v134, v126, v178
	v_fmac_f32_e32 v134, v127, v179
	v_fmac_f32_e32 v135, v124, v180
	v_fmac_f32_e32 v135, v125, v181
	v_fmac_f32_e32 v135, v126, v182
	v_fmac_f32_e32 v135, v127, v183
	ds_read_b128 v[168:171], v153 offset:6144
	ds_read_b128 v[172:175], v153 offset:14352
	ds_read_b128 v[176:179], v153 offset:22560
	ds_read_b128 v[180:183], v153 offset:30768
	s_waitcnt lgkmcnt(4)
	v_fmac_f32_e32 v136, v124, v148
	v_fmac_f32_e32 v136, v125, v149
	v_fmac_f32_e32 v136, v126, v150
	v_fmac_f32_e32 v136, v127, v151
	v_fmac_f32_e32 v137, v124, v186
	v_fmac_f32_e32 v137, v125, v187
	v_fmac_f32_e32 v137, v126, v188
	v_fmac_f32_e32 v137, v127, v189
	v_fmac_f32_e32 v138, v124, v194
	v_fmac_f32_e32 v138, v125, v195
	v_fmac_f32_e32 v138, v126, v196
	v_fmac_f32_e32 v138, v127, v197
	v_fmac_f32_e32 v139, v124, v198
	v_fmac_f32_e32 v139, v125, v199
	v_fmac_f32_e32 v139, v126, v200
	v_fmac_f32_e32 v139, v127, v201
	ds_read_b128 v[148:151], v153 offset:38976
	ds_read_b128 v[186:189], v153 offset:47184
	ds_read_b128 v[194:197], v153 offset:55392
	ds_read_b128 v[198:201], v153 offset:63600
	s_waitcnt lgkmcnt(4)
	v_fmac_f32_e32 v140, v124, v168
	v_fmac_f32_e32 v140, v125, v169
	v_fmac_f32_e32 v140, v126, v170
	v_fmac_f32_e32 v140, v127, v171
	v_fmac_f32_e32 v141, v124, v172
	v_fmac_f32_e32 v141, v125, v173
	v_fmac_f32_e32 v141, v126, v174
	v_fmac_f32_e32 v141, v127, v175
	v_fmac_f32_e32 v142, v124, v176
	v_fmac_f32_e32 v142, v125, v177
	v_fmac_f32_e32 v142, v126, v178
	v_fmac_f32_e32 v142, v127, v179
	v_fmac_f32_e32 v143, v124, v180
	v_fmac_f32_e32 v143, v125, v181
	v_fmac_f32_e32 v143, v126, v182
	v_fmac_f32_e32 v143, v127, v183
	ds_read_b128 v[168:171], v152 offset:7168
	ds_read_b128 v[172:175], v152 offset:15376
	ds_read_b128 v[176:179], v152 offset:23584
	ds_read_b128 v[180:183], v152 offset:31792
	s_waitcnt lgkmcnt(4)
	v_fmac_f32_e32 v144, v124, v148
	v_fmac_f32_e32 v144, v125, v149
	v_fmac_f32_e32 v144, v126, v150
	v_fmac_f32_e32 v144, v127, v151
	v_fmac_f32_e32 v145, v124, v186
	v_fmac_f32_e32 v145, v125, v187
	v_fmac_f32_e32 v145, v126, v188
	v_fmac_f32_e32 v145, v127, v189
	v_fmac_f32_e32 v146, v124, v194
	v_fmac_f32_e32 v146, v125, v195
	v_fmac_f32_e32 v146, v126, v196
	v_fmac_f32_e32 v146, v127, v197
	v_fmac_f32_e32 v147, v124, v198
	v_fmac_f32_e32 v147, v125, v199
	v_fmac_f32_e32 v147, v126, v200
	v_fmac_f32_e32 v147, v127, v201
	ds_read_b128 v[148:151], v152 offset:40000
	ds_read_b128 v[186:189], v152 offset:48208
	ds_read_b128 v[194:197], v152 offset:56416
	ds_read_b128 v[198:201], v152 offset:64624
	s_waitcnt lgkmcnt(4)
	v_fmac_f32_e32 v132, v128, v168
	v_fmac_f32_e32 v132, v129, v169
	v_fmac_f32_e32 v132, v130, v170
	v_fmac_f32_e32 v132, v131, v171
	v_fmac_f32_e32 v133, v128, v172
	v_fmac_f32_e32 v133, v129, v173
	v_fmac_f32_e32 v133, v130, v174
	v_fmac_f32_e32 v133, v131, v175
	v_fmac_f32_e32 v134, v128, v176
	v_fmac_f32_e32 v134, v129, v177
	v_fmac_f32_e32 v134, v130, v178
	v_fmac_f32_e32 v134, v131, v179
	v_fmac_f32_e32 v135, v128, v180
	v_fmac_f32_e32 v135, v129, v181
	v_fmac_f32_e32 v135, v130, v182
	v_fmac_f32_e32 v135, v131, v183
	ds_read_b128 v[168:171], v153 offset:7168
	ds_read_b128 v[172:175], v153 offset:15376
	ds_read_b128 v[176:179], v153 offset:23584
	ds_read_b128 v[180:183], v153 offset:31792
	s_waitcnt lgkmcnt(4)
	v_fmac_f32_e32 v136, v128, v148
	v_fmac_f32_e32 v136, v129, v149
	v_fmac_f32_e32 v136, v130, v150
	v_fmac_f32_e32 v136, v131, v151
	v_fmac_f32_e32 v137, v128, v186
	v_fmac_f32_e32 v137, v129, v187
	v_fmac_f32_e32 v137, v130, v188
	v_fmac_f32_e32 v137, v131, v189
	v_fmac_f32_e32 v138, v128, v194
	v_fmac_f32_e32 v138, v129, v195
	v_fmac_f32_e32 v138, v130, v196
	v_fmac_f32_e32 v138, v131, v197
	v_fmac_f32_e32 v139, v128, v198
	v_fmac_f32_e32 v139, v129, v199
	v_fmac_f32_e32 v139, v130, v200
	v_fmac_f32_e32 v139, v131, v201
	ds_read_b128 v[148:151], v153 offset:40000
	ds_read_b128 v[186:189], v153 offset:48208
	ds_read_b128 v[194:197], v153 offset:56416
	ds_read_b128 v[198:201], v153 offset:64624
	s_waitcnt lgkmcnt(4)
	v_fmac_f32_e32 v140, v128, v168
	v_fmac_f32_e32 v140, v129, v169
	v_fmac_f32_e32 v140, v130, v170
	v_fmac_f32_e32 v140, v131, v171
	v_fmac_f32_e32 v141, v128, v172
	v_fmac_f32_e32 v141, v129, v173
	v_fmac_f32_e32 v141, v130, v174
	v_fmac_f32_e32 v141, v131, v175
	v_fmac_f32_e32 v142, v128, v176
	v_fmac_f32_e32 v142, v129, v177
	v_fmac_f32_e32 v142, v130, v178
	v_fmac_f32_e32 v142, v131, v179
	v_fmac_f32_e32 v143, v128, v180
	v_fmac_f32_e32 v143, v129, v181
	v_fmac_f32_e32 v143, v130, v182
	v_fmac_f32_e32 v143, v131, v183
	s_waitcnt lgkmcnt(0)
	v_fmac_f32_e32 v144, v128, v148
	v_fmac_f32_e32 v144, v129, v149
	v_fmac_f32_e32 v144, v130, v150
	v_fmac_f32_e32 v144, v131, v151
	v_fmac_f32_e32 v145, v128, v186
	v_fmac_f32_e32 v145, v129, v187
	v_fmac_f32_e32 v145, v130, v188
	v_fmac_f32_e32 v145, v131, v189
	v_fmac_f32_e32 v146, v128, v194
	v_fmac_f32_e32 v146, v129, v195
	v_fmac_f32_e32 v146, v130, v196
	v_fmac_f32_e32 v146, v131, v197
	v_fmac_f32_e32 v147, v128, v198
	v_fmac_f32_e32 v147, v129, v199
	v_fmac_f32_e32 v147, v130, v200
	v_fmac_f32_e32 v147, v131, v201
	s_add_i32 s11, s10, 0x1000
	s_lshr_b32 s0, s11, 8
	s_mul_i32 s0, s0, 57
	s_lshr_b32 s0, s0, 9
	s_mul_i32 s1, s0, 0x900
	s_sub_i32 s43, s11, s1
	s_lshl_b32 s1, s11, 13
	s_add_u32 s12, s48, s1
	s_addc_u32 s13, s49, 0
	s_add_u32 s14, s12, 0x1000
	s_addc_u32 s15, s13, 0
	global_load_dwordx4 v[100:103], v1, s[12:13]
	global_load_dwordx4 v[104:107], v1, s[12:13] offset:1024
	global_load_dwordx4 v[108:111], v1, s[12:13] offset:2048
	global_load_dwordx4 v[112:115], v1, s[12:13] offset:3072
	global_load_dwordx4 v[116:119], v1, s[14:15]
	global_load_dwordx4 v[120:123], v1, s[14:15] offset:1024
	global_load_dwordx4 v[124:127], v1, s[14:15] offset:2048
	global_load_dwordx4 v[128:131], v1, s[14:15] offset:3072
	v_cndmask_b32_e64 v242, v133, v132, s[62:63]
	v_cndmask_b32_e64 v132, v132, v133, s[62:63]
	v_cndmask_b32_e64 v243, v135, v134, s[62:63]
	v_cndmask_b32_e64 v134, v134, v135, s[62:63]
	v_cndmask_b32_e64 v244, v137, v136, s[62:63]
	v_cndmask_b32_e64 v136, v136, v137, s[62:63]
	v_cndmask_b32_e64 v245, v139, v138, s[62:63]
	v_cndmask_b32_e64 v138, v138, v139, s[62:63]
	v_cndmask_b32_e64 v246, v141, v140, s[62:63]
	v_cndmask_b32_e64 v140, v140, v141, s[62:63]
	v_cndmask_b32_e64 v248, v143, v142, s[62:63]
	v_cndmask_b32_e64 v142, v142, v143, s[62:63]
	v_cndmask_b32_e64 v249, v145, v144, s[62:63]
	v_cndmask_b32_e64 v144, v144, v145, s[62:63]
	v_cndmask_b32_e64 v250, v147, v146, s[62:63]
	v_cndmask_b32_e64 v146, v146, v147, s[62:63]
	v_add_f32_dpp v132, v242, v132 quad_perm:[1,0,3,2] row_mask:0xf bank_mask:0xf
	v_add_f32_dpp v134, v243, v134 quad_perm:[1,0,3,2] row_mask:0xf bank_mask:0xf
	v_add_f32_dpp v136, v244, v136 quad_perm:[1,0,3,2] row_mask:0xf bank_mask:0xf
	v_add_f32_dpp v138, v245, v138 quad_perm:[1,0,3,2] row_mask:0xf bank_mask:0xf
	v_add_f32_dpp v140, v246, v140 quad_perm:[1,0,3,2] row_mask:0xf bank_mask:0xf
	v_add_f32_dpp v142, v248, v142 quad_perm:[1,0,3,2] row_mask:0xf bank_mask:0xf
	v_add_f32_dpp v144, v249, v144 quad_perm:[1,0,3,2] row_mask:0xf bank_mask:0xf
	v_add_f32_dpp v146, v250, v146 quad_perm:[1,0,3,2] row_mask:0xf bank_mask:0xf
	v_cndmask_b32_e64 v242, v134, v132, s[64:65]
	v_cndmask_b32_e64 v132, v132, v134, s[64:65]
	v_cndmask_b32_e64 v243, v138, v136, s[64:65]
	v_cndmask_b32_e64 v136, v136, v138, s[64:65]
	v_cndmask_b32_e64 v244, v142, v140, s[64:65]
	v_cndmask_b32_e64 v140, v140, v142, s[64:65]
	v_cndmask_b32_e64 v245, v146, v144, s[64:65]
	v_cndmask_b32_e64 v144, v144, v146, s[64:65]
	s_nop 0
	v_add_f32_dpp v132, v242, v132 quad_perm:[2,3,0,1] row_mask:0xf bank_mask:0xf
	v_add_f32_dpp v136, v243, v136 quad_perm:[2,3,0,1] row_mask:0xf bank_mask:0xf
	v_add_f32_dpp v140, v244, v140 quad_perm:[2,3,0,1] row_mask:0xf bank_mask:0xf
	v_add_f32_dpp v144, v245, v144 quad_perm:[2,3,0,1] row_mask:0xf bank_mask:0xf
	v_cndmask_b32_e64 v242, v136, v132, s[66:67]
	v_cndmask_b32_e64 v132, v132, v136, s[66:67]
	v_cndmask_b32_e64 v243, v144, v140, s[66:67]
	v_cndmask_b32_e64 v140, v140, v144, s[66:67]
	s_nop 1
	v_add_f32_dpp v246, v242, v132 row_shl:4 row_mask:0xf bank_mask:0x5
	v_add_f32_dpp v246, v242, v132 row_shr:4 row_mask:0xf bank_mask:0xa
	v_add_f32_dpp v248, v243, v140 row_shl:4 row_mask:0xf bank_mask:0x5
	v_add_f32_dpp v248, v243, v140 row_shr:4 row_mask:0xf bank_mask:0xa
	v_cndmask_b32_e64 v242, v248, v246, s[68:69]
	v_cndmask_b32_e64 v243, v246, v248, s[68:69]
	s_nop 1
	v_add_f32_dpp v191, v242, v243 row_ror:8 row_mask:0xf bank_mask:0xf
	s_nop 0
	ds_bpermute_b32 v193, v165, v191
	s_waitcnt lgkmcnt(0)
	v_add_f32_e32 v191, v191, v193
	ds_bpermute_b32 v193, v166, v191
	s_waitcnt lgkmcnt(0)
	v_add_f32_e32 v191, v191, v193
	v_mov_b32_e32 v193, v191
	s_nop 1
	v_max_f32_dpp v193, v193, v193 quad_perm:[1,0,3,2] row_mask:0xf bank_mask:0xf
	s_nop 1
	v_max_f32_dpp v193, v193, v193 quad_perm:[2,3,0,1] row_mask:0xf bank_mask:0xf
	s_nop 1
	v_max_f32_dpp v193, v193, v193 row_half_mirror row_mask:0xf bank_mask:0xf
	s_nop 1
	v_max_f32_dpp v193, v193, v193 row_mirror row_mask:0xf bank_mask:0xf
	v_sub_f32_e32 v191, v191, v193
	v_mul_f32_e32 v191, 0x3fb8aa3b, v191
	v_exp_f32_e32 v191, v191
	s_nop 0
	v_mov_b32_e32 v193, v191
	s_nop 1
	v_add_f32_dpp v193, v193, v193 quad_perm:[1,0,3,2] row_mask:0xf bank_mask:0xf
	s_nop 1
	v_add_f32_dpp v193, v193, v193 quad_perm:[2,3,0,1] row_mask:0xf bank_mask:0xf
	s_nop 1
	v_add_f32_dpp v193, v193, v193 row_half_mirror row_mask:0xf bank_mask:0xf
	s_nop 1
	v_add_f32_dpp v193, v193, v193 row_mirror row_mask:0xf bank_mask:0xf
	v_rcp_f32_e32 v193, v193
	s_nop 0
	v_mul_f32_e32 v191, v191, v193
	s_mov_b64 exec, 0xffff
	global_store_dword v164, v191, s[34:35]
	s_mov_b64 exec, -1
	s_waitcnt vmcnt(9)
	s_add_i32 s11, s10, 0x800
	s_lshr_b32 s0, s11, 8
	s_mul_i32 s0, s0, 57
	s_lshr_b32 s0, s0, 9
	s_mul_i32 s1, s0, 0x900
	s_sub_i32 s43, s11, s1
	s_lshl_b32 s1, s11, 12
	s_add_u32 s16, s50, s1
	s_addc_u32 s17, s51, 0
	s_mul_i32 s1, s0, 0x24000
	s_lshl_b32 s2, s43, 2
	s_add_i32 s1, s1, s2
	s_add_u32 s34, s54, s1
	s_addc_u32 s35, s55, 0
	v_mul_f32_e32 v184, v204, v204
	v_fmac_f32_e32 v184, v205, v205
	v_fmac_f32_e32 v184, v206, v206
	v_fmac_f32_e32 v184, v207, v207
	v_fmac_f32_e32 v184, v208, v208
	v_fmac_f32_e32 v184, v209, v209
	v_fmac_f32_e32 v184, v210, v210
	v_fmac_f32_e32 v184, v211, v211
	v_fmac_f32_e32 v184, v212, v212
	v_fmac_f32_e32 v184, v213, v213
	v_fmac_f32_e32 v184, v214, v214
	v_fmac_f32_e32 v184, v215, v215
	v_fmac_f32_e32 v184, v216, v216
	v_fmac_f32_e32 v184, v217, v217
	v_fmac_f32_e32 v184, v218, v218
	v_fmac_f32_e32 v184, v219, v219
	v_fmac_f32_e32 v184, v226, v226
	v_fmac_f32_e32 v184, v227, v227
	v_fmac_f32_e32 v184, v228, v228
	v_fmac_f32_e32 v184, v229, v229
	v_fmac_f32_e32 v184, v230, v230
	v_fmac_f32_e32 v184, v231, v231
	v_fmac_f32_e32 v184, v232, v232
	v_fmac_f32_e32 v184, v233, v233
	v_fmac_f32_e32 v184, v234, v234
	v_fmac_f32_e32 v184, v235, v235
	v_fmac_f32_e32 v184, v236, v236
	v_fmac_f32_e32 v184, v237, v237
	v_fmac_f32_e32 v184, v238, v238
	v_fmac_f32_e32 v184, v239, v239
	v_fmac_f32_e32 v184, v240, v240
	v_fmac_f32_e32 v184, v241, v241
	ds_read_b128 v[168:171], v152 offset:0
	ds_read_b128 v[172:175], v152 offset:8208
	ds_read_b128 v[176:179], v152 offset:16416
	ds_read_b128 v[180:183], v152 offset:24624
	s_nop 0
	v_add_f32_dpp v184, v184, v184 quad_perm:[1,0,3,2] row_mask:0xf bank_mask:0xf
	s_nop 1
	v_add_f32_dpp v184, v184, v184 quad_perm:[2,3,0,1] row_mask:0xf bank_mask:0xf
	s_nop 1
	v_add_f32_dpp v184, v184, v184 row_half_mirror row_mask:0xf bank_mask:0xf
	s_nop 1
	v_add_f32_dpp v184, v184, v184 row_mirror row_mask:0xf bank_mask:0xf
	s_nop 1
	v_readlane_b32 s0, v184, 0
	v_readlane_b32 s1, v184, 16
	v_readlane_b32 s2, v184, 32
	v_readlane_b32 s3, v184, 48
	v_fma_f32 v4, v4, v36, v4
	v_fma_f32 v5, v5, v37, v5
	v_fma_f32 v6, v6, v38, v6
	v_fma_f32 v7, v7, v39, v7
	v_fma_f32 v8, v8, v40, v8
	v_fma_f32 v9, v9, v41, v9
	v_fma_f32 v10, v10, v42, v10
	v_fma_f32 v11, v11, v43, v11
	v_fma_f32 v12, v12, v44, v12
	v_fma_f32 v13, v13, v45, v13
	v_fma_f32 v14, v14, v46, v14
	v_fma_f32 v15, v15, v47, v15
	v_fma_f32 v16, v16, v48, v16
	v_fma_f32 v17, v17, v49, v17
	v_fma_f32 v18, v18, v50, v18
	v_fma_f32 v19, v19, v51, v19
	v_fma_f32 v20, v20, v52, v20
	v_fma_f32 v21, v21, v53, v21
	v_fma_f32 v22, v22, v54, v22
	v_fma_f32 v23, v23, v55, v23
	v_fma_f32 v24, v24, v56, v24
	v_fma_f32 v25, v25, v57, v25
	v_fma_f32 v26, v26, v58, v26
	v_fma_f32 v27, v27, v59, v27
	v_fma_f32 v28, v28, v60, v28
	v_fma_f32 v29, v29, v61, v29
	v_fma_f32 v30, v30, v62, v30
	v_fma_f32 v31, v31, v63, v31
	v_fma_f32 v32, v32, v64, v32
	v_fma_f32 v33, v33, v65, v33
	v_fma_f32 v34, v34, v66, v34
	v_fma_f32 v35, v35, v67, v35
	v_mov_b32_e32 v190, s0
	v_add_f32_e32 v190, s1, v190
	v_add_f32_e32 v190, s2, v190
	v_add_f32_e32 v190, s3, v190
	v_mul_f32_e32 v190, 0x3a000000, v190
	v_add_f32_e32 v190, 0x358637bd, v190
	v_rsq_f32_e32 v190, v190
	s_nop 0
	v_mul_f32_e32 v4, v4, v190
	v_mul_f32_e32 v5, v5, v190
	v_mul_f32_e32 v6, v6, v190
	v_mul_f32_e32 v7, v7, v190
	v_mul_f32_e32 v8, v8, v190
	v_mul_f32_e32 v9, v9, v190
	v_mul_f32_e32 v10, v10, v190
	v_mul_f32_e32 v11, v11, v190
	v_mul_f32_e32 v12, v12, v190
	v_mul_f32_e32 v13, v13, v190
	v_mul_f32_e32 v14, v14, v190
	v_mul_f32_e32 v15, v15, v190
	v_mul_f32_e32 v16, v16, v190
	v_mul_f32_e32 v17, v17, v190
	v_mul_f32_e32 v18, v18, v190
	v_mul_f32_e32 v19, v19, v190
	v_mul_f32_e32 v20, v20, v190
	v_mul_f32_e32 v21, v21, v190
	v_mul_f32_e32 v22, v22, v190
	v_mul_f32_e32 v23, v23, v190
	v_mul_f32_e32 v24, v24, v190
	v_mul_f32_e32 v25, v25, v190
	v_mul_f32_e32 v26, v26, v190
	v_mul_f32_e32 v27, v27, v190
	v_mul_f32_e32 v28, v28, v190
	v_mul_f32_e32 v29, v29, v190
	v_mul_f32_e32 v30, v30, v190
	v_mul_f32_e32 v31, v31, v190
	v_mul_f32_e32 v32, v32, v190
	v_mul_f32_e32 v33, v33, v190
	v_mul_f32_e32 v34, v34, v190
	v_mul_f32_e32 v35, v35, v190
	v_fma_f32 v204, v204, v4, v68
	v_fma_f32 v205, v205, v5, v69
	v_fma_f32 v206, v206, v6, v70
	v_fma_f32 v207, v207, v7, v71
	v_fma_f32 v208, v208, v8, v72
	v_fma_f32 v209, v209, v9, v73
	v_fma_f32 v210, v210, v10, v74
	v_fma_f32 v211, v211, v11, v75
	v_fma_f32 v212, v212, v12, v76
	v_fma_f32 v213, v213, v13, v77
	v_fma_f32 v214, v214, v14, v78
	v_fma_f32 v215, v215, v15, v79
	v_fma_f32 v216, v216, v16, v80
	v_fma_f32 v217, v217, v17, v81
	v_fma_f32 v218, v218, v18, v82
	v_fma_f32 v219, v219, v19, v83
	v_fma_f32 v226, v226, v20, v84
	v_fma_f32 v227, v227, v21, v85
	v_fma_f32 v228, v228, v22, v86
	v_fma_f32 v229, v229, v23, v87
	v_fma_f32 v230, v230, v24, v88
	v_fma_f32 v231, v231, v25, v89
	v_fma_f32 v232, v232, v26, v90
	v_fma_f32 v233, v233, v27, v91
	v_fma_f32 v234, v234, v28, v92
	v_fma_f32 v235, v235, v29, v93
	v_fma_f32 v236, v236, v30, v94
	v_fma_f32 v237, v237, v31, v95
	v_fma_f32 v238, v238, v32, v96
	v_fma_f32 v239, v239, v33, v97
	v_fma_f32 v240, v240, v34, v98
	v_fma_f32 v241, v241, v35, v99
	v_cvt_pk_bf16_f32 v242, v204, v205
	v_cvt_pk_bf16_f32 v243, v206, v207
	global_store_dwordx2 v2, v[242:243], s[16:17]
	v_cvt_pk_bf16_f32 v244, v208, v209
	v_cvt_pk_bf16_f32 v245, v210, v211
	global_store_dwordx2 v2, v[244:245], s[16:17] offset:512
	v_cvt_pk_bf16_f32 v242, v212, v213
	v_cvt_pk_bf16_f32 v243, v214, v215
	global_store_dwordx2 v2, v[242:243], s[16:17] offset:1024
	v_cvt_pk_bf16_f32 v244, v216, v217
	v_cvt_pk_bf16_f32 v245, v218, v219
	global_store_dwordx2 v2, v[244:245], s[16:17] offset:1536
	v_cvt_pk_bf16_f32 v242, v226, v227
	v_cvt_pk_bf16_f32 v243, v228, v229
	global_store_dwordx2 v2, v[242:243], s[16:17] offset:2048
	v_cvt_pk_bf16_f32 v244, v230, v231
	v_cvt_pk_bf16_f32 v245, v232, v233
	global_store_dwordx2 v2, v[244:245], s[16:17] offset:2560
	v_cvt_pk_bf16_f32 v242, v234, v235
	v_cvt_pk_bf16_f32 v243, v236, v237
	global_store_dwordx2 v2, v[242:243], s[16:17] offset:3072
	v_cvt_pk_bf16_f32 v244, v238, v239
	v_cvt_pk_bf16_f32 v245, v240, v241
	global_store_dwordx2 v2, v[244:245], s[16:17] offset:3584
	s_add_i32 s11, s10, 0x1000
	s_lshr_b32 s0, s11, 8
	s_mul_i32 s0, s0, 57
	s_lshr_b32 s0, s0, 9
	s_mul_i32 s1, s0, 0x900
	s_sub_i32 s43, s11, s1
	s_cmpk_lt_u32 s43, 0x100
	s_cselect_b32 s0, 8, s0
	s_mul_i32 s1, s0, 0xc000
	s_add_u32 s18, s52, s1
	s_addc_u32 s19, s53, 0
	s_add_u32 s18, s18, 0x6000
	s_addc_u32 s19, s19, 0
	s_add_u32 s22, s18, 0x1000
	s_addc_u32 s23, s19, 0
	s_add_u32 s28, s18, 0x2000
	s_addc_u32 s29, s19, 0
	s_add_u32 s30, s18, 0x3000
	s_addc_u32 s31, s19, 0
	global_load_dwordx4 v[4:7], v1, s[56:57]
	global_load_dwordx4 v[36:39], v1, s[28:29]
	global_load_dwordx4 v[68:71], v1, s[18:19]
	global_load_dwordx4 v[8:11], v1, s[56:57] offset:1024
	global_load_dwordx4 v[40:43], v1, s[28:29] offset:1024
	global_load_dwordx4 v[72:75], v1, s[18:19] offset:1024
	global_load_dwordx4 v[12:15], v1, s[56:57] offset:2048
	global_load_dwordx4 v[44:47], v1, s[28:29] offset:2048
	global_load_dwordx4 v[76:79], v1, s[18:19] offset:2048
	global_load_dwordx4 v[16:19], v1, s[56:57] offset:3072
	global_load_dwordx4 v[48:51], v1, s[28:29] offset:3072
	global_load_dwordx4 v[80:83], v1, s[18:19] offset:3072
	global_load_dwordx4 v[20:23], v1, s[58:59]
	global_load_dwordx4 v[52:55], v1, s[30:31]
	global_load_dwordx4 v[84:87], v1, s[22:23]
	global_load_dwordx4 v[24:27], v1, s[58:59] offset:1024
	global_load_dwordx4 v[56:59], v1, s[30:31] offset:1024
	global_load_dwordx4 v[88:91], v1, s[22:23] offset:1024
	global_load_dwordx4 v[28:31], v1, s[58:59] offset:2048
	global_load_dwordx4 v[60:63], v1, s[30:31] offset:2048
	global_load_dwordx4 v[92:95], v1, s[22:23] offset:2048
	global_load_dwordx4 v[32:35], v1, s[58:59] offset:3072
	global_load_dwordx4 v[64:67], v1, s[30:31] offset:3072
	global_load_dwordx4 v[96:99], v1, s[22:23] offset:3072
	v_mov_b32_e32 v132, 0
	v_mov_b32_e32 v133, 0
	v_mov_b32_e32 v134, 0
	v_mov_b32_e32 v135, 0
	v_mov_b32_e32 v136, 0
	v_mov_b32_e32 v137, 0
	v_mov_b32_e32 v138, 0
	v_mov_b32_e32 v139, 0
	v_mov_b32_e32 v140, 0
	v_mov_b32_e32 v141, 0
	v_mov_b32_e32 v142, 0
	v_mov_b32_e32 v143, 0
	v_mov_b32_e32 v144, 0
	v_mov_b32_e32 v145, 0
	v_mov_b32_e32 v146, 0
	v_mov_b32_e32 v147, 0
	ds_read_b128 v[148:151], v152 offset:32832
	ds_read_b128 v[186:189], v152 offset:41040
	ds_read_b128 v[194:197], v152 offset:49248
	ds_read_b128 v[198:201], v152 offset:57456
	s_waitcnt lgkmcnt(4)
	v_fmac_f32_e32 v132, v204, v168
	v_fmac_f32_e32 v132, v205, v169
	v_fmac_f32_e32 v132, v206, v170
	v_fmac_f32_e32 v132, v207, v171
	v_fmac_f32_e32 v133, v204, v172
	v_fmac_f32_e32 v133, v205, v173
	v_fmac_f32_e32 v133, v206, v174
	v_fmac_f32_e32 v133, v207, v175
	v_fmac_f32_e32 v134, v204, v176
	v_fmac_f32_e32 v134, v205, v177
	v_fmac_f32_e32 v134, v206, v178
	v_fmac_f32_e32 v134, v207, v179
	v_fmac_f32_e32 v135, v204, v180
	v_fmac_f32_e32 v135, v205, v181
	v_fmac_f32_e32 v135, v206, v182
	v_fmac_f32_e32 v135, v207, v183
	ds_read_b128 v[168:171], v153 offset:0
	ds_read_b128 v[172:175], v153 offset:8208
	ds_read_b128 v[176:179], v153 offset:16416
	ds_read_b128 v[180:183], v153 offset:24624
	s_waitcnt lgkmcnt(4)
	v_fmac_f32_e32 v136, v204, v148
	v_fmac_f32_e32 v136, v205, v149
	v_fmac_f32_e32 v136, v206, v150
	v_fmac_f32_e32 v136, v207, v151
	v_fmac_f32_e32 v137, v204, v186
	v_fmac_f32_e32 v137, v205, v187
	v_fmac_f32_e32 v137, v206, v188
	v_fmac_f32_e32 v137, v207, v189
	v_fmac_f32_e32 v138, v204, v194
	v_fmac_f32_e32 v138, v205, v195
	v_fmac_f32_e32 v138, v206, v196
	v_fmac_f32_e32 v138, v207, v197
	v_fmac_f32_e32 v139, v204, v198
	v_fmac_f32_e32 v139, v205, v199
	v_fmac_f32_e32 v139, v206, v200
	v_fmac_f32_e32 v139, v207, v201
	ds_read_b128 v[148:151], v153 offset:32832
	ds_read_b128 v[186:189], v153 offset:41040
	ds_read_b128 v[194:197], v153 offset:49248
	ds_read_b128 v[198:201], v153 offset:57456
	s_waitcnt lgkmcnt(4)
	v_fmac_f32_e32 v140, v204, v168
	v_fmac_f32_e32 v140, v205, v169
	v_fmac_f32_e32 v140, v206, v170
	v_fmac_f32_e32 v140, v207, v171
	v_fmac_f32_e32 v141, v204, v172
	v_fmac_f32_e32 v141, v205, v173
	v_fmac_f32_e32 v141, v206, v174
	v_fmac_f32_e32 v141, v207, v175
	v_fmac_f32_e32 v142, v204, v176
	v_fmac_f32_e32 v142, v205, v177
	v_fmac_f32_e32 v142, v206, v178
	v_fmac_f32_e32 v142, v207, v179
	v_fmac_f32_e32 v143, v204, v180
	v_fmac_f32_e32 v143, v205, v181
	v_fmac_f32_e32 v143, v206, v182
	v_fmac_f32_e32 v143, v207, v183
	ds_read_b128 v[168:171], v152 offset:1024
	ds_read_b128 v[172:175], v152 offset:9232
	ds_read_b128 v[176:179], v152 offset:17440
	ds_read_b128 v[180:183], v152 offset:25648
	s_waitcnt lgkmcnt(4)
	v_fmac_f32_e32 v144, v204, v148
	v_fmac_f32_e32 v144, v205, v149
	v_fmac_f32_e32 v144, v206, v150
	v_fmac_f32_e32 v144, v207, v151
	v_fmac_f32_e32 v145, v204, v186
	v_fmac_f32_e32 v145, v205, v187
	v_fmac_f32_e32 v145, v206, v188
	v_fmac_f32_e32 v145, v207, v189
	v_fmac_f32_e32 v146, v204, v194
	v_fmac_f32_e32 v146, v205, v195
	v_fmac_f32_e32 v146, v206, v196
	v_fmac_f32_e32 v146, v207, v197
	v_fmac_f32_e32 v147, v204, v198
	v_fmac_f32_e32 v147, v205, v199
	v_fmac_f32_e32 v147, v206, v200
	v_fmac_f32_e32 v147, v207, v201
	ds_read_b128 v[148:151], v152 offset:33856
	ds_read_b128 v[186:189], v152 offset:42064
	ds_read_b128 v[194:197], v152 offset:50272
	ds_read_b128 v[198:201], v152 offset:58480
	s_waitcnt lgkmcnt(4)
	v_fmac_f32_e32 v132, v208, v168
	v_fmac_f32_e32 v132, v209, v169
	v_fmac_f32_e32 v132, v210, v170
	v_fmac_f32_e32 v132, v211, v171
	v_fmac_f32_e32 v133, v208, v172
	v_fmac_f32_e32 v133, v209, v173
	v_fmac_f32_e32 v133, v210, v174
	v_fmac_f32_e32 v133, v211, v175
	v_fmac_f32_e32 v134, v208, v176
	v_fmac_f32_e32 v134, v209, v177
	v_fmac_f32_e32 v134, v210, v178
	v_fmac_f32_e32 v134, v211, v179
	v_fmac_f32_e32 v135, v208, v180
	v_fmac_f32_e32 v135, v209, v181
	v_fmac_f32_e32 v135, v210, v182
	v_fmac_f32_e32 v135, v211, v183
	ds_read_b128 v[168:171], v153 offset:1024
	ds_read_b128 v[172:175], v153 offset:9232
	ds_read_b128 v[176:179], v153 offset:17440
	ds_read_b128 v[180:183], v153 offset:25648
	s_waitcnt lgkmcnt(4)
	v_fmac_f32_e32 v136, v208, v148
	v_fmac_f32_e32 v136, v209, v149
	v_fmac_f32_e32 v136, v210, v150
	v_fmac_f32_e32 v136, v211, v151
	v_fmac_f32_e32 v137, v208, v186
	v_fmac_f32_e32 v137, v209, v187
	v_fmac_f32_e32 v137, v210, v188
	v_fmac_f32_e32 v137, v211, v189
	v_fmac_f32_e32 v138, v208, v194
	v_fmac_f32_e32 v138, v209, v195
	v_fmac_f32_e32 v138, v210, v196
	v_fmac_f32_e32 v138, v211, v197
	v_fmac_f32_e32 v139, v208, v198
	v_fmac_f32_e32 v139, v209, v199
	v_fmac_f32_e32 v139, v210, v200
	v_fmac_f32_e32 v139, v211, v201
	ds_read_b128 v[148:151], v153 offset:33856
	ds_read_b128 v[186:189], v153 offset:42064
	ds_read_b128 v[194:197], v153 offset:50272
	ds_read_b128 v[198:201], v153 offset:58480
	s_waitcnt lgkmcnt(4)
	v_fmac_f32_e32 v140, v208, v168
	v_fmac_f32_e32 v140, v209, v169
	v_fmac_f32_e32 v140, v210, v170
	v_fmac_f32_e32 v140, v211, v171
	v_fmac_f32_e32 v141, v208, v172
	v_fmac_f32_e32 v141, v209, v173
	v_fmac_f32_e32 v141, v210, v174
	v_fmac_f32_e32 v141, v211, v175
	v_fmac_f32_e32 v142, v208, v176
	v_fmac_f32_e32 v142, v209, v177
	v_fmac_f32_e32 v142, v210, v178
	v_fmac_f32_e32 v142, v211, v179
	v_fmac_f32_e32 v143, v208, v180
	v_fmac_f32_e32 v143, v209, v181
	v_fmac_f32_e32 v143, v210, v182
	v_fmac_f32_e32 v143, v211, v183
	ds_read_b128 v[168:171], v152 offset:2048
	ds_read_b128 v[172:175], v152 offset:10256
	ds_read_b128 v[176:179], v152 offset:18464
	ds_read_b128 v[180:183], v152 offset:26672
	s_waitcnt lgkmcnt(4)
	v_fmac_f32_e32 v144, v208, v148
	v_fmac_f32_e32 v144, v209, v149
	v_fmac_f32_e32 v144, v210, v150
	v_fmac_f32_e32 v144, v211, v151
	v_fmac_f32_e32 v145, v208, v186
	v_fmac_f32_e32 v145, v209, v187
	v_fmac_f32_e32 v145, v210, v188
	v_fmac_f32_e32 v145, v211, v189
	v_fmac_f32_e32 v146, v208, v194
	v_fmac_f32_e32 v146, v209, v195
	v_fmac_f32_e32 v146, v210, v196
	v_fmac_f32_e32 v146, v211, v197
	v_fmac_f32_e32 v147, v208, v198
	v_fmac_f32_e32 v147, v209, v199
	v_fmac_f32_e32 v147, v210, v200
	v_fmac_f32_e32 v147, v211, v201
	ds_read_b128 v[148:151], v152 offset:34880
	ds_read_b128 v[186:189], v152 offset:43088
	ds_read_b128 v[194:197], v152 offset:51296
	ds_read_b128 v[198:201], v152 offset:59504
	s_waitcnt lgkmcnt(4)
	v_fmac_f32_e32 v132, v212, v168
	v_fmac_f32_e32 v132, v213, v169
	v_fmac_f32_e32 v132, v214, v170
	v_fmac_f32_e32 v132, v215, v171
	v_fmac_f32_e32 v133, v212, v172
	v_fmac_f32_e32 v133, v213, v173
	v_fmac_f32_e32 v133, v214, v174
	v_fmac_f32_e32 v133, v215, v175
	v_fmac_f32_e32 v134, v212, v176
	v_fmac_f32_e32 v134, v213, v177
	v_fmac_f32_e32 v134, v214, v178
	v_fmac_f32_e32 v134, v215, v179
	v_fmac_f32_e32 v135, v212, v180
	v_fmac_f32_e32 v135, v213, v181
	v_fmac_f32_e32 v135, v214, v182
	v_fmac_f32_e32 v135, v215, v183
	ds_read_b128 v[168:171], v153 offset:2048
	ds_read_b128 v[172:175], v153 offset:10256
	ds_read_b128 v[176:179], v153 offset:18464
	ds_read_b128 v[180:183], v153 offset:26672
	s_waitcnt lgkmcnt(4)
	v_fmac_f32_e32 v136, v212, v148
	v_fmac_f32_e32 v136, v213, v149
	v_fmac_f32_e32 v136, v214, v150
	v_fmac_f32_e32 v136, v215, v151
	v_fmac_f32_e32 v137, v212, v186
	v_fmac_f32_e32 v137, v213, v187
	v_fmac_f32_e32 v137, v214, v188
	v_fmac_f32_e32 v137, v215, v189
	v_fmac_f32_e32 v138, v212, v194
	v_fmac_f32_e32 v138, v213, v195
	v_fmac_f32_e32 v138, v214, v196
	v_fmac_f32_e32 v138, v215, v197
	v_fmac_f32_e32 v139, v212, v198
	v_fmac_f32_e32 v139, v213, v199
	v_fmac_f32_e32 v139, v214, v200
	v_fmac_f32_e32 v139, v215, v201
	ds_read_b128 v[148:151], v153 offset:34880
	ds_read_b128 v[186:189], v153 offset:43088
	ds_read_b128 v[194:197], v153 offset:51296
	ds_read_b128 v[198:201], v153 offset:59504
	s_waitcnt lgkmcnt(4)
	v_fmac_f32_e32 v140, v212, v168
	v_fmac_f32_e32 v140, v213, v169
	v_fmac_f32_e32 v140, v214, v170
	v_fmac_f32_e32 v140, v215, v171
	v_fmac_f32_e32 v141, v212, v172
	v_fmac_f32_e32 v141, v213, v173
	v_fmac_f32_e32 v141, v214, v174
	v_fmac_f32_e32 v141, v215, v175
	v_fmac_f32_e32 v142, v212, v176
	v_fmac_f32_e32 v142, v213, v177
	v_fmac_f32_e32 v142, v214, v178
	v_fmac_f32_e32 v142, v215, v179
	v_fmac_f32_e32 v143, v212, v180
	v_fmac_f32_e32 v143, v213, v181
	v_fmac_f32_e32 v143, v214, v182
	v_fmac_f32_e32 v143, v215, v183
	ds_read_b128 v[168:171], v152 offset:3072
	ds_read_b128 v[172:175], v152 offset:11280
	ds_read_b128 v[176:179], v152 offset:19488
	ds_read_b128 v[180:183], v152 offset:27696
	s_waitcnt lgkmcnt(4)
	v_fmac_f32_e32 v144, v212, v148
	v_fmac_f32_e32 v144, v213, v149
	v_fmac_f32_e32 v144, v214, v150
	v_fmac_f32_e32 v144, v215, v151
	v_fmac_f32_e32 v145, v212, v186
	v_fmac_f32_e32 v145, v213, v187
	v_fmac_f32_e32 v145, v214, v188
	v_fmac_f32_e32 v145, v215, v189
	v_fmac_f32_e32 v146, v212, v194
	v_fmac_f32_e32 v146, v213, v195
	v_fmac_f32_e32 v146, v214, v196
	v_fmac_f32_e32 v146, v215, v197
	v_fmac_f32_e32 v147, v212, v198
	v_fmac_f32_e32 v147, v213, v199
	v_fmac_f32_e32 v147, v214, v200
	v_fmac_f32_e32 v147, v215, v201
	ds_read_b128 v[148:151], v152 offset:35904
	ds_read_b128 v[186:189], v152 offset:44112
	ds_read_b128 v[194:197], v152 offset:52320
	ds_read_b128 v[198:201], v152 offset:60528
	s_waitcnt lgkmcnt(4)
	v_fmac_f32_e32 v132, v216, v168
	v_fmac_f32_e32 v132, v217, v169
	v_fmac_f32_e32 v132, v218, v170
	v_fmac_f32_e32 v132, v219, v171
	v_fmac_f32_e32 v133, v216, v172
	v_fmac_f32_e32 v133, v217, v173
	v_fmac_f32_e32 v133, v218, v174
	v_fmac_f32_e32 v133, v219, v175
	v_fmac_f32_e32 v134, v216, v176
	v_fmac_f32_e32 v134, v217, v177
	v_fmac_f32_e32 v134, v218, v178
	v_fmac_f32_e32 v134, v219, v179
	v_fmac_f32_e32 v135, v216, v180
	v_fmac_f32_e32 v135, v217, v181
	v_fmac_f32_e32 v135, v218, v182
	v_fmac_f32_e32 v135, v219, v183
	ds_read_b128 v[168:171], v153 offset:3072
	ds_read_b128 v[172:175], v153 offset:11280
	ds_read_b128 v[176:179], v153 offset:19488
	ds_read_b128 v[180:183], v153 offset:27696
	s_waitcnt lgkmcnt(4)
	v_fmac_f32_e32 v136, v216, v148
	v_fmac_f32_e32 v136, v217, v149
	v_fmac_f32_e32 v136, v218, v150
	v_fmac_f32_e32 v136, v219, v151
	v_fmac_f32_e32 v137, v216, v186
	v_fmac_f32_e32 v137, v217, v187
	v_fmac_f32_e32 v137, v218, v188
	v_fmac_f32_e32 v137, v219, v189
	v_fmac_f32_e32 v138, v216, v194
	v_fmac_f32_e32 v138, v217, v195
	v_fmac_f32_e32 v138, v218, v196
	v_fmac_f32_e32 v138, v219, v197
	v_fmac_f32_e32 v139, v216, v198
	v_fmac_f32_e32 v139, v217, v199
	v_fmac_f32_e32 v139, v218, v200
	v_fmac_f32_e32 v139, v219, v201
	ds_read_b128 v[148:151], v153 offset:35904
	ds_read_b128 v[186:189], v153 offset:44112
	ds_read_b128 v[194:197], v153 offset:52320
	ds_read_b128 v[198:201], v153 offset:60528
	s_waitcnt lgkmcnt(4)
	v_fmac_f32_e32 v140, v216, v168
	v_fmac_f32_e32 v140, v217, v169
	v_fmac_f32_e32 v140, v218, v170
	v_fmac_f32_e32 v140, v219, v171
	v_fmac_f32_e32 v141, v216, v172
	v_fmac_f32_e32 v141, v217, v173
	v_fmac_f32_e32 v141, v218, v174
	v_fmac_f32_e32 v141, v219, v175
	v_fmac_f32_e32 v142, v216, v176
	v_fmac_f32_e32 v142, v217, v177
	v_fmac_f32_e32 v142, v218, v178
	v_fmac_f32_e32 v142, v219, v179
	v_fmac_f32_e32 v143, v216, v180
	v_fmac_f32_e32 v143, v217, v181
	v_fmac_f32_e32 v143, v218, v182
	v_fmac_f32_e32 v143, v219, v183
	ds_read_b128 v[168:171], v152 offset:4096
	ds_read_b128 v[172:175], v152 offset:12304
	ds_read_b128 v[176:179], v152 offset:20512
	ds_read_b128 v[180:183], v152 offset:28720
	s_waitcnt lgkmcnt(4)
	v_fmac_f32_e32 v144, v216, v148
	v_fmac_f32_e32 v144, v217, v149
	v_fmac_f32_e32 v144, v218, v150
	v_fmac_f32_e32 v144, v219, v151
	v_fmac_f32_e32 v145, v216, v186
	v_fmac_f32_e32 v145, v217, v187
	v_fmac_f32_e32 v145, v218, v188
	v_fmac_f32_e32 v145, v219, v189
	v_fmac_f32_e32 v146, v216, v194
	v_fmac_f32_e32 v146, v217, v195
	v_fmac_f32_e32 v146, v218, v196
	v_fmac_f32_e32 v146, v219, v197
	v_fmac_f32_e32 v147, v216, v198
	v_fmac_f32_e32 v147, v217, v199
	v_fmac_f32_e32 v147, v218, v200
	v_fmac_f32_e32 v147, v219, v201
	ds_read_b128 v[148:151], v152 offset:36928
	ds_read_b128 v[186:189], v152 offset:45136
	ds_read_b128 v[194:197], v152 offset:53344
	ds_read_b128 v[198:201], v152 offset:61552
	s_waitcnt lgkmcnt(4)
	v_fmac_f32_e32 v132, v226, v168
	v_fmac_f32_e32 v132, v227, v169
	v_fmac_f32_e32 v132, v228, v170
	v_fmac_f32_e32 v132, v229, v171
	v_fmac_f32_e32 v133, v226, v172
	v_fmac_f32_e32 v133, v227, v173
	v_fmac_f32_e32 v133, v228, v174
	v_fmac_f32_e32 v133, v229, v175
	v_fmac_f32_e32 v134, v226, v176
	v_fmac_f32_e32 v134, v227, v177
	v_fmac_f32_e32 v134, v228, v178
	v_fmac_f32_e32 v134, v229, v179
	v_fmac_f32_e32 v135, v226, v180
	v_fmac_f32_e32 v135, v227, v181
	v_fmac_f32_e32 v135, v228, v182
	v_fmac_f32_e32 v135, v229, v183
	ds_read_b128 v[168:171], v153 offset:4096
	ds_read_b128 v[172:175], v153 offset:12304
	ds_read_b128 v[176:179], v153 offset:20512
	ds_read_b128 v[180:183], v153 offset:28720
	s_waitcnt lgkmcnt(4)
	v_fmac_f32_e32 v136, v226, v148
	v_fmac_f32_e32 v136, v227, v149
	v_fmac_f32_e32 v136, v228, v150
	v_fmac_f32_e32 v136, v229, v151
	v_fmac_f32_e32 v137, v226, v186
	v_fmac_f32_e32 v137, v227, v187
	v_fmac_f32_e32 v137, v228, v188
	v_fmac_f32_e32 v137, v229, v189
	v_fmac_f32_e32 v138, v226, v194
	v_fmac_f32_e32 v138, v227, v195
	v_fmac_f32_e32 v138, v228, v196
	v_fmac_f32_e32 v138, v229, v197
	v_fmac_f32_e32 v139, v226, v198
	v_fmac_f32_e32 v139, v227, v199
	v_fmac_f32_e32 v139, v228, v200
	v_fmac_f32_e32 v139, v229, v201
	ds_read_b128 v[148:151], v153 offset:36928
	ds_read_b128 v[186:189], v153 offset:45136
	ds_read_b128 v[194:197], v153 offset:53344
	ds_read_b128 v[198:201], v153 offset:61552
	s_waitcnt lgkmcnt(4)
	v_fmac_f32_e32 v140, v226, v168
	v_fmac_f32_e32 v140, v227, v169
	v_fmac_f32_e32 v140, v228, v170
	v_fmac_f32_e32 v140, v229, v171
	v_fmac_f32_e32 v141, v226, v172
	v_fmac_f32_e32 v141, v227, v173
	v_fmac_f32_e32 v141, v228, v174
	v_fmac_f32_e32 v141, v229, v175
	v_fmac_f32_e32 v142, v226, v176
	v_fmac_f32_e32 v142, v227, v177
	v_fmac_f32_e32 v142, v228, v178
	v_fmac_f32_e32 v142, v229, v179
	v_fmac_f32_e32 v143, v226, v180
	v_fmac_f32_e32 v143, v227, v181
	v_fmac_f32_e32 v143, v228, v182
	v_fmac_f32_e32 v143, v229, v183
	ds_read_b128 v[168:171], v152 offset:5120
	ds_read_b128 v[172:175], v152 offset:13328
	ds_read_b128 v[176:179], v152 offset:21536
	ds_read_b128 v[180:183], v152 offset:29744
	s_waitcnt lgkmcnt(4)
	v_fmac_f32_e32 v144, v226, v148
	v_fmac_f32_e32 v144, v227, v149
	v_fmac_f32_e32 v144, v228, v150
	v_fmac_f32_e32 v144, v229, v151
	v_fmac_f32_e32 v145, v226, v186
	v_fmac_f32_e32 v145, v227, v187
	v_fmac_f32_e32 v145, v228, v188
	v_fmac_f32_e32 v145, v229, v189
	v_fmac_f32_e32 v146, v226, v194
	v_fmac_f32_e32 v146, v227, v195
	v_fmac_f32_e32 v146, v228, v196
	v_fmac_f32_e32 v146, v229, v197
	v_fmac_f32_e32 v147, v226, v198
	v_fmac_f32_e32 v147, v227, v199
	v_fmac_f32_e32 v147, v228, v200
	v_fmac_f32_e32 v147, v229, v201
	ds_read_b128 v[148:151], v152 offset:37952
	ds_read_b128 v[186:189], v152 offset:46160
	ds_read_b128 v[194:197], v152 offset:54368
	ds_read_b128 v[198:201], v152 offset:62576
	s_waitcnt lgkmcnt(4)
	v_fmac_f32_e32 v132, v230, v168
	v_fmac_f32_e32 v132, v231, v169
	v_fmac_f32_e32 v132, v232, v170
	v_fmac_f32_e32 v132, v233, v171
	v_fmac_f32_e32 v133, v230, v172
	v_fmac_f32_e32 v133, v231, v173
	v_fmac_f32_e32 v133, v232, v174
	v_fmac_f32_e32 v133, v233, v175
	v_fmac_f32_e32 v134, v230, v176
	v_fmac_f32_e32 v134, v231, v177
	v_fmac_f32_e32 v134, v232, v178
	v_fmac_f32_e32 v134, v233, v179
	v_fmac_f32_e32 v135, v230, v180
	v_fmac_f32_e32 v135, v231, v181
	v_fmac_f32_e32 v135, v232, v182
	v_fmac_f32_e32 v135, v233, v183
	ds_read_b128 v[168:171], v153 offset:5120
	ds_read_b128 v[172:175], v153 offset:13328
	ds_read_b128 v[176:179], v153 offset:21536
	ds_read_b128 v[180:183], v153 offset:29744
	s_waitcnt lgkmcnt(4)
	v_fmac_f32_e32 v136, v230, v148
	v_fmac_f32_e32 v136, v231, v149
	v_fmac_f32_e32 v136, v232, v150
	v_fmac_f32_e32 v136, v233, v151
	v_fmac_f32_e32 v137, v230, v186
	v_fmac_f32_e32 v137, v231, v187
	v_fmac_f32_e32 v137, v232, v188
	v_fmac_f32_e32 v137, v233, v189
	v_fmac_f32_e32 v138, v230, v194
	v_fmac_f32_e32 v138, v231, v195
	v_fmac_f32_e32 v138, v232, v196
	v_fmac_f32_e32 v138, v233, v197
	v_fmac_f32_e32 v139, v230, v198
	v_fmac_f32_e32 v139, v231, v199
	v_fmac_f32_e32 v139, v232, v200
	v_fmac_f32_e32 v139, v233, v201
	ds_read_b128 v[148:151], v153 offset:37952
	ds_read_b128 v[186:189], v153 offset:46160
	ds_read_b128 v[194:197], v153 offset:54368
	ds_read_b128 v[198:201], v153 offset:62576
	s_waitcnt lgkmcnt(4)
	v_fmac_f32_e32 v140, v230, v168
	v_fmac_f32_e32 v140, v231, v169
	v_fmac_f32_e32 v140, v232, v170
	v_fmac_f32_e32 v140, v233, v171
	v_fmac_f32_e32 v141, v230, v172
	v_fmac_f32_e32 v141, v231, v173
	v_fmac_f32_e32 v141, v232, v174
	v_fmac_f32_e32 v141, v233, v175
	v_fmac_f32_e32 v142, v230, v176
	v_fmac_f32_e32 v142, v231, v177
	v_fmac_f32_e32 v142, v232, v178
	v_fmac_f32_e32 v142, v233, v179
	v_fmac_f32_e32 v143, v230, v180
	v_fmac_f32_e32 v143, v231, v181
	v_fmac_f32_e32 v143, v232, v182
	v_fmac_f32_e32 v143, v233, v183
	ds_read_b128 v[168:171], v152 offset:6144
	ds_read_b128 v[172:175], v152 offset:14352
	ds_read_b128 v[176:179], v152 offset:22560
	ds_read_b128 v[180:183], v152 offset:30768
	s_waitcnt lgkmcnt(4)
	v_fmac_f32_e32 v144, v230, v148
	v_fmac_f32_e32 v144, v231, v149
	v_fmac_f32_e32 v144, v232, v150
	v_fmac_f32_e32 v144, v233, v151
	v_fmac_f32_e32 v145, v230, v186
	v_fmac_f32_e32 v145, v231, v187
	v_fmac_f32_e32 v145, v232, v188
	v_fmac_f32_e32 v145, v233, v189
	v_fmac_f32_e32 v146, v230, v194
	v_fmac_f32_e32 v146, v231, v195
	v_fmac_f32_e32 v146, v232, v196
	v_fmac_f32_e32 v146, v233, v197
	v_fmac_f32_e32 v147, v230, v198
	v_fmac_f32_e32 v147, v231, v199
	v_fmac_f32_e32 v147, v232, v200
	v_fmac_f32_e32 v147, v233, v201
	ds_read_b128 v[148:151], v152 offset:38976
	ds_read_b128 v[186:189], v152 offset:47184
	ds_read_b128 v[194:197], v152 offset:55392
	ds_read_b128 v[198:201], v152 offset:63600
	s_waitcnt lgkmcnt(4)
	v_fmac_f32_e32 v132, v234, v168
	v_fmac_f32_e32 v132, v235, v169
	v_fmac_f32_e32 v132, v236, v170
	v_fmac_f32_e32 v132, v237, v171
	v_fmac_f32_e32 v133, v234, v172
	v_fmac_f32_e32 v133, v235, v173
	v_fmac_f32_e32 v133, v236, v174
	v_fmac_f32_e32 v133, v237, v175
	v_fmac_f32_e32 v134, v234, v176
	v_fmac_f32_e32 v134, v235, v177
	v_fmac_f32_e32 v134, v236, v178
	v_fmac_f32_e32 v134, v237, v179
	v_fmac_f32_e32 v135, v234, v180
	v_fmac_f32_e32 v135, v235, v181
	v_fmac_f32_e32 v135, v236, v182
	v_fmac_f32_e32 v135, v237, v183
	ds_read_b128 v[168:171], v153 offset:6144
	ds_read_b128 v[172:175], v153 offset:14352
	ds_read_b128 v[176:179], v153 offset:22560
	ds_read_b128 v[180:183], v153 offset:30768
	s_waitcnt lgkmcnt(4)
	v_fmac_f32_e32 v136, v234, v148
	v_fmac_f32_e32 v136, v235, v149
	v_fmac_f32_e32 v136, v236, v150
	v_fmac_f32_e32 v136, v237, v151
	v_fmac_f32_e32 v137, v234, v186
	v_fmac_f32_e32 v137, v235, v187
	v_fmac_f32_e32 v137, v236, v188
	v_fmac_f32_e32 v137, v237, v189
	v_fmac_f32_e32 v138, v234, v194
	v_fmac_f32_e32 v138, v235, v195
	v_fmac_f32_e32 v138, v236, v196
	v_fmac_f32_e32 v138, v237, v197
	v_fmac_f32_e32 v139, v234, v198
	v_fmac_f32_e32 v139, v235, v199
	v_fmac_f32_e32 v139, v236, v200
	v_fmac_f32_e32 v139, v237, v201
	ds_read_b128 v[148:151], v153 offset:38976
	ds_read_b128 v[186:189], v153 offset:47184
	ds_read_b128 v[194:197], v153 offset:55392
	ds_read_b128 v[198:201], v153 offset:63600
	s_waitcnt lgkmcnt(4)
	v_fmac_f32_e32 v140, v234, v168
	v_fmac_f32_e32 v140, v235, v169
	v_fmac_f32_e32 v140, v236, v170
	v_fmac_f32_e32 v140, v237, v171
	v_fmac_f32_e32 v141, v234, v172
	v_fmac_f32_e32 v141, v235, v173
	v_fmac_f32_e32 v141, v236, v174
	v_fmac_f32_e32 v141, v237, v175
	v_fmac_f32_e32 v142, v234, v176
	v_fmac_f32_e32 v142, v235, v177
	v_fmac_f32_e32 v142, v236, v178
	v_fmac_f32_e32 v142, v237, v179
	v_fmac_f32_e32 v143, v234, v180
	v_fmac_f32_e32 v143, v235, v181
	v_fmac_f32_e32 v143, v236, v182
	v_fmac_f32_e32 v143, v237, v183
	ds_read_b128 v[168:171], v152 offset:7168
	ds_read_b128 v[172:175], v152 offset:15376
	ds_read_b128 v[176:179], v152 offset:23584
	ds_read_b128 v[180:183], v152 offset:31792
	s_waitcnt lgkmcnt(4)
	v_fmac_f32_e32 v144, v234, v148
	v_fmac_f32_e32 v144, v235, v149
	v_fmac_f32_e32 v144, v236, v150
	v_fmac_f32_e32 v144, v237, v151
	v_fmac_f32_e32 v145, v234, v186
	v_fmac_f32_e32 v145, v235, v187
	v_fmac_f32_e32 v145, v236, v188
	v_fmac_f32_e32 v145, v237, v189
	v_fmac_f32_e32 v146, v234, v194
	v_fmac_f32_e32 v146, v235, v195
	v_fmac_f32_e32 v146, v236, v196
	v_fmac_f32_e32 v146, v237, v197
	v_fmac_f32_e32 v147, v234, v198
	v_fmac_f32_e32 v147, v235, v199
	v_fmac_f32_e32 v147, v236, v200
	v_fmac_f32_e32 v147, v237, v201
	ds_read_b128 v[148:151], v152 offset:40000
	ds_read_b128 v[186:189], v152 offset:48208
	ds_read_b128 v[194:197], v152 offset:56416
	ds_read_b128 v[198:201], v152 offset:64624
	s_waitcnt lgkmcnt(4)
	v_fmac_f32_e32 v132, v238, v168
	v_fmac_f32_e32 v132, v239, v169
	v_fmac_f32_e32 v132, v240, v170
	v_fmac_f32_e32 v132, v241, v171
	v_fmac_f32_e32 v133, v238, v172
	v_fmac_f32_e32 v133, v239, v173
	v_fmac_f32_e32 v133, v240, v174
	v_fmac_f32_e32 v133, v241, v175
	v_fmac_f32_e32 v134, v238, v176
	v_fmac_f32_e32 v134, v239, v177
	v_fmac_f32_e32 v134, v240, v178
	v_fmac_f32_e32 v134, v241, v179
	v_fmac_f32_e32 v135, v238, v180
	v_fmac_f32_e32 v135, v239, v181
	v_fmac_f32_e32 v135, v240, v182
	v_fmac_f32_e32 v135, v241, v183
	ds_read_b128 v[168:171], v153 offset:7168
	ds_read_b128 v[172:175], v153 offset:15376
	ds_read_b128 v[176:179], v153 offset:23584
	ds_read_b128 v[180:183], v153 offset:31792
	s_waitcnt lgkmcnt(4)
	v_fmac_f32_e32 v136, v238, v148
	v_fmac_f32_e32 v136, v239, v149
	v_fmac_f32_e32 v136, v240, v150
	v_fmac_f32_e32 v136, v241, v151
	v_fmac_f32_e32 v137, v238, v186
	v_fmac_f32_e32 v137, v239, v187
	v_fmac_f32_e32 v137, v240, v188
	v_fmac_f32_e32 v137, v241, v189
	v_fmac_f32_e32 v138, v238, v194
	v_fmac_f32_e32 v138, v239, v195
	v_fmac_f32_e32 v138, v240, v196
	v_fmac_f32_e32 v138, v241, v197
	v_fmac_f32_e32 v139, v238, v198
	v_fmac_f32_e32 v139, v239, v199
	v_fmac_f32_e32 v139, v240, v200
	v_fmac_f32_e32 v139, v241, v201
	ds_read_b128 v[148:151], v153 offset:40000
	ds_read_b128 v[186:189], v153 offset:48208
	ds_read_b128 v[194:197], v153 offset:56416
	ds_read_b128 v[198:201], v153 offset:64624
	s_waitcnt lgkmcnt(4)
	v_fmac_f32_e32 v140, v238, v168
	v_fmac_f32_e32 v140, v239, v169
	v_fmac_f32_e32 v140, v240, v170
	v_fmac_f32_e32 v140, v241, v171
	v_fmac_f32_e32 v141, v238, v172
	v_fmac_f32_e32 v141, v239, v173
	v_fmac_f32_e32 v141, v240, v174
	v_fmac_f32_e32 v141, v241, v175
	v_fmac_f32_e32 v142, v238, v176
	v_fmac_f32_e32 v142, v239, v177
	v_fmac_f32_e32 v142, v240, v178
	v_fmac_f32_e32 v142, v241, v179
	v_fmac_f32_e32 v143, v238, v180
	v_fmac_f32_e32 v143, v239, v181
	v_fmac_f32_e32 v143, v240, v182
	v_fmac_f32_e32 v143, v241, v183
	s_waitcnt lgkmcnt(0)
	v_fmac_f32_e32 v144, v238, v148
	v_fmac_f32_e32 v144, v239, v149
	v_fmac_f32_e32 v144, v240, v150
	v_fmac_f32_e32 v144, v241, v151
	v_fmac_f32_e32 v145, v238, v186
	v_fmac_f32_e32 v145, v239, v187
	v_fmac_f32_e32 v145, v240, v188
	v_fmac_f32_e32 v145, v241, v189
	v_fmac_f32_e32 v146, v238, v194
	v_fmac_f32_e32 v146, v239, v195
	v_fmac_f32_e32 v146, v240, v196
	v_fmac_f32_e32 v146, v241, v197
	v_fmac_f32_e32 v147, v238, v198
	v_fmac_f32_e32 v147, v239, v199
	v_fmac_f32_e32 v147, v240, v200
	v_fmac_f32_e32 v147, v241, v201
	s_add_i32 s11, s10, 0x1800
	s_lshr_b32 s0, s11, 8
	s_mul_i32 s0, s0, 57
	s_lshr_b32 s0, s0, 9
	s_mul_i32 s1, s0, 0x900
	s_sub_i32 s43, s11, s1
	s_lshl_b32 s1, s11, 13
	s_add_u32 s12, s48, s1
	s_addc_u32 s13, s49, 0
	s_add_u32 s14, s12, 0x1000
	s_addc_u32 s15, s13, 0
	global_load_dwordx4 v[204:207], v1, s[12:13]
	global_load_dwordx4 v[208:211], v1, s[12:13] offset:1024
	global_load_dwordx4 v[212:215], v1, s[12:13] offset:2048
	global_load_dwordx4 v[216:219], v1, s[12:13] offset:3072
	global_load_dwordx4 v[226:229], v1, s[14:15]
	global_load_dwordx4 v[230:233], v1, s[14:15] offset:1024
	global_load_dwordx4 v[234:237], v1, s[14:15] offset:2048
	global_load_dwordx4 v[238:241], v1, s[14:15] offset:3072
	v_cndmask_b32_e64 v242, v133, v132, s[62:63]
	v_cndmask_b32_e64 v132, v132, v133, s[62:63]
	v_cndmask_b32_e64 v243, v135, v134, s[62:63]
	v_cndmask_b32_e64 v134, v134, v135, s[62:63]
	v_cndmask_b32_e64 v244, v137, v136, s[62:63]
	v_cndmask_b32_e64 v136, v136, v137, s[62:63]
	v_cndmask_b32_e64 v245, v139, v138, s[62:63]
	v_cndmask_b32_e64 v138, v138, v139, s[62:63]
	v_cndmask_b32_e64 v246, v141, v140, s[62:63]
	v_cndmask_b32_e64 v140, v140, v141, s[62:63]
	v_cndmask_b32_e64 v248, v143, v142, s[62:63]
	v_cndmask_b32_e64 v142, v142, v143, s[62:63]
	v_cndmask_b32_e64 v249, v145, v144, s[62:63]
	v_cndmask_b32_e64 v144, v144, v145, s[62:63]
	v_cndmask_b32_e64 v250, v147, v146, s[62:63]
	v_cndmask_b32_e64 v146, v146, v147, s[62:63]
	v_add_f32_dpp v132, v242, v132 quad_perm:[1,0,3,2] row_mask:0xf bank_mask:0xf
	v_add_f32_dpp v134, v243, v134 quad_perm:[1,0,3,2] row_mask:0xf bank_mask:0xf
	v_add_f32_dpp v136, v244, v136 quad_perm:[1,0,3,2] row_mask:0xf bank_mask:0xf
	v_add_f32_dpp v138, v245, v138 quad_perm:[1,0,3,2] row_mask:0xf bank_mask:0xf
	v_add_f32_dpp v140, v246, v140 quad_perm:[1,0,3,2] row_mask:0xf bank_mask:0xf
	v_add_f32_dpp v142, v248, v142 quad_perm:[1,0,3,2] row_mask:0xf bank_mask:0xf
	v_add_f32_dpp v144, v249, v144 quad_perm:[1,0,3,2] row_mask:0xf bank_mask:0xf
	v_add_f32_dpp v146, v250, v146 quad_perm:[1,0,3,2] row_mask:0xf bank_mask:0xf
	v_cndmask_b32_e64 v242, v134, v132, s[64:65]
	v_cndmask_b32_e64 v132, v132, v134, s[64:65]
	v_cndmask_b32_e64 v243, v138, v136, s[64:65]
	v_cndmask_b32_e64 v136, v136, v138, s[64:65]
	v_cndmask_b32_e64 v244, v142, v140, s[64:65]
	v_cndmask_b32_e64 v140, v140, v142, s[64:65]
	v_cndmask_b32_e64 v245, v146, v144, s[64:65]
	v_cndmask_b32_e64 v144, v144, v146, s[64:65]
	s_nop 0
	v_add_f32_dpp v132, v242, v132 quad_perm:[2,3,0,1] row_mask:0xf bank_mask:0xf
	v_add_f32_dpp v136, v243, v136 quad_perm:[2,3,0,1] row_mask:0xf bank_mask:0xf
	v_add_f32_dpp v140, v244, v140 quad_perm:[2,3,0,1] row_mask:0xf bank_mask:0xf
	v_add_f32_dpp v144, v245, v144 quad_perm:[2,3,0,1] row_mask:0xf bank_mask:0xf
	v_cndmask_b32_e64 v242, v136, v132, s[66:67]
	v_cndmask_b32_e64 v132, v132, v136, s[66:67]
	v_cndmask_b32_e64 v243, v144, v140, s[66:67]
	v_cndmask_b32_e64 v140, v140, v144, s[66:67]
	s_nop 1
	v_add_f32_dpp v246, v242, v132 row_shl:4 row_mask:0xf bank_mask:0x5
	v_add_f32_dpp v246, v242, v132 row_shr:4 row_mask:0xf bank_mask:0xa
	v_add_f32_dpp v248, v243, v140 row_shl:4 row_mask:0xf bank_mask:0x5
	v_add_f32_dpp v248, v243, v140 row_shr:4 row_mask:0xf bank_mask:0xa
	v_cndmask_b32_e64 v242, v248, v246, s[68:69]
	v_cndmask_b32_e64 v243, v246, v248, s[68:69]
	s_nop 1
	v_add_f32_dpp v191, v242, v243 row_ror:8 row_mask:0xf bank_mask:0xf
	s_nop 0
	ds_bpermute_b32 v193, v165, v191
	s_waitcnt lgkmcnt(0)
	v_add_f32_e32 v191, v191, v193
	ds_bpermute_b32 v193, v166, v191
	s_waitcnt lgkmcnt(0)
	v_add_f32_e32 v191, v191, v193
	v_mov_b32_e32 v193, v191
	s_nop 1
	v_max_f32_dpp v193, v193, v193 quad_perm:[1,0,3,2] row_mask:0xf bank_mask:0xf
	s_nop 1
	v_max_f32_dpp v193, v193, v193 quad_perm:[2,3,0,1] row_mask:0xf bank_mask:0xf
	s_nop 1
	v_max_f32_dpp v193, v193, v193 row_half_mirror row_mask:0xf bank_mask:0xf
	s_nop 1
	v_max_f32_dpp v193, v193, v193 row_mirror row_mask:0xf bank_mask:0xf
	v_sub_f32_e32 v191, v191, v193
	v_mul_f32_e32 v191, 0x3fb8aa3b, v191
	v_exp_f32_e32 v191, v191
	s_nop 0
	v_mov_b32_e32 v193, v191
	s_nop 1
	v_add_f32_dpp v193, v193, v193 quad_perm:[1,0,3,2] row_mask:0xf bank_mask:0xf
	s_nop 1
	v_add_f32_dpp v193, v193, v193 quad_perm:[2,3,0,1] row_mask:0xf bank_mask:0xf
	s_nop 1
	v_add_f32_dpp v193, v193, v193 row_half_mirror row_mask:0xf bank_mask:0xf
	s_nop 1
	v_add_f32_dpp v193, v193, v193 row_mirror row_mask:0xf bank_mask:0xf
	v_rcp_f32_e32 v193, v193
	s_nop 0
	v_mul_f32_e32 v191, v191, v193
	s_mov_b64 exec, 0xffff
	global_store_dword v164, v191, s[34:35]
	s_mov_b64 exec, -1
	s_waitcnt vmcnt(9)
	s_add_i32 s11, s10, 0x1000
	s_lshr_b32 s0, s11, 8
	s_mul_i32 s0, s0, 57
	s_lshr_b32 s0, s0, 9
	s_mul_i32 s1, s0, 0x900
	s_sub_i32 s43, s11, s1
	s_lshl_b32 s1, s11, 12
	s_add_u32 s16, s50, s1
	s_addc_u32 s17, s51, 0
	s_mul_i32 s1, s0, 0x24000
	s_lshl_b32 s2, s43, 2
	s_add_i32 s1, s1, s2
	s_add_u32 s34, s54, s1
	s_addc_u32 s35, s55, 0
	v_mul_f32_e32 v184, v100, v100
	v_fmac_f32_e32 v184, v101, v101
	v_fmac_f32_e32 v184, v102, v102
	v_fmac_f32_e32 v184, v103, v103
	v_fmac_f32_e32 v184, v104, v104
	v_fmac_f32_e32 v184, v105, v105
	v_fmac_f32_e32 v184, v106, v106
	v_fmac_f32_e32 v184, v107, v107
	v_fmac_f32_e32 v184, v108, v108
	v_fmac_f32_e32 v184, v109, v109
	v_fmac_f32_e32 v184, v110, v110
	v_fmac_f32_e32 v184, v111, v111
	v_fmac_f32_e32 v184, v112, v112
	v_fmac_f32_e32 v184, v113, v113
	v_fmac_f32_e32 v184, v114, v114
	v_fmac_f32_e32 v184, v115, v115
	v_fmac_f32_e32 v184, v116, v116
	v_fmac_f32_e32 v184, v117, v117
	v_fmac_f32_e32 v184, v118, v118
	v_fmac_f32_e32 v184, v119, v119
	v_fmac_f32_e32 v184, v120, v120
	v_fmac_f32_e32 v184, v121, v121
	v_fmac_f32_e32 v184, v122, v122
	v_fmac_f32_e32 v184, v123, v123
	v_fmac_f32_e32 v184, v124, v124
	v_fmac_f32_e32 v184, v125, v125
	v_fmac_f32_e32 v184, v126, v126
	v_fmac_f32_e32 v184, v127, v127
	v_fmac_f32_e32 v184, v128, v128
	v_fmac_f32_e32 v184, v129, v129
	v_fmac_f32_e32 v184, v130, v130
	v_fmac_f32_e32 v184, v131, v131
	ds_read_b128 v[168:171], v152 offset:0
	ds_read_b128 v[172:175], v152 offset:8208
	ds_read_b128 v[176:179], v152 offset:16416
	ds_read_b128 v[180:183], v152 offset:24624
	s_nop 0
	v_add_f32_dpp v184, v184, v184 quad_perm:[1,0,3,2] row_mask:0xf bank_mask:0xf
	s_nop 1
	v_add_f32_dpp v184, v184, v184 quad_perm:[2,3,0,1] row_mask:0xf bank_mask:0xf
	s_nop 1
	v_add_f32_dpp v184, v184, v184 row_half_mirror row_mask:0xf bank_mask:0xf
	s_nop 1
	v_add_f32_dpp v184, v184, v184 row_mirror row_mask:0xf bank_mask:0xf
	s_nop 1
	v_readlane_b32 s0, v184, 0
	v_readlane_b32 s1, v184, 16
	v_readlane_b32 s2, v184, 32
	v_readlane_b32 s3, v184, 48
	v_fma_f32 v4, v4, v36, v4
	v_fma_f32 v5, v5, v37, v5
	v_fma_f32 v6, v6, v38, v6
	v_fma_f32 v7, v7, v39, v7
	v_fma_f32 v8, v8, v40, v8
	v_fma_f32 v9, v9, v41, v9
	v_fma_f32 v10, v10, v42, v10
	v_fma_f32 v11, v11, v43, v11
	v_fma_f32 v12, v12, v44, v12
	v_fma_f32 v13, v13, v45, v13
	v_fma_f32 v14, v14, v46, v14
	v_fma_f32 v15, v15, v47, v15
	v_fma_f32 v16, v16, v48, v16
	v_fma_f32 v17, v17, v49, v17
	v_fma_f32 v18, v18, v50, v18
	v_fma_f32 v19, v19, v51, v19
	v_fma_f32 v20, v20, v52, v20
	v_fma_f32 v21, v21, v53, v21
	v_fma_f32 v22, v22, v54, v22
	v_fma_f32 v23, v23, v55, v23
	v_fma_f32 v24, v24, v56, v24
	v_fma_f32 v25, v25, v57, v25
	v_fma_f32 v26, v26, v58, v26
	v_fma_f32 v27, v27, v59, v27
	v_fma_f32 v28, v28, v60, v28
	v_fma_f32 v29, v29, v61, v29
	v_fma_f32 v30, v30, v62, v30
	v_fma_f32 v31, v31, v63, v31
	v_fma_f32 v32, v32, v64, v32
	v_fma_f32 v33, v33, v65, v33
	v_fma_f32 v34, v34, v66, v34
	v_fma_f32 v35, v35, v67, v35
	v_mov_b32_e32 v190, s0
	v_add_f32_e32 v190, s1, v190
	v_add_f32_e32 v190, s2, v190
	v_add_f32_e32 v190, s3, v190
	v_mul_f32_e32 v190, 0x3a000000, v190
	v_add_f32_e32 v190, 0x358637bd, v190
	v_rsq_f32_e32 v190, v190
	s_nop 0
	v_mul_f32_e32 v4, v4, v190
	v_mul_f32_e32 v5, v5, v190
	v_mul_f32_e32 v6, v6, v190
	v_mul_f32_e32 v7, v7, v190
	v_mul_f32_e32 v8, v8, v190
	v_mul_f32_e32 v9, v9, v190
	v_mul_f32_e32 v10, v10, v190
	v_mul_f32_e32 v11, v11, v190
	v_mul_f32_e32 v12, v12, v190
	v_mul_f32_e32 v13, v13, v190
	v_mul_f32_e32 v14, v14, v190
	v_mul_f32_e32 v15, v15, v190
	v_mul_f32_e32 v16, v16, v190
	v_mul_f32_e32 v17, v17, v190
	v_mul_f32_e32 v18, v18, v190
	v_mul_f32_e32 v19, v19, v190
	v_mul_f32_e32 v20, v20, v190
	v_mul_f32_e32 v21, v21, v190
	v_mul_f32_e32 v22, v22, v190
	v_mul_f32_e32 v23, v23, v190
	v_mul_f32_e32 v24, v24, v190
	v_mul_f32_e32 v25, v25, v190
	v_mul_f32_e32 v26, v26, v190
	v_mul_f32_e32 v27, v27, v190
	v_mul_f32_e32 v28, v28, v190
	v_mul_f32_e32 v29, v29, v190
	v_mul_f32_e32 v30, v30, v190
	v_mul_f32_e32 v31, v31, v190
	v_mul_f32_e32 v32, v32, v190
	v_mul_f32_e32 v33, v33, v190
	v_mul_f32_e32 v34, v34, v190
	v_mul_f32_e32 v35, v35, v190
	v_fma_f32 v100, v100, v4, v68
	v_fma_f32 v101, v101, v5, v69
	v_fma_f32 v102, v102, v6, v70
	v_fma_f32 v103, v103, v7, v71
	v_fma_f32 v104, v104, v8, v72
	v_fma_f32 v105, v105, v9, v73
	v_fma_f32 v106, v106, v10, v74
	v_fma_f32 v107, v107, v11, v75
	v_fma_f32 v108, v108, v12, v76
	v_fma_f32 v109, v109, v13, v77
	v_fma_f32 v110, v110, v14, v78
	v_fma_f32 v111, v111, v15, v79
	v_fma_f32 v112, v112, v16, v80
	v_fma_f32 v113, v113, v17, v81
	v_fma_f32 v114, v114, v18, v82
	v_fma_f32 v115, v115, v19, v83
	v_fma_f32 v116, v116, v20, v84
	v_fma_f32 v117, v117, v21, v85
	v_fma_f32 v118, v118, v22, v86
	v_fma_f32 v119, v119, v23, v87
	v_fma_f32 v120, v120, v24, v88
	v_fma_f32 v121, v121, v25, v89
	v_fma_f32 v122, v122, v26, v90
	v_fma_f32 v123, v123, v27, v91
	v_fma_f32 v124, v124, v28, v92
	v_fma_f32 v125, v125, v29, v93
	v_fma_f32 v126, v126, v30, v94
	v_fma_f32 v127, v127, v31, v95
	v_fma_f32 v128, v128, v32, v96
	v_fma_f32 v129, v129, v33, v97
	v_fma_f32 v130, v130, v34, v98
	v_fma_f32 v131, v131, v35, v99
	v_cvt_pk_bf16_f32 v242, v100, v101
	v_cvt_pk_bf16_f32 v243, v102, v103
	global_store_dwordx2 v2, v[242:243], s[16:17]
	v_cvt_pk_bf16_f32 v244, v104, v105
	v_cvt_pk_bf16_f32 v245, v106, v107
	global_store_dwordx2 v2, v[244:245], s[16:17] offset:512
	v_cvt_pk_bf16_f32 v242, v108, v109
	v_cvt_pk_bf16_f32 v243, v110, v111
	global_store_dwordx2 v2, v[242:243], s[16:17] offset:1024
	v_cvt_pk_bf16_f32 v244, v112, v113
	v_cvt_pk_bf16_f32 v245, v114, v115
	global_store_dwordx2 v2, v[244:245], s[16:17] offset:1536
	v_cvt_pk_bf16_f32 v242, v116, v117
	v_cvt_pk_bf16_f32 v243, v118, v119
	global_store_dwordx2 v2, v[242:243], s[16:17] offset:2048
	v_cvt_pk_bf16_f32 v244, v120, v121
	v_cvt_pk_bf16_f32 v245, v122, v123
	global_store_dwordx2 v2, v[244:245], s[16:17] offset:2560
	v_cvt_pk_bf16_f32 v242, v124, v125
	v_cvt_pk_bf16_f32 v243, v126, v127
	global_store_dwordx2 v2, v[242:243], s[16:17] offset:3072
	v_cvt_pk_bf16_f32 v244, v128, v129
	v_cvt_pk_bf16_f32 v245, v130, v131
	global_store_dwordx2 v2, v[244:245], s[16:17] offset:3584
	s_add_i32 s11, s10, 0x1800
	s_lshr_b32 s0, s11, 8
	s_mul_i32 s0, s0, 57
	s_lshr_b32 s0, s0, 9
	s_mul_i32 s1, s0, 0x900
	s_sub_i32 s43, s11, s1
	s_cmpk_lt_u32 s43, 0x100
	s_cselect_b32 s0, 8, s0
	s_mul_i32 s1, s0, 0xc000
	s_add_u32 s18, s52, s1
	s_addc_u32 s19, s53, 0
	s_add_u32 s18, s18, 0x6000
	s_addc_u32 s19, s19, 0
	s_add_u32 s22, s18, 0x1000
	s_addc_u32 s23, s19, 0
	s_add_u32 s28, s18, 0x2000
	s_addc_u32 s29, s19, 0
	s_add_u32 s30, s18, 0x3000
	s_addc_u32 s31, s19, 0
	global_load_dwordx4 v[4:7], v1, s[56:57]
	global_load_dwordx4 v[36:39], v1, s[28:29]
	global_load_dwordx4 v[68:71], v1, s[18:19]
	global_load_dwordx4 v[8:11], v1, s[56:57] offset:1024
	global_load_dwordx4 v[40:43], v1, s[28:29] offset:1024
	global_load_dwordx4 v[72:75], v1, s[18:19] offset:1024
	global_load_dwordx4 v[12:15], v1, s[56:57] offset:2048
	global_load_dwordx4 v[44:47], v1, s[28:29] offset:2048
	global_load_dwordx4 v[76:79], v1, s[18:19] offset:2048
	global_load_dwordx4 v[16:19], v1, s[56:57] offset:3072
	global_load_dwordx4 v[48:51], v1, s[28:29] offset:3072
	global_load_dwordx4 v[80:83], v1, s[18:19] offset:3072
	global_load_dwordx4 v[20:23], v1, s[58:59]
	global_load_dwordx4 v[52:55], v1, s[30:31]
	global_load_dwordx4 v[84:87], v1, s[22:23]
	global_load_dwordx4 v[24:27], v1, s[58:59] offset:1024
	global_load_dwordx4 v[56:59], v1, s[30:31] offset:1024
	global_load_dwordx4 v[88:91], v1, s[22:23] offset:1024
	global_load_dwordx4 v[28:31], v1, s[58:59] offset:2048
	global_load_dwordx4 v[60:63], v1, s[30:31] offset:2048
	global_load_dwordx4 v[92:95], v1, s[22:23] offset:2048
	global_load_dwordx4 v[32:35], v1, s[58:59] offset:3072
	global_load_dwordx4 v[64:67], v1, s[30:31] offset:3072
	global_load_dwordx4 v[96:99], v1, s[22:23] offset:3072
	v_mov_b32_e32 v132, 0
	v_mov_b32_e32 v133, 0
	v_mov_b32_e32 v134, 0
	v_mov_b32_e32 v135, 0
	v_mov_b32_e32 v136, 0
	v_mov_b32_e32 v137, 0
	v_mov_b32_e32 v138, 0
	v_mov_b32_e32 v139, 0
	v_mov_b32_e32 v140, 0
	v_mov_b32_e32 v141, 0
	v_mov_b32_e32 v142, 0
	v_mov_b32_e32 v143, 0
	v_mov_b32_e32 v144, 0
	v_mov_b32_e32 v145, 0
	v_mov_b32_e32 v146, 0
	v_mov_b32_e32 v147, 0
	ds_read_b128 v[148:151], v152 offset:32832
	ds_read_b128 v[186:189], v152 offset:41040
	ds_read_b128 v[194:197], v152 offset:49248
	ds_read_b128 v[198:201], v152 offset:57456
	s_waitcnt lgkmcnt(4)
	v_fmac_f32_e32 v132, v100, v168
	v_fmac_f32_e32 v132, v101, v169
	v_fmac_f32_e32 v132, v102, v170
	v_fmac_f32_e32 v132, v103, v171
	v_fmac_f32_e32 v133, v100, v172
	v_fmac_f32_e32 v133, v101, v173
	v_fmac_f32_e32 v133, v102, v174
	v_fmac_f32_e32 v133, v103, v175
	v_fmac_f32_e32 v134, v100, v176
	v_fmac_f32_e32 v134, v101, v177
	v_fmac_f32_e32 v134, v102, v178
	v_fmac_f32_e32 v134, v103, v179
	v_fmac_f32_e32 v135, v100, v180
	v_fmac_f32_e32 v135, v101, v181
	v_fmac_f32_e32 v135, v102, v182
	v_fmac_f32_e32 v135, v103, v183
	ds_read_b128 v[168:171], v153 offset:0
	ds_read_b128 v[172:175], v153 offset:8208
	ds_read_b128 v[176:179], v153 offset:16416
	ds_read_b128 v[180:183], v153 offset:24624
	s_waitcnt lgkmcnt(4)
	v_fmac_f32_e32 v136, v100, v148
	v_fmac_f32_e32 v136, v101, v149
	v_fmac_f32_e32 v136, v102, v150
	v_fmac_f32_e32 v136, v103, v151
	v_fmac_f32_e32 v137, v100, v186
	v_fmac_f32_e32 v137, v101, v187
	v_fmac_f32_e32 v137, v102, v188
	v_fmac_f32_e32 v137, v103, v189
	v_fmac_f32_e32 v138, v100, v194
	v_fmac_f32_e32 v138, v101, v195
	v_fmac_f32_e32 v138, v102, v196
	v_fmac_f32_e32 v138, v103, v197
	v_fmac_f32_e32 v139, v100, v198
	v_fmac_f32_e32 v139, v101, v199
	v_fmac_f32_e32 v139, v102, v200
	v_fmac_f32_e32 v139, v103, v201
	ds_read_b128 v[148:151], v153 offset:32832
	ds_read_b128 v[186:189], v153 offset:41040
	ds_read_b128 v[194:197], v153 offset:49248
	ds_read_b128 v[198:201], v153 offset:57456
	s_waitcnt lgkmcnt(4)
	v_fmac_f32_e32 v140, v100, v168
	v_fmac_f32_e32 v140, v101, v169
	v_fmac_f32_e32 v140, v102, v170
	v_fmac_f32_e32 v140, v103, v171
	v_fmac_f32_e32 v141, v100, v172
	v_fmac_f32_e32 v141, v101, v173
	v_fmac_f32_e32 v141, v102, v174
	v_fmac_f32_e32 v141, v103, v175
	v_fmac_f32_e32 v142, v100, v176
	v_fmac_f32_e32 v142, v101, v177
	v_fmac_f32_e32 v142, v102, v178
	v_fmac_f32_e32 v142, v103, v179
	v_fmac_f32_e32 v143, v100, v180
	v_fmac_f32_e32 v143, v101, v181
	v_fmac_f32_e32 v143, v102, v182
	v_fmac_f32_e32 v143, v103, v183
	ds_read_b128 v[168:171], v152 offset:1024
	ds_read_b128 v[172:175], v152 offset:9232
	ds_read_b128 v[176:179], v152 offset:17440
	ds_read_b128 v[180:183], v152 offset:25648
	s_waitcnt lgkmcnt(4)
	v_fmac_f32_e32 v144, v100, v148
	v_fmac_f32_e32 v144, v101, v149
	v_fmac_f32_e32 v144, v102, v150
	v_fmac_f32_e32 v144, v103, v151
	v_fmac_f32_e32 v145, v100, v186
	v_fmac_f32_e32 v145, v101, v187
	v_fmac_f32_e32 v145, v102, v188
	v_fmac_f32_e32 v145, v103, v189
	v_fmac_f32_e32 v146, v100, v194
	v_fmac_f32_e32 v146, v101, v195
	v_fmac_f32_e32 v146, v102, v196
	v_fmac_f32_e32 v146, v103, v197
	v_fmac_f32_e32 v147, v100, v198
	v_fmac_f32_e32 v147, v101, v199
	v_fmac_f32_e32 v147, v102, v200
	v_fmac_f32_e32 v147, v103, v201
	ds_read_b128 v[148:151], v152 offset:33856
	ds_read_b128 v[186:189], v152 offset:42064
	ds_read_b128 v[194:197], v152 offset:50272
	ds_read_b128 v[198:201], v152 offset:58480
	s_waitcnt lgkmcnt(4)
	v_fmac_f32_e32 v132, v104, v168
	v_fmac_f32_e32 v132, v105, v169
	v_fmac_f32_e32 v132, v106, v170
	v_fmac_f32_e32 v132, v107, v171
	v_fmac_f32_e32 v133, v104, v172
	v_fmac_f32_e32 v133, v105, v173
	v_fmac_f32_e32 v133, v106, v174
	v_fmac_f32_e32 v133, v107, v175
	v_fmac_f32_e32 v134, v104, v176
	v_fmac_f32_e32 v134, v105, v177
	v_fmac_f32_e32 v134, v106, v178
	v_fmac_f32_e32 v134, v107, v179
	v_fmac_f32_e32 v135, v104, v180
	v_fmac_f32_e32 v135, v105, v181
	v_fmac_f32_e32 v135, v106, v182
	v_fmac_f32_e32 v135, v107, v183
	ds_read_b128 v[168:171], v153 offset:1024
	ds_read_b128 v[172:175], v153 offset:9232
	ds_read_b128 v[176:179], v153 offset:17440
	ds_read_b128 v[180:183], v153 offset:25648
	s_waitcnt lgkmcnt(4)
	v_fmac_f32_e32 v136, v104, v148
	v_fmac_f32_e32 v136, v105, v149
	v_fmac_f32_e32 v136, v106, v150
	v_fmac_f32_e32 v136, v107, v151
	v_fmac_f32_e32 v137, v104, v186
	v_fmac_f32_e32 v137, v105, v187
	v_fmac_f32_e32 v137, v106, v188
	v_fmac_f32_e32 v137, v107, v189
	v_fmac_f32_e32 v138, v104, v194
	v_fmac_f32_e32 v138, v105, v195
	v_fmac_f32_e32 v138, v106, v196
	v_fmac_f32_e32 v138, v107, v197
	v_fmac_f32_e32 v139, v104, v198
	v_fmac_f32_e32 v139, v105, v199
	v_fmac_f32_e32 v139, v106, v200
	v_fmac_f32_e32 v139, v107, v201
	ds_read_b128 v[148:151], v153 offset:33856
	ds_read_b128 v[186:189], v153 offset:42064
	ds_read_b128 v[194:197], v153 offset:50272
	ds_read_b128 v[198:201], v153 offset:58480
	s_waitcnt lgkmcnt(4)
	v_fmac_f32_e32 v140, v104, v168
	v_fmac_f32_e32 v140, v105, v169
	v_fmac_f32_e32 v140, v106, v170
	v_fmac_f32_e32 v140, v107, v171
	v_fmac_f32_e32 v141, v104, v172
	v_fmac_f32_e32 v141, v105, v173
	v_fmac_f32_e32 v141, v106, v174
	v_fmac_f32_e32 v141, v107, v175
	v_fmac_f32_e32 v142, v104, v176
	v_fmac_f32_e32 v142, v105, v177
	v_fmac_f32_e32 v142, v106, v178
	v_fmac_f32_e32 v142, v107, v179
	v_fmac_f32_e32 v143, v104, v180
	v_fmac_f32_e32 v143, v105, v181
	v_fmac_f32_e32 v143, v106, v182
	v_fmac_f32_e32 v143, v107, v183
	ds_read_b128 v[168:171], v152 offset:2048
	ds_read_b128 v[172:175], v152 offset:10256
	ds_read_b128 v[176:179], v152 offset:18464
	ds_read_b128 v[180:183], v152 offset:26672
	s_waitcnt lgkmcnt(4)
	v_fmac_f32_e32 v144, v104, v148
	v_fmac_f32_e32 v144, v105, v149
	v_fmac_f32_e32 v144, v106, v150
	v_fmac_f32_e32 v144, v107, v151
	v_fmac_f32_e32 v145, v104, v186
	v_fmac_f32_e32 v145, v105, v187
	v_fmac_f32_e32 v145, v106, v188
	v_fmac_f32_e32 v145, v107, v189
	v_fmac_f32_e32 v146, v104, v194
	v_fmac_f32_e32 v146, v105, v195
	v_fmac_f32_e32 v146, v106, v196
	v_fmac_f32_e32 v146, v107, v197
	v_fmac_f32_e32 v147, v104, v198
	v_fmac_f32_e32 v147, v105, v199
	v_fmac_f32_e32 v147, v106, v200
	v_fmac_f32_e32 v147, v107, v201
	ds_read_b128 v[148:151], v152 offset:34880
	ds_read_b128 v[186:189], v152 offset:43088
	ds_read_b128 v[194:197], v152 offset:51296
	ds_read_b128 v[198:201], v152 offset:59504
	s_waitcnt lgkmcnt(4)
	v_fmac_f32_e32 v132, v108, v168
	v_fmac_f32_e32 v132, v109, v169
	v_fmac_f32_e32 v132, v110, v170
	v_fmac_f32_e32 v132, v111, v171
	v_fmac_f32_e32 v133, v108, v172
	v_fmac_f32_e32 v133, v109, v173
	v_fmac_f32_e32 v133, v110, v174
	v_fmac_f32_e32 v133, v111, v175
	v_fmac_f32_e32 v134, v108, v176
	v_fmac_f32_e32 v134, v109, v177
	v_fmac_f32_e32 v134, v110, v178
	v_fmac_f32_e32 v134, v111, v179
	v_fmac_f32_e32 v135, v108, v180
	v_fmac_f32_e32 v135, v109, v181
	v_fmac_f32_e32 v135, v110, v182
	v_fmac_f32_e32 v135, v111, v183
	ds_read_b128 v[168:171], v153 offset:2048
	ds_read_b128 v[172:175], v153 offset:10256
	ds_read_b128 v[176:179], v153 offset:18464
	ds_read_b128 v[180:183], v153 offset:26672
	s_waitcnt lgkmcnt(4)
	v_fmac_f32_e32 v136, v108, v148
	v_fmac_f32_e32 v136, v109, v149
	v_fmac_f32_e32 v136, v110, v150
	v_fmac_f32_e32 v136, v111, v151
	v_fmac_f32_e32 v137, v108, v186
	v_fmac_f32_e32 v137, v109, v187
	v_fmac_f32_e32 v137, v110, v188
	v_fmac_f32_e32 v137, v111, v189
	v_fmac_f32_e32 v138, v108, v194
	v_fmac_f32_e32 v138, v109, v195
	v_fmac_f32_e32 v138, v110, v196
	v_fmac_f32_e32 v138, v111, v197
	v_fmac_f32_e32 v139, v108, v198
	v_fmac_f32_e32 v139, v109, v199
	v_fmac_f32_e32 v139, v110, v200
	v_fmac_f32_e32 v139, v111, v201
	ds_read_b128 v[148:151], v153 offset:34880
	ds_read_b128 v[186:189], v153 offset:43088
	ds_read_b128 v[194:197], v153 offset:51296
	ds_read_b128 v[198:201], v153 offset:59504
	s_waitcnt lgkmcnt(4)
	v_fmac_f32_e32 v140, v108, v168
	v_fmac_f32_e32 v140, v109, v169
	v_fmac_f32_e32 v140, v110, v170
	v_fmac_f32_e32 v140, v111, v171
	v_fmac_f32_e32 v141, v108, v172
	v_fmac_f32_e32 v141, v109, v173
	v_fmac_f32_e32 v141, v110, v174
	v_fmac_f32_e32 v141, v111, v175
	v_fmac_f32_e32 v142, v108, v176
	v_fmac_f32_e32 v142, v109, v177
	v_fmac_f32_e32 v142, v110, v178
	v_fmac_f32_e32 v142, v111, v179
	v_fmac_f32_e32 v143, v108, v180
	v_fmac_f32_e32 v143, v109, v181
	v_fmac_f32_e32 v143, v110, v182
	v_fmac_f32_e32 v143, v111, v183
	ds_read_b128 v[168:171], v152 offset:3072
	ds_read_b128 v[172:175], v152 offset:11280
	ds_read_b128 v[176:179], v152 offset:19488
	ds_read_b128 v[180:183], v152 offset:27696
	s_waitcnt lgkmcnt(4)
	v_fmac_f32_e32 v144, v108, v148
	v_fmac_f32_e32 v144, v109, v149
	v_fmac_f32_e32 v144, v110, v150
	v_fmac_f32_e32 v144, v111, v151
	v_fmac_f32_e32 v145, v108, v186
	v_fmac_f32_e32 v145, v109, v187
	v_fmac_f32_e32 v145, v110, v188
	v_fmac_f32_e32 v145, v111, v189
	v_fmac_f32_e32 v146, v108, v194
	v_fmac_f32_e32 v146, v109, v195
	v_fmac_f32_e32 v146, v110, v196
	v_fmac_f32_e32 v146, v111, v197
	v_fmac_f32_e32 v147, v108, v198
	v_fmac_f32_e32 v147, v109, v199
	v_fmac_f32_e32 v147, v110, v200
	v_fmac_f32_e32 v147, v111, v201
	ds_read_b128 v[148:151], v152 offset:35904
	ds_read_b128 v[186:189], v152 offset:44112
	ds_read_b128 v[194:197], v152 offset:52320
	ds_read_b128 v[198:201], v152 offset:60528
	s_waitcnt lgkmcnt(4)
	v_fmac_f32_e32 v132, v112, v168
	v_fmac_f32_e32 v132, v113, v169
	v_fmac_f32_e32 v132, v114, v170
	v_fmac_f32_e32 v132, v115, v171
	v_fmac_f32_e32 v133, v112, v172
	v_fmac_f32_e32 v133, v113, v173
	v_fmac_f32_e32 v133, v114, v174
	v_fmac_f32_e32 v133, v115, v175
	v_fmac_f32_e32 v134, v112, v176
	v_fmac_f32_e32 v134, v113, v177
	v_fmac_f32_e32 v134, v114, v178
	v_fmac_f32_e32 v134, v115, v179
	v_fmac_f32_e32 v135, v112, v180
	v_fmac_f32_e32 v135, v113, v181
	v_fmac_f32_e32 v135, v114, v182
	v_fmac_f32_e32 v135, v115, v183
	ds_read_b128 v[168:171], v153 offset:3072
	ds_read_b128 v[172:175], v153 offset:11280
	ds_read_b128 v[176:179], v153 offset:19488
	ds_read_b128 v[180:183], v153 offset:27696
	s_waitcnt lgkmcnt(4)
	v_fmac_f32_e32 v136, v112, v148
	v_fmac_f32_e32 v136, v113, v149
	v_fmac_f32_e32 v136, v114, v150
	v_fmac_f32_e32 v136, v115, v151
	v_fmac_f32_e32 v137, v112, v186
	v_fmac_f32_e32 v137, v113, v187
	v_fmac_f32_e32 v137, v114, v188
	v_fmac_f32_e32 v137, v115, v189
	v_fmac_f32_e32 v138, v112, v194
	v_fmac_f32_e32 v138, v113, v195
	v_fmac_f32_e32 v138, v114, v196
	v_fmac_f32_e32 v138, v115, v197
	v_fmac_f32_e32 v139, v112, v198
	v_fmac_f32_e32 v139, v113, v199
	v_fmac_f32_e32 v139, v114, v200
	v_fmac_f32_e32 v139, v115, v201
	ds_read_b128 v[148:151], v153 offset:35904
	ds_read_b128 v[186:189], v153 offset:44112
	ds_read_b128 v[194:197], v153 offset:52320
	ds_read_b128 v[198:201], v153 offset:60528
	s_waitcnt lgkmcnt(4)
	v_fmac_f32_e32 v140, v112, v168
	v_fmac_f32_e32 v140, v113, v169
	v_fmac_f32_e32 v140, v114, v170
	v_fmac_f32_e32 v140, v115, v171
	v_fmac_f32_e32 v141, v112, v172
	v_fmac_f32_e32 v141, v113, v173
	v_fmac_f32_e32 v141, v114, v174
	v_fmac_f32_e32 v141, v115, v175
	v_fmac_f32_e32 v142, v112, v176
	v_fmac_f32_e32 v142, v113, v177
	v_fmac_f32_e32 v142, v114, v178
	v_fmac_f32_e32 v142, v115, v179
	v_fmac_f32_e32 v143, v112, v180
	v_fmac_f32_e32 v143, v113, v181
	v_fmac_f32_e32 v143, v114, v182
	v_fmac_f32_e32 v143, v115, v183
	ds_read_b128 v[168:171], v152 offset:4096
	ds_read_b128 v[172:175], v152 offset:12304
	ds_read_b128 v[176:179], v152 offset:20512
	ds_read_b128 v[180:183], v152 offset:28720
	s_waitcnt lgkmcnt(4)
	v_fmac_f32_e32 v144, v112, v148
	v_fmac_f32_e32 v144, v113, v149
	v_fmac_f32_e32 v144, v114, v150
	v_fmac_f32_e32 v144, v115, v151
	v_fmac_f32_e32 v145, v112, v186
	v_fmac_f32_e32 v145, v113, v187
	v_fmac_f32_e32 v145, v114, v188
	v_fmac_f32_e32 v145, v115, v189
	v_fmac_f32_e32 v146, v112, v194
	v_fmac_f32_e32 v146, v113, v195
	v_fmac_f32_e32 v146, v114, v196
	v_fmac_f32_e32 v146, v115, v197
	v_fmac_f32_e32 v147, v112, v198
	v_fmac_f32_e32 v147, v113, v199
	v_fmac_f32_e32 v147, v114, v200
	v_fmac_f32_e32 v147, v115, v201
	ds_read_b128 v[148:151], v152 offset:36928
	ds_read_b128 v[186:189], v152 offset:45136
	ds_read_b128 v[194:197], v152 offset:53344
	ds_read_b128 v[198:201], v152 offset:61552
	s_waitcnt lgkmcnt(4)
	v_fmac_f32_e32 v132, v116, v168
	v_fmac_f32_e32 v132, v117, v169
	v_fmac_f32_e32 v132, v118, v170
	v_fmac_f32_e32 v132, v119, v171
	v_fmac_f32_e32 v133, v116, v172
	v_fmac_f32_e32 v133, v117, v173
	v_fmac_f32_e32 v133, v118, v174
	v_fmac_f32_e32 v133, v119, v175
	v_fmac_f32_e32 v134, v116, v176
	v_fmac_f32_e32 v134, v117, v177
	v_fmac_f32_e32 v134, v118, v178
	v_fmac_f32_e32 v134, v119, v179
	v_fmac_f32_e32 v135, v116, v180
	v_fmac_f32_e32 v135, v117, v181
	v_fmac_f32_e32 v135, v118, v182
	v_fmac_f32_e32 v135, v119, v183
	ds_read_b128 v[168:171], v153 offset:4096
	ds_read_b128 v[172:175], v153 offset:12304
	ds_read_b128 v[176:179], v153 offset:20512
	ds_read_b128 v[180:183], v153 offset:28720
	s_waitcnt lgkmcnt(4)
	v_fmac_f32_e32 v136, v116, v148
	v_fmac_f32_e32 v136, v117, v149
	v_fmac_f32_e32 v136, v118, v150
	v_fmac_f32_e32 v136, v119, v151
	v_fmac_f32_e32 v137, v116, v186
	v_fmac_f32_e32 v137, v117, v187
	v_fmac_f32_e32 v137, v118, v188
	v_fmac_f32_e32 v137, v119, v189
	v_fmac_f32_e32 v138, v116, v194
	v_fmac_f32_e32 v138, v117, v195
	v_fmac_f32_e32 v138, v118, v196
	v_fmac_f32_e32 v138, v119, v197
	v_fmac_f32_e32 v139, v116, v198
	v_fmac_f32_e32 v139, v117, v199
	v_fmac_f32_e32 v139, v118, v200
	v_fmac_f32_e32 v139, v119, v201
	ds_read_b128 v[148:151], v153 offset:36928
	ds_read_b128 v[186:189], v153 offset:45136
	ds_read_b128 v[194:197], v153 offset:53344
	ds_read_b128 v[198:201], v153 offset:61552
	s_waitcnt lgkmcnt(4)
	v_fmac_f32_e32 v140, v116, v168
	v_fmac_f32_e32 v140, v117, v169
	v_fmac_f32_e32 v140, v118, v170
	v_fmac_f32_e32 v140, v119, v171
	v_fmac_f32_e32 v141, v116, v172
	v_fmac_f32_e32 v141, v117, v173
	v_fmac_f32_e32 v141, v118, v174
	v_fmac_f32_e32 v141, v119, v175
	v_fmac_f32_e32 v142, v116, v176
	v_fmac_f32_e32 v142, v117, v177
	v_fmac_f32_e32 v142, v118, v178
	v_fmac_f32_e32 v142, v119, v179
	v_fmac_f32_e32 v143, v116, v180
	v_fmac_f32_e32 v143, v117, v181
	v_fmac_f32_e32 v143, v118, v182
	v_fmac_f32_e32 v143, v119, v183
	ds_read_b128 v[168:171], v152 offset:5120
	ds_read_b128 v[172:175], v152 offset:13328
	ds_read_b128 v[176:179], v152 offset:21536
	ds_read_b128 v[180:183], v152 offset:29744
	s_waitcnt lgkmcnt(4)
	v_fmac_f32_e32 v144, v116, v148
	v_fmac_f32_e32 v144, v117, v149
	v_fmac_f32_e32 v144, v118, v150
	v_fmac_f32_e32 v144, v119, v151
	v_fmac_f32_e32 v145, v116, v186
	v_fmac_f32_e32 v145, v117, v187
	v_fmac_f32_e32 v145, v118, v188
	v_fmac_f32_e32 v145, v119, v189
	v_fmac_f32_e32 v146, v116, v194
	v_fmac_f32_e32 v146, v117, v195
	v_fmac_f32_e32 v146, v118, v196
	v_fmac_f32_e32 v146, v119, v197
	v_fmac_f32_e32 v147, v116, v198
	v_fmac_f32_e32 v147, v117, v199
	v_fmac_f32_e32 v147, v118, v200
	v_fmac_f32_e32 v147, v119, v201
	ds_read_b128 v[148:151], v152 offset:37952
	ds_read_b128 v[186:189], v152 offset:46160
	ds_read_b128 v[194:197], v152 offset:54368
	ds_read_b128 v[198:201], v152 offset:62576
	s_waitcnt lgkmcnt(4)
	v_fmac_f32_e32 v132, v120, v168
	v_fmac_f32_e32 v132, v121, v169
	v_fmac_f32_e32 v132, v122, v170
	v_fmac_f32_e32 v132, v123, v171
	v_fmac_f32_e32 v133, v120, v172
	v_fmac_f32_e32 v133, v121, v173
	v_fmac_f32_e32 v133, v122, v174
	v_fmac_f32_e32 v133, v123, v175
	v_fmac_f32_e32 v134, v120, v176
	v_fmac_f32_e32 v134, v121, v177
	v_fmac_f32_e32 v134, v122, v178
	v_fmac_f32_e32 v134, v123, v179
	v_fmac_f32_e32 v135, v120, v180
	v_fmac_f32_e32 v135, v121, v181
	v_fmac_f32_e32 v135, v122, v182
	v_fmac_f32_e32 v135, v123, v183
	ds_read_b128 v[168:171], v153 offset:5120
	ds_read_b128 v[172:175], v153 offset:13328
	ds_read_b128 v[176:179], v153 offset:21536
	ds_read_b128 v[180:183], v153 offset:29744
	s_waitcnt lgkmcnt(4)
	v_fmac_f32_e32 v136, v120, v148
	v_fmac_f32_e32 v136, v121, v149
	v_fmac_f32_e32 v136, v122, v150
	v_fmac_f32_e32 v136, v123, v151
	v_fmac_f32_e32 v137, v120, v186
	v_fmac_f32_e32 v137, v121, v187
	v_fmac_f32_e32 v137, v122, v188
	v_fmac_f32_e32 v137, v123, v189
	v_fmac_f32_e32 v138, v120, v194
	v_fmac_f32_e32 v138, v121, v195
	v_fmac_f32_e32 v138, v122, v196
	v_fmac_f32_e32 v138, v123, v197
	v_fmac_f32_e32 v139, v120, v198
	v_fmac_f32_e32 v139, v121, v199
	v_fmac_f32_e32 v139, v122, v200
	v_fmac_f32_e32 v139, v123, v201
	ds_read_b128 v[148:151], v153 offset:37952
	ds_read_b128 v[186:189], v153 offset:46160
	ds_read_b128 v[194:197], v153 offset:54368
	ds_read_b128 v[198:201], v153 offset:62576
	s_waitcnt lgkmcnt(4)
	v_fmac_f32_e32 v140, v120, v168
	v_fmac_f32_e32 v140, v121, v169
	v_fmac_f32_e32 v140, v122, v170
	v_fmac_f32_e32 v140, v123, v171
	v_fmac_f32_e32 v141, v120, v172
	v_fmac_f32_e32 v141, v121, v173
	v_fmac_f32_e32 v141, v122, v174
	v_fmac_f32_e32 v141, v123, v175
	v_fmac_f32_e32 v142, v120, v176
	v_fmac_f32_e32 v142, v121, v177
	v_fmac_f32_e32 v142, v122, v178
	v_fmac_f32_e32 v142, v123, v179
	v_fmac_f32_e32 v143, v120, v180
	v_fmac_f32_e32 v143, v121, v181
	v_fmac_f32_e32 v143, v122, v182
	v_fmac_f32_e32 v143, v123, v183
	ds_read_b128 v[168:171], v152 offset:6144
	ds_read_b128 v[172:175], v152 offset:14352
	ds_read_b128 v[176:179], v152 offset:22560
	ds_read_b128 v[180:183], v152 offset:30768
	s_waitcnt lgkmcnt(4)
	v_fmac_f32_e32 v144, v120, v148
	v_fmac_f32_e32 v144, v121, v149
	v_fmac_f32_e32 v144, v122, v150
	v_fmac_f32_e32 v144, v123, v151
	v_fmac_f32_e32 v145, v120, v186
	v_fmac_f32_e32 v145, v121, v187
	v_fmac_f32_e32 v145, v122, v188
	v_fmac_f32_e32 v145, v123, v189
	v_fmac_f32_e32 v146, v120, v194
	v_fmac_f32_e32 v146, v121, v195
	v_fmac_f32_e32 v146, v122, v196
	v_fmac_f32_e32 v146, v123, v197
	v_fmac_f32_e32 v147, v120, v198
	v_fmac_f32_e32 v147, v121, v199
	v_fmac_f32_e32 v147, v122, v200
	v_fmac_f32_e32 v147, v123, v201
	ds_read_b128 v[148:151], v152 offset:38976
	ds_read_b128 v[186:189], v152 offset:47184
	ds_read_b128 v[194:197], v152 offset:55392
	ds_read_b128 v[198:201], v152 offset:63600
	s_waitcnt lgkmcnt(4)
	v_fmac_f32_e32 v132, v124, v168
	v_fmac_f32_e32 v132, v125, v169
	v_fmac_f32_e32 v132, v126, v170
	v_fmac_f32_e32 v132, v127, v171
	v_fmac_f32_e32 v133, v124, v172
	v_fmac_f32_e32 v133, v125, v173
	v_fmac_f32_e32 v133, v126, v174
	v_fmac_f32_e32 v133, v127, v175
	v_fmac_f32_e32 v134, v124, v176
	v_fmac_f32_e32 v134, v125, v177
	v_fmac_f32_e32 v134, v126, v178
	v_fmac_f32_e32 v134, v127, v179
	v_fmac_f32_e32 v135, v124, v180
	v_fmac_f32_e32 v135, v125, v181
	v_fmac_f32_e32 v135, v126, v182
	v_fmac_f32_e32 v135, v127, v183
	ds_read_b128 v[168:171], v153 offset:6144
	ds_read_b128 v[172:175], v153 offset:14352
	ds_read_b128 v[176:179], v153 offset:22560
	ds_read_b128 v[180:183], v153 offset:30768
	s_waitcnt lgkmcnt(4)
	v_fmac_f32_e32 v136, v124, v148
	v_fmac_f32_e32 v136, v125, v149
	v_fmac_f32_e32 v136, v126, v150
	v_fmac_f32_e32 v136, v127, v151
	v_fmac_f32_e32 v137, v124, v186
	v_fmac_f32_e32 v137, v125, v187
	v_fmac_f32_e32 v137, v126, v188
	v_fmac_f32_e32 v137, v127, v189
	v_fmac_f32_e32 v138, v124, v194
	v_fmac_f32_e32 v138, v125, v195
	v_fmac_f32_e32 v138, v126, v196
	v_fmac_f32_e32 v138, v127, v197
	v_fmac_f32_e32 v139, v124, v198
	v_fmac_f32_e32 v139, v125, v199
	v_fmac_f32_e32 v139, v126, v200
	v_fmac_f32_e32 v139, v127, v201
	ds_read_b128 v[148:151], v153 offset:38976
	ds_read_b128 v[186:189], v153 offset:47184
	ds_read_b128 v[194:197], v153 offset:55392
	ds_read_b128 v[198:201], v153 offset:63600
	s_waitcnt lgkmcnt(4)
	v_fmac_f32_e32 v140, v124, v168
	v_fmac_f32_e32 v140, v125, v169
	v_fmac_f32_e32 v140, v126, v170
	v_fmac_f32_e32 v140, v127, v171
	v_fmac_f32_e32 v141, v124, v172
	v_fmac_f32_e32 v141, v125, v173
	v_fmac_f32_e32 v141, v126, v174
	v_fmac_f32_e32 v141, v127, v175
	v_fmac_f32_e32 v142, v124, v176
	v_fmac_f32_e32 v142, v125, v177
	v_fmac_f32_e32 v142, v126, v178
	v_fmac_f32_e32 v142, v127, v179
	v_fmac_f32_e32 v143, v124, v180
	v_fmac_f32_e32 v143, v125, v181
	v_fmac_f32_e32 v143, v126, v182
	v_fmac_f32_e32 v143, v127, v183
	ds_read_b128 v[168:171], v152 offset:7168
	ds_read_b128 v[172:175], v152 offset:15376
	ds_read_b128 v[176:179], v152 offset:23584
	ds_read_b128 v[180:183], v152 offset:31792
	s_waitcnt lgkmcnt(4)
	v_fmac_f32_e32 v144, v124, v148
	v_fmac_f32_e32 v144, v125, v149
	v_fmac_f32_e32 v144, v126, v150
	v_fmac_f32_e32 v144, v127, v151
	v_fmac_f32_e32 v145, v124, v186
	v_fmac_f32_e32 v145, v125, v187
	v_fmac_f32_e32 v145, v126, v188
	v_fmac_f32_e32 v145, v127, v189
	v_fmac_f32_e32 v146, v124, v194
	v_fmac_f32_e32 v146, v125, v195
	v_fmac_f32_e32 v146, v126, v196
	v_fmac_f32_e32 v146, v127, v197
	v_fmac_f32_e32 v147, v124, v198
	v_fmac_f32_e32 v147, v125, v199
	v_fmac_f32_e32 v147, v126, v200
	v_fmac_f32_e32 v147, v127, v201
	ds_read_b128 v[148:151], v152 offset:40000
	ds_read_b128 v[186:189], v152 offset:48208
	ds_read_b128 v[194:197], v152 offset:56416
	ds_read_b128 v[198:201], v152 offset:64624
	s_waitcnt lgkmcnt(4)
	v_fmac_f32_e32 v132, v128, v168
	v_fmac_f32_e32 v132, v129, v169
	v_fmac_f32_e32 v132, v130, v170
	v_fmac_f32_e32 v132, v131, v171
	v_fmac_f32_e32 v133, v128, v172
	v_fmac_f32_e32 v133, v129, v173
	v_fmac_f32_e32 v133, v130, v174
	v_fmac_f32_e32 v133, v131, v175
	v_fmac_f32_e32 v134, v128, v176
	v_fmac_f32_e32 v134, v129, v177
	v_fmac_f32_e32 v134, v130, v178
	v_fmac_f32_e32 v134, v131, v179
	v_fmac_f32_e32 v135, v128, v180
	v_fmac_f32_e32 v135, v129, v181
	v_fmac_f32_e32 v135, v130, v182
	v_fmac_f32_e32 v135, v131, v183
	ds_read_b128 v[168:171], v153 offset:7168
	ds_read_b128 v[172:175], v153 offset:15376
	ds_read_b128 v[176:179], v153 offset:23584
	ds_read_b128 v[180:183], v153 offset:31792
	s_waitcnt lgkmcnt(4)
	v_fmac_f32_e32 v136, v128, v148
	v_fmac_f32_e32 v136, v129, v149
	v_fmac_f32_e32 v136, v130, v150
	v_fmac_f32_e32 v136, v131, v151
	v_fmac_f32_e32 v137, v128, v186
	v_fmac_f32_e32 v137, v129, v187
	v_fmac_f32_e32 v137, v130, v188
	v_fmac_f32_e32 v137, v131, v189
	v_fmac_f32_e32 v138, v128, v194
	v_fmac_f32_e32 v138, v129, v195
	v_fmac_f32_e32 v138, v130, v196
	v_fmac_f32_e32 v138, v131, v197
	v_fmac_f32_e32 v139, v128, v198
	v_fmac_f32_e32 v139, v129, v199
	v_fmac_f32_e32 v139, v130, v200
	v_fmac_f32_e32 v139, v131, v201
	ds_read_b128 v[148:151], v153 offset:40000
	ds_read_b128 v[186:189], v153 offset:48208
	ds_read_b128 v[194:197], v153 offset:56416
	ds_read_b128 v[198:201], v153 offset:64624
	s_waitcnt lgkmcnt(4)
	v_fmac_f32_e32 v140, v128, v168
	v_fmac_f32_e32 v140, v129, v169
	v_fmac_f32_e32 v140, v130, v170
	v_fmac_f32_e32 v140, v131, v171
	v_fmac_f32_e32 v141, v128, v172
	v_fmac_f32_e32 v141, v129, v173
	v_fmac_f32_e32 v141, v130, v174
	v_fmac_f32_e32 v141, v131, v175
	v_fmac_f32_e32 v142, v128, v176
	v_fmac_f32_e32 v142, v129, v177
	v_fmac_f32_e32 v142, v130, v178
	v_fmac_f32_e32 v142, v131, v179
	v_fmac_f32_e32 v143, v128, v180
	v_fmac_f32_e32 v143, v129, v181
	v_fmac_f32_e32 v143, v130, v182
	v_fmac_f32_e32 v143, v131, v183
	s_waitcnt lgkmcnt(0)
	v_fmac_f32_e32 v144, v128, v148
	v_fmac_f32_e32 v144, v129, v149
	v_fmac_f32_e32 v144, v130, v150
	v_fmac_f32_e32 v144, v131, v151
	v_fmac_f32_e32 v145, v128, v186
	v_fmac_f32_e32 v145, v129, v187
	v_fmac_f32_e32 v145, v130, v188
	v_fmac_f32_e32 v145, v131, v189
	v_fmac_f32_e32 v146, v128, v194
	v_fmac_f32_e32 v146, v129, v195
	v_fmac_f32_e32 v146, v130, v196
	v_fmac_f32_e32 v146, v131, v197
	v_fmac_f32_e32 v147, v128, v198
	v_fmac_f32_e32 v147, v129, v199
	v_fmac_f32_e32 v147, v130, v200
	v_fmac_f32_e32 v147, v131, v201
	s_add_i32 s11, s10, 0x2000
	s_lshr_b32 s0, s11, 8
	s_mul_i32 s0, s0, 57
	s_lshr_b32 s0, s0, 9
	s_mul_i32 s1, s0, 0x900
	s_sub_i32 s43, s11, s1
	s_lshl_b32 s1, s11, 13
	s_add_u32 s12, s48, s1
	s_addc_u32 s13, s49, 0
	s_add_u32 s14, s12, 0x1000
	s_addc_u32 s15, s13, 0
	global_load_dwordx4 v[100:103], v1, s[12:13]
	global_load_dwordx4 v[104:107], v1, s[12:13] offset:1024
	global_load_dwordx4 v[108:111], v1, s[12:13] offset:2048
	global_load_dwordx4 v[112:115], v1, s[12:13] offset:3072
	global_load_dwordx4 v[116:119], v1, s[14:15]
	global_load_dwordx4 v[120:123], v1, s[14:15] offset:1024
	global_load_dwordx4 v[124:127], v1, s[14:15] offset:2048
	global_load_dwordx4 v[128:131], v1, s[14:15] offset:3072
	v_cndmask_b32_e64 v242, v133, v132, s[62:63]
	v_cndmask_b32_e64 v132, v132, v133, s[62:63]
	v_cndmask_b32_e64 v243, v135, v134, s[62:63]
	v_cndmask_b32_e64 v134, v134, v135, s[62:63]
	v_cndmask_b32_e64 v244, v137, v136, s[62:63]
	v_cndmask_b32_e64 v136, v136, v137, s[62:63]
	v_cndmask_b32_e64 v245, v139, v138, s[62:63]
	v_cndmask_b32_e64 v138, v138, v139, s[62:63]
	v_cndmask_b32_e64 v246, v141, v140, s[62:63]
	v_cndmask_b32_e64 v140, v140, v141, s[62:63]
	v_cndmask_b32_e64 v248, v143, v142, s[62:63]
	v_cndmask_b32_e64 v142, v142, v143, s[62:63]
	v_cndmask_b32_e64 v249, v145, v144, s[62:63]
	v_cndmask_b32_e64 v144, v144, v145, s[62:63]
	v_cndmask_b32_e64 v250, v147, v146, s[62:63]
	v_cndmask_b32_e64 v146, v146, v147, s[62:63]
	v_add_f32_dpp v132, v242, v132 quad_perm:[1,0,3,2] row_mask:0xf bank_mask:0xf
	v_add_f32_dpp v134, v243, v134 quad_perm:[1,0,3,2] row_mask:0xf bank_mask:0xf
	v_add_f32_dpp v136, v244, v136 quad_perm:[1,0,3,2] row_mask:0xf bank_mask:0xf
	v_add_f32_dpp v138, v245, v138 quad_perm:[1,0,3,2] row_mask:0xf bank_mask:0xf
	v_add_f32_dpp v140, v246, v140 quad_perm:[1,0,3,2] row_mask:0xf bank_mask:0xf
	v_add_f32_dpp v142, v248, v142 quad_perm:[1,0,3,2] row_mask:0xf bank_mask:0xf
	v_add_f32_dpp v144, v249, v144 quad_perm:[1,0,3,2] row_mask:0xf bank_mask:0xf
	v_add_f32_dpp v146, v250, v146 quad_perm:[1,0,3,2] row_mask:0xf bank_mask:0xf
	v_cndmask_b32_e64 v242, v134, v132, s[64:65]
	v_cndmask_b32_e64 v132, v132, v134, s[64:65]
	v_cndmask_b32_e64 v243, v138, v136, s[64:65]
	v_cndmask_b32_e64 v136, v136, v138, s[64:65]
	v_cndmask_b32_e64 v244, v142, v140, s[64:65]
	v_cndmask_b32_e64 v140, v140, v142, s[64:65]
	v_cndmask_b32_e64 v245, v146, v144, s[64:65]
	v_cndmask_b32_e64 v144, v144, v146, s[64:65]
	s_nop 0
	v_add_f32_dpp v132, v242, v132 quad_perm:[2,3,0,1] row_mask:0xf bank_mask:0xf
	v_add_f32_dpp v136, v243, v136 quad_perm:[2,3,0,1] row_mask:0xf bank_mask:0xf
	v_add_f32_dpp v140, v244, v140 quad_perm:[2,3,0,1] row_mask:0xf bank_mask:0xf
	v_add_f32_dpp v144, v245, v144 quad_perm:[2,3,0,1] row_mask:0xf bank_mask:0xf
	v_cndmask_b32_e64 v242, v136, v132, s[66:67]
	v_cndmask_b32_e64 v132, v132, v136, s[66:67]
	v_cndmask_b32_e64 v243, v144, v140, s[66:67]
	v_cndmask_b32_e64 v140, v140, v144, s[66:67]
	s_nop 1
	v_add_f32_dpp v246, v242, v132 row_shl:4 row_mask:0xf bank_mask:0x5
	v_add_f32_dpp v246, v242, v132 row_shr:4 row_mask:0xf bank_mask:0xa
	v_add_f32_dpp v248, v243, v140 row_shl:4 row_mask:0xf bank_mask:0x5
	v_add_f32_dpp v248, v243, v140 row_shr:4 row_mask:0xf bank_mask:0xa
	v_cndmask_b32_e64 v242, v248, v246, s[68:69]
	v_cndmask_b32_e64 v243, v246, v248, s[68:69]
	s_nop 1
	v_add_f32_dpp v191, v242, v243 row_ror:8 row_mask:0xf bank_mask:0xf
	s_nop 0
	ds_bpermute_b32 v193, v165, v191
	s_waitcnt lgkmcnt(0)
	v_add_f32_e32 v191, v191, v193
	ds_bpermute_b32 v193, v166, v191
	s_waitcnt lgkmcnt(0)
	v_add_f32_e32 v191, v191, v193
	v_mov_b32_e32 v193, v191
	s_nop 1
	v_max_f32_dpp v193, v193, v193 quad_perm:[1,0,3,2] row_mask:0xf bank_mask:0xf
	s_nop 1
	v_max_f32_dpp v193, v193, v193 quad_perm:[2,3,0,1] row_mask:0xf bank_mask:0xf
	s_nop 1
	v_max_f32_dpp v193, v193, v193 row_half_mirror row_mask:0xf bank_mask:0xf
	s_nop 1
	v_max_f32_dpp v193, v193, v193 row_mirror row_mask:0xf bank_mask:0xf
	v_sub_f32_e32 v191, v191, v193
	v_mul_f32_e32 v191, 0x3fb8aa3b, v191
	v_exp_f32_e32 v191, v191
	s_nop 0
	v_mov_b32_e32 v193, v191
	s_nop 1
	v_add_f32_dpp v193, v193, v193 quad_perm:[1,0,3,2] row_mask:0xf bank_mask:0xf
	s_nop 1
	v_add_f32_dpp v193, v193, v193 quad_perm:[2,3,0,1] row_mask:0xf bank_mask:0xf
	s_nop 1
	v_add_f32_dpp v193, v193, v193 row_half_mirror row_mask:0xf bank_mask:0xf
	s_nop 1
	v_add_f32_dpp v193, v193, v193 row_mirror row_mask:0xf bank_mask:0xf
	v_rcp_f32_e32 v193, v193
	s_nop 0
	v_mul_f32_e32 v191, v191, v193
	s_mov_b64 exec, 0xffff
	global_store_dword v164, v191, s[34:35]
	s_mov_b64 exec, -1
	s_waitcnt vmcnt(9)
	s_add_i32 s11, s10, 0x1800
	s_lshr_b32 s0, s11, 8
	s_mul_i32 s0, s0, 57
	s_lshr_b32 s0, s0, 9
	s_mul_i32 s1, s0, 0x900
	s_sub_i32 s43, s11, s1
	s_lshl_b32 s1, s11, 12
	s_add_u32 s16, s50, s1
	s_addc_u32 s17, s51, 0
	s_mul_i32 s1, s0, 0x24000
	s_lshl_b32 s2, s43, 2
	s_add_i32 s1, s1, s2
	s_add_u32 s34, s54, s1
	s_addc_u32 s35, s55, 0
	v_mul_f32_e32 v184, v204, v204
	v_fmac_f32_e32 v184, v205, v205
	v_fmac_f32_e32 v184, v206, v206
	v_fmac_f32_e32 v184, v207, v207
	v_fmac_f32_e32 v184, v208, v208
	v_fmac_f32_e32 v184, v209, v209
	v_fmac_f32_e32 v184, v210, v210
	v_fmac_f32_e32 v184, v211, v211
	v_fmac_f32_e32 v184, v212, v212
	v_fmac_f32_e32 v184, v213, v213
	v_fmac_f32_e32 v184, v214, v214
	v_fmac_f32_e32 v184, v215, v215
	v_fmac_f32_e32 v184, v216, v216
	v_fmac_f32_e32 v184, v217, v217
	v_fmac_f32_e32 v184, v218, v218
	v_fmac_f32_e32 v184, v219, v219
	v_fmac_f32_e32 v184, v226, v226
	v_fmac_f32_e32 v184, v227, v227
	v_fmac_f32_e32 v184, v228, v228
	v_fmac_f32_e32 v184, v229, v229
	v_fmac_f32_e32 v184, v230, v230
	v_fmac_f32_e32 v184, v231, v231
	v_fmac_f32_e32 v184, v232, v232
	v_fmac_f32_e32 v184, v233, v233
	v_fmac_f32_e32 v184, v234, v234
	v_fmac_f32_e32 v184, v235, v235
	v_fmac_f32_e32 v184, v236, v236
	v_fmac_f32_e32 v184, v237, v237
	v_fmac_f32_e32 v184, v238, v238
	v_fmac_f32_e32 v184, v239, v239
	v_fmac_f32_e32 v184, v240, v240
	v_fmac_f32_e32 v184, v241, v241
	ds_read_b128 v[168:171], v152 offset:0
	ds_read_b128 v[172:175], v152 offset:8208
	ds_read_b128 v[176:179], v152 offset:16416
	ds_read_b128 v[180:183], v152 offset:24624
	s_nop 0
	v_add_f32_dpp v184, v184, v184 quad_perm:[1,0,3,2] row_mask:0xf bank_mask:0xf
	s_nop 1
	v_add_f32_dpp v184, v184, v184 quad_perm:[2,3,0,1] row_mask:0xf bank_mask:0xf
	s_nop 1
	v_add_f32_dpp v184, v184, v184 row_half_mirror row_mask:0xf bank_mask:0xf
	s_nop 1
	v_add_f32_dpp v184, v184, v184 row_mirror row_mask:0xf bank_mask:0xf
	s_nop 1
	v_readlane_b32 s0, v184, 0
	v_readlane_b32 s1, v184, 16
	v_readlane_b32 s2, v184, 32
	v_readlane_b32 s3, v184, 48
	v_fma_f32 v4, v4, v36, v4
	v_fma_f32 v5, v5, v37, v5
	v_fma_f32 v6, v6, v38, v6
	v_fma_f32 v7, v7, v39, v7
	v_fma_f32 v8, v8, v40, v8
	v_fma_f32 v9, v9, v41, v9
	v_fma_f32 v10, v10, v42, v10
	v_fma_f32 v11, v11, v43, v11
	v_fma_f32 v12, v12, v44, v12
	v_fma_f32 v13, v13, v45, v13
	v_fma_f32 v14, v14, v46, v14
	v_fma_f32 v15, v15, v47, v15
	v_fma_f32 v16, v16, v48, v16
	v_fma_f32 v17, v17, v49, v17
	v_fma_f32 v18, v18, v50, v18
	v_fma_f32 v19, v19, v51, v19
	v_fma_f32 v20, v20, v52, v20
	v_fma_f32 v21, v21, v53, v21
	v_fma_f32 v22, v22, v54, v22
	v_fma_f32 v23, v23, v55, v23
	v_fma_f32 v24, v24, v56, v24
	v_fma_f32 v25, v25, v57, v25
	v_fma_f32 v26, v26, v58, v26
	v_fma_f32 v27, v27, v59, v27
	v_fma_f32 v28, v28, v60, v28
	v_fma_f32 v29, v29, v61, v29
	v_fma_f32 v30, v30, v62, v30
	v_fma_f32 v31, v31, v63, v31
	v_fma_f32 v32, v32, v64, v32
	v_fma_f32 v33, v33, v65, v33
	v_fma_f32 v34, v34, v66, v34
	v_fma_f32 v35, v35, v67, v35
	v_mov_b32_e32 v190, s0
	v_add_f32_e32 v190, s1, v190
	v_add_f32_e32 v190, s2, v190
	v_add_f32_e32 v190, s3, v190
	v_mul_f32_e32 v190, 0x3a000000, v190
	v_add_f32_e32 v190, 0x358637bd, v190
	v_rsq_f32_e32 v190, v190
	s_nop 0
	v_mul_f32_e32 v4, v4, v190
	v_mul_f32_e32 v5, v5, v190
	v_mul_f32_e32 v6, v6, v190
	v_mul_f32_e32 v7, v7, v190
	v_mul_f32_e32 v8, v8, v190
	v_mul_f32_e32 v9, v9, v190
	v_mul_f32_e32 v10, v10, v190
	v_mul_f32_e32 v11, v11, v190
	v_mul_f32_e32 v12, v12, v190
	v_mul_f32_e32 v13, v13, v190
	v_mul_f32_e32 v14, v14, v190
	v_mul_f32_e32 v15, v15, v190
	v_mul_f32_e32 v16, v16, v190
	v_mul_f32_e32 v17, v17, v190
	v_mul_f32_e32 v18, v18, v190
	v_mul_f32_e32 v19, v19, v190
	v_mul_f32_e32 v20, v20, v190
	v_mul_f32_e32 v21, v21, v190
	v_mul_f32_e32 v22, v22, v190
	v_mul_f32_e32 v23, v23, v190
	v_mul_f32_e32 v24, v24, v190
	v_mul_f32_e32 v25, v25, v190
	v_mul_f32_e32 v26, v26, v190
	v_mul_f32_e32 v27, v27, v190
	v_mul_f32_e32 v28, v28, v190
	v_mul_f32_e32 v29, v29, v190
	v_mul_f32_e32 v30, v30, v190
	v_mul_f32_e32 v31, v31, v190
	v_mul_f32_e32 v32, v32, v190
	v_mul_f32_e32 v33, v33, v190
	v_mul_f32_e32 v34, v34, v190
	v_mul_f32_e32 v35, v35, v190
	v_fma_f32 v204, v204, v4, v68
	v_fma_f32 v205, v205, v5, v69
	v_fma_f32 v206, v206, v6, v70
	v_fma_f32 v207, v207, v7, v71
	v_fma_f32 v208, v208, v8, v72
	v_fma_f32 v209, v209, v9, v73
	v_fma_f32 v210, v210, v10, v74
	v_fma_f32 v211, v211, v11, v75
	v_fma_f32 v212, v212, v12, v76
	v_fma_f32 v213, v213, v13, v77
	v_fma_f32 v214, v214, v14, v78
	v_fma_f32 v215, v215, v15, v79
	v_fma_f32 v216, v216, v16, v80
	v_fma_f32 v217, v217, v17, v81
	v_fma_f32 v218, v218, v18, v82
	v_fma_f32 v219, v219, v19, v83
	v_fma_f32 v226, v226, v20, v84
	v_fma_f32 v227, v227, v21, v85
	v_fma_f32 v228, v228, v22, v86
	v_fma_f32 v229, v229, v23, v87
	v_fma_f32 v230, v230, v24, v88
	v_fma_f32 v231, v231, v25, v89
	v_fma_f32 v232, v232, v26, v90
	v_fma_f32 v233, v233, v27, v91
	v_fma_f32 v234, v234, v28, v92
	v_fma_f32 v235, v235, v29, v93
	v_fma_f32 v236, v236, v30, v94
	v_fma_f32 v237, v237, v31, v95
	v_fma_f32 v238, v238, v32, v96
	v_fma_f32 v239, v239, v33, v97
	v_fma_f32 v240, v240, v34, v98
	v_fma_f32 v241, v241, v35, v99
	v_cvt_pk_bf16_f32 v242, v204, v205
	v_cvt_pk_bf16_f32 v243, v206, v207
	global_store_dwordx2 v2, v[242:243], s[16:17]
	v_cvt_pk_bf16_f32 v244, v208, v209
	v_cvt_pk_bf16_f32 v245, v210, v211
	global_store_dwordx2 v2, v[244:245], s[16:17] offset:512
	v_cvt_pk_bf16_f32 v242, v212, v213
	v_cvt_pk_bf16_f32 v243, v214, v215
	global_store_dwordx2 v2, v[242:243], s[16:17] offset:1024
	v_cvt_pk_bf16_f32 v244, v216, v217
	v_cvt_pk_bf16_f32 v245, v218, v219
	global_store_dwordx2 v2, v[244:245], s[16:17] offset:1536
	v_cvt_pk_bf16_f32 v242, v226, v227
	v_cvt_pk_bf16_f32 v243, v228, v229
	global_store_dwordx2 v2, v[242:243], s[16:17] offset:2048
	v_cvt_pk_bf16_f32 v244, v230, v231
	v_cvt_pk_bf16_f32 v245, v232, v233
	global_store_dwordx2 v2, v[244:245], s[16:17] offset:2560
	v_cvt_pk_bf16_f32 v242, v234, v235
	v_cvt_pk_bf16_f32 v243, v236, v237
	global_store_dwordx2 v2, v[242:243], s[16:17] offset:3072
	v_cvt_pk_bf16_f32 v244, v238, v239
	v_cvt_pk_bf16_f32 v245, v240, v241
	global_store_dwordx2 v2, v[244:245], s[16:17] offset:3584
	s_add_i32 s11, s10, 0x2000
	s_lshr_b32 s0, s11, 8
	s_mul_i32 s0, s0, 57
	s_lshr_b32 s0, s0, 9
	s_mul_i32 s1, s0, 0x900
	s_sub_i32 s43, s11, s1
	s_cmpk_lt_u32 s43, 0x100
	s_cselect_b32 s0, 8, s0
	s_mul_i32 s1, s0, 0xc000
	s_add_u32 s18, s52, s1
	s_addc_u32 s19, s53, 0
	s_add_u32 s18, s18, 0x6000
	s_addc_u32 s19, s19, 0
	s_add_u32 s22, s18, 0x1000
	s_addc_u32 s23, s19, 0
	s_add_u32 s28, s18, 0x2000
	s_addc_u32 s29, s19, 0
	s_add_u32 s30, s18, 0x3000
	s_addc_u32 s31, s19, 0
	global_load_dwordx4 v[4:7], v1, s[56:57]
	global_load_dwordx4 v[36:39], v1, s[28:29]
	global_load_dwordx4 v[68:71], v1, s[18:19]
	global_load_dwordx4 v[8:11], v1, s[56:57] offset:1024
	global_load_dwordx4 v[40:43], v1, s[28:29] offset:1024
	global_load_dwordx4 v[72:75], v1, s[18:19] offset:1024
	global_load_dwordx4 v[12:15], v1, s[56:57] offset:2048
	global_load_dwordx4 v[44:47], v1, s[28:29] offset:2048
	global_load_dwordx4 v[76:79], v1, s[18:19] offset:2048
	global_load_dwordx4 v[16:19], v1, s[56:57] offset:3072
	global_load_dwordx4 v[48:51], v1, s[28:29] offset:3072
	global_load_dwordx4 v[80:83], v1, s[18:19] offset:3072
	global_load_dwordx4 v[20:23], v1, s[58:59]
	global_load_dwordx4 v[52:55], v1, s[30:31]
	global_load_dwordx4 v[84:87], v1, s[22:23]
	global_load_dwordx4 v[24:27], v1, s[58:59] offset:1024
	global_load_dwordx4 v[56:59], v1, s[30:31] offset:1024
	global_load_dwordx4 v[88:91], v1, s[22:23] offset:1024
	global_load_dwordx4 v[28:31], v1, s[58:59] offset:2048
	global_load_dwordx4 v[60:63], v1, s[30:31] offset:2048
	global_load_dwordx4 v[92:95], v1, s[22:23] offset:2048
	global_load_dwordx4 v[32:35], v1, s[58:59] offset:3072
	global_load_dwordx4 v[64:67], v1, s[30:31] offset:3072
	global_load_dwordx4 v[96:99], v1, s[22:23] offset:3072
	v_mov_b32_e32 v132, 0
	v_mov_b32_e32 v133, 0
	v_mov_b32_e32 v134, 0
	v_mov_b32_e32 v135, 0
	v_mov_b32_e32 v136, 0
	v_mov_b32_e32 v137, 0
	v_mov_b32_e32 v138, 0
	v_mov_b32_e32 v139, 0
	v_mov_b32_e32 v140, 0
	v_mov_b32_e32 v141, 0
	v_mov_b32_e32 v142, 0
	v_mov_b32_e32 v143, 0
	v_mov_b32_e32 v144, 0
	v_mov_b32_e32 v145, 0
	v_mov_b32_e32 v146, 0
	v_mov_b32_e32 v147, 0
	ds_read_b128 v[148:151], v152 offset:32832
	ds_read_b128 v[186:189], v152 offset:41040
	ds_read_b128 v[194:197], v152 offset:49248
	ds_read_b128 v[198:201], v152 offset:57456
	s_waitcnt lgkmcnt(4)
	v_fmac_f32_e32 v132, v204, v168
	v_fmac_f32_e32 v132, v205, v169
	v_fmac_f32_e32 v132, v206, v170
	v_fmac_f32_e32 v132, v207, v171
	v_fmac_f32_e32 v133, v204, v172
	v_fmac_f32_e32 v133, v205, v173
	v_fmac_f32_e32 v133, v206, v174
	v_fmac_f32_e32 v133, v207, v175
	v_fmac_f32_e32 v134, v204, v176
	v_fmac_f32_e32 v134, v205, v177
	v_fmac_f32_e32 v134, v206, v178
	v_fmac_f32_e32 v134, v207, v179
	v_fmac_f32_e32 v135, v204, v180
	v_fmac_f32_e32 v135, v205, v181
	v_fmac_f32_e32 v135, v206, v182
	v_fmac_f32_e32 v135, v207, v183
	ds_read_b128 v[168:171], v153 offset:0
	ds_read_b128 v[172:175], v153 offset:8208
	ds_read_b128 v[176:179], v153 offset:16416
	ds_read_b128 v[180:183], v153 offset:24624
	s_waitcnt lgkmcnt(4)
	v_fmac_f32_e32 v136, v204, v148
	v_fmac_f32_e32 v136, v205, v149
	v_fmac_f32_e32 v136, v206, v150
	v_fmac_f32_e32 v136, v207, v151
	v_fmac_f32_e32 v137, v204, v186
	v_fmac_f32_e32 v137, v205, v187
	v_fmac_f32_e32 v137, v206, v188
	v_fmac_f32_e32 v137, v207, v189
	v_fmac_f32_e32 v138, v204, v194
	v_fmac_f32_e32 v138, v205, v195
	v_fmac_f32_e32 v138, v206, v196
	v_fmac_f32_e32 v138, v207, v197
	v_fmac_f32_e32 v139, v204, v198
	v_fmac_f32_e32 v139, v205, v199
	v_fmac_f32_e32 v139, v206, v200
	v_fmac_f32_e32 v139, v207, v201
	ds_read_b128 v[148:151], v153 offset:32832
	ds_read_b128 v[186:189], v153 offset:41040
	ds_read_b128 v[194:197], v153 offset:49248
	ds_read_b128 v[198:201], v153 offset:57456
	s_waitcnt lgkmcnt(4)
	v_fmac_f32_e32 v140, v204, v168
	v_fmac_f32_e32 v140, v205, v169
	v_fmac_f32_e32 v140, v206, v170
	v_fmac_f32_e32 v140, v207, v171
	v_fmac_f32_e32 v141, v204, v172
	v_fmac_f32_e32 v141, v205, v173
	v_fmac_f32_e32 v141, v206, v174
	v_fmac_f32_e32 v141, v207, v175
	v_fmac_f32_e32 v142, v204, v176
	v_fmac_f32_e32 v142, v205, v177
	v_fmac_f32_e32 v142, v206, v178
	v_fmac_f32_e32 v142, v207, v179
	v_fmac_f32_e32 v143, v204, v180
	v_fmac_f32_e32 v143, v205, v181
	v_fmac_f32_e32 v143, v206, v182
	v_fmac_f32_e32 v143, v207, v183
	ds_read_b128 v[168:171], v152 offset:1024
	ds_read_b128 v[172:175], v152 offset:9232
	ds_read_b128 v[176:179], v152 offset:17440
	ds_read_b128 v[180:183], v152 offset:25648
	s_waitcnt lgkmcnt(4)
	v_fmac_f32_e32 v144, v204, v148
	v_fmac_f32_e32 v144, v205, v149
	v_fmac_f32_e32 v144, v206, v150
	v_fmac_f32_e32 v144, v207, v151
	v_fmac_f32_e32 v145, v204, v186
	v_fmac_f32_e32 v145, v205, v187
	v_fmac_f32_e32 v145, v206, v188
	v_fmac_f32_e32 v145, v207, v189
	v_fmac_f32_e32 v146, v204, v194
	v_fmac_f32_e32 v146, v205, v195
	v_fmac_f32_e32 v146, v206, v196
	v_fmac_f32_e32 v146, v207, v197
	v_fmac_f32_e32 v147, v204, v198
	v_fmac_f32_e32 v147, v205, v199
	v_fmac_f32_e32 v147, v206, v200
	v_fmac_f32_e32 v147, v207, v201
	ds_read_b128 v[148:151], v152 offset:33856
	ds_read_b128 v[186:189], v152 offset:42064
	ds_read_b128 v[194:197], v152 offset:50272
	ds_read_b128 v[198:201], v152 offset:58480
	s_waitcnt lgkmcnt(4)
	v_fmac_f32_e32 v132, v208, v168
	v_fmac_f32_e32 v132, v209, v169
	v_fmac_f32_e32 v132, v210, v170
	v_fmac_f32_e32 v132, v211, v171
	v_fmac_f32_e32 v133, v208, v172
	v_fmac_f32_e32 v133, v209, v173
	v_fmac_f32_e32 v133, v210, v174
	v_fmac_f32_e32 v133, v211, v175
	v_fmac_f32_e32 v134, v208, v176
	v_fmac_f32_e32 v134, v209, v177
	v_fmac_f32_e32 v134, v210, v178
	v_fmac_f32_e32 v134, v211, v179
	v_fmac_f32_e32 v135, v208, v180
	v_fmac_f32_e32 v135, v209, v181
	v_fmac_f32_e32 v135, v210, v182
	v_fmac_f32_e32 v135, v211, v183
	ds_read_b128 v[168:171], v153 offset:1024
	ds_read_b128 v[172:175], v153 offset:9232
	ds_read_b128 v[176:179], v153 offset:17440
	ds_read_b128 v[180:183], v153 offset:25648
	s_waitcnt lgkmcnt(4)
	v_fmac_f32_e32 v136, v208, v148
	v_fmac_f32_e32 v136, v209, v149
	v_fmac_f32_e32 v136, v210, v150
	v_fmac_f32_e32 v136, v211, v151
	v_fmac_f32_e32 v137, v208, v186
	v_fmac_f32_e32 v137, v209, v187
	v_fmac_f32_e32 v137, v210, v188
	v_fmac_f32_e32 v137, v211, v189
	v_fmac_f32_e32 v138, v208, v194
	v_fmac_f32_e32 v138, v209, v195
	v_fmac_f32_e32 v138, v210, v196
	v_fmac_f32_e32 v138, v211, v197
	v_fmac_f32_e32 v139, v208, v198
	v_fmac_f32_e32 v139, v209, v199
	v_fmac_f32_e32 v139, v210, v200
	v_fmac_f32_e32 v139, v211, v201
	ds_read_b128 v[148:151], v153 offset:33856
	ds_read_b128 v[186:189], v153 offset:42064
	ds_read_b128 v[194:197], v153 offset:50272
	ds_read_b128 v[198:201], v153 offset:58480
	s_waitcnt lgkmcnt(4)
	v_fmac_f32_e32 v140, v208, v168
	v_fmac_f32_e32 v140, v209, v169
	v_fmac_f32_e32 v140, v210, v170
	v_fmac_f32_e32 v140, v211, v171
	v_fmac_f32_e32 v141, v208, v172
	v_fmac_f32_e32 v141, v209, v173
	v_fmac_f32_e32 v141, v210, v174
	v_fmac_f32_e32 v141, v211, v175
	v_fmac_f32_e32 v142, v208, v176
	v_fmac_f32_e32 v142, v209, v177
	v_fmac_f32_e32 v142, v210, v178
	v_fmac_f32_e32 v142, v211, v179
	v_fmac_f32_e32 v143, v208, v180
	v_fmac_f32_e32 v143, v209, v181
	v_fmac_f32_e32 v143, v210, v182
	v_fmac_f32_e32 v143, v211, v183
	ds_read_b128 v[168:171], v152 offset:2048
	ds_read_b128 v[172:175], v152 offset:10256
	ds_read_b128 v[176:179], v152 offset:18464
	ds_read_b128 v[180:183], v152 offset:26672
	s_waitcnt lgkmcnt(4)
	v_fmac_f32_e32 v144, v208, v148
	v_fmac_f32_e32 v144, v209, v149
	v_fmac_f32_e32 v144, v210, v150
	v_fmac_f32_e32 v144, v211, v151
	v_fmac_f32_e32 v145, v208, v186
	v_fmac_f32_e32 v145, v209, v187
	v_fmac_f32_e32 v145, v210, v188
	v_fmac_f32_e32 v145, v211, v189
	v_fmac_f32_e32 v146, v208, v194
	v_fmac_f32_e32 v146, v209, v195
	v_fmac_f32_e32 v146, v210, v196
	v_fmac_f32_e32 v146, v211, v197
	v_fmac_f32_e32 v147, v208, v198
	v_fmac_f32_e32 v147, v209, v199
	v_fmac_f32_e32 v147, v210, v200
	v_fmac_f32_e32 v147, v211, v201
	ds_read_b128 v[148:151], v152 offset:34880
	ds_read_b128 v[186:189], v152 offset:43088
	ds_read_b128 v[194:197], v152 offset:51296
	ds_read_b128 v[198:201], v152 offset:59504
	s_waitcnt lgkmcnt(4)
	v_fmac_f32_e32 v132, v212, v168
	v_fmac_f32_e32 v132, v213, v169
	v_fmac_f32_e32 v132, v214, v170
	v_fmac_f32_e32 v132, v215, v171
	v_fmac_f32_e32 v133, v212, v172
	v_fmac_f32_e32 v133, v213, v173
	v_fmac_f32_e32 v133, v214, v174
	v_fmac_f32_e32 v133, v215, v175
	v_fmac_f32_e32 v134, v212, v176
	v_fmac_f32_e32 v134, v213, v177
	v_fmac_f32_e32 v134, v214, v178
	v_fmac_f32_e32 v134, v215, v179
	v_fmac_f32_e32 v135, v212, v180
	v_fmac_f32_e32 v135, v213, v181
	v_fmac_f32_e32 v135, v214, v182
	v_fmac_f32_e32 v135, v215, v183
	ds_read_b128 v[168:171], v153 offset:2048
	ds_read_b128 v[172:175], v153 offset:10256
	ds_read_b128 v[176:179], v153 offset:18464
	ds_read_b128 v[180:183], v153 offset:26672
	s_waitcnt lgkmcnt(4)
	v_fmac_f32_e32 v136, v212, v148
	v_fmac_f32_e32 v136, v213, v149
	v_fmac_f32_e32 v136, v214, v150
	v_fmac_f32_e32 v136, v215, v151
	v_fmac_f32_e32 v137, v212, v186
	v_fmac_f32_e32 v137, v213, v187
	v_fmac_f32_e32 v137, v214, v188
	v_fmac_f32_e32 v137, v215, v189
	v_fmac_f32_e32 v138, v212, v194
	v_fmac_f32_e32 v138, v213, v195
	v_fmac_f32_e32 v138, v214, v196
	v_fmac_f32_e32 v138, v215, v197
	v_fmac_f32_e32 v139, v212, v198
	v_fmac_f32_e32 v139, v213, v199
	v_fmac_f32_e32 v139, v214, v200
	v_fmac_f32_e32 v139, v215, v201
	ds_read_b128 v[148:151], v153 offset:34880
	ds_read_b128 v[186:189], v153 offset:43088
	ds_read_b128 v[194:197], v153 offset:51296
	ds_read_b128 v[198:201], v153 offset:59504
	s_waitcnt lgkmcnt(4)
	v_fmac_f32_e32 v140, v212, v168
	v_fmac_f32_e32 v140, v213, v169
	v_fmac_f32_e32 v140, v214, v170
	v_fmac_f32_e32 v140, v215, v171
	v_fmac_f32_e32 v141, v212, v172
	v_fmac_f32_e32 v141, v213, v173
	v_fmac_f32_e32 v141, v214, v174
	v_fmac_f32_e32 v141, v215, v175
	v_fmac_f32_e32 v142, v212, v176
	v_fmac_f32_e32 v142, v213, v177
	v_fmac_f32_e32 v142, v214, v178
	v_fmac_f32_e32 v142, v215, v179
	v_fmac_f32_e32 v143, v212, v180
	v_fmac_f32_e32 v143, v213, v181
	v_fmac_f32_e32 v143, v214, v182
	v_fmac_f32_e32 v143, v215, v183
	ds_read_b128 v[168:171], v152 offset:3072
	ds_read_b128 v[172:175], v152 offset:11280
	ds_read_b128 v[176:179], v152 offset:19488
	ds_read_b128 v[180:183], v152 offset:27696
	s_waitcnt lgkmcnt(4)
	v_fmac_f32_e32 v144, v212, v148
	v_fmac_f32_e32 v144, v213, v149
	v_fmac_f32_e32 v144, v214, v150
	v_fmac_f32_e32 v144, v215, v151
	v_fmac_f32_e32 v145, v212, v186
	v_fmac_f32_e32 v145, v213, v187
	v_fmac_f32_e32 v145, v214, v188
	v_fmac_f32_e32 v145, v215, v189
	v_fmac_f32_e32 v146, v212, v194
	v_fmac_f32_e32 v146, v213, v195
	v_fmac_f32_e32 v146, v214, v196
	v_fmac_f32_e32 v146, v215, v197
	v_fmac_f32_e32 v147, v212, v198
	v_fmac_f32_e32 v147, v213, v199
	v_fmac_f32_e32 v147, v214, v200
	v_fmac_f32_e32 v147, v215, v201
	ds_read_b128 v[148:151], v152 offset:35904
	ds_read_b128 v[186:189], v152 offset:44112
	ds_read_b128 v[194:197], v152 offset:52320
	ds_read_b128 v[198:201], v152 offset:60528
	s_waitcnt lgkmcnt(4)
	v_fmac_f32_e32 v132, v216, v168
	v_fmac_f32_e32 v132, v217, v169
	v_fmac_f32_e32 v132, v218, v170
	v_fmac_f32_e32 v132, v219, v171
	v_fmac_f32_e32 v133, v216, v172
	v_fmac_f32_e32 v133, v217, v173
	v_fmac_f32_e32 v133, v218, v174
	v_fmac_f32_e32 v133, v219, v175
	v_fmac_f32_e32 v134, v216, v176
	v_fmac_f32_e32 v134, v217, v177
	v_fmac_f32_e32 v134, v218, v178
	v_fmac_f32_e32 v134, v219, v179
	v_fmac_f32_e32 v135, v216, v180
	v_fmac_f32_e32 v135, v217, v181
	v_fmac_f32_e32 v135, v218, v182
	v_fmac_f32_e32 v135, v219, v183
	ds_read_b128 v[168:171], v153 offset:3072
	ds_read_b128 v[172:175], v153 offset:11280
	ds_read_b128 v[176:179], v153 offset:19488
	ds_read_b128 v[180:183], v153 offset:27696
	s_waitcnt lgkmcnt(4)
	v_fmac_f32_e32 v136, v216, v148
	v_fmac_f32_e32 v136, v217, v149
	v_fmac_f32_e32 v136, v218, v150
	v_fmac_f32_e32 v136, v219, v151
	v_fmac_f32_e32 v137, v216, v186
	v_fmac_f32_e32 v137, v217, v187
	v_fmac_f32_e32 v137, v218, v188
	v_fmac_f32_e32 v137, v219, v189
	v_fmac_f32_e32 v138, v216, v194
	v_fmac_f32_e32 v138, v217, v195
	v_fmac_f32_e32 v138, v218, v196
	v_fmac_f32_e32 v138, v219, v197
	v_fmac_f32_e32 v139, v216, v198
	v_fmac_f32_e32 v139, v217, v199
	v_fmac_f32_e32 v139, v218, v200
	v_fmac_f32_e32 v139, v219, v201
	ds_read_b128 v[148:151], v153 offset:35904
	ds_read_b128 v[186:189], v153 offset:44112
	ds_read_b128 v[194:197], v153 offset:52320
	ds_read_b128 v[198:201], v153 offset:60528
	s_waitcnt lgkmcnt(4)
	v_fmac_f32_e32 v140, v216, v168
	v_fmac_f32_e32 v140, v217, v169
	v_fmac_f32_e32 v140, v218, v170
	v_fmac_f32_e32 v140, v219, v171
	v_fmac_f32_e32 v141, v216, v172
	v_fmac_f32_e32 v141, v217, v173
	v_fmac_f32_e32 v141, v218, v174
	v_fmac_f32_e32 v141, v219, v175
	v_fmac_f32_e32 v142, v216, v176
	v_fmac_f32_e32 v142, v217, v177
	v_fmac_f32_e32 v142, v218, v178
	v_fmac_f32_e32 v142, v219, v179
	v_fmac_f32_e32 v143, v216, v180
	v_fmac_f32_e32 v143, v217, v181
	v_fmac_f32_e32 v143, v218, v182
	v_fmac_f32_e32 v143, v219, v183
	ds_read_b128 v[168:171], v152 offset:4096
	ds_read_b128 v[172:175], v152 offset:12304
	ds_read_b128 v[176:179], v152 offset:20512
	ds_read_b128 v[180:183], v152 offset:28720
	s_waitcnt lgkmcnt(4)
	v_fmac_f32_e32 v144, v216, v148
	v_fmac_f32_e32 v144, v217, v149
	v_fmac_f32_e32 v144, v218, v150
	v_fmac_f32_e32 v144, v219, v151
	v_fmac_f32_e32 v145, v216, v186
	v_fmac_f32_e32 v145, v217, v187
	v_fmac_f32_e32 v145, v218, v188
	v_fmac_f32_e32 v145, v219, v189
	v_fmac_f32_e32 v146, v216, v194
	v_fmac_f32_e32 v146, v217, v195
	v_fmac_f32_e32 v146, v218, v196
	v_fmac_f32_e32 v146, v219, v197
	v_fmac_f32_e32 v147, v216, v198
	v_fmac_f32_e32 v147, v217, v199
	v_fmac_f32_e32 v147, v218, v200
	v_fmac_f32_e32 v147, v219, v201
	ds_read_b128 v[148:151], v152 offset:36928
	ds_read_b128 v[186:189], v152 offset:45136
	ds_read_b128 v[194:197], v152 offset:53344
	ds_read_b128 v[198:201], v152 offset:61552
	s_waitcnt lgkmcnt(4)
	v_fmac_f32_e32 v132, v226, v168
	v_fmac_f32_e32 v132, v227, v169
	v_fmac_f32_e32 v132, v228, v170
	v_fmac_f32_e32 v132, v229, v171
	v_fmac_f32_e32 v133, v226, v172
	v_fmac_f32_e32 v133, v227, v173
	v_fmac_f32_e32 v133, v228, v174
	v_fmac_f32_e32 v133, v229, v175
	v_fmac_f32_e32 v134, v226, v176
	v_fmac_f32_e32 v134, v227, v177
	v_fmac_f32_e32 v134, v228, v178
	v_fmac_f32_e32 v134, v229, v179
	v_fmac_f32_e32 v135, v226, v180
	v_fmac_f32_e32 v135, v227, v181
	v_fmac_f32_e32 v135, v228, v182
	v_fmac_f32_e32 v135, v229, v183
	ds_read_b128 v[168:171], v153 offset:4096
	ds_read_b128 v[172:175], v153 offset:12304
	ds_read_b128 v[176:179], v153 offset:20512
	ds_read_b128 v[180:183], v153 offset:28720
	s_waitcnt lgkmcnt(4)
	v_fmac_f32_e32 v136, v226, v148
	v_fmac_f32_e32 v136, v227, v149
	v_fmac_f32_e32 v136, v228, v150
	v_fmac_f32_e32 v136, v229, v151
	v_fmac_f32_e32 v137, v226, v186
	v_fmac_f32_e32 v137, v227, v187
	v_fmac_f32_e32 v137, v228, v188
	v_fmac_f32_e32 v137, v229, v189
	v_fmac_f32_e32 v138, v226, v194
	v_fmac_f32_e32 v138, v227, v195
	v_fmac_f32_e32 v138, v228, v196
	v_fmac_f32_e32 v138, v229, v197
	v_fmac_f32_e32 v139, v226, v198
	v_fmac_f32_e32 v139, v227, v199
	v_fmac_f32_e32 v139, v228, v200
	v_fmac_f32_e32 v139, v229, v201
	ds_read_b128 v[148:151], v153 offset:36928
	ds_read_b128 v[186:189], v153 offset:45136
	ds_read_b128 v[194:197], v153 offset:53344
	ds_read_b128 v[198:201], v153 offset:61552
	s_waitcnt lgkmcnt(4)
	v_fmac_f32_e32 v140, v226, v168
	v_fmac_f32_e32 v140, v227, v169
	v_fmac_f32_e32 v140, v228, v170
	v_fmac_f32_e32 v140, v229, v171
	v_fmac_f32_e32 v141, v226, v172
	v_fmac_f32_e32 v141, v227, v173
	v_fmac_f32_e32 v141, v228, v174
	v_fmac_f32_e32 v141, v229, v175
	v_fmac_f32_e32 v142, v226, v176
	v_fmac_f32_e32 v142, v227, v177
	v_fmac_f32_e32 v142, v228, v178
	v_fmac_f32_e32 v142, v229, v179
	v_fmac_f32_e32 v143, v226, v180
	v_fmac_f32_e32 v143, v227, v181
	v_fmac_f32_e32 v143, v228, v182
	v_fmac_f32_e32 v143, v229, v183
	ds_read_b128 v[168:171], v152 offset:5120
	ds_read_b128 v[172:175], v152 offset:13328
	ds_read_b128 v[176:179], v152 offset:21536
	ds_read_b128 v[180:183], v152 offset:29744
	s_waitcnt lgkmcnt(4)
	v_fmac_f32_e32 v144, v226, v148
	v_fmac_f32_e32 v144, v227, v149
	v_fmac_f32_e32 v144, v228, v150
	v_fmac_f32_e32 v144, v229, v151
	v_fmac_f32_e32 v145, v226, v186
	v_fmac_f32_e32 v145, v227, v187
	v_fmac_f32_e32 v145, v228, v188
	v_fmac_f32_e32 v145, v229, v189
	v_fmac_f32_e32 v146, v226, v194
	v_fmac_f32_e32 v146, v227, v195
	v_fmac_f32_e32 v146, v228, v196
	v_fmac_f32_e32 v146, v229, v197
	v_fmac_f32_e32 v147, v226, v198
	v_fmac_f32_e32 v147, v227, v199
	v_fmac_f32_e32 v147, v228, v200
	v_fmac_f32_e32 v147, v229, v201
	ds_read_b128 v[148:151], v152 offset:37952
	ds_read_b128 v[186:189], v152 offset:46160
	ds_read_b128 v[194:197], v152 offset:54368
	ds_read_b128 v[198:201], v152 offset:62576
	s_waitcnt lgkmcnt(4)
	v_fmac_f32_e32 v132, v230, v168
	v_fmac_f32_e32 v132, v231, v169
	v_fmac_f32_e32 v132, v232, v170
	v_fmac_f32_e32 v132, v233, v171
	v_fmac_f32_e32 v133, v230, v172
	v_fmac_f32_e32 v133, v231, v173
	v_fmac_f32_e32 v133, v232, v174
	v_fmac_f32_e32 v133, v233, v175
	v_fmac_f32_e32 v134, v230, v176
	v_fmac_f32_e32 v134, v231, v177
	v_fmac_f32_e32 v134, v232, v178
	v_fmac_f32_e32 v134, v233, v179
	v_fmac_f32_e32 v135, v230, v180
	v_fmac_f32_e32 v135, v231, v181
	v_fmac_f32_e32 v135, v232, v182
	v_fmac_f32_e32 v135, v233, v183
	ds_read_b128 v[168:171], v153 offset:5120
	ds_read_b128 v[172:175], v153 offset:13328
	ds_read_b128 v[176:179], v153 offset:21536
	ds_read_b128 v[180:183], v153 offset:29744
	s_waitcnt lgkmcnt(4)
	v_fmac_f32_e32 v136, v230, v148
	v_fmac_f32_e32 v136, v231, v149
	v_fmac_f32_e32 v136, v232, v150
	v_fmac_f32_e32 v136, v233, v151
	v_fmac_f32_e32 v137, v230, v186
	v_fmac_f32_e32 v137, v231, v187
	v_fmac_f32_e32 v137, v232, v188
	v_fmac_f32_e32 v137, v233, v189
	v_fmac_f32_e32 v138, v230, v194
	v_fmac_f32_e32 v138, v231, v195
	v_fmac_f32_e32 v138, v232, v196
	v_fmac_f32_e32 v138, v233, v197
	v_fmac_f32_e32 v139, v230, v198
	v_fmac_f32_e32 v139, v231, v199
	v_fmac_f32_e32 v139, v232, v200
	v_fmac_f32_e32 v139, v233, v201
	ds_read_b128 v[148:151], v153 offset:37952
	ds_read_b128 v[186:189], v153 offset:46160
	ds_read_b128 v[194:197], v153 offset:54368
	ds_read_b128 v[198:201], v153 offset:62576
	s_waitcnt lgkmcnt(4)
	v_fmac_f32_e32 v140, v230, v168
	v_fmac_f32_e32 v140, v231, v169
	v_fmac_f32_e32 v140, v232, v170
	v_fmac_f32_e32 v140, v233, v171
	v_fmac_f32_e32 v141, v230, v172
	v_fmac_f32_e32 v141, v231, v173
	v_fmac_f32_e32 v141, v232, v174
	v_fmac_f32_e32 v141, v233, v175
	v_fmac_f32_e32 v142, v230, v176
	v_fmac_f32_e32 v142, v231, v177
	v_fmac_f32_e32 v142, v232, v178
	v_fmac_f32_e32 v142, v233, v179
	v_fmac_f32_e32 v143, v230, v180
	v_fmac_f32_e32 v143, v231, v181
	v_fmac_f32_e32 v143, v232, v182
	v_fmac_f32_e32 v143, v233, v183
	ds_read_b128 v[168:171], v152 offset:6144
	ds_read_b128 v[172:175], v152 offset:14352
	ds_read_b128 v[176:179], v152 offset:22560
	ds_read_b128 v[180:183], v152 offset:30768
	s_waitcnt lgkmcnt(4)
	v_fmac_f32_e32 v144, v230, v148
	v_fmac_f32_e32 v144, v231, v149
	v_fmac_f32_e32 v144, v232, v150
	v_fmac_f32_e32 v144, v233, v151
	v_fmac_f32_e32 v145, v230, v186
	v_fmac_f32_e32 v145, v231, v187
	v_fmac_f32_e32 v145, v232, v188
	v_fmac_f32_e32 v145, v233, v189
	v_fmac_f32_e32 v146, v230, v194
	v_fmac_f32_e32 v146, v231, v195
	v_fmac_f32_e32 v146, v232, v196
	v_fmac_f32_e32 v146, v233, v197
	v_fmac_f32_e32 v147, v230, v198
	v_fmac_f32_e32 v147, v231, v199
	v_fmac_f32_e32 v147, v232, v200
	v_fmac_f32_e32 v147, v233, v201
	ds_read_b128 v[148:151], v152 offset:38976
	ds_read_b128 v[186:189], v152 offset:47184
	ds_read_b128 v[194:197], v152 offset:55392
	ds_read_b128 v[198:201], v152 offset:63600
	s_waitcnt lgkmcnt(4)
	v_fmac_f32_e32 v132, v234, v168
	v_fmac_f32_e32 v132, v235, v169
	v_fmac_f32_e32 v132, v236, v170
	v_fmac_f32_e32 v132, v237, v171
	v_fmac_f32_e32 v133, v234, v172
	v_fmac_f32_e32 v133, v235, v173
	v_fmac_f32_e32 v133, v236, v174
	v_fmac_f32_e32 v133, v237, v175
	v_fmac_f32_e32 v134, v234, v176
	v_fmac_f32_e32 v134, v235, v177
	v_fmac_f32_e32 v134, v236, v178
	v_fmac_f32_e32 v134, v237, v179
	v_fmac_f32_e32 v135, v234, v180
	v_fmac_f32_e32 v135, v235, v181
	v_fmac_f32_e32 v135, v236, v182
	v_fmac_f32_e32 v135, v237, v183
	ds_read_b128 v[168:171], v153 offset:6144
	ds_read_b128 v[172:175], v153 offset:14352
	ds_read_b128 v[176:179], v153 offset:22560
	ds_read_b128 v[180:183], v153 offset:30768
	s_waitcnt lgkmcnt(4)
	v_fmac_f32_e32 v136, v234, v148
	v_fmac_f32_e32 v136, v235, v149
	v_fmac_f32_e32 v136, v236, v150
	v_fmac_f32_e32 v136, v237, v151
	v_fmac_f32_e32 v137, v234, v186
	v_fmac_f32_e32 v137, v235, v187
	v_fmac_f32_e32 v137, v236, v188
	v_fmac_f32_e32 v137, v237, v189
	v_fmac_f32_e32 v138, v234, v194
	v_fmac_f32_e32 v138, v235, v195
	v_fmac_f32_e32 v138, v236, v196
	v_fmac_f32_e32 v138, v237, v197
	v_fmac_f32_e32 v139, v234, v198
	v_fmac_f32_e32 v139, v235, v199
	v_fmac_f32_e32 v139, v236, v200
	v_fmac_f32_e32 v139, v237, v201
	ds_read_b128 v[148:151], v153 offset:38976
	ds_read_b128 v[186:189], v153 offset:47184
	ds_read_b128 v[194:197], v153 offset:55392
	ds_read_b128 v[198:201], v153 offset:63600
	s_waitcnt lgkmcnt(4)
	v_fmac_f32_e32 v140, v234, v168
	v_fmac_f32_e32 v140, v235, v169
	v_fmac_f32_e32 v140, v236, v170
	v_fmac_f32_e32 v140, v237, v171
	v_fmac_f32_e32 v141, v234, v172
	v_fmac_f32_e32 v141, v235, v173
	v_fmac_f32_e32 v141, v236, v174
	v_fmac_f32_e32 v141, v237, v175
	v_fmac_f32_e32 v142, v234, v176
	v_fmac_f32_e32 v142, v235, v177
	v_fmac_f32_e32 v142, v236, v178
	v_fmac_f32_e32 v142, v237, v179
	v_fmac_f32_e32 v143, v234, v180
	v_fmac_f32_e32 v143, v235, v181
	v_fmac_f32_e32 v143, v236, v182
	v_fmac_f32_e32 v143, v237, v183
	ds_read_b128 v[168:171], v152 offset:7168
	ds_read_b128 v[172:175], v152 offset:15376
	ds_read_b128 v[176:179], v152 offset:23584
	ds_read_b128 v[180:183], v152 offset:31792
	s_waitcnt lgkmcnt(4)
	v_fmac_f32_e32 v144, v234, v148
	v_fmac_f32_e32 v144, v235, v149
	v_fmac_f32_e32 v144, v236, v150
	v_fmac_f32_e32 v144, v237, v151
	v_fmac_f32_e32 v145, v234, v186
	v_fmac_f32_e32 v145, v235, v187
	v_fmac_f32_e32 v145, v236, v188
	v_fmac_f32_e32 v145, v237, v189
	v_fmac_f32_e32 v146, v234, v194
	v_fmac_f32_e32 v146, v235, v195
	v_fmac_f32_e32 v146, v236, v196
	v_fmac_f32_e32 v146, v237, v197
	v_fmac_f32_e32 v147, v234, v198
	v_fmac_f32_e32 v147, v235, v199
	v_fmac_f32_e32 v147, v236, v200
	v_fmac_f32_e32 v147, v237, v201
	ds_read_b128 v[148:151], v152 offset:40000
	ds_read_b128 v[186:189], v152 offset:48208
	ds_read_b128 v[194:197], v152 offset:56416
	ds_read_b128 v[198:201], v152 offset:64624
	s_waitcnt lgkmcnt(4)
	v_fmac_f32_e32 v132, v238, v168
	v_fmac_f32_e32 v132, v239, v169
	v_fmac_f32_e32 v132, v240, v170
	v_fmac_f32_e32 v132, v241, v171
	v_fmac_f32_e32 v133, v238, v172
	v_fmac_f32_e32 v133, v239, v173
	v_fmac_f32_e32 v133, v240, v174
	v_fmac_f32_e32 v133, v241, v175
	v_fmac_f32_e32 v134, v238, v176
	v_fmac_f32_e32 v134, v239, v177
	v_fmac_f32_e32 v134, v240, v178
	v_fmac_f32_e32 v134, v241, v179
	v_fmac_f32_e32 v135, v238, v180
	v_fmac_f32_e32 v135, v239, v181
	v_fmac_f32_e32 v135, v240, v182
	v_fmac_f32_e32 v135, v241, v183
	ds_read_b128 v[168:171], v153 offset:7168
	ds_read_b128 v[172:175], v153 offset:15376
	ds_read_b128 v[176:179], v153 offset:23584
	ds_read_b128 v[180:183], v153 offset:31792
	s_waitcnt lgkmcnt(4)
	v_fmac_f32_e32 v136, v238, v148
	v_fmac_f32_e32 v136, v239, v149
	v_fmac_f32_e32 v136, v240, v150
	v_fmac_f32_e32 v136, v241, v151
	v_fmac_f32_e32 v137, v238, v186
	v_fmac_f32_e32 v137, v239, v187
	v_fmac_f32_e32 v137, v240, v188
	v_fmac_f32_e32 v137, v241, v189
	v_fmac_f32_e32 v138, v238, v194
	v_fmac_f32_e32 v138, v239, v195
	v_fmac_f32_e32 v138, v240, v196
	v_fmac_f32_e32 v138, v241, v197
	v_fmac_f32_e32 v139, v238, v198
	v_fmac_f32_e32 v139, v239, v199
	v_fmac_f32_e32 v139, v240, v200
	v_fmac_f32_e32 v139, v241, v201
	ds_read_b128 v[148:151], v153 offset:40000
	ds_read_b128 v[186:189], v153 offset:48208
	ds_read_b128 v[194:197], v153 offset:56416
	ds_read_b128 v[198:201], v153 offset:64624
	s_waitcnt lgkmcnt(4)
	v_fmac_f32_e32 v140, v238, v168
	v_fmac_f32_e32 v140, v239, v169
	v_fmac_f32_e32 v140, v240, v170
	v_fmac_f32_e32 v140, v241, v171
	v_fmac_f32_e32 v141, v238, v172
	v_fmac_f32_e32 v141, v239, v173
	v_fmac_f32_e32 v141, v240, v174
	v_fmac_f32_e32 v141, v241, v175
	v_fmac_f32_e32 v142, v238, v176
	v_fmac_f32_e32 v142, v239, v177
	v_fmac_f32_e32 v142, v240, v178
	v_fmac_f32_e32 v142, v241, v179
	v_fmac_f32_e32 v143, v238, v180
	v_fmac_f32_e32 v143, v239, v181
	v_fmac_f32_e32 v143, v240, v182
	v_fmac_f32_e32 v143, v241, v183
	s_waitcnt lgkmcnt(0)
	v_fmac_f32_e32 v144, v238, v148
	v_fmac_f32_e32 v144, v239, v149
	v_fmac_f32_e32 v144, v240, v150
	v_fmac_f32_e32 v144, v241, v151
	v_fmac_f32_e32 v145, v238, v186
	v_fmac_f32_e32 v145, v239, v187
	v_fmac_f32_e32 v145, v240, v188
	v_fmac_f32_e32 v145, v241, v189
	v_fmac_f32_e32 v146, v238, v194
	v_fmac_f32_e32 v146, v239, v195
	v_fmac_f32_e32 v146, v240, v196
	v_fmac_f32_e32 v146, v241, v197
	v_fmac_f32_e32 v147, v238, v198
	v_fmac_f32_e32 v147, v239, v199
	v_fmac_f32_e32 v147, v240, v200
	v_fmac_f32_e32 v147, v241, v201
	s_add_i32 s11, s10, 0x2800
	s_lshr_b32 s0, s11, 8
	s_mul_i32 s0, s0, 57
	s_lshr_b32 s0, s0, 9
	s_mul_i32 s1, s0, 0x900
	s_sub_i32 s43, s11, s1
	s_lshl_b32 s1, s11, 13
	s_add_u32 s12, s48, s1
	s_addc_u32 s13, s49, 0
	s_add_u32 s14, s12, 0x1000
	s_addc_u32 s15, s13, 0
	global_load_dwordx4 v[204:207], v1, s[12:13]
	global_load_dwordx4 v[208:211], v1, s[12:13] offset:1024
	global_load_dwordx4 v[212:215], v1, s[12:13] offset:2048
	global_load_dwordx4 v[216:219], v1, s[12:13] offset:3072
	global_load_dwordx4 v[226:229], v1, s[14:15]
	global_load_dwordx4 v[230:233], v1, s[14:15] offset:1024
	global_load_dwordx4 v[234:237], v1, s[14:15] offset:2048
	global_load_dwordx4 v[238:241], v1, s[14:15] offset:3072
	v_cndmask_b32_e64 v242, v133, v132, s[62:63]
	v_cndmask_b32_e64 v132, v132, v133, s[62:63]
	v_cndmask_b32_e64 v243, v135, v134, s[62:63]
	v_cndmask_b32_e64 v134, v134, v135, s[62:63]
	v_cndmask_b32_e64 v244, v137, v136, s[62:63]
	v_cndmask_b32_e64 v136, v136, v137, s[62:63]
	v_cndmask_b32_e64 v245, v139, v138, s[62:63]
	v_cndmask_b32_e64 v138, v138, v139, s[62:63]
	v_cndmask_b32_e64 v246, v141, v140, s[62:63]
	v_cndmask_b32_e64 v140, v140, v141, s[62:63]
	v_cndmask_b32_e64 v248, v143, v142, s[62:63]
	v_cndmask_b32_e64 v142, v142, v143, s[62:63]
	v_cndmask_b32_e64 v249, v145, v144, s[62:63]
	v_cndmask_b32_e64 v144, v144, v145, s[62:63]
	v_cndmask_b32_e64 v250, v147, v146, s[62:63]
	v_cndmask_b32_e64 v146, v146, v147, s[62:63]
	v_add_f32_dpp v132, v242, v132 quad_perm:[1,0,3,2] row_mask:0xf bank_mask:0xf
	v_add_f32_dpp v134, v243, v134 quad_perm:[1,0,3,2] row_mask:0xf bank_mask:0xf
	v_add_f32_dpp v136, v244, v136 quad_perm:[1,0,3,2] row_mask:0xf bank_mask:0xf
	v_add_f32_dpp v138, v245, v138 quad_perm:[1,0,3,2] row_mask:0xf bank_mask:0xf
	v_add_f32_dpp v140, v246, v140 quad_perm:[1,0,3,2] row_mask:0xf bank_mask:0xf
	v_add_f32_dpp v142, v248, v142 quad_perm:[1,0,3,2] row_mask:0xf bank_mask:0xf
	v_add_f32_dpp v144, v249, v144 quad_perm:[1,0,3,2] row_mask:0xf bank_mask:0xf
	v_add_f32_dpp v146, v250, v146 quad_perm:[1,0,3,2] row_mask:0xf bank_mask:0xf
	v_cndmask_b32_e64 v242, v134, v132, s[64:65]
	v_cndmask_b32_e64 v132, v132, v134, s[64:65]
	v_cndmask_b32_e64 v243, v138, v136, s[64:65]
	v_cndmask_b32_e64 v136, v136, v138, s[64:65]
	v_cndmask_b32_e64 v244, v142, v140, s[64:65]
	v_cndmask_b32_e64 v140, v140, v142, s[64:65]
	v_cndmask_b32_e64 v245, v146, v144, s[64:65]
	v_cndmask_b32_e64 v144, v144, v146, s[64:65]
	s_nop 0
	v_add_f32_dpp v132, v242, v132 quad_perm:[2,3,0,1] row_mask:0xf bank_mask:0xf
	v_add_f32_dpp v136, v243, v136 quad_perm:[2,3,0,1] row_mask:0xf bank_mask:0xf
	v_add_f32_dpp v140, v244, v140 quad_perm:[2,3,0,1] row_mask:0xf bank_mask:0xf
	v_add_f32_dpp v144, v245, v144 quad_perm:[2,3,0,1] row_mask:0xf bank_mask:0xf
	v_cndmask_b32_e64 v242, v136, v132, s[66:67]
	v_cndmask_b32_e64 v132, v132, v136, s[66:67]
	v_cndmask_b32_e64 v243, v144, v140, s[66:67]
	v_cndmask_b32_e64 v140, v140, v144, s[66:67]
	s_nop 1
	v_add_f32_dpp v246, v242, v132 row_shl:4 row_mask:0xf bank_mask:0x5
	v_add_f32_dpp v246, v242, v132 row_shr:4 row_mask:0xf bank_mask:0xa
	v_add_f32_dpp v248, v243, v140 row_shl:4 row_mask:0xf bank_mask:0x5
	v_add_f32_dpp v248, v243, v140 row_shr:4 row_mask:0xf bank_mask:0xa
	v_cndmask_b32_e64 v242, v248, v246, s[68:69]
	v_cndmask_b32_e64 v243, v246, v248, s[68:69]
	s_nop 1
	v_add_f32_dpp v191, v242, v243 row_ror:8 row_mask:0xf bank_mask:0xf
	s_nop 0
	ds_bpermute_b32 v193, v165, v191
	s_waitcnt lgkmcnt(0)
	v_add_f32_e32 v191, v191, v193
	ds_bpermute_b32 v193, v166, v191
	s_waitcnt lgkmcnt(0)
	v_add_f32_e32 v191, v191, v193
	v_mov_b32_e32 v193, v191
	s_nop 1
	v_max_f32_dpp v193, v193, v193 quad_perm:[1,0,3,2] row_mask:0xf bank_mask:0xf
	s_nop 1
	v_max_f32_dpp v193, v193, v193 quad_perm:[2,3,0,1] row_mask:0xf bank_mask:0xf
	s_nop 1
	v_max_f32_dpp v193, v193, v193 row_half_mirror row_mask:0xf bank_mask:0xf
	s_nop 1
	v_max_f32_dpp v193, v193, v193 row_mirror row_mask:0xf bank_mask:0xf
	v_sub_f32_e32 v191, v191, v193
	v_mul_f32_e32 v191, 0x3fb8aa3b, v191
	v_exp_f32_e32 v191, v191
	s_nop 0
	v_mov_b32_e32 v193, v191
	s_nop 1
	v_add_f32_dpp v193, v193, v193 quad_perm:[1,0,3,2] row_mask:0xf bank_mask:0xf
	s_nop 1
	v_add_f32_dpp v193, v193, v193 quad_perm:[2,3,0,1] row_mask:0xf bank_mask:0xf
	s_nop 1
	v_add_f32_dpp v193, v193, v193 row_half_mirror row_mask:0xf bank_mask:0xf
	s_nop 1
	v_add_f32_dpp v193, v193, v193 row_mirror row_mask:0xf bank_mask:0xf
	v_rcp_f32_e32 v193, v193
	s_nop 0
	v_mul_f32_e32 v191, v191, v193
	s_mov_b64 exec, 0xffff
	global_store_dword v164, v191, s[34:35]
	s_mov_b64 exec, -1
	s_waitcnt vmcnt(9)
	s_add_i32 s11, s10, 0x2000
	s_lshr_b32 s0, s11, 8
	s_mul_i32 s0, s0, 57
	s_lshr_b32 s0, s0, 9
	s_mul_i32 s1, s0, 0x900
	s_sub_i32 s43, s11, s1
	s_lshl_b32 s1, s11, 12
	s_add_u32 s16, s50, s1
	s_addc_u32 s17, s51, 0
	s_mul_i32 s1, s0, 0x24000
	s_lshl_b32 s2, s43, 2
	s_add_i32 s1, s1, s2
	s_add_u32 s34, s54, s1
	s_addc_u32 s35, s55, 0
	v_mul_f32_e32 v184, v100, v100
	v_fmac_f32_e32 v184, v101, v101
	v_fmac_f32_e32 v184, v102, v102
	v_fmac_f32_e32 v184, v103, v103
	v_fmac_f32_e32 v184, v104, v104
	v_fmac_f32_e32 v184, v105, v105
	v_fmac_f32_e32 v184, v106, v106
	v_fmac_f32_e32 v184, v107, v107
	v_fmac_f32_e32 v184, v108, v108
	v_fmac_f32_e32 v184, v109, v109
	v_fmac_f32_e32 v184, v110, v110
	v_fmac_f32_e32 v184, v111, v111
	v_fmac_f32_e32 v184, v112, v112
	v_fmac_f32_e32 v184, v113, v113
	v_fmac_f32_e32 v184, v114, v114
	v_fmac_f32_e32 v184, v115, v115
	v_fmac_f32_e32 v184, v116, v116
	v_fmac_f32_e32 v184, v117, v117
	v_fmac_f32_e32 v184, v118, v118
	v_fmac_f32_e32 v184, v119, v119
	v_fmac_f32_e32 v184, v120, v120
	v_fmac_f32_e32 v184, v121, v121
	v_fmac_f32_e32 v184, v122, v122
	v_fmac_f32_e32 v184, v123, v123
	v_fmac_f32_e32 v184, v124, v124
	v_fmac_f32_e32 v184, v125, v125
	v_fmac_f32_e32 v184, v126, v126
	v_fmac_f32_e32 v184, v127, v127
	v_fmac_f32_e32 v184, v128, v128
	v_fmac_f32_e32 v184, v129, v129
	v_fmac_f32_e32 v184, v130, v130
	v_fmac_f32_e32 v184, v131, v131
	ds_read_b128 v[168:171], v152 offset:0
	ds_read_b128 v[172:175], v152 offset:8208
	ds_read_b128 v[176:179], v152 offset:16416
	ds_read_b128 v[180:183], v152 offset:24624
	s_nop 0
	v_add_f32_dpp v184, v184, v184 quad_perm:[1,0,3,2] row_mask:0xf bank_mask:0xf
	s_nop 1
	v_add_f32_dpp v184, v184, v184 quad_perm:[2,3,0,1] row_mask:0xf bank_mask:0xf
	s_nop 1
	v_add_f32_dpp v184, v184, v184 row_half_mirror row_mask:0xf bank_mask:0xf
	s_nop 1
	v_add_f32_dpp v184, v184, v184 row_mirror row_mask:0xf bank_mask:0xf
	s_nop 1
	v_readlane_b32 s0, v184, 0
	v_readlane_b32 s1, v184, 16
	v_readlane_b32 s2, v184, 32
	v_readlane_b32 s3, v184, 48
	v_fma_f32 v4, v4, v36, v4
	v_fma_f32 v5, v5, v37, v5
	v_fma_f32 v6, v6, v38, v6
	v_fma_f32 v7, v7, v39, v7
	v_fma_f32 v8, v8, v40, v8
	v_fma_f32 v9, v9, v41, v9
	v_fma_f32 v10, v10, v42, v10
	v_fma_f32 v11, v11, v43, v11
	v_fma_f32 v12, v12, v44, v12
	v_fma_f32 v13, v13, v45, v13
	v_fma_f32 v14, v14, v46, v14
	v_fma_f32 v15, v15, v47, v15
	v_fma_f32 v16, v16, v48, v16
	v_fma_f32 v17, v17, v49, v17
	v_fma_f32 v18, v18, v50, v18
	v_fma_f32 v19, v19, v51, v19
	v_fma_f32 v20, v20, v52, v20
	v_fma_f32 v21, v21, v53, v21
	v_fma_f32 v22, v22, v54, v22
	v_fma_f32 v23, v23, v55, v23
	v_fma_f32 v24, v24, v56, v24
	v_fma_f32 v25, v25, v57, v25
	v_fma_f32 v26, v26, v58, v26
	v_fma_f32 v27, v27, v59, v27
	v_fma_f32 v28, v28, v60, v28
	v_fma_f32 v29, v29, v61, v29
	v_fma_f32 v30, v30, v62, v30
	v_fma_f32 v31, v31, v63, v31
	v_fma_f32 v32, v32, v64, v32
	v_fma_f32 v33, v33, v65, v33
	v_fma_f32 v34, v34, v66, v34
	v_fma_f32 v35, v35, v67, v35
	v_mov_b32_e32 v190, s0
	v_add_f32_e32 v190, s1, v190
	v_add_f32_e32 v190, s2, v190
	v_add_f32_e32 v190, s3, v190
	v_mul_f32_e32 v190, 0x3a000000, v190
	v_add_f32_e32 v190, 0x358637bd, v190
	v_rsq_f32_e32 v190, v190
	s_nop 0
	v_mul_f32_e32 v4, v4, v190
	v_mul_f32_e32 v5, v5, v190
	v_mul_f32_e32 v6, v6, v190
	v_mul_f32_e32 v7, v7, v190
	v_mul_f32_e32 v8, v8, v190
	v_mul_f32_e32 v9, v9, v190
	v_mul_f32_e32 v10, v10, v190
	v_mul_f32_e32 v11, v11, v190
	v_mul_f32_e32 v12, v12, v190
	v_mul_f32_e32 v13, v13, v190
	v_mul_f32_e32 v14, v14, v190
	v_mul_f32_e32 v15, v15, v190
	v_mul_f32_e32 v16, v16, v190
	v_mul_f32_e32 v17, v17, v190
	v_mul_f32_e32 v18, v18, v190
	v_mul_f32_e32 v19, v19, v190
	v_mul_f32_e32 v20, v20, v190
	v_mul_f32_e32 v21, v21, v190
	v_mul_f32_e32 v22, v22, v190
	v_mul_f32_e32 v23, v23, v190
	v_mul_f32_e32 v24, v24, v190
	v_mul_f32_e32 v25, v25, v190
	v_mul_f32_e32 v26, v26, v190
	v_mul_f32_e32 v27, v27, v190
	v_mul_f32_e32 v28, v28, v190
	v_mul_f32_e32 v29, v29, v190
	v_mul_f32_e32 v30, v30, v190
	v_mul_f32_e32 v31, v31, v190
	v_mul_f32_e32 v32, v32, v190
	v_mul_f32_e32 v33, v33, v190
	v_mul_f32_e32 v34, v34, v190
	v_mul_f32_e32 v35, v35, v190
	v_fma_f32 v100, v100, v4, v68
	v_fma_f32 v101, v101, v5, v69
	v_fma_f32 v102, v102, v6, v70
	v_fma_f32 v103, v103, v7, v71
	v_fma_f32 v104, v104, v8, v72
	v_fma_f32 v105, v105, v9, v73
	v_fma_f32 v106, v106, v10, v74
	v_fma_f32 v107, v107, v11, v75
	v_fma_f32 v108, v108, v12, v76
	v_fma_f32 v109, v109, v13, v77
	v_fma_f32 v110, v110, v14, v78
	v_fma_f32 v111, v111, v15, v79
	v_fma_f32 v112, v112, v16, v80
	v_fma_f32 v113, v113, v17, v81
	v_fma_f32 v114, v114, v18, v82
	v_fma_f32 v115, v115, v19, v83
	v_fma_f32 v116, v116, v20, v84
	v_fma_f32 v117, v117, v21, v85
	v_fma_f32 v118, v118, v22, v86
	v_fma_f32 v119, v119, v23, v87
	v_fma_f32 v120, v120, v24, v88
	v_fma_f32 v121, v121, v25, v89
	v_fma_f32 v122, v122, v26, v90
	v_fma_f32 v123, v123, v27, v91
	v_fma_f32 v124, v124, v28, v92
	v_fma_f32 v125, v125, v29, v93
	v_fma_f32 v126, v126, v30, v94
	v_fma_f32 v127, v127, v31, v95
	v_fma_f32 v128, v128, v32, v96
	v_fma_f32 v129, v129, v33, v97
	v_fma_f32 v130, v130, v34, v98
	v_fma_f32 v131, v131, v35, v99
	v_cvt_pk_bf16_f32 v242, v100, v101
	v_cvt_pk_bf16_f32 v243, v102, v103
	global_store_dwordx2 v2, v[242:243], s[16:17]
	v_cvt_pk_bf16_f32 v244, v104, v105
	v_cvt_pk_bf16_f32 v245, v106, v107
	global_store_dwordx2 v2, v[244:245], s[16:17] offset:512
	v_cvt_pk_bf16_f32 v242, v108, v109
	v_cvt_pk_bf16_f32 v243, v110, v111
	global_store_dwordx2 v2, v[242:243], s[16:17] offset:1024
	v_cvt_pk_bf16_f32 v244, v112, v113
	v_cvt_pk_bf16_f32 v245, v114, v115
	global_store_dwordx2 v2, v[244:245], s[16:17] offset:1536
	v_cvt_pk_bf16_f32 v242, v116, v117
	v_cvt_pk_bf16_f32 v243, v118, v119
	global_store_dwordx2 v2, v[242:243], s[16:17] offset:2048
	v_cvt_pk_bf16_f32 v244, v120, v121
	v_cvt_pk_bf16_f32 v245, v122, v123
	global_store_dwordx2 v2, v[244:245], s[16:17] offset:2560
	v_cvt_pk_bf16_f32 v242, v124, v125
	v_cvt_pk_bf16_f32 v243, v126, v127
	global_store_dwordx2 v2, v[242:243], s[16:17] offset:3072
	v_cvt_pk_bf16_f32 v244, v128, v129
	v_cvt_pk_bf16_f32 v245, v130, v131
	global_store_dwordx2 v2, v[244:245], s[16:17] offset:3584
	s_add_i32 s11, s10, 0x2800
	s_lshr_b32 s0, s11, 8
	s_mul_i32 s0, s0, 57
	s_lshr_b32 s0, s0, 9
	s_mul_i32 s1, s0, 0x900
	s_sub_i32 s43, s11, s1
	s_cmpk_lt_u32 s43, 0x100
	s_cselect_b32 s0, 8, s0
	s_mul_i32 s1, s0, 0xc000
	s_add_u32 s18, s52, s1
	s_addc_u32 s19, s53, 0
	s_add_u32 s18, s18, 0x6000
	s_addc_u32 s19, s19, 0
	s_add_u32 s22, s18, 0x1000
	s_addc_u32 s23, s19, 0
	s_add_u32 s28, s18, 0x2000
	s_addc_u32 s29, s19, 0
	s_add_u32 s30, s18, 0x3000
	s_addc_u32 s31, s19, 0
	global_load_dwordx4 v[4:7], v1, s[56:57]
	global_load_dwordx4 v[36:39], v1, s[28:29]
	global_load_dwordx4 v[68:71], v1, s[18:19]
	global_load_dwordx4 v[8:11], v1, s[56:57] offset:1024
	global_load_dwordx4 v[40:43], v1, s[28:29] offset:1024
	global_load_dwordx4 v[72:75], v1, s[18:19] offset:1024
	global_load_dwordx4 v[12:15], v1, s[56:57] offset:2048
	global_load_dwordx4 v[44:47], v1, s[28:29] offset:2048
	global_load_dwordx4 v[76:79], v1, s[18:19] offset:2048
	global_load_dwordx4 v[16:19], v1, s[56:57] offset:3072
	global_load_dwordx4 v[48:51], v1, s[28:29] offset:3072
	global_load_dwordx4 v[80:83], v1, s[18:19] offset:3072
	global_load_dwordx4 v[20:23], v1, s[58:59]
	global_load_dwordx4 v[52:55], v1, s[30:31]
	global_load_dwordx4 v[84:87], v1, s[22:23]
	global_load_dwordx4 v[24:27], v1, s[58:59] offset:1024
	global_load_dwordx4 v[56:59], v1, s[30:31] offset:1024
	global_load_dwordx4 v[88:91], v1, s[22:23] offset:1024
	global_load_dwordx4 v[28:31], v1, s[58:59] offset:2048
	global_load_dwordx4 v[60:63], v1, s[30:31] offset:2048
	global_load_dwordx4 v[92:95], v1, s[22:23] offset:2048
	global_load_dwordx4 v[32:35], v1, s[58:59] offset:3072
	global_load_dwordx4 v[64:67], v1, s[30:31] offset:3072
	global_load_dwordx4 v[96:99], v1, s[22:23] offset:3072
	v_mov_b32_e32 v132, 0
	v_mov_b32_e32 v133, 0
	v_mov_b32_e32 v134, 0
	v_mov_b32_e32 v135, 0
	v_mov_b32_e32 v136, 0
	v_mov_b32_e32 v137, 0
	v_mov_b32_e32 v138, 0
	v_mov_b32_e32 v139, 0
	v_mov_b32_e32 v140, 0
	v_mov_b32_e32 v141, 0
	v_mov_b32_e32 v142, 0
	v_mov_b32_e32 v143, 0
	v_mov_b32_e32 v144, 0
	v_mov_b32_e32 v145, 0
	v_mov_b32_e32 v146, 0
	v_mov_b32_e32 v147, 0
	ds_read_b128 v[148:151], v152 offset:32832
	ds_read_b128 v[186:189], v152 offset:41040
	ds_read_b128 v[194:197], v152 offset:49248
	ds_read_b128 v[198:201], v152 offset:57456
	s_waitcnt lgkmcnt(4)
	v_fmac_f32_e32 v132, v100, v168
	v_fmac_f32_e32 v132, v101, v169
	v_fmac_f32_e32 v132, v102, v170
	v_fmac_f32_e32 v132, v103, v171
	v_fmac_f32_e32 v133, v100, v172
	v_fmac_f32_e32 v133, v101, v173
	v_fmac_f32_e32 v133, v102, v174
	v_fmac_f32_e32 v133, v103, v175
	v_fmac_f32_e32 v134, v100, v176
	v_fmac_f32_e32 v134, v101, v177
	v_fmac_f32_e32 v134, v102, v178
	v_fmac_f32_e32 v134, v103, v179
	v_fmac_f32_e32 v135, v100, v180
	v_fmac_f32_e32 v135, v101, v181
	v_fmac_f32_e32 v135, v102, v182
	v_fmac_f32_e32 v135, v103, v183
	ds_read_b128 v[168:171], v153 offset:0
	ds_read_b128 v[172:175], v153 offset:8208
	ds_read_b128 v[176:179], v153 offset:16416
	ds_read_b128 v[180:183], v153 offset:24624
	s_waitcnt lgkmcnt(4)
	v_fmac_f32_e32 v136, v100, v148
	v_fmac_f32_e32 v136, v101, v149
	v_fmac_f32_e32 v136, v102, v150
	v_fmac_f32_e32 v136, v103, v151
	v_fmac_f32_e32 v137, v100, v186
	v_fmac_f32_e32 v137, v101, v187
	v_fmac_f32_e32 v137, v102, v188
	v_fmac_f32_e32 v137, v103, v189
	v_fmac_f32_e32 v138, v100, v194
	v_fmac_f32_e32 v138, v101, v195
	v_fmac_f32_e32 v138, v102, v196
	v_fmac_f32_e32 v138, v103, v197
	v_fmac_f32_e32 v139, v100, v198
	v_fmac_f32_e32 v139, v101, v199
	v_fmac_f32_e32 v139, v102, v200
	v_fmac_f32_e32 v139, v103, v201
	ds_read_b128 v[148:151], v153 offset:32832
	ds_read_b128 v[186:189], v153 offset:41040
	ds_read_b128 v[194:197], v153 offset:49248
	ds_read_b128 v[198:201], v153 offset:57456
	s_waitcnt lgkmcnt(4)
	v_fmac_f32_e32 v140, v100, v168
	v_fmac_f32_e32 v140, v101, v169
	v_fmac_f32_e32 v140, v102, v170
	v_fmac_f32_e32 v140, v103, v171
	v_fmac_f32_e32 v141, v100, v172
	v_fmac_f32_e32 v141, v101, v173
	v_fmac_f32_e32 v141, v102, v174
	v_fmac_f32_e32 v141, v103, v175
	v_fmac_f32_e32 v142, v100, v176
	v_fmac_f32_e32 v142, v101, v177
	v_fmac_f32_e32 v142, v102, v178
	v_fmac_f32_e32 v142, v103, v179
	v_fmac_f32_e32 v143, v100, v180
	v_fmac_f32_e32 v143, v101, v181
	v_fmac_f32_e32 v143, v102, v182
	v_fmac_f32_e32 v143, v103, v183
	ds_read_b128 v[168:171], v152 offset:1024
	ds_read_b128 v[172:175], v152 offset:9232
	ds_read_b128 v[176:179], v152 offset:17440
	ds_read_b128 v[180:183], v152 offset:25648
	s_waitcnt lgkmcnt(4)
	v_fmac_f32_e32 v144, v100, v148
	v_fmac_f32_e32 v144, v101, v149
	v_fmac_f32_e32 v144, v102, v150
	v_fmac_f32_e32 v144, v103, v151
	v_fmac_f32_e32 v145, v100, v186
	v_fmac_f32_e32 v145, v101, v187
	v_fmac_f32_e32 v145, v102, v188
	v_fmac_f32_e32 v145, v103, v189
	v_fmac_f32_e32 v146, v100, v194
	v_fmac_f32_e32 v146, v101, v195
	v_fmac_f32_e32 v146, v102, v196
	v_fmac_f32_e32 v146, v103, v197
	v_fmac_f32_e32 v147, v100, v198
	v_fmac_f32_e32 v147, v101, v199
	v_fmac_f32_e32 v147, v102, v200
	v_fmac_f32_e32 v147, v103, v201
	ds_read_b128 v[148:151], v152 offset:33856
	ds_read_b128 v[186:189], v152 offset:42064
	ds_read_b128 v[194:197], v152 offset:50272
	ds_read_b128 v[198:201], v152 offset:58480
	s_waitcnt lgkmcnt(4)
	v_fmac_f32_e32 v132, v104, v168
	v_fmac_f32_e32 v132, v105, v169
	v_fmac_f32_e32 v132, v106, v170
	v_fmac_f32_e32 v132, v107, v171
	v_fmac_f32_e32 v133, v104, v172
	v_fmac_f32_e32 v133, v105, v173
	v_fmac_f32_e32 v133, v106, v174
	v_fmac_f32_e32 v133, v107, v175
	v_fmac_f32_e32 v134, v104, v176
	v_fmac_f32_e32 v134, v105, v177
	v_fmac_f32_e32 v134, v106, v178
	v_fmac_f32_e32 v134, v107, v179
	v_fmac_f32_e32 v135, v104, v180
	v_fmac_f32_e32 v135, v105, v181
	v_fmac_f32_e32 v135, v106, v182
	v_fmac_f32_e32 v135, v107, v183
	ds_read_b128 v[168:171], v153 offset:1024
	ds_read_b128 v[172:175], v153 offset:9232
	ds_read_b128 v[176:179], v153 offset:17440
	ds_read_b128 v[180:183], v153 offset:25648
	s_waitcnt lgkmcnt(4)
	v_fmac_f32_e32 v136, v104, v148
	v_fmac_f32_e32 v136, v105, v149
	v_fmac_f32_e32 v136, v106, v150
	v_fmac_f32_e32 v136, v107, v151
	v_fmac_f32_e32 v137, v104, v186
	v_fmac_f32_e32 v137, v105, v187
	v_fmac_f32_e32 v137, v106, v188
	v_fmac_f32_e32 v137, v107, v189
	v_fmac_f32_e32 v138, v104, v194
	v_fmac_f32_e32 v138, v105, v195
	v_fmac_f32_e32 v138, v106, v196
	v_fmac_f32_e32 v138, v107, v197
	v_fmac_f32_e32 v139, v104, v198
	v_fmac_f32_e32 v139, v105, v199
	v_fmac_f32_e32 v139, v106, v200
	v_fmac_f32_e32 v139, v107, v201
	ds_read_b128 v[148:151], v153 offset:33856
	ds_read_b128 v[186:189], v153 offset:42064
	ds_read_b128 v[194:197], v153 offset:50272
	ds_read_b128 v[198:201], v153 offset:58480
	s_waitcnt lgkmcnt(4)
	v_fmac_f32_e32 v140, v104, v168
	v_fmac_f32_e32 v140, v105, v169
	v_fmac_f32_e32 v140, v106, v170
	v_fmac_f32_e32 v140, v107, v171
	v_fmac_f32_e32 v141, v104, v172
	v_fmac_f32_e32 v141, v105, v173
	v_fmac_f32_e32 v141, v106, v174
	v_fmac_f32_e32 v141, v107, v175
	v_fmac_f32_e32 v142, v104, v176
	v_fmac_f32_e32 v142, v105, v177
	v_fmac_f32_e32 v142, v106, v178
	v_fmac_f32_e32 v142, v107, v179
	v_fmac_f32_e32 v143, v104, v180
	v_fmac_f32_e32 v143, v105, v181
	v_fmac_f32_e32 v143, v106, v182
	v_fmac_f32_e32 v143, v107, v183
	ds_read_b128 v[168:171], v152 offset:2048
	ds_read_b128 v[172:175], v152 offset:10256
	ds_read_b128 v[176:179], v152 offset:18464
	ds_read_b128 v[180:183], v152 offset:26672
	s_waitcnt lgkmcnt(4)
	v_fmac_f32_e32 v144, v104, v148
	v_fmac_f32_e32 v144, v105, v149
	v_fmac_f32_e32 v144, v106, v150
	v_fmac_f32_e32 v144, v107, v151
	v_fmac_f32_e32 v145, v104, v186
	v_fmac_f32_e32 v145, v105, v187
	v_fmac_f32_e32 v145, v106, v188
	v_fmac_f32_e32 v145, v107, v189
	v_fmac_f32_e32 v146, v104, v194
	v_fmac_f32_e32 v146, v105, v195
	v_fmac_f32_e32 v146, v106, v196
	v_fmac_f32_e32 v146, v107, v197
	v_fmac_f32_e32 v147, v104, v198
	v_fmac_f32_e32 v147, v105, v199
	v_fmac_f32_e32 v147, v106, v200
	v_fmac_f32_e32 v147, v107, v201
	ds_read_b128 v[148:151], v152 offset:34880
	ds_read_b128 v[186:189], v152 offset:43088
	ds_read_b128 v[194:197], v152 offset:51296
	ds_read_b128 v[198:201], v152 offset:59504
	s_waitcnt lgkmcnt(4)
	v_fmac_f32_e32 v132, v108, v168
	v_fmac_f32_e32 v132, v109, v169
	v_fmac_f32_e32 v132, v110, v170
	v_fmac_f32_e32 v132, v111, v171
	v_fmac_f32_e32 v133, v108, v172
	v_fmac_f32_e32 v133, v109, v173
	v_fmac_f32_e32 v133, v110, v174
	v_fmac_f32_e32 v133, v111, v175
	v_fmac_f32_e32 v134, v108, v176
	v_fmac_f32_e32 v134, v109, v177
	v_fmac_f32_e32 v134, v110, v178
	v_fmac_f32_e32 v134, v111, v179
	v_fmac_f32_e32 v135, v108, v180
	v_fmac_f32_e32 v135, v109, v181
	v_fmac_f32_e32 v135, v110, v182
	v_fmac_f32_e32 v135, v111, v183
	ds_read_b128 v[168:171], v153 offset:2048
	ds_read_b128 v[172:175], v153 offset:10256
	ds_read_b128 v[176:179], v153 offset:18464
	ds_read_b128 v[180:183], v153 offset:26672
	s_waitcnt lgkmcnt(4)
	v_fmac_f32_e32 v136, v108, v148
	v_fmac_f32_e32 v136, v109, v149
	v_fmac_f32_e32 v136, v110, v150
	v_fmac_f32_e32 v136, v111, v151
	v_fmac_f32_e32 v137, v108, v186
	v_fmac_f32_e32 v137, v109, v187
	v_fmac_f32_e32 v137, v110, v188
	v_fmac_f32_e32 v137, v111, v189
	v_fmac_f32_e32 v138, v108, v194
	v_fmac_f32_e32 v138, v109, v195
	v_fmac_f32_e32 v138, v110, v196
	v_fmac_f32_e32 v138, v111, v197
	v_fmac_f32_e32 v139, v108, v198
	v_fmac_f32_e32 v139, v109, v199
	v_fmac_f32_e32 v139, v110, v200
	v_fmac_f32_e32 v139, v111, v201
	ds_read_b128 v[148:151], v153 offset:34880
	ds_read_b128 v[186:189], v153 offset:43088
	ds_read_b128 v[194:197], v153 offset:51296
	ds_read_b128 v[198:201], v153 offset:59504
	s_waitcnt lgkmcnt(4)
	v_fmac_f32_e32 v140, v108, v168
	v_fmac_f32_e32 v140, v109, v169
	v_fmac_f32_e32 v140, v110, v170
	v_fmac_f32_e32 v140, v111, v171
	v_fmac_f32_e32 v141, v108, v172
	v_fmac_f32_e32 v141, v109, v173
	v_fmac_f32_e32 v141, v110, v174
	v_fmac_f32_e32 v141, v111, v175
	v_fmac_f32_e32 v142, v108, v176
	v_fmac_f32_e32 v142, v109, v177
	v_fmac_f32_e32 v142, v110, v178
	v_fmac_f32_e32 v142, v111, v179
	v_fmac_f32_e32 v143, v108, v180
	v_fmac_f32_e32 v143, v109, v181
	v_fmac_f32_e32 v143, v110, v182
	v_fmac_f32_e32 v143, v111, v183
	ds_read_b128 v[168:171], v152 offset:3072
	ds_read_b128 v[172:175], v152 offset:11280
	ds_read_b128 v[176:179], v152 offset:19488
	ds_read_b128 v[180:183], v152 offset:27696
	s_waitcnt lgkmcnt(4)
	v_fmac_f32_e32 v144, v108, v148
	v_fmac_f32_e32 v144, v109, v149
	v_fmac_f32_e32 v144, v110, v150
	v_fmac_f32_e32 v144, v111, v151
	v_fmac_f32_e32 v145, v108, v186
	v_fmac_f32_e32 v145, v109, v187
	v_fmac_f32_e32 v145, v110, v188
	v_fmac_f32_e32 v145, v111, v189
	v_fmac_f32_e32 v146, v108, v194
	v_fmac_f32_e32 v146, v109, v195
	v_fmac_f32_e32 v146, v110, v196
	v_fmac_f32_e32 v146, v111, v197
	v_fmac_f32_e32 v147, v108, v198
	v_fmac_f32_e32 v147, v109, v199
	v_fmac_f32_e32 v147, v110, v200
	v_fmac_f32_e32 v147, v111, v201
	ds_read_b128 v[148:151], v152 offset:35904
	ds_read_b128 v[186:189], v152 offset:44112
	ds_read_b128 v[194:197], v152 offset:52320
	ds_read_b128 v[198:201], v152 offset:60528
	s_waitcnt lgkmcnt(4)
	v_fmac_f32_e32 v132, v112, v168
	v_fmac_f32_e32 v132, v113, v169
	v_fmac_f32_e32 v132, v114, v170
	v_fmac_f32_e32 v132, v115, v171
	v_fmac_f32_e32 v133, v112, v172
	v_fmac_f32_e32 v133, v113, v173
	v_fmac_f32_e32 v133, v114, v174
	v_fmac_f32_e32 v133, v115, v175
	v_fmac_f32_e32 v134, v112, v176
	v_fmac_f32_e32 v134, v113, v177
	v_fmac_f32_e32 v134, v114, v178
	v_fmac_f32_e32 v134, v115, v179
	v_fmac_f32_e32 v135, v112, v180
	v_fmac_f32_e32 v135, v113, v181
	v_fmac_f32_e32 v135, v114, v182
	v_fmac_f32_e32 v135, v115, v183
	ds_read_b128 v[168:171], v153 offset:3072
	ds_read_b128 v[172:175], v153 offset:11280
	ds_read_b128 v[176:179], v153 offset:19488
	ds_read_b128 v[180:183], v153 offset:27696
	s_waitcnt lgkmcnt(4)
	v_fmac_f32_e32 v136, v112, v148
	v_fmac_f32_e32 v136, v113, v149
	v_fmac_f32_e32 v136, v114, v150
	v_fmac_f32_e32 v136, v115, v151
	v_fmac_f32_e32 v137, v112, v186
	v_fmac_f32_e32 v137, v113, v187
	v_fmac_f32_e32 v137, v114, v188
	v_fmac_f32_e32 v137, v115, v189
	v_fmac_f32_e32 v138, v112, v194
	v_fmac_f32_e32 v138, v113, v195
	v_fmac_f32_e32 v138, v114, v196
	v_fmac_f32_e32 v138, v115, v197
	v_fmac_f32_e32 v139, v112, v198
	v_fmac_f32_e32 v139, v113, v199
	v_fmac_f32_e32 v139, v114, v200
	v_fmac_f32_e32 v139, v115, v201
	ds_read_b128 v[148:151], v153 offset:35904
	ds_read_b128 v[186:189], v153 offset:44112
	ds_read_b128 v[194:197], v153 offset:52320
	ds_read_b128 v[198:201], v153 offset:60528
	s_waitcnt lgkmcnt(4)
	v_fmac_f32_e32 v140, v112, v168
	v_fmac_f32_e32 v140, v113, v169
	v_fmac_f32_e32 v140, v114, v170
	v_fmac_f32_e32 v140, v115, v171
	v_fmac_f32_e32 v141, v112, v172
	v_fmac_f32_e32 v141, v113, v173
	v_fmac_f32_e32 v141, v114, v174
	v_fmac_f32_e32 v141, v115, v175
	v_fmac_f32_e32 v142, v112, v176
	v_fmac_f32_e32 v142, v113, v177
	v_fmac_f32_e32 v142, v114, v178
	v_fmac_f32_e32 v142, v115, v179
	v_fmac_f32_e32 v143, v112, v180
	v_fmac_f32_e32 v143, v113, v181
	v_fmac_f32_e32 v143, v114, v182
	v_fmac_f32_e32 v143, v115, v183
	ds_read_b128 v[168:171], v152 offset:4096
	ds_read_b128 v[172:175], v152 offset:12304
	ds_read_b128 v[176:179], v152 offset:20512
	ds_read_b128 v[180:183], v152 offset:28720
	s_waitcnt lgkmcnt(4)
	v_fmac_f32_e32 v144, v112, v148
	v_fmac_f32_e32 v144, v113, v149
	v_fmac_f32_e32 v144, v114, v150
	v_fmac_f32_e32 v144, v115, v151
	v_fmac_f32_e32 v145, v112, v186
	v_fmac_f32_e32 v145, v113, v187
	v_fmac_f32_e32 v145, v114, v188
	v_fmac_f32_e32 v145, v115, v189
	v_fmac_f32_e32 v146, v112, v194
	v_fmac_f32_e32 v146, v113, v195
	v_fmac_f32_e32 v146, v114, v196
	v_fmac_f32_e32 v146, v115, v197
	v_fmac_f32_e32 v147, v112, v198
	v_fmac_f32_e32 v147, v113, v199
	v_fmac_f32_e32 v147, v114, v200
	v_fmac_f32_e32 v147, v115, v201
	ds_read_b128 v[148:151], v152 offset:36928
	ds_read_b128 v[186:189], v152 offset:45136
	ds_read_b128 v[194:197], v152 offset:53344
	ds_read_b128 v[198:201], v152 offset:61552
	s_waitcnt lgkmcnt(4)
	v_fmac_f32_e32 v132, v116, v168
	v_fmac_f32_e32 v132, v117, v169
	v_fmac_f32_e32 v132, v118, v170
	v_fmac_f32_e32 v132, v119, v171
	v_fmac_f32_e32 v133, v116, v172
	v_fmac_f32_e32 v133, v117, v173
	v_fmac_f32_e32 v133, v118, v174
	v_fmac_f32_e32 v133, v119, v175
	v_fmac_f32_e32 v134, v116, v176
	v_fmac_f32_e32 v134, v117, v177
	v_fmac_f32_e32 v134, v118, v178
	v_fmac_f32_e32 v134, v119, v179
	v_fmac_f32_e32 v135, v116, v180
	v_fmac_f32_e32 v135, v117, v181
	v_fmac_f32_e32 v135, v118, v182
	v_fmac_f32_e32 v135, v119, v183
	ds_read_b128 v[168:171], v153 offset:4096
	ds_read_b128 v[172:175], v153 offset:12304
	ds_read_b128 v[176:179], v153 offset:20512
	ds_read_b128 v[180:183], v153 offset:28720
	s_waitcnt lgkmcnt(4)
	v_fmac_f32_e32 v136, v116, v148
	v_fmac_f32_e32 v136, v117, v149
	v_fmac_f32_e32 v136, v118, v150
	v_fmac_f32_e32 v136, v119, v151
	v_fmac_f32_e32 v137, v116, v186
	v_fmac_f32_e32 v137, v117, v187
	v_fmac_f32_e32 v137, v118, v188
	v_fmac_f32_e32 v137, v119, v189
	v_fmac_f32_e32 v138, v116, v194
	v_fmac_f32_e32 v138, v117, v195
	v_fmac_f32_e32 v138, v118, v196
	v_fmac_f32_e32 v138, v119, v197
	v_fmac_f32_e32 v139, v116, v198
	v_fmac_f32_e32 v139, v117, v199
	v_fmac_f32_e32 v139, v118, v200
	v_fmac_f32_e32 v139, v119, v201
	ds_read_b128 v[148:151], v153 offset:36928
	ds_read_b128 v[186:189], v153 offset:45136
	ds_read_b128 v[194:197], v153 offset:53344
	ds_read_b128 v[198:201], v153 offset:61552
	s_waitcnt lgkmcnt(4)
	v_fmac_f32_e32 v140, v116, v168
	v_fmac_f32_e32 v140, v117, v169
	v_fmac_f32_e32 v140, v118, v170
	v_fmac_f32_e32 v140, v119, v171
	v_fmac_f32_e32 v141, v116, v172
	v_fmac_f32_e32 v141, v117, v173
	v_fmac_f32_e32 v141, v118, v174
	v_fmac_f32_e32 v141, v119, v175
	v_fmac_f32_e32 v142, v116, v176
	v_fmac_f32_e32 v142, v117, v177
	v_fmac_f32_e32 v142, v118, v178
	v_fmac_f32_e32 v142, v119, v179
	v_fmac_f32_e32 v143, v116, v180
	v_fmac_f32_e32 v143, v117, v181
	v_fmac_f32_e32 v143, v118, v182
	v_fmac_f32_e32 v143, v119, v183
	ds_read_b128 v[168:171], v152 offset:5120
	ds_read_b128 v[172:175], v152 offset:13328
	ds_read_b128 v[176:179], v152 offset:21536
	ds_read_b128 v[180:183], v152 offset:29744
	s_waitcnt lgkmcnt(4)
	v_fmac_f32_e32 v144, v116, v148
	v_fmac_f32_e32 v144, v117, v149
	v_fmac_f32_e32 v144, v118, v150
	v_fmac_f32_e32 v144, v119, v151
	v_fmac_f32_e32 v145, v116, v186
	v_fmac_f32_e32 v145, v117, v187
	v_fmac_f32_e32 v145, v118, v188
	v_fmac_f32_e32 v145, v119, v189
	v_fmac_f32_e32 v146, v116, v194
	v_fmac_f32_e32 v146, v117, v195
	v_fmac_f32_e32 v146, v118, v196
	v_fmac_f32_e32 v146, v119, v197
	v_fmac_f32_e32 v147, v116, v198
	v_fmac_f32_e32 v147, v117, v199
	v_fmac_f32_e32 v147, v118, v200
	v_fmac_f32_e32 v147, v119, v201
	ds_read_b128 v[148:151], v152 offset:37952
	ds_read_b128 v[186:189], v152 offset:46160
	ds_read_b128 v[194:197], v152 offset:54368
	ds_read_b128 v[198:201], v152 offset:62576
	s_waitcnt lgkmcnt(4)
	v_fmac_f32_e32 v132, v120, v168
	v_fmac_f32_e32 v132, v121, v169
	v_fmac_f32_e32 v132, v122, v170
	v_fmac_f32_e32 v132, v123, v171
	v_fmac_f32_e32 v133, v120, v172
	v_fmac_f32_e32 v133, v121, v173
	v_fmac_f32_e32 v133, v122, v174
	v_fmac_f32_e32 v133, v123, v175
	v_fmac_f32_e32 v134, v120, v176
	v_fmac_f32_e32 v134, v121, v177
	v_fmac_f32_e32 v134, v122, v178
	v_fmac_f32_e32 v134, v123, v179
	v_fmac_f32_e32 v135, v120, v180
	v_fmac_f32_e32 v135, v121, v181
	v_fmac_f32_e32 v135, v122, v182
	v_fmac_f32_e32 v135, v123, v183
	ds_read_b128 v[168:171], v153 offset:5120
	ds_read_b128 v[172:175], v153 offset:13328
	ds_read_b128 v[176:179], v153 offset:21536
	ds_read_b128 v[180:183], v153 offset:29744
	s_waitcnt lgkmcnt(4)
	v_fmac_f32_e32 v136, v120, v148
	v_fmac_f32_e32 v136, v121, v149
	v_fmac_f32_e32 v136, v122, v150
	v_fmac_f32_e32 v136, v123, v151
	v_fmac_f32_e32 v137, v120, v186
	v_fmac_f32_e32 v137, v121, v187
	v_fmac_f32_e32 v137, v122, v188
	v_fmac_f32_e32 v137, v123, v189
	v_fmac_f32_e32 v138, v120, v194
	v_fmac_f32_e32 v138, v121, v195
	v_fmac_f32_e32 v138, v122, v196
	v_fmac_f32_e32 v138, v123, v197
	v_fmac_f32_e32 v139, v120, v198
	v_fmac_f32_e32 v139, v121, v199
	v_fmac_f32_e32 v139, v122, v200
	v_fmac_f32_e32 v139, v123, v201
	ds_read_b128 v[148:151], v153 offset:37952
	ds_read_b128 v[186:189], v153 offset:46160
	ds_read_b128 v[194:197], v153 offset:54368
	ds_read_b128 v[198:201], v153 offset:62576
	s_waitcnt lgkmcnt(4)
	v_fmac_f32_e32 v140, v120, v168
	v_fmac_f32_e32 v140, v121, v169
	v_fmac_f32_e32 v140, v122, v170
	v_fmac_f32_e32 v140, v123, v171
	v_fmac_f32_e32 v141, v120, v172
	v_fmac_f32_e32 v141, v121, v173
	v_fmac_f32_e32 v141, v122, v174
	v_fmac_f32_e32 v141, v123, v175
	v_fmac_f32_e32 v142, v120, v176
	v_fmac_f32_e32 v142, v121, v177
	v_fmac_f32_e32 v142, v122, v178
	v_fmac_f32_e32 v142, v123, v179
	v_fmac_f32_e32 v143, v120, v180
	v_fmac_f32_e32 v143, v121, v181
	v_fmac_f32_e32 v143, v122, v182
	v_fmac_f32_e32 v143, v123, v183
	ds_read_b128 v[168:171], v152 offset:6144
	ds_read_b128 v[172:175], v152 offset:14352
	ds_read_b128 v[176:179], v152 offset:22560
	ds_read_b128 v[180:183], v152 offset:30768
	s_waitcnt lgkmcnt(4)
	v_fmac_f32_e32 v144, v120, v148
	v_fmac_f32_e32 v144, v121, v149
	v_fmac_f32_e32 v144, v122, v150
	v_fmac_f32_e32 v144, v123, v151
	v_fmac_f32_e32 v145, v120, v186
	v_fmac_f32_e32 v145, v121, v187
	v_fmac_f32_e32 v145, v122, v188
	v_fmac_f32_e32 v145, v123, v189
	v_fmac_f32_e32 v146, v120, v194
	v_fmac_f32_e32 v146, v121, v195
	v_fmac_f32_e32 v146, v122, v196
	v_fmac_f32_e32 v146, v123, v197
	v_fmac_f32_e32 v147, v120, v198
	v_fmac_f32_e32 v147, v121, v199
	v_fmac_f32_e32 v147, v122, v200
	v_fmac_f32_e32 v147, v123, v201
	ds_read_b128 v[148:151], v152 offset:38976
	ds_read_b128 v[186:189], v152 offset:47184
	ds_read_b128 v[194:197], v152 offset:55392
	ds_read_b128 v[198:201], v152 offset:63600
	s_waitcnt lgkmcnt(4)
	v_fmac_f32_e32 v132, v124, v168
	v_fmac_f32_e32 v132, v125, v169
	v_fmac_f32_e32 v132, v126, v170
	v_fmac_f32_e32 v132, v127, v171
	v_fmac_f32_e32 v133, v124, v172
	v_fmac_f32_e32 v133, v125, v173
	v_fmac_f32_e32 v133, v126, v174
	v_fmac_f32_e32 v133, v127, v175
	v_fmac_f32_e32 v134, v124, v176
	v_fmac_f32_e32 v134, v125, v177
	v_fmac_f32_e32 v134, v126, v178
	v_fmac_f32_e32 v134, v127, v179
	v_fmac_f32_e32 v135, v124, v180
	v_fmac_f32_e32 v135, v125, v181
	v_fmac_f32_e32 v135, v126, v182
	v_fmac_f32_e32 v135, v127, v183
	ds_read_b128 v[168:171], v153 offset:6144
	ds_read_b128 v[172:175], v153 offset:14352
	ds_read_b128 v[176:179], v153 offset:22560
	ds_read_b128 v[180:183], v153 offset:30768
	s_waitcnt lgkmcnt(4)
	v_fmac_f32_e32 v136, v124, v148
	v_fmac_f32_e32 v136, v125, v149
	v_fmac_f32_e32 v136, v126, v150
	v_fmac_f32_e32 v136, v127, v151
	v_fmac_f32_e32 v137, v124, v186
	v_fmac_f32_e32 v137, v125, v187
	v_fmac_f32_e32 v137, v126, v188
	v_fmac_f32_e32 v137, v127, v189
	v_fmac_f32_e32 v138, v124, v194
	v_fmac_f32_e32 v138, v125, v195
	v_fmac_f32_e32 v138, v126, v196
	v_fmac_f32_e32 v138, v127, v197
	v_fmac_f32_e32 v139, v124, v198
	v_fmac_f32_e32 v139, v125, v199
	v_fmac_f32_e32 v139, v126, v200
	v_fmac_f32_e32 v139, v127, v201
	ds_read_b128 v[148:151], v153 offset:38976
	ds_read_b128 v[186:189], v153 offset:47184
	ds_read_b128 v[194:197], v153 offset:55392
	ds_read_b128 v[198:201], v153 offset:63600
	s_waitcnt lgkmcnt(4)
	v_fmac_f32_e32 v140, v124, v168
	v_fmac_f32_e32 v140, v125, v169
	v_fmac_f32_e32 v140, v126, v170
	v_fmac_f32_e32 v140, v127, v171
	v_fmac_f32_e32 v141, v124, v172
	v_fmac_f32_e32 v141, v125, v173
	v_fmac_f32_e32 v141, v126, v174
	v_fmac_f32_e32 v141, v127, v175
	v_fmac_f32_e32 v142, v124, v176
	v_fmac_f32_e32 v142, v125, v177
	v_fmac_f32_e32 v142, v126, v178
	v_fmac_f32_e32 v142, v127, v179
	v_fmac_f32_e32 v143, v124, v180
	v_fmac_f32_e32 v143, v125, v181
	v_fmac_f32_e32 v143, v126, v182
	v_fmac_f32_e32 v143, v127, v183
	ds_read_b128 v[168:171], v152 offset:7168
	ds_read_b128 v[172:175], v152 offset:15376
	ds_read_b128 v[176:179], v152 offset:23584
	ds_read_b128 v[180:183], v152 offset:31792
	s_waitcnt lgkmcnt(4)
	v_fmac_f32_e32 v144, v124, v148
	v_fmac_f32_e32 v144, v125, v149
	v_fmac_f32_e32 v144, v126, v150
	v_fmac_f32_e32 v144, v127, v151
	v_fmac_f32_e32 v145, v124, v186
	v_fmac_f32_e32 v145, v125, v187
	v_fmac_f32_e32 v145, v126, v188
	v_fmac_f32_e32 v145, v127, v189
	v_fmac_f32_e32 v146, v124, v194
	v_fmac_f32_e32 v146, v125, v195
	v_fmac_f32_e32 v146, v126, v196
	v_fmac_f32_e32 v146, v127, v197
	v_fmac_f32_e32 v147, v124, v198
	v_fmac_f32_e32 v147, v125, v199
	v_fmac_f32_e32 v147, v126, v200
	v_fmac_f32_e32 v147, v127, v201
	ds_read_b128 v[148:151], v152 offset:40000
	ds_read_b128 v[186:189], v152 offset:48208
	ds_read_b128 v[194:197], v152 offset:56416
	ds_read_b128 v[198:201], v152 offset:64624
	s_waitcnt lgkmcnt(4)
	v_fmac_f32_e32 v132, v128, v168
	v_fmac_f32_e32 v132, v129, v169
	v_fmac_f32_e32 v132, v130, v170
	v_fmac_f32_e32 v132, v131, v171
	v_fmac_f32_e32 v133, v128, v172
	v_fmac_f32_e32 v133, v129, v173
	v_fmac_f32_e32 v133, v130, v174
	v_fmac_f32_e32 v133, v131, v175
	v_fmac_f32_e32 v134, v128, v176
	v_fmac_f32_e32 v134, v129, v177
	v_fmac_f32_e32 v134, v130, v178
	v_fmac_f32_e32 v134, v131, v179
	v_fmac_f32_e32 v135, v128, v180
	v_fmac_f32_e32 v135, v129, v181
	v_fmac_f32_e32 v135, v130, v182
	v_fmac_f32_e32 v135, v131, v183
	ds_read_b128 v[168:171], v153 offset:7168
	ds_read_b128 v[172:175], v153 offset:15376
	ds_read_b128 v[176:179], v153 offset:23584
	ds_read_b128 v[180:183], v153 offset:31792
	s_waitcnt lgkmcnt(4)
	v_fmac_f32_e32 v136, v128, v148
	v_fmac_f32_e32 v136, v129, v149
	v_fmac_f32_e32 v136, v130, v150
	v_fmac_f32_e32 v136, v131, v151
	v_fmac_f32_e32 v137, v128, v186
	v_fmac_f32_e32 v137, v129, v187
	v_fmac_f32_e32 v137, v130, v188
	v_fmac_f32_e32 v137, v131, v189
	v_fmac_f32_e32 v138, v128, v194
	v_fmac_f32_e32 v138, v129, v195
	v_fmac_f32_e32 v138, v130, v196
	v_fmac_f32_e32 v138, v131, v197
	v_fmac_f32_e32 v139, v128, v198
	v_fmac_f32_e32 v139, v129, v199
	v_fmac_f32_e32 v139, v130, v200
	v_fmac_f32_e32 v139, v131, v201
	ds_read_b128 v[148:151], v153 offset:40000
	ds_read_b128 v[186:189], v153 offset:48208
	ds_read_b128 v[194:197], v153 offset:56416
	ds_read_b128 v[198:201], v153 offset:64624
	s_waitcnt lgkmcnt(4)
	v_fmac_f32_e32 v140, v128, v168
	v_fmac_f32_e32 v140, v129, v169
	v_fmac_f32_e32 v140, v130, v170
	v_fmac_f32_e32 v140, v131, v171
	v_fmac_f32_e32 v141, v128, v172
	v_fmac_f32_e32 v141, v129, v173
	v_fmac_f32_e32 v141, v130, v174
	v_fmac_f32_e32 v141, v131, v175
	v_fmac_f32_e32 v142, v128, v176
	v_fmac_f32_e32 v142, v129, v177
	v_fmac_f32_e32 v142, v130, v178
	v_fmac_f32_e32 v142, v131, v179
	v_fmac_f32_e32 v143, v128, v180
	v_fmac_f32_e32 v143, v129, v181
	v_fmac_f32_e32 v143, v130, v182
	v_fmac_f32_e32 v143, v131, v183
	s_waitcnt lgkmcnt(0)
	v_fmac_f32_e32 v144, v128, v148
	v_fmac_f32_e32 v144, v129, v149
	v_fmac_f32_e32 v144, v130, v150
	v_fmac_f32_e32 v144, v131, v151
	v_fmac_f32_e32 v145, v128, v186
	v_fmac_f32_e32 v145, v129, v187
	v_fmac_f32_e32 v145, v130, v188
	v_fmac_f32_e32 v145, v131, v189
	v_fmac_f32_e32 v146, v128, v194
	v_fmac_f32_e32 v146, v129, v195
	v_fmac_f32_e32 v146, v130, v196
	v_fmac_f32_e32 v146, v131, v197
	v_fmac_f32_e32 v147, v128, v198
	v_fmac_f32_e32 v147, v129, v199
	v_fmac_f32_e32 v147, v130, v200
	v_fmac_f32_e32 v147, v131, v201
	s_add_i32 s11, s10, 0x3000
	s_lshr_b32 s0, s11, 8
	s_mul_i32 s0, s0, 57
	s_lshr_b32 s0, s0, 9
	s_mul_i32 s1, s0, 0x900
	s_sub_i32 s43, s11, s1
	s_lshl_b32 s1, s11, 13
	s_add_u32 s12, s48, s1
	s_addc_u32 s13, s49, 0
	s_add_u32 s14, s12, 0x1000
	s_addc_u32 s15, s13, 0
	global_load_dwordx4 v[100:103], v1, s[12:13]
	global_load_dwordx4 v[104:107], v1, s[12:13] offset:1024
	global_load_dwordx4 v[108:111], v1, s[12:13] offset:2048
	global_load_dwordx4 v[112:115], v1, s[12:13] offset:3072
	global_load_dwordx4 v[116:119], v1, s[14:15]
	global_load_dwordx4 v[120:123], v1, s[14:15] offset:1024
	global_load_dwordx4 v[124:127], v1, s[14:15] offset:2048
	global_load_dwordx4 v[128:131], v1, s[14:15] offset:3072
	v_cndmask_b32_e64 v242, v133, v132, s[62:63]
	v_cndmask_b32_e64 v132, v132, v133, s[62:63]
	v_cndmask_b32_e64 v243, v135, v134, s[62:63]
	v_cndmask_b32_e64 v134, v134, v135, s[62:63]
	v_cndmask_b32_e64 v244, v137, v136, s[62:63]
	v_cndmask_b32_e64 v136, v136, v137, s[62:63]
	v_cndmask_b32_e64 v245, v139, v138, s[62:63]
	v_cndmask_b32_e64 v138, v138, v139, s[62:63]
	v_cndmask_b32_e64 v246, v141, v140, s[62:63]
	v_cndmask_b32_e64 v140, v140, v141, s[62:63]
	v_cndmask_b32_e64 v248, v143, v142, s[62:63]
	v_cndmask_b32_e64 v142, v142, v143, s[62:63]
	v_cndmask_b32_e64 v249, v145, v144, s[62:63]
	v_cndmask_b32_e64 v144, v144, v145, s[62:63]
	v_cndmask_b32_e64 v250, v147, v146, s[62:63]
	v_cndmask_b32_e64 v146, v146, v147, s[62:63]
	v_add_f32_dpp v132, v242, v132 quad_perm:[1,0,3,2] row_mask:0xf bank_mask:0xf
	v_add_f32_dpp v134, v243, v134 quad_perm:[1,0,3,2] row_mask:0xf bank_mask:0xf
	v_add_f32_dpp v136, v244, v136 quad_perm:[1,0,3,2] row_mask:0xf bank_mask:0xf
	v_add_f32_dpp v138, v245, v138 quad_perm:[1,0,3,2] row_mask:0xf bank_mask:0xf
	v_add_f32_dpp v140, v246, v140 quad_perm:[1,0,3,2] row_mask:0xf bank_mask:0xf
	v_add_f32_dpp v142, v248, v142 quad_perm:[1,0,3,2] row_mask:0xf bank_mask:0xf
	v_add_f32_dpp v144, v249, v144 quad_perm:[1,0,3,2] row_mask:0xf bank_mask:0xf
	v_add_f32_dpp v146, v250, v146 quad_perm:[1,0,3,2] row_mask:0xf bank_mask:0xf
	v_cndmask_b32_e64 v242, v134, v132, s[64:65]
	v_cndmask_b32_e64 v132, v132, v134, s[64:65]
	v_cndmask_b32_e64 v243, v138, v136, s[64:65]
	v_cndmask_b32_e64 v136, v136, v138, s[64:65]
	v_cndmask_b32_e64 v244, v142, v140, s[64:65]
	v_cndmask_b32_e64 v140, v140, v142, s[64:65]
	v_cndmask_b32_e64 v245, v146, v144, s[64:65]
	v_cndmask_b32_e64 v144, v144, v146, s[64:65]
	s_nop 0
	v_add_f32_dpp v132, v242, v132 quad_perm:[2,3,0,1] row_mask:0xf bank_mask:0xf
	v_add_f32_dpp v136, v243, v136 quad_perm:[2,3,0,1] row_mask:0xf bank_mask:0xf
	v_add_f32_dpp v140, v244, v140 quad_perm:[2,3,0,1] row_mask:0xf bank_mask:0xf
	v_add_f32_dpp v144, v245, v144 quad_perm:[2,3,0,1] row_mask:0xf bank_mask:0xf
	v_cndmask_b32_e64 v242, v136, v132, s[66:67]
	v_cndmask_b32_e64 v132, v132, v136, s[66:67]
	v_cndmask_b32_e64 v243, v144, v140, s[66:67]
	v_cndmask_b32_e64 v140, v140, v144, s[66:67]
	s_nop 1
	v_add_f32_dpp v246, v242, v132 row_shl:4 row_mask:0xf bank_mask:0x5
	v_add_f32_dpp v246, v242, v132 row_shr:4 row_mask:0xf bank_mask:0xa
	v_add_f32_dpp v248, v243, v140 row_shl:4 row_mask:0xf bank_mask:0x5
	v_add_f32_dpp v248, v243, v140 row_shr:4 row_mask:0xf bank_mask:0xa
	v_cndmask_b32_e64 v242, v248, v246, s[68:69]
	v_cndmask_b32_e64 v243, v246, v248, s[68:69]
	s_nop 1
	v_add_f32_dpp v191, v242, v243 row_ror:8 row_mask:0xf bank_mask:0xf
	s_nop 0
	ds_bpermute_b32 v193, v165, v191
	s_waitcnt lgkmcnt(0)
	v_add_f32_e32 v191, v191, v193
	ds_bpermute_b32 v193, v166, v191
	s_waitcnt lgkmcnt(0)
	v_add_f32_e32 v191, v191, v193
	v_mov_b32_e32 v193, v191
	s_nop 1
	v_max_f32_dpp v193, v193, v193 quad_perm:[1,0,3,2] row_mask:0xf bank_mask:0xf
	s_nop 1
	v_max_f32_dpp v193, v193, v193 quad_perm:[2,3,0,1] row_mask:0xf bank_mask:0xf
	s_nop 1
	v_max_f32_dpp v193, v193, v193 row_half_mirror row_mask:0xf bank_mask:0xf
	s_nop 1
	v_max_f32_dpp v193, v193, v193 row_mirror row_mask:0xf bank_mask:0xf
	v_sub_f32_e32 v191, v191, v193
	v_mul_f32_e32 v191, 0x3fb8aa3b, v191
	v_exp_f32_e32 v191, v191
	s_nop 0
	v_mov_b32_e32 v193, v191
	s_nop 1
	v_add_f32_dpp v193, v193, v193 quad_perm:[1,0,3,2] row_mask:0xf bank_mask:0xf
	s_nop 1
	v_add_f32_dpp v193, v193, v193 quad_perm:[2,3,0,1] row_mask:0xf bank_mask:0xf
	s_nop 1
	v_add_f32_dpp v193, v193, v193 row_half_mirror row_mask:0xf bank_mask:0xf
	s_nop 1
	v_add_f32_dpp v193, v193, v193 row_mirror row_mask:0xf bank_mask:0xf
	v_rcp_f32_e32 v193, v193
	s_nop 0
	v_mul_f32_e32 v191, v191, v193
	s_mov_b64 exec, 0xffff
	global_store_dword v164, v191, s[34:35]
	s_mov_b64 exec, -1
	s_waitcnt vmcnt(9)
	s_add_i32 s11, s10, 0x2800
	s_lshr_b32 s0, s11, 8
	s_mul_i32 s0, s0, 57
	s_lshr_b32 s0, s0, 9
	s_mul_i32 s1, s0, 0x900
	s_sub_i32 s43, s11, s1
	s_lshl_b32 s1, s11, 12
	s_add_u32 s16, s50, s1
	s_addc_u32 s17, s51, 0
	s_mul_i32 s1, s0, 0x24000
	s_lshl_b32 s2, s43, 2
	s_add_i32 s1, s1, s2
	s_add_u32 s34, s54, s1
	s_addc_u32 s35, s55, 0
	v_mul_f32_e32 v184, v204, v204
	v_fmac_f32_e32 v184, v205, v205
	v_fmac_f32_e32 v184, v206, v206
	v_fmac_f32_e32 v184, v207, v207
	v_fmac_f32_e32 v184, v208, v208
	v_fmac_f32_e32 v184, v209, v209
	v_fmac_f32_e32 v184, v210, v210
	v_fmac_f32_e32 v184, v211, v211
	v_fmac_f32_e32 v184, v212, v212
	v_fmac_f32_e32 v184, v213, v213
	v_fmac_f32_e32 v184, v214, v214
	v_fmac_f32_e32 v184, v215, v215
	v_fmac_f32_e32 v184, v216, v216
	v_fmac_f32_e32 v184, v217, v217
	v_fmac_f32_e32 v184, v218, v218
	v_fmac_f32_e32 v184, v219, v219
	v_fmac_f32_e32 v184, v226, v226
	v_fmac_f32_e32 v184, v227, v227
	v_fmac_f32_e32 v184, v228, v228
	v_fmac_f32_e32 v184, v229, v229
	v_fmac_f32_e32 v184, v230, v230
	v_fmac_f32_e32 v184, v231, v231
	v_fmac_f32_e32 v184, v232, v232
	v_fmac_f32_e32 v184, v233, v233
	v_fmac_f32_e32 v184, v234, v234
	v_fmac_f32_e32 v184, v235, v235
	v_fmac_f32_e32 v184, v236, v236
	v_fmac_f32_e32 v184, v237, v237
	v_fmac_f32_e32 v184, v238, v238
	v_fmac_f32_e32 v184, v239, v239
	v_fmac_f32_e32 v184, v240, v240
	v_fmac_f32_e32 v184, v241, v241
	ds_read_b128 v[168:171], v152 offset:0
	ds_read_b128 v[172:175], v152 offset:8208
	ds_read_b128 v[176:179], v152 offset:16416
	ds_read_b128 v[180:183], v152 offset:24624
	s_nop 0
	v_add_f32_dpp v184, v184, v184 quad_perm:[1,0,3,2] row_mask:0xf bank_mask:0xf
	s_nop 1
	v_add_f32_dpp v184, v184, v184 quad_perm:[2,3,0,1] row_mask:0xf bank_mask:0xf
	s_nop 1
	v_add_f32_dpp v184, v184, v184 row_half_mirror row_mask:0xf bank_mask:0xf
	s_nop 1
	v_add_f32_dpp v184, v184, v184 row_mirror row_mask:0xf bank_mask:0xf
	s_nop 1
	v_readlane_b32 s0, v184, 0
	v_readlane_b32 s1, v184, 16
	v_readlane_b32 s2, v184, 32
	v_readlane_b32 s3, v184, 48
	v_fma_f32 v4, v4, v36, v4
	v_fma_f32 v5, v5, v37, v5
	v_fma_f32 v6, v6, v38, v6
	v_fma_f32 v7, v7, v39, v7
	v_fma_f32 v8, v8, v40, v8
	v_fma_f32 v9, v9, v41, v9
	v_fma_f32 v10, v10, v42, v10
	v_fma_f32 v11, v11, v43, v11
	v_fma_f32 v12, v12, v44, v12
	v_fma_f32 v13, v13, v45, v13
	v_fma_f32 v14, v14, v46, v14
	v_fma_f32 v15, v15, v47, v15
	v_fma_f32 v16, v16, v48, v16
	v_fma_f32 v17, v17, v49, v17
	v_fma_f32 v18, v18, v50, v18
	v_fma_f32 v19, v19, v51, v19
	v_fma_f32 v20, v20, v52, v20
	v_fma_f32 v21, v21, v53, v21
	v_fma_f32 v22, v22, v54, v22
	v_fma_f32 v23, v23, v55, v23
	v_fma_f32 v24, v24, v56, v24
	v_fma_f32 v25, v25, v57, v25
	v_fma_f32 v26, v26, v58, v26
	v_fma_f32 v27, v27, v59, v27
	v_fma_f32 v28, v28, v60, v28
	v_fma_f32 v29, v29, v61, v29
	v_fma_f32 v30, v30, v62, v30
	v_fma_f32 v31, v31, v63, v31
	v_fma_f32 v32, v32, v64, v32
	v_fma_f32 v33, v33, v65, v33
	v_fma_f32 v34, v34, v66, v34
	v_fma_f32 v35, v35, v67, v35
	v_mov_b32_e32 v190, s0
	v_add_f32_e32 v190, s1, v190
	v_add_f32_e32 v190, s2, v190
	v_add_f32_e32 v190, s3, v190
	v_mul_f32_e32 v190, 0x3a000000, v190
	v_add_f32_e32 v190, 0x358637bd, v190
	v_rsq_f32_e32 v190, v190
	s_nop 0
	v_mul_f32_e32 v4, v4, v190
	v_mul_f32_e32 v5, v5, v190
	v_mul_f32_e32 v6, v6, v190
	v_mul_f32_e32 v7, v7, v190
	v_mul_f32_e32 v8, v8, v190
	v_mul_f32_e32 v9, v9, v190
	v_mul_f32_e32 v10, v10, v190
	v_mul_f32_e32 v11, v11, v190
	v_mul_f32_e32 v12, v12, v190
	v_mul_f32_e32 v13, v13, v190
	v_mul_f32_e32 v14, v14, v190
	v_mul_f32_e32 v15, v15, v190
	v_mul_f32_e32 v16, v16, v190
	v_mul_f32_e32 v17, v17, v190
	v_mul_f32_e32 v18, v18, v190
	v_mul_f32_e32 v19, v19, v190
	v_mul_f32_e32 v20, v20, v190
	v_mul_f32_e32 v21, v21, v190
	v_mul_f32_e32 v22, v22, v190
	v_mul_f32_e32 v23, v23, v190
	v_mul_f32_e32 v24, v24, v190
	v_mul_f32_e32 v25, v25, v190
	v_mul_f32_e32 v26, v26, v190
	v_mul_f32_e32 v27, v27, v190
	v_mul_f32_e32 v28, v28, v190
	v_mul_f32_e32 v29, v29, v190
	v_mul_f32_e32 v30, v30, v190
	v_mul_f32_e32 v31, v31, v190
	v_mul_f32_e32 v32, v32, v190
	v_mul_f32_e32 v33, v33, v190
	v_mul_f32_e32 v34, v34, v190
	v_mul_f32_e32 v35, v35, v190
	v_fma_f32 v204, v204, v4, v68
	v_fma_f32 v205, v205, v5, v69
	v_fma_f32 v206, v206, v6, v70
	v_fma_f32 v207, v207, v7, v71
	v_fma_f32 v208, v208, v8, v72
	v_fma_f32 v209, v209, v9, v73
	v_fma_f32 v210, v210, v10, v74
	v_fma_f32 v211, v211, v11, v75
	v_fma_f32 v212, v212, v12, v76
	v_fma_f32 v213, v213, v13, v77
	v_fma_f32 v214, v214, v14, v78
	v_fma_f32 v215, v215, v15, v79
	v_fma_f32 v216, v216, v16, v80
	v_fma_f32 v217, v217, v17, v81
	v_fma_f32 v218, v218, v18, v82
	v_fma_f32 v219, v219, v19, v83
	v_fma_f32 v226, v226, v20, v84
	v_fma_f32 v227, v227, v21, v85
	v_fma_f32 v228, v228, v22, v86
	v_fma_f32 v229, v229, v23, v87
	v_fma_f32 v230, v230, v24, v88
	v_fma_f32 v231, v231, v25, v89
	v_fma_f32 v232, v232, v26, v90
	v_fma_f32 v233, v233, v27, v91
	v_fma_f32 v234, v234, v28, v92
	v_fma_f32 v235, v235, v29, v93
	v_fma_f32 v236, v236, v30, v94
	v_fma_f32 v237, v237, v31, v95
	v_fma_f32 v238, v238, v32, v96
	v_fma_f32 v239, v239, v33, v97
	v_fma_f32 v240, v240, v34, v98
	v_fma_f32 v241, v241, v35, v99
	v_cvt_pk_bf16_f32 v242, v204, v205
	v_cvt_pk_bf16_f32 v243, v206, v207
	global_store_dwordx2 v2, v[242:243], s[16:17]
	v_cvt_pk_bf16_f32 v244, v208, v209
	v_cvt_pk_bf16_f32 v245, v210, v211
	global_store_dwordx2 v2, v[244:245], s[16:17] offset:512
	v_cvt_pk_bf16_f32 v242, v212, v213
	v_cvt_pk_bf16_f32 v243, v214, v215
	global_store_dwordx2 v2, v[242:243], s[16:17] offset:1024
	v_cvt_pk_bf16_f32 v244, v216, v217
	v_cvt_pk_bf16_f32 v245, v218, v219
	global_store_dwordx2 v2, v[244:245], s[16:17] offset:1536
	v_cvt_pk_bf16_f32 v242, v226, v227
	v_cvt_pk_bf16_f32 v243, v228, v229
	global_store_dwordx2 v2, v[242:243], s[16:17] offset:2048
	v_cvt_pk_bf16_f32 v244, v230, v231
	v_cvt_pk_bf16_f32 v245, v232, v233
	global_store_dwordx2 v2, v[244:245], s[16:17] offset:2560
	v_cvt_pk_bf16_f32 v242, v234, v235
	v_cvt_pk_bf16_f32 v243, v236, v237
	global_store_dwordx2 v2, v[242:243], s[16:17] offset:3072
	v_cvt_pk_bf16_f32 v244, v238, v239
	v_cvt_pk_bf16_f32 v245, v240, v241
	global_store_dwordx2 v2, v[244:245], s[16:17] offset:3584
	s_add_i32 s11, s10, 0x3000
	s_lshr_b32 s0, s11, 8
	s_mul_i32 s0, s0, 57
	s_lshr_b32 s0, s0, 9
	s_mul_i32 s1, s0, 0x900
	s_sub_i32 s43, s11, s1
	s_cmpk_lt_u32 s43, 0x100
	s_cselect_b32 s0, 8, s0
	s_mul_i32 s1, s0, 0xc000
	s_add_u32 s18, s52, s1
	s_addc_u32 s19, s53, 0
	s_add_u32 s18, s18, 0x6000
	s_addc_u32 s19, s19, 0
	s_add_u32 s22, s18, 0x1000
	s_addc_u32 s23, s19, 0
	s_add_u32 s28, s18, 0x2000
	s_addc_u32 s29, s19, 0
	s_add_u32 s30, s18, 0x3000
	s_addc_u32 s31, s19, 0
	global_load_dwordx4 v[4:7], v1, s[56:57]
	global_load_dwordx4 v[36:39], v1, s[28:29]
	global_load_dwordx4 v[68:71], v1, s[18:19]
	global_load_dwordx4 v[8:11], v1, s[56:57] offset:1024
	global_load_dwordx4 v[40:43], v1, s[28:29] offset:1024
	global_load_dwordx4 v[72:75], v1, s[18:19] offset:1024
	global_load_dwordx4 v[12:15], v1, s[56:57] offset:2048
	global_load_dwordx4 v[44:47], v1, s[28:29] offset:2048
	global_load_dwordx4 v[76:79], v1, s[18:19] offset:2048
	global_load_dwordx4 v[16:19], v1, s[56:57] offset:3072
	global_load_dwordx4 v[48:51], v1, s[28:29] offset:3072
	global_load_dwordx4 v[80:83], v1, s[18:19] offset:3072
	global_load_dwordx4 v[20:23], v1, s[58:59]
	global_load_dwordx4 v[52:55], v1, s[30:31]
	global_load_dwordx4 v[84:87], v1, s[22:23]
	global_load_dwordx4 v[24:27], v1, s[58:59] offset:1024
	global_load_dwordx4 v[56:59], v1, s[30:31] offset:1024
	global_load_dwordx4 v[88:91], v1, s[22:23] offset:1024
	global_load_dwordx4 v[28:31], v1, s[58:59] offset:2048
	global_load_dwordx4 v[60:63], v1, s[30:31] offset:2048
	global_load_dwordx4 v[92:95], v1, s[22:23] offset:2048
	global_load_dwordx4 v[32:35], v1, s[58:59] offset:3072
	global_load_dwordx4 v[64:67], v1, s[30:31] offset:3072
	global_load_dwordx4 v[96:99], v1, s[22:23] offset:3072
	v_mov_b32_e32 v132, 0
	v_mov_b32_e32 v133, 0
	v_mov_b32_e32 v134, 0
	v_mov_b32_e32 v135, 0
	v_mov_b32_e32 v136, 0
	v_mov_b32_e32 v137, 0
	v_mov_b32_e32 v138, 0
	v_mov_b32_e32 v139, 0
	v_mov_b32_e32 v140, 0
	v_mov_b32_e32 v141, 0
	v_mov_b32_e32 v142, 0
	v_mov_b32_e32 v143, 0
	v_mov_b32_e32 v144, 0
	v_mov_b32_e32 v145, 0
	v_mov_b32_e32 v146, 0
	v_mov_b32_e32 v147, 0
	ds_read_b128 v[148:151], v152 offset:32832
	ds_read_b128 v[186:189], v152 offset:41040
	ds_read_b128 v[194:197], v152 offset:49248
	ds_read_b128 v[198:201], v152 offset:57456
	s_waitcnt lgkmcnt(4)
	v_fmac_f32_e32 v132, v204, v168
	v_fmac_f32_e32 v132, v205, v169
	v_fmac_f32_e32 v132, v206, v170
	v_fmac_f32_e32 v132, v207, v171
	v_fmac_f32_e32 v133, v204, v172
	v_fmac_f32_e32 v133, v205, v173
	v_fmac_f32_e32 v133, v206, v174
	v_fmac_f32_e32 v133, v207, v175
	v_fmac_f32_e32 v134, v204, v176
	v_fmac_f32_e32 v134, v205, v177
	v_fmac_f32_e32 v134, v206, v178
	v_fmac_f32_e32 v134, v207, v179
	v_fmac_f32_e32 v135, v204, v180
	v_fmac_f32_e32 v135, v205, v181
	v_fmac_f32_e32 v135, v206, v182
	v_fmac_f32_e32 v135, v207, v183
	ds_read_b128 v[168:171], v153 offset:0
	ds_read_b128 v[172:175], v153 offset:8208
	ds_read_b128 v[176:179], v153 offset:16416
	ds_read_b128 v[180:183], v153 offset:24624
	s_waitcnt lgkmcnt(4)
	v_fmac_f32_e32 v136, v204, v148
	v_fmac_f32_e32 v136, v205, v149
	v_fmac_f32_e32 v136, v206, v150
	v_fmac_f32_e32 v136, v207, v151
	v_fmac_f32_e32 v137, v204, v186
	v_fmac_f32_e32 v137, v205, v187
	v_fmac_f32_e32 v137, v206, v188
	v_fmac_f32_e32 v137, v207, v189
	v_fmac_f32_e32 v138, v204, v194
	v_fmac_f32_e32 v138, v205, v195
	v_fmac_f32_e32 v138, v206, v196
	v_fmac_f32_e32 v138, v207, v197
	v_fmac_f32_e32 v139, v204, v198
	v_fmac_f32_e32 v139, v205, v199
	v_fmac_f32_e32 v139, v206, v200
	v_fmac_f32_e32 v139, v207, v201
	ds_read_b128 v[148:151], v153 offset:32832
	ds_read_b128 v[186:189], v153 offset:41040
	ds_read_b128 v[194:197], v153 offset:49248
	ds_read_b128 v[198:201], v153 offset:57456
	s_waitcnt lgkmcnt(4)
	v_fmac_f32_e32 v140, v204, v168
	v_fmac_f32_e32 v140, v205, v169
	v_fmac_f32_e32 v140, v206, v170
	v_fmac_f32_e32 v140, v207, v171
	v_fmac_f32_e32 v141, v204, v172
	v_fmac_f32_e32 v141, v205, v173
	v_fmac_f32_e32 v141, v206, v174
	v_fmac_f32_e32 v141, v207, v175
	v_fmac_f32_e32 v142, v204, v176
	v_fmac_f32_e32 v142, v205, v177
	v_fmac_f32_e32 v142, v206, v178
	v_fmac_f32_e32 v142, v207, v179
	v_fmac_f32_e32 v143, v204, v180
	v_fmac_f32_e32 v143, v205, v181
	v_fmac_f32_e32 v143, v206, v182
	v_fmac_f32_e32 v143, v207, v183
	ds_read_b128 v[168:171], v152 offset:1024
	ds_read_b128 v[172:175], v152 offset:9232
	ds_read_b128 v[176:179], v152 offset:17440
	ds_read_b128 v[180:183], v152 offset:25648
	s_waitcnt lgkmcnt(4)
	v_fmac_f32_e32 v144, v204, v148
	v_fmac_f32_e32 v144, v205, v149
	v_fmac_f32_e32 v144, v206, v150
	v_fmac_f32_e32 v144, v207, v151
	v_fmac_f32_e32 v145, v204, v186
	v_fmac_f32_e32 v145, v205, v187
	v_fmac_f32_e32 v145, v206, v188
	v_fmac_f32_e32 v145, v207, v189
	v_fmac_f32_e32 v146, v204, v194
	v_fmac_f32_e32 v146, v205, v195
	v_fmac_f32_e32 v146, v206, v196
	v_fmac_f32_e32 v146, v207, v197
	v_fmac_f32_e32 v147, v204, v198
	v_fmac_f32_e32 v147, v205, v199
	v_fmac_f32_e32 v147, v206, v200
	v_fmac_f32_e32 v147, v207, v201
	ds_read_b128 v[148:151], v152 offset:33856
	ds_read_b128 v[186:189], v152 offset:42064
	ds_read_b128 v[194:197], v152 offset:50272
	ds_read_b128 v[198:201], v152 offset:58480
	s_waitcnt lgkmcnt(4)
	v_fmac_f32_e32 v132, v208, v168
	v_fmac_f32_e32 v132, v209, v169
	v_fmac_f32_e32 v132, v210, v170
	v_fmac_f32_e32 v132, v211, v171
	v_fmac_f32_e32 v133, v208, v172
	v_fmac_f32_e32 v133, v209, v173
	v_fmac_f32_e32 v133, v210, v174
	v_fmac_f32_e32 v133, v211, v175
	v_fmac_f32_e32 v134, v208, v176
	v_fmac_f32_e32 v134, v209, v177
	v_fmac_f32_e32 v134, v210, v178
	v_fmac_f32_e32 v134, v211, v179
	v_fmac_f32_e32 v135, v208, v180
	v_fmac_f32_e32 v135, v209, v181
	v_fmac_f32_e32 v135, v210, v182
	v_fmac_f32_e32 v135, v211, v183
	ds_read_b128 v[168:171], v153 offset:1024
	ds_read_b128 v[172:175], v153 offset:9232
	ds_read_b128 v[176:179], v153 offset:17440
	ds_read_b128 v[180:183], v153 offset:25648
	s_waitcnt lgkmcnt(4)
	v_fmac_f32_e32 v136, v208, v148
	v_fmac_f32_e32 v136, v209, v149
	v_fmac_f32_e32 v136, v210, v150
	v_fmac_f32_e32 v136, v211, v151
	v_fmac_f32_e32 v137, v208, v186
	v_fmac_f32_e32 v137, v209, v187
	v_fmac_f32_e32 v137, v210, v188
	v_fmac_f32_e32 v137, v211, v189
	v_fmac_f32_e32 v138, v208, v194
	v_fmac_f32_e32 v138, v209, v195
	v_fmac_f32_e32 v138, v210, v196
	v_fmac_f32_e32 v138, v211, v197
	v_fmac_f32_e32 v139, v208, v198
	v_fmac_f32_e32 v139, v209, v199
	v_fmac_f32_e32 v139, v210, v200
	v_fmac_f32_e32 v139, v211, v201
	ds_read_b128 v[148:151], v153 offset:33856
	ds_read_b128 v[186:189], v153 offset:42064
	ds_read_b128 v[194:197], v153 offset:50272
	ds_read_b128 v[198:201], v153 offset:58480
	s_waitcnt lgkmcnt(4)
	v_fmac_f32_e32 v140, v208, v168
	v_fmac_f32_e32 v140, v209, v169
	v_fmac_f32_e32 v140, v210, v170
	v_fmac_f32_e32 v140, v211, v171
	v_fmac_f32_e32 v141, v208, v172
	v_fmac_f32_e32 v141, v209, v173
	v_fmac_f32_e32 v141, v210, v174
	v_fmac_f32_e32 v141, v211, v175
	v_fmac_f32_e32 v142, v208, v176
	v_fmac_f32_e32 v142, v209, v177
	v_fmac_f32_e32 v142, v210, v178
	v_fmac_f32_e32 v142, v211, v179
	v_fmac_f32_e32 v143, v208, v180
	v_fmac_f32_e32 v143, v209, v181
	v_fmac_f32_e32 v143, v210, v182
	v_fmac_f32_e32 v143, v211, v183
	ds_read_b128 v[168:171], v152 offset:2048
	ds_read_b128 v[172:175], v152 offset:10256
	ds_read_b128 v[176:179], v152 offset:18464
	ds_read_b128 v[180:183], v152 offset:26672
	s_waitcnt lgkmcnt(4)
	v_fmac_f32_e32 v144, v208, v148
	v_fmac_f32_e32 v144, v209, v149
	v_fmac_f32_e32 v144, v210, v150
	v_fmac_f32_e32 v144, v211, v151
	v_fmac_f32_e32 v145, v208, v186
	v_fmac_f32_e32 v145, v209, v187
	v_fmac_f32_e32 v145, v210, v188
	v_fmac_f32_e32 v145, v211, v189
	v_fmac_f32_e32 v146, v208, v194
	v_fmac_f32_e32 v146, v209, v195
	v_fmac_f32_e32 v146, v210, v196
	v_fmac_f32_e32 v146, v211, v197
	v_fmac_f32_e32 v147, v208, v198
	v_fmac_f32_e32 v147, v209, v199
	v_fmac_f32_e32 v147, v210, v200
	v_fmac_f32_e32 v147, v211, v201
	ds_read_b128 v[148:151], v152 offset:34880
	ds_read_b128 v[186:189], v152 offset:43088
	ds_read_b128 v[194:197], v152 offset:51296
	ds_read_b128 v[198:201], v152 offset:59504
	s_waitcnt lgkmcnt(4)
	v_fmac_f32_e32 v132, v212, v168
	v_fmac_f32_e32 v132, v213, v169
	v_fmac_f32_e32 v132, v214, v170
	v_fmac_f32_e32 v132, v215, v171
	v_fmac_f32_e32 v133, v212, v172
	v_fmac_f32_e32 v133, v213, v173
	v_fmac_f32_e32 v133, v214, v174
	v_fmac_f32_e32 v133, v215, v175
	v_fmac_f32_e32 v134, v212, v176
	v_fmac_f32_e32 v134, v213, v177
	v_fmac_f32_e32 v134, v214, v178
	v_fmac_f32_e32 v134, v215, v179
	v_fmac_f32_e32 v135, v212, v180
	v_fmac_f32_e32 v135, v213, v181
	v_fmac_f32_e32 v135, v214, v182
	v_fmac_f32_e32 v135, v215, v183
	ds_read_b128 v[168:171], v153 offset:2048
	ds_read_b128 v[172:175], v153 offset:10256
	ds_read_b128 v[176:179], v153 offset:18464
	ds_read_b128 v[180:183], v153 offset:26672
	s_waitcnt lgkmcnt(4)
	v_fmac_f32_e32 v136, v212, v148
	v_fmac_f32_e32 v136, v213, v149
	v_fmac_f32_e32 v136, v214, v150
	v_fmac_f32_e32 v136, v215, v151
	v_fmac_f32_e32 v137, v212, v186
	v_fmac_f32_e32 v137, v213, v187
	v_fmac_f32_e32 v137, v214, v188
	v_fmac_f32_e32 v137, v215, v189
	v_fmac_f32_e32 v138, v212, v194
	v_fmac_f32_e32 v138, v213, v195
	v_fmac_f32_e32 v138, v214, v196
	v_fmac_f32_e32 v138, v215, v197
	v_fmac_f32_e32 v139, v212, v198
	v_fmac_f32_e32 v139, v213, v199
	v_fmac_f32_e32 v139, v214, v200
	v_fmac_f32_e32 v139, v215, v201
	ds_read_b128 v[148:151], v153 offset:34880
	ds_read_b128 v[186:189], v153 offset:43088
	ds_read_b128 v[194:197], v153 offset:51296
	ds_read_b128 v[198:201], v153 offset:59504
	s_waitcnt lgkmcnt(4)
	v_fmac_f32_e32 v140, v212, v168
	v_fmac_f32_e32 v140, v213, v169
	v_fmac_f32_e32 v140, v214, v170
	v_fmac_f32_e32 v140, v215, v171
	v_fmac_f32_e32 v141, v212, v172
	v_fmac_f32_e32 v141, v213, v173
	v_fmac_f32_e32 v141, v214, v174
	v_fmac_f32_e32 v141, v215, v175
	v_fmac_f32_e32 v142, v212, v176
	v_fmac_f32_e32 v142, v213, v177
	v_fmac_f32_e32 v142, v214, v178
	v_fmac_f32_e32 v142, v215, v179
	v_fmac_f32_e32 v143, v212, v180
	v_fmac_f32_e32 v143, v213, v181
	v_fmac_f32_e32 v143, v214, v182
	v_fmac_f32_e32 v143, v215, v183
	ds_read_b128 v[168:171], v152 offset:3072
	ds_read_b128 v[172:175], v152 offset:11280
	ds_read_b128 v[176:179], v152 offset:19488
	ds_read_b128 v[180:183], v152 offset:27696
	s_waitcnt lgkmcnt(4)
	v_fmac_f32_e32 v144, v212, v148
	v_fmac_f32_e32 v144, v213, v149
	v_fmac_f32_e32 v144, v214, v150
	v_fmac_f32_e32 v144, v215, v151
	v_fmac_f32_e32 v145, v212, v186
	v_fmac_f32_e32 v145, v213, v187
	v_fmac_f32_e32 v145, v214, v188
	v_fmac_f32_e32 v145, v215, v189
	v_fmac_f32_e32 v146, v212, v194
	v_fmac_f32_e32 v146, v213, v195
	v_fmac_f32_e32 v146, v214, v196
	v_fmac_f32_e32 v146, v215, v197
	v_fmac_f32_e32 v147, v212, v198
	v_fmac_f32_e32 v147, v213, v199
	v_fmac_f32_e32 v147, v214, v200
	v_fmac_f32_e32 v147, v215, v201
	ds_read_b128 v[148:151], v152 offset:35904
	ds_read_b128 v[186:189], v152 offset:44112
	ds_read_b128 v[194:197], v152 offset:52320
	ds_read_b128 v[198:201], v152 offset:60528
	s_waitcnt lgkmcnt(4)
	v_fmac_f32_e32 v132, v216, v168
	v_fmac_f32_e32 v132, v217, v169
	v_fmac_f32_e32 v132, v218, v170
	v_fmac_f32_e32 v132, v219, v171
	v_fmac_f32_e32 v133, v216, v172
	v_fmac_f32_e32 v133, v217, v173
	v_fmac_f32_e32 v133, v218, v174
	v_fmac_f32_e32 v133, v219, v175
	v_fmac_f32_e32 v134, v216, v176
	v_fmac_f32_e32 v134, v217, v177
	v_fmac_f32_e32 v134, v218, v178
	v_fmac_f32_e32 v134, v219, v179
	v_fmac_f32_e32 v135, v216, v180
	v_fmac_f32_e32 v135, v217, v181
	v_fmac_f32_e32 v135, v218, v182
	v_fmac_f32_e32 v135, v219, v183
	ds_read_b128 v[168:171], v153 offset:3072
	ds_read_b128 v[172:175], v153 offset:11280
	ds_read_b128 v[176:179], v153 offset:19488
	ds_read_b128 v[180:183], v153 offset:27696
	s_waitcnt lgkmcnt(4)
	v_fmac_f32_e32 v136, v216, v148
	v_fmac_f32_e32 v136, v217, v149
	v_fmac_f32_e32 v136, v218, v150
	v_fmac_f32_e32 v136, v219, v151
	v_fmac_f32_e32 v137, v216, v186
	v_fmac_f32_e32 v137, v217, v187
	v_fmac_f32_e32 v137, v218, v188
	v_fmac_f32_e32 v137, v219, v189
	v_fmac_f32_e32 v138, v216, v194
	v_fmac_f32_e32 v138, v217, v195
	v_fmac_f32_e32 v138, v218, v196
	v_fmac_f32_e32 v138, v219, v197
	v_fmac_f32_e32 v139, v216, v198
	v_fmac_f32_e32 v139, v217, v199
	v_fmac_f32_e32 v139, v218, v200
	v_fmac_f32_e32 v139, v219, v201
	ds_read_b128 v[148:151], v153 offset:35904
	ds_read_b128 v[186:189], v153 offset:44112
	ds_read_b128 v[194:197], v153 offset:52320
	ds_read_b128 v[198:201], v153 offset:60528
	s_waitcnt lgkmcnt(4)
	v_fmac_f32_e32 v140, v216, v168
	v_fmac_f32_e32 v140, v217, v169
	v_fmac_f32_e32 v140, v218, v170
	v_fmac_f32_e32 v140, v219, v171
	v_fmac_f32_e32 v141, v216, v172
	v_fmac_f32_e32 v141, v217, v173
	v_fmac_f32_e32 v141, v218, v174
	v_fmac_f32_e32 v141, v219, v175
	v_fmac_f32_e32 v142, v216, v176
	v_fmac_f32_e32 v142, v217, v177
	v_fmac_f32_e32 v142, v218, v178
	v_fmac_f32_e32 v142, v219, v179
	v_fmac_f32_e32 v143, v216, v180
	v_fmac_f32_e32 v143, v217, v181
	v_fmac_f32_e32 v143, v218, v182
	v_fmac_f32_e32 v143, v219, v183
	ds_read_b128 v[168:171], v152 offset:4096
	ds_read_b128 v[172:175], v152 offset:12304
	ds_read_b128 v[176:179], v152 offset:20512
	ds_read_b128 v[180:183], v152 offset:28720
	s_waitcnt lgkmcnt(4)
	v_fmac_f32_e32 v144, v216, v148
	v_fmac_f32_e32 v144, v217, v149
	v_fmac_f32_e32 v144, v218, v150
	v_fmac_f32_e32 v144, v219, v151
	v_fmac_f32_e32 v145, v216, v186
	v_fmac_f32_e32 v145, v217, v187
	v_fmac_f32_e32 v145, v218, v188
	v_fmac_f32_e32 v145, v219, v189
	v_fmac_f32_e32 v146, v216, v194
	v_fmac_f32_e32 v146, v217, v195
	v_fmac_f32_e32 v146, v218, v196
	v_fmac_f32_e32 v146, v219, v197
	v_fmac_f32_e32 v147, v216, v198
	v_fmac_f32_e32 v147, v217, v199
	v_fmac_f32_e32 v147, v218, v200
	v_fmac_f32_e32 v147, v219, v201
	ds_read_b128 v[148:151], v152 offset:36928
	ds_read_b128 v[186:189], v152 offset:45136
	ds_read_b128 v[194:197], v152 offset:53344
	ds_read_b128 v[198:201], v152 offset:61552
	s_waitcnt lgkmcnt(4)
	v_fmac_f32_e32 v132, v226, v168
	v_fmac_f32_e32 v132, v227, v169
	v_fmac_f32_e32 v132, v228, v170
	v_fmac_f32_e32 v132, v229, v171
	v_fmac_f32_e32 v133, v226, v172
	v_fmac_f32_e32 v133, v227, v173
	v_fmac_f32_e32 v133, v228, v174
	v_fmac_f32_e32 v133, v229, v175
	v_fmac_f32_e32 v134, v226, v176
	v_fmac_f32_e32 v134, v227, v177
	v_fmac_f32_e32 v134, v228, v178
	v_fmac_f32_e32 v134, v229, v179
	v_fmac_f32_e32 v135, v226, v180
	v_fmac_f32_e32 v135, v227, v181
	v_fmac_f32_e32 v135, v228, v182
	v_fmac_f32_e32 v135, v229, v183
	ds_read_b128 v[168:171], v153 offset:4096
	ds_read_b128 v[172:175], v153 offset:12304
	ds_read_b128 v[176:179], v153 offset:20512
	ds_read_b128 v[180:183], v153 offset:28720
	s_waitcnt lgkmcnt(4)
	v_fmac_f32_e32 v136, v226, v148
	v_fmac_f32_e32 v136, v227, v149
	v_fmac_f32_e32 v136, v228, v150
	v_fmac_f32_e32 v136, v229, v151
	v_fmac_f32_e32 v137, v226, v186
	v_fmac_f32_e32 v137, v227, v187
	v_fmac_f32_e32 v137, v228, v188
	v_fmac_f32_e32 v137, v229, v189
	v_fmac_f32_e32 v138, v226, v194
	v_fmac_f32_e32 v138, v227, v195
	v_fmac_f32_e32 v138, v228, v196
	v_fmac_f32_e32 v138, v229, v197
	v_fmac_f32_e32 v139, v226, v198
	v_fmac_f32_e32 v139, v227, v199
	v_fmac_f32_e32 v139, v228, v200
	v_fmac_f32_e32 v139, v229, v201
	ds_read_b128 v[148:151], v153 offset:36928
	ds_read_b128 v[186:189], v153 offset:45136
	ds_read_b128 v[194:197], v153 offset:53344
	ds_read_b128 v[198:201], v153 offset:61552
	s_waitcnt lgkmcnt(4)
	v_fmac_f32_e32 v140, v226, v168
	v_fmac_f32_e32 v140, v227, v169
	v_fmac_f32_e32 v140, v228, v170
	v_fmac_f32_e32 v140, v229, v171
	v_fmac_f32_e32 v141, v226, v172
	v_fmac_f32_e32 v141, v227, v173
	v_fmac_f32_e32 v141, v228, v174
	v_fmac_f32_e32 v141, v229, v175
	v_fmac_f32_e32 v142, v226, v176
	v_fmac_f32_e32 v142, v227, v177
	v_fmac_f32_e32 v142, v228, v178
	v_fmac_f32_e32 v142, v229, v179
	v_fmac_f32_e32 v143, v226, v180
	v_fmac_f32_e32 v143, v227, v181
	v_fmac_f32_e32 v143, v228, v182
	v_fmac_f32_e32 v143, v229, v183
	ds_read_b128 v[168:171], v152 offset:5120
	ds_read_b128 v[172:175], v152 offset:13328
	ds_read_b128 v[176:179], v152 offset:21536
	ds_read_b128 v[180:183], v152 offset:29744
	s_waitcnt lgkmcnt(4)
	v_fmac_f32_e32 v144, v226, v148
	v_fmac_f32_e32 v144, v227, v149
	v_fmac_f32_e32 v144, v228, v150
	v_fmac_f32_e32 v144, v229, v151
	v_fmac_f32_e32 v145, v226, v186
	v_fmac_f32_e32 v145, v227, v187
	v_fmac_f32_e32 v145, v228, v188
	v_fmac_f32_e32 v145, v229, v189
	v_fmac_f32_e32 v146, v226, v194
	v_fmac_f32_e32 v146, v227, v195
	v_fmac_f32_e32 v146, v228, v196
	v_fmac_f32_e32 v146, v229, v197
	v_fmac_f32_e32 v147, v226, v198
	v_fmac_f32_e32 v147, v227, v199
	v_fmac_f32_e32 v147, v228, v200
	v_fmac_f32_e32 v147, v229, v201
	ds_read_b128 v[148:151], v152 offset:37952
	ds_read_b128 v[186:189], v152 offset:46160
	ds_read_b128 v[194:197], v152 offset:54368
	ds_read_b128 v[198:201], v152 offset:62576
	s_waitcnt lgkmcnt(4)
	v_fmac_f32_e32 v132, v230, v168
	v_fmac_f32_e32 v132, v231, v169
	v_fmac_f32_e32 v132, v232, v170
	v_fmac_f32_e32 v132, v233, v171
	v_fmac_f32_e32 v133, v230, v172
	v_fmac_f32_e32 v133, v231, v173
	v_fmac_f32_e32 v133, v232, v174
	v_fmac_f32_e32 v133, v233, v175
	v_fmac_f32_e32 v134, v230, v176
	v_fmac_f32_e32 v134, v231, v177
	v_fmac_f32_e32 v134, v232, v178
	v_fmac_f32_e32 v134, v233, v179
	v_fmac_f32_e32 v135, v230, v180
	v_fmac_f32_e32 v135, v231, v181
	v_fmac_f32_e32 v135, v232, v182
	v_fmac_f32_e32 v135, v233, v183
	ds_read_b128 v[168:171], v153 offset:5120
	ds_read_b128 v[172:175], v153 offset:13328
	ds_read_b128 v[176:179], v153 offset:21536
	ds_read_b128 v[180:183], v153 offset:29744
	s_waitcnt lgkmcnt(4)
	v_fmac_f32_e32 v136, v230, v148
	v_fmac_f32_e32 v136, v231, v149
	v_fmac_f32_e32 v136, v232, v150
	v_fmac_f32_e32 v136, v233, v151
	v_fmac_f32_e32 v137, v230, v186
	v_fmac_f32_e32 v137, v231, v187
	v_fmac_f32_e32 v137, v232, v188
	v_fmac_f32_e32 v137, v233, v189
	v_fmac_f32_e32 v138, v230, v194
	v_fmac_f32_e32 v138, v231, v195
	v_fmac_f32_e32 v138, v232, v196
	v_fmac_f32_e32 v138, v233, v197
	v_fmac_f32_e32 v139, v230, v198
	v_fmac_f32_e32 v139, v231, v199
	v_fmac_f32_e32 v139, v232, v200
	v_fmac_f32_e32 v139, v233, v201
	ds_read_b128 v[148:151], v153 offset:37952
	ds_read_b128 v[186:189], v153 offset:46160
	ds_read_b128 v[194:197], v153 offset:54368
	ds_read_b128 v[198:201], v153 offset:62576
	s_waitcnt lgkmcnt(4)
	v_fmac_f32_e32 v140, v230, v168
	v_fmac_f32_e32 v140, v231, v169
	v_fmac_f32_e32 v140, v232, v170
	v_fmac_f32_e32 v140, v233, v171
	v_fmac_f32_e32 v141, v230, v172
	v_fmac_f32_e32 v141, v231, v173
	v_fmac_f32_e32 v141, v232, v174
	v_fmac_f32_e32 v141, v233, v175
	v_fmac_f32_e32 v142, v230, v176
	v_fmac_f32_e32 v142, v231, v177
	v_fmac_f32_e32 v142, v232, v178
	v_fmac_f32_e32 v142, v233, v179
	v_fmac_f32_e32 v143, v230, v180
	v_fmac_f32_e32 v143, v231, v181
	v_fmac_f32_e32 v143, v232, v182
	v_fmac_f32_e32 v143, v233, v183
	ds_read_b128 v[168:171], v152 offset:6144
	ds_read_b128 v[172:175], v152 offset:14352
	ds_read_b128 v[176:179], v152 offset:22560
	ds_read_b128 v[180:183], v152 offset:30768
	s_waitcnt lgkmcnt(4)
	v_fmac_f32_e32 v144, v230, v148
	v_fmac_f32_e32 v144, v231, v149
	v_fmac_f32_e32 v144, v232, v150
	v_fmac_f32_e32 v144, v233, v151
	v_fmac_f32_e32 v145, v230, v186
	v_fmac_f32_e32 v145, v231, v187
	v_fmac_f32_e32 v145, v232, v188
	v_fmac_f32_e32 v145, v233, v189
	v_fmac_f32_e32 v146, v230, v194
	v_fmac_f32_e32 v146, v231, v195
	v_fmac_f32_e32 v146, v232, v196
	v_fmac_f32_e32 v146, v233, v197
	v_fmac_f32_e32 v147, v230, v198
	v_fmac_f32_e32 v147, v231, v199
	v_fmac_f32_e32 v147, v232, v200
	v_fmac_f32_e32 v147, v233, v201
	ds_read_b128 v[148:151], v152 offset:38976
	ds_read_b128 v[186:189], v152 offset:47184
	ds_read_b128 v[194:197], v152 offset:55392
	ds_read_b128 v[198:201], v152 offset:63600
	s_waitcnt lgkmcnt(4)
	v_fmac_f32_e32 v132, v234, v168
	v_fmac_f32_e32 v132, v235, v169
	v_fmac_f32_e32 v132, v236, v170
	v_fmac_f32_e32 v132, v237, v171
	v_fmac_f32_e32 v133, v234, v172
	v_fmac_f32_e32 v133, v235, v173
	v_fmac_f32_e32 v133, v236, v174
	v_fmac_f32_e32 v133, v237, v175
	v_fmac_f32_e32 v134, v234, v176
	v_fmac_f32_e32 v134, v235, v177
	v_fmac_f32_e32 v134, v236, v178
	v_fmac_f32_e32 v134, v237, v179
	v_fmac_f32_e32 v135, v234, v180
	v_fmac_f32_e32 v135, v235, v181
	v_fmac_f32_e32 v135, v236, v182
	v_fmac_f32_e32 v135, v237, v183
	ds_read_b128 v[168:171], v153 offset:6144
	ds_read_b128 v[172:175], v153 offset:14352
	ds_read_b128 v[176:179], v153 offset:22560
	ds_read_b128 v[180:183], v153 offset:30768
	s_waitcnt lgkmcnt(4)
	v_fmac_f32_e32 v136, v234, v148
	v_fmac_f32_e32 v136, v235, v149
	v_fmac_f32_e32 v136, v236, v150
	v_fmac_f32_e32 v136, v237, v151
	v_fmac_f32_e32 v137, v234, v186
	v_fmac_f32_e32 v137, v235, v187
	v_fmac_f32_e32 v137, v236, v188
	v_fmac_f32_e32 v137, v237, v189
	v_fmac_f32_e32 v138, v234, v194
	v_fmac_f32_e32 v138, v235, v195
	v_fmac_f32_e32 v138, v236, v196
	v_fmac_f32_e32 v138, v237, v197
	v_fmac_f32_e32 v139, v234, v198
	v_fmac_f32_e32 v139, v235, v199
	v_fmac_f32_e32 v139, v236, v200
	v_fmac_f32_e32 v139, v237, v201
	ds_read_b128 v[148:151], v153 offset:38976
	ds_read_b128 v[186:189], v153 offset:47184
	ds_read_b128 v[194:197], v153 offset:55392
	ds_read_b128 v[198:201], v153 offset:63600
	s_waitcnt lgkmcnt(4)
	v_fmac_f32_e32 v140, v234, v168
	v_fmac_f32_e32 v140, v235, v169
	v_fmac_f32_e32 v140, v236, v170
	v_fmac_f32_e32 v140, v237, v171
	v_fmac_f32_e32 v141, v234, v172
	v_fmac_f32_e32 v141, v235, v173
	v_fmac_f32_e32 v141, v236, v174
	v_fmac_f32_e32 v141, v237, v175
	v_fmac_f32_e32 v142, v234, v176
	v_fmac_f32_e32 v142, v235, v177
	v_fmac_f32_e32 v142, v236, v178
	v_fmac_f32_e32 v142, v237, v179
	v_fmac_f32_e32 v143, v234, v180
	v_fmac_f32_e32 v143, v235, v181
	v_fmac_f32_e32 v143, v236, v182
	v_fmac_f32_e32 v143, v237, v183
	ds_read_b128 v[168:171], v152 offset:7168
	ds_read_b128 v[172:175], v152 offset:15376
	ds_read_b128 v[176:179], v152 offset:23584
	ds_read_b128 v[180:183], v152 offset:31792
	s_waitcnt lgkmcnt(4)
	v_fmac_f32_e32 v144, v234, v148
	v_fmac_f32_e32 v144, v235, v149
	v_fmac_f32_e32 v144, v236, v150
	v_fmac_f32_e32 v144, v237, v151
	v_fmac_f32_e32 v145, v234, v186
	v_fmac_f32_e32 v145, v235, v187
	v_fmac_f32_e32 v145, v236, v188
	v_fmac_f32_e32 v145, v237, v189
	v_fmac_f32_e32 v146, v234, v194
	v_fmac_f32_e32 v146, v235, v195
	v_fmac_f32_e32 v146, v236, v196
	v_fmac_f32_e32 v146, v237, v197
	v_fmac_f32_e32 v147, v234, v198
	v_fmac_f32_e32 v147, v235, v199
	v_fmac_f32_e32 v147, v236, v200
	v_fmac_f32_e32 v147, v237, v201
	ds_read_b128 v[148:151], v152 offset:40000
	ds_read_b128 v[186:189], v152 offset:48208
	ds_read_b128 v[194:197], v152 offset:56416
	ds_read_b128 v[198:201], v152 offset:64624
	s_waitcnt lgkmcnt(4)
	v_fmac_f32_e32 v132, v238, v168
	v_fmac_f32_e32 v132, v239, v169
	v_fmac_f32_e32 v132, v240, v170
	v_fmac_f32_e32 v132, v241, v171
	v_fmac_f32_e32 v133, v238, v172
	v_fmac_f32_e32 v133, v239, v173
	v_fmac_f32_e32 v133, v240, v174
	v_fmac_f32_e32 v133, v241, v175
	v_fmac_f32_e32 v134, v238, v176
	v_fmac_f32_e32 v134, v239, v177
	v_fmac_f32_e32 v134, v240, v178
	v_fmac_f32_e32 v134, v241, v179
	v_fmac_f32_e32 v135, v238, v180
	v_fmac_f32_e32 v135, v239, v181
	v_fmac_f32_e32 v135, v240, v182
	v_fmac_f32_e32 v135, v241, v183
	ds_read_b128 v[168:171], v153 offset:7168
	ds_read_b128 v[172:175], v153 offset:15376
	ds_read_b128 v[176:179], v153 offset:23584
	ds_read_b128 v[180:183], v153 offset:31792
	s_waitcnt lgkmcnt(4)
	v_fmac_f32_e32 v136, v238, v148
	v_fmac_f32_e32 v136, v239, v149
	v_fmac_f32_e32 v136, v240, v150
	v_fmac_f32_e32 v136, v241, v151
	v_fmac_f32_e32 v137, v238, v186
	v_fmac_f32_e32 v137, v239, v187
	v_fmac_f32_e32 v137, v240, v188
	v_fmac_f32_e32 v137, v241, v189
	v_fmac_f32_e32 v138, v238, v194
	v_fmac_f32_e32 v138, v239, v195
	v_fmac_f32_e32 v138, v240, v196
	v_fmac_f32_e32 v138, v241, v197
	v_fmac_f32_e32 v139, v238, v198
	v_fmac_f32_e32 v139, v239, v199
	v_fmac_f32_e32 v139, v240, v200
	v_fmac_f32_e32 v139, v241, v201
	ds_read_b128 v[148:151], v153 offset:40000
	ds_read_b128 v[186:189], v153 offset:48208
	ds_read_b128 v[194:197], v153 offset:56416
	ds_read_b128 v[198:201], v153 offset:64624
	s_waitcnt lgkmcnt(4)
	v_fmac_f32_e32 v140, v238, v168
	v_fmac_f32_e32 v140, v239, v169
	v_fmac_f32_e32 v140, v240, v170
	v_fmac_f32_e32 v140, v241, v171
	v_fmac_f32_e32 v141, v238, v172
	v_fmac_f32_e32 v141, v239, v173
	v_fmac_f32_e32 v141, v240, v174
	v_fmac_f32_e32 v141, v241, v175
	v_fmac_f32_e32 v142, v238, v176
	v_fmac_f32_e32 v142, v239, v177
	v_fmac_f32_e32 v142, v240, v178
	v_fmac_f32_e32 v142, v241, v179
	v_fmac_f32_e32 v143, v238, v180
	v_fmac_f32_e32 v143, v239, v181
	v_fmac_f32_e32 v143, v240, v182
	v_fmac_f32_e32 v143, v241, v183
	s_waitcnt lgkmcnt(0)
	v_fmac_f32_e32 v144, v238, v148
	v_fmac_f32_e32 v144, v239, v149
	v_fmac_f32_e32 v144, v240, v150
	v_fmac_f32_e32 v144, v241, v151
	v_fmac_f32_e32 v145, v238, v186
	v_fmac_f32_e32 v145, v239, v187
	v_fmac_f32_e32 v145, v240, v188
	v_fmac_f32_e32 v145, v241, v189
	v_fmac_f32_e32 v146, v238, v194
	v_fmac_f32_e32 v146, v239, v195
	v_fmac_f32_e32 v146, v240, v196
	v_fmac_f32_e32 v146, v241, v197
	v_fmac_f32_e32 v147, v238, v198
	v_fmac_f32_e32 v147, v239, v199
	v_fmac_f32_e32 v147, v240, v200
	v_fmac_f32_e32 v147, v241, v201
	s_add_i32 s11, s10, 0x3800
	s_lshr_b32 s0, s11, 8
	s_mul_i32 s0, s0, 57
	s_lshr_b32 s0, s0, 9
	s_mul_i32 s1, s0, 0x900
	s_sub_i32 s43, s11, s1
	s_lshl_b32 s1, s11, 13
	s_add_u32 s12, s48, s1
	s_addc_u32 s13, s49, 0
	s_add_u32 s14, s12, 0x1000
	s_addc_u32 s15, s13, 0
	global_load_dwordx4 v[204:207], v1, s[12:13]
	global_load_dwordx4 v[208:211], v1, s[12:13] offset:1024
	global_load_dwordx4 v[212:215], v1, s[12:13] offset:2048
	global_load_dwordx4 v[216:219], v1, s[12:13] offset:3072
	global_load_dwordx4 v[226:229], v1, s[14:15]
	global_load_dwordx4 v[230:233], v1, s[14:15] offset:1024
	global_load_dwordx4 v[234:237], v1, s[14:15] offset:2048
	global_load_dwordx4 v[238:241], v1, s[14:15] offset:3072
	v_cndmask_b32_e64 v242, v133, v132, s[62:63]
	v_cndmask_b32_e64 v132, v132, v133, s[62:63]
	v_cndmask_b32_e64 v243, v135, v134, s[62:63]
	v_cndmask_b32_e64 v134, v134, v135, s[62:63]
	v_cndmask_b32_e64 v244, v137, v136, s[62:63]
	v_cndmask_b32_e64 v136, v136, v137, s[62:63]
	v_cndmask_b32_e64 v245, v139, v138, s[62:63]
	v_cndmask_b32_e64 v138, v138, v139, s[62:63]
	v_cndmask_b32_e64 v246, v141, v140, s[62:63]
	v_cndmask_b32_e64 v140, v140, v141, s[62:63]
	v_cndmask_b32_e64 v248, v143, v142, s[62:63]
	v_cndmask_b32_e64 v142, v142, v143, s[62:63]
	v_cndmask_b32_e64 v249, v145, v144, s[62:63]
	v_cndmask_b32_e64 v144, v144, v145, s[62:63]
	v_cndmask_b32_e64 v250, v147, v146, s[62:63]
	v_cndmask_b32_e64 v146, v146, v147, s[62:63]
	v_add_f32_dpp v132, v242, v132 quad_perm:[1,0,3,2] row_mask:0xf bank_mask:0xf
	v_add_f32_dpp v134, v243, v134 quad_perm:[1,0,3,2] row_mask:0xf bank_mask:0xf
	v_add_f32_dpp v136, v244, v136 quad_perm:[1,0,3,2] row_mask:0xf bank_mask:0xf
	v_add_f32_dpp v138, v245, v138 quad_perm:[1,0,3,2] row_mask:0xf bank_mask:0xf
	v_add_f32_dpp v140, v246, v140 quad_perm:[1,0,3,2] row_mask:0xf bank_mask:0xf
	v_add_f32_dpp v142, v248, v142 quad_perm:[1,0,3,2] row_mask:0xf bank_mask:0xf
	v_add_f32_dpp v144, v249, v144 quad_perm:[1,0,3,2] row_mask:0xf bank_mask:0xf
	v_add_f32_dpp v146, v250, v146 quad_perm:[1,0,3,2] row_mask:0xf bank_mask:0xf
	v_cndmask_b32_e64 v242, v134, v132, s[64:65]
	v_cndmask_b32_e64 v132, v132, v134, s[64:65]
	v_cndmask_b32_e64 v243, v138, v136, s[64:65]
	v_cndmask_b32_e64 v136, v136, v138, s[64:65]
	v_cndmask_b32_e64 v244, v142, v140, s[64:65]
	v_cndmask_b32_e64 v140, v140, v142, s[64:65]
	v_cndmask_b32_e64 v245, v146, v144, s[64:65]
	v_cndmask_b32_e64 v144, v144, v146, s[64:65]
	s_nop 0
	v_add_f32_dpp v132, v242, v132 quad_perm:[2,3,0,1] row_mask:0xf bank_mask:0xf
	v_add_f32_dpp v136, v243, v136 quad_perm:[2,3,0,1] row_mask:0xf bank_mask:0xf
	v_add_f32_dpp v140, v244, v140 quad_perm:[2,3,0,1] row_mask:0xf bank_mask:0xf
	v_add_f32_dpp v144, v245, v144 quad_perm:[2,3,0,1] row_mask:0xf bank_mask:0xf
	v_cndmask_b32_e64 v242, v136, v132, s[66:67]
	v_cndmask_b32_e64 v132, v132, v136, s[66:67]
	v_cndmask_b32_e64 v243, v144, v140, s[66:67]
	v_cndmask_b32_e64 v140, v140, v144, s[66:67]
	s_nop 1
	v_add_f32_dpp v246, v242, v132 row_shl:4 row_mask:0xf bank_mask:0x5
	v_add_f32_dpp v246, v242, v132 row_shr:4 row_mask:0xf bank_mask:0xa
	v_add_f32_dpp v248, v243, v140 row_shl:4 row_mask:0xf bank_mask:0x5
	v_add_f32_dpp v248, v243, v140 row_shr:4 row_mask:0xf bank_mask:0xa
	v_cndmask_b32_e64 v242, v248, v246, s[68:69]
	v_cndmask_b32_e64 v243, v246, v248, s[68:69]
	s_nop 1
	v_add_f32_dpp v191, v242, v243 row_ror:8 row_mask:0xf bank_mask:0xf
	s_nop 0
	ds_bpermute_b32 v193, v165, v191
	s_waitcnt lgkmcnt(0)
	v_add_f32_e32 v191, v191, v193
	ds_bpermute_b32 v193, v166, v191
	s_waitcnt lgkmcnt(0)
	v_add_f32_e32 v191, v191, v193
	v_mov_b32_e32 v193, v191
	s_nop 1
	v_max_f32_dpp v193, v193, v193 quad_perm:[1,0,3,2] row_mask:0xf bank_mask:0xf
	s_nop 1
	v_max_f32_dpp v193, v193, v193 quad_perm:[2,3,0,1] row_mask:0xf bank_mask:0xf
	s_nop 1
	v_max_f32_dpp v193, v193, v193 row_half_mirror row_mask:0xf bank_mask:0xf
	s_nop 1
	v_max_f32_dpp v193, v193, v193 row_mirror row_mask:0xf bank_mask:0xf
	v_sub_f32_e32 v191, v191, v193
	v_mul_f32_e32 v191, 0x3fb8aa3b, v191
	v_exp_f32_e32 v191, v191
	s_nop 0
	v_mov_b32_e32 v193, v191
	s_nop 1
	v_add_f32_dpp v193, v193, v193 quad_perm:[1,0,3,2] row_mask:0xf bank_mask:0xf
	s_nop 1
	v_add_f32_dpp v193, v193, v193 quad_perm:[2,3,0,1] row_mask:0xf bank_mask:0xf
	s_nop 1
	v_add_f32_dpp v193, v193, v193 row_half_mirror row_mask:0xf bank_mask:0xf
	s_nop 1
	v_add_f32_dpp v193, v193, v193 row_mirror row_mask:0xf bank_mask:0xf
	v_rcp_f32_e32 v193, v193
	s_nop 0
	v_mul_f32_e32 v191, v191, v193
	s_mov_b64 exec, 0xffff
	global_store_dword v164, v191, s[34:35]
	s_mov_b64 exec, -1
	s_waitcnt vmcnt(9)
	s_add_i32 s11, s10, 0x3000
	s_lshr_b32 s0, s11, 8
	s_mul_i32 s0, s0, 57
	s_lshr_b32 s0, s0, 9
	s_mul_i32 s1, s0, 0x900
	s_sub_i32 s43, s11, s1
	s_lshl_b32 s1, s11, 12
	s_add_u32 s16, s50, s1
	s_addc_u32 s17, s51, 0
	s_mul_i32 s1, s0, 0x24000
	s_lshl_b32 s2, s43, 2
	s_add_i32 s1, s1, s2
	s_add_u32 s34, s54, s1
	s_addc_u32 s35, s55, 0
	v_mul_f32_e32 v184, v100, v100
	v_fmac_f32_e32 v184, v101, v101
	v_fmac_f32_e32 v184, v102, v102
	v_fmac_f32_e32 v184, v103, v103
	v_fmac_f32_e32 v184, v104, v104
	v_fmac_f32_e32 v184, v105, v105
	v_fmac_f32_e32 v184, v106, v106
	v_fmac_f32_e32 v184, v107, v107
	v_fmac_f32_e32 v184, v108, v108
	v_fmac_f32_e32 v184, v109, v109
	v_fmac_f32_e32 v184, v110, v110
	v_fmac_f32_e32 v184, v111, v111
	v_fmac_f32_e32 v184, v112, v112
	v_fmac_f32_e32 v184, v113, v113
	v_fmac_f32_e32 v184, v114, v114
	v_fmac_f32_e32 v184, v115, v115
	v_fmac_f32_e32 v184, v116, v116
	v_fmac_f32_e32 v184, v117, v117
	v_fmac_f32_e32 v184, v118, v118
	v_fmac_f32_e32 v184, v119, v119
	v_fmac_f32_e32 v184, v120, v120
	v_fmac_f32_e32 v184, v121, v121
	v_fmac_f32_e32 v184, v122, v122
	v_fmac_f32_e32 v184, v123, v123
	v_fmac_f32_e32 v184, v124, v124
	v_fmac_f32_e32 v184, v125, v125
	v_fmac_f32_e32 v184, v126, v126
	v_fmac_f32_e32 v184, v127, v127
	v_fmac_f32_e32 v184, v128, v128
	v_fmac_f32_e32 v184, v129, v129
	v_fmac_f32_e32 v184, v130, v130
	v_fmac_f32_e32 v184, v131, v131
	ds_read_b128 v[168:171], v152 offset:0
	ds_read_b128 v[172:175], v152 offset:8208
	ds_read_b128 v[176:179], v152 offset:16416
	ds_read_b128 v[180:183], v152 offset:24624
	s_nop 0
	v_add_f32_dpp v184, v184, v184 quad_perm:[1,0,3,2] row_mask:0xf bank_mask:0xf
	s_nop 1
	v_add_f32_dpp v184, v184, v184 quad_perm:[2,3,0,1] row_mask:0xf bank_mask:0xf
	s_nop 1
	v_add_f32_dpp v184, v184, v184 row_half_mirror row_mask:0xf bank_mask:0xf
	s_nop 1
	v_add_f32_dpp v184, v184, v184 row_mirror row_mask:0xf bank_mask:0xf
	s_nop 1
	v_readlane_b32 s0, v184, 0
	v_readlane_b32 s1, v184, 16
	v_readlane_b32 s2, v184, 32
	v_readlane_b32 s3, v184, 48
	v_fma_f32 v4, v4, v36, v4
	v_fma_f32 v5, v5, v37, v5
	v_fma_f32 v6, v6, v38, v6
	v_fma_f32 v7, v7, v39, v7
	v_fma_f32 v8, v8, v40, v8
	v_fma_f32 v9, v9, v41, v9
	v_fma_f32 v10, v10, v42, v10
	v_fma_f32 v11, v11, v43, v11
	v_fma_f32 v12, v12, v44, v12
	v_fma_f32 v13, v13, v45, v13
	v_fma_f32 v14, v14, v46, v14
	v_fma_f32 v15, v15, v47, v15
	v_fma_f32 v16, v16, v48, v16
	v_fma_f32 v17, v17, v49, v17
	v_fma_f32 v18, v18, v50, v18
	v_fma_f32 v19, v19, v51, v19
	v_fma_f32 v20, v20, v52, v20
	v_fma_f32 v21, v21, v53, v21
	v_fma_f32 v22, v22, v54, v22
	v_fma_f32 v23, v23, v55, v23
	v_fma_f32 v24, v24, v56, v24
	v_fma_f32 v25, v25, v57, v25
	v_fma_f32 v26, v26, v58, v26
	v_fma_f32 v27, v27, v59, v27
	v_fma_f32 v28, v28, v60, v28
	v_fma_f32 v29, v29, v61, v29
	v_fma_f32 v30, v30, v62, v30
	v_fma_f32 v31, v31, v63, v31
	v_fma_f32 v32, v32, v64, v32
	v_fma_f32 v33, v33, v65, v33
	v_fma_f32 v34, v34, v66, v34
	v_fma_f32 v35, v35, v67, v35
	v_mov_b32_e32 v190, s0
	v_add_f32_e32 v190, s1, v190
	v_add_f32_e32 v190, s2, v190
	v_add_f32_e32 v190, s3, v190
	v_mul_f32_e32 v190, 0x3a000000, v190
	v_add_f32_e32 v190, 0x358637bd, v190
	v_rsq_f32_e32 v190, v190
	s_nop 0
	v_mul_f32_e32 v4, v4, v190
	v_mul_f32_e32 v5, v5, v190
	v_mul_f32_e32 v6, v6, v190
	v_mul_f32_e32 v7, v7, v190
	v_mul_f32_e32 v8, v8, v190
	v_mul_f32_e32 v9, v9, v190
	v_mul_f32_e32 v10, v10, v190
	v_mul_f32_e32 v11, v11, v190
	v_mul_f32_e32 v12, v12, v190
	v_mul_f32_e32 v13, v13, v190
	v_mul_f32_e32 v14, v14, v190
	v_mul_f32_e32 v15, v15, v190
	v_mul_f32_e32 v16, v16, v190
	v_mul_f32_e32 v17, v17, v190
	v_mul_f32_e32 v18, v18, v190
	v_mul_f32_e32 v19, v19, v190
	v_mul_f32_e32 v20, v20, v190
	v_mul_f32_e32 v21, v21, v190
	v_mul_f32_e32 v22, v22, v190
	v_mul_f32_e32 v23, v23, v190
	v_mul_f32_e32 v24, v24, v190
	v_mul_f32_e32 v25, v25, v190
	v_mul_f32_e32 v26, v26, v190
	v_mul_f32_e32 v27, v27, v190
	v_mul_f32_e32 v28, v28, v190
	v_mul_f32_e32 v29, v29, v190
	v_mul_f32_e32 v30, v30, v190
	v_mul_f32_e32 v31, v31, v190
	v_mul_f32_e32 v32, v32, v190
	v_mul_f32_e32 v33, v33, v190
	v_mul_f32_e32 v34, v34, v190
	v_mul_f32_e32 v35, v35, v190
	v_fma_f32 v100, v100, v4, v68
	v_fma_f32 v101, v101, v5, v69
	v_fma_f32 v102, v102, v6, v70
	v_fma_f32 v103, v103, v7, v71
	v_fma_f32 v104, v104, v8, v72
	v_fma_f32 v105, v105, v9, v73
	v_fma_f32 v106, v106, v10, v74
	v_fma_f32 v107, v107, v11, v75
	v_fma_f32 v108, v108, v12, v76
	v_fma_f32 v109, v109, v13, v77
	v_fma_f32 v110, v110, v14, v78
	v_fma_f32 v111, v111, v15, v79
	v_fma_f32 v112, v112, v16, v80
	v_fma_f32 v113, v113, v17, v81
	v_fma_f32 v114, v114, v18, v82
	v_fma_f32 v115, v115, v19, v83
	v_fma_f32 v116, v116, v20, v84
	v_fma_f32 v117, v117, v21, v85
	v_fma_f32 v118, v118, v22, v86
	v_fma_f32 v119, v119, v23, v87
	v_fma_f32 v120, v120, v24, v88
	v_fma_f32 v121, v121, v25, v89
	v_fma_f32 v122, v122, v26, v90
	v_fma_f32 v123, v123, v27, v91
	v_fma_f32 v124, v124, v28, v92
	v_fma_f32 v125, v125, v29, v93
	v_fma_f32 v126, v126, v30, v94
	v_fma_f32 v127, v127, v31, v95
	v_fma_f32 v128, v128, v32, v96
	v_fma_f32 v129, v129, v33, v97
	v_fma_f32 v130, v130, v34, v98
	v_fma_f32 v131, v131, v35, v99
	v_cvt_pk_bf16_f32 v242, v100, v101
	v_cvt_pk_bf16_f32 v243, v102, v103
	global_store_dwordx2 v2, v[242:243], s[16:17]
	v_cvt_pk_bf16_f32 v244, v104, v105
	v_cvt_pk_bf16_f32 v245, v106, v107
	global_store_dwordx2 v2, v[244:245], s[16:17] offset:512
	v_cvt_pk_bf16_f32 v242, v108, v109
	v_cvt_pk_bf16_f32 v243, v110, v111
	global_store_dwordx2 v2, v[242:243], s[16:17] offset:1024
	v_cvt_pk_bf16_f32 v244, v112, v113
	v_cvt_pk_bf16_f32 v245, v114, v115
	global_store_dwordx2 v2, v[244:245], s[16:17] offset:1536
	v_cvt_pk_bf16_f32 v242, v116, v117
	v_cvt_pk_bf16_f32 v243, v118, v119
	global_store_dwordx2 v2, v[242:243], s[16:17] offset:2048
	v_cvt_pk_bf16_f32 v244, v120, v121
	v_cvt_pk_bf16_f32 v245, v122, v123
	global_store_dwordx2 v2, v[244:245], s[16:17] offset:2560
	v_cvt_pk_bf16_f32 v242, v124, v125
	v_cvt_pk_bf16_f32 v243, v126, v127
	global_store_dwordx2 v2, v[242:243], s[16:17] offset:3072
	v_cvt_pk_bf16_f32 v244, v128, v129
	v_cvt_pk_bf16_f32 v245, v130, v131
	global_store_dwordx2 v2, v[244:245], s[16:17] offset:3584
	s_add_i32 s11, s10, 0x3800
	s_lshr_b32 s0, s11, 8
	s_mul_i32 s0, s0, 57
	s_lshr_b32 s0, s0, 9
	s_mul_i32 s1, s0, 0x900
	s_sub_i32 s43, s11, s1
	s_cmpk_lt_u32 s43, 0x100
	s_cselect_b32 s0, 8, s0
	s_mul_i32 s1, s0, 0xc000
	s_add_u32 s18, s52, s1
	s_addc_u32 s19, s53, 0
	s_add_u32 s18, s18, 0x6000
	s_addc_u32 s19, s19, 0
	s_add_u32 s22, s18, 0x1000
	s_addc_u32 s23, s19, 0
	s_add_u32 s28, s18, 0x2000
	s_addc_u32 s29, s19, 0
	s_add_u32 s30, s18, 0x3000
	s_addc_u32 s31, s19, 0
	global_load_dwordx4 v[4:7], v1, s[56:57]
	global_load_dwordx4 v[36:39], v1, s[28:29]
	global_load_dwordx4 v[68:71], v1, s[18:19]
	global_load_dwordx4 v[8:11], v1, s[56:57] offset:1024
	global_load_dwordx4 v[40:43], v1, s[28:29] offset:1024
	global_load_dwordx4 v[72:75], v1, s[18:19] offset:1024
	global_load_dwordx4 v[12:15], v1, s[56:57] offset:2048
	global_load_dwordx4 v[44:47], v1, s[28:29] offset:2048
	global_load_dwordx4 v[76:79], v1, s[18:19] offset:2048
	global_load_dwordx4 v[16:19], v1, s[56:57] offset:3072
	global_load_dwordx4 v[48:51], v1, s[28:29] offset:3072
	global_load_dwordx4 v[80:83], v1, s[18:19] offset:3072
	global_load_dwordx4 v[20:23], v1, s[58:59]
	global_load_dwordx4 v[52:55], v1, s[30:31]
	global_load_dwordx4 v[84:87], v1, s[22:23]
	global_load_dwordx4 v[24:27], v1, s[58:59] offset:1024
	global_load_dwordx4 v[56:59], v1, s[30:31] offset:1024
	global_load_dwordx4 v[88:91], v1, s[22:23] offset:1024
	global_load_dwordx4 v[28:31], v1, s[58:59] offset:2048
	global_load_dwordx4 v[60:63], v1, s[30:31] offset:2048
	global_load_dwordx4 v[92:95], v1, s[22:23] offset:2048
	global_load_dwordx4 v[32:35], v1, s[58:59] offset:3072
	global_load_dwordx4 v[64:67], v1, s[30:31] offset:3072
	global_load_dwordx4 v[96:99], v1, s[22:23] offset:3072
	v_mov_b32_e32 v132, 0
	v_mov_b32_e32 v133, 0
	v_mov_b32_e32 v134, 0
	v_mov_b32_e32 v135, 0
	v_mov_b32_e32 v136, 0
	v_mov_b32_e32 v137, 0
	v_mov_b32_e32 v138, 0
	v_mov_b32_e32 v139, 0
	v_mov_b32_e32 v140, 0
	v_mov_b32_e32 v141, 0
	v_mov_b32_e32 v142, 0
	v_mov_b32_e32 v143, 0
	v_mov_b32_e32 v144, 0
	v_mov_b32_e32 v145, 0
	v_mov_b32_e32 v146, 0
	v_mov_b32_e32 v147, 0
	ds_read_b128 v[148:151], v152 offset:32832
	ds_read_b128 v[186:189], v152 offset:41040
	ds_read_b128 v[194:197], v152 offset:49248
	ds_read_b128 v[198:201], v152 offset:57456
	s_waitcnt lgkmcnt(4)
	v_fmac_f32_e32 v132, v100, v168
	v_fmac_f32_e32 v132, v101, v169
	v_fmac_f32_e32 v132, v102, v170
	v_fmac_f32_e32 v132, v103, v171
	v_fmac_f32_e32 v133, v100, v172
	v_fmac_f32_e32 v133, v101, v173
	v_fmac_f32_e32 v133, v102, v174
	v_fmac_f32_e32 v133, v103, v175
	v_fmac_f32_e32 v134, v100, v176
	v_fmac_f32_e32 v134, v101, v177
	v_fmac_f32_e32 v134, v102, v178
	v_fmac_f32_e32 v134, v103, v179
	v_fmac_f32_e32 v135, v100, v180
	v_fmac_f32_e32 v135, v101, v181
	v_fmac_f32_e32 v135, v102, v182
	v_fmac_f32_e32 v135, v103, v183
	ds_read_b128 v[168:171], v153 offset:0
	ds_read_b128 v[172:175], v153 offset:8208
	ds_read_b128 v[176:179], v153 offset:16416
	ds_read_b128 v[180:183], v153 offset:24624
	s_waitcnt lgkmcnt(4)
	v_fmac_f32_e32 v136, v100, v148
	v_fmac_f32_e32 v136, v101, v149
	v_fmac_f32_e32 v136, v102, v150
	v_fmac_f32_e32 v136, v103, v151
	v_fmac_f32_e32 v137, v100, v186
	v_fmac_f32_e32 v137, v101, v187
	v_fmac_f32_e32 v137, v102, v188
	v_fmac_f32_e32 v137, v103, v189
	v_fmac_f32_e32 v138, v100, v194
	v_fmac_f32_e32 v138, v101, v195
	v_fmac_f32_e32 v138, v102, v196
	v_fmac_f32_e32 v138, v103, v197
	v_fmac_f32_e32 v139, v100, v198
	v_fmac_f32_e32 v139, v101, v199
	v_fmac_f32_e32 v139, v102, v200
	v_fmac_f32_e32 v139, v103, v201
	ds_read_b128 v[148:151], v153 offset:32832
	ds_read_b128 v[186:189], v153 offset:41040
	ds_read_b128 v[194:197], v153 offset:49248
	ds_read_b128 v[198:201], v153 offset:57456
	s_waitcnt lgkmcnt(4)
	v_fmac_f32_e32 v140, v100, v168
	v_fmac_f32_e32 v140, v101, v169
	v_fmac_f32_e32 v140, v102, v170
	v_fmac_f32_e32 v140, v103, v171
	v_fmac_f32_e32 v141, v100, v172
	v_fmac_f32_e32 v141, v101, v173
	v_fmac_f32_e32 v141, v102, v174
	v_fmac_f32_e32 v141, v103, v175
	v_fmac_f32_e32 v142, v100, v176
	v_fmac_f32_e32 v142, v101, v177
	v_fmac_f32_e32 v142, v102, v178
	v_fmac_f32_e32 v142, v103, v179
	v_fmac_f32_e32 v143, v100, v180
	v_fmac_f32_e32 v143, v101, v181
	v_fmac_f32_e32 v143, v102, v182
	v_fmac_f32_e32 v143, v103, v183
	ds_read_b128 v[168:171], v152 offset:1024
	ds_read_b128 v[172:175], v152 offset:9232
	ds_read_b128 v[176:179], v152 offset:17440
	ds_read_b128 v[180:183], v152 offset:25648
	s_waitcnt lgkmcnt(4)
	v_fmac_f32_e32 v144, v100, v148
	v_fmac_f32_e32 v144, v101, v149
	v_fmac_f32_e32 v144, v102, v150
	v_fmac_f32_e32 v144, v103, v151
	v_fmac_f32_e32 v145, v100, v186
	v_fmac_f32_e32 v145, v101, v187
	v_fmac_f32_e32 v145, v102, v188
	v_fmac_f32_e32 v145, v103, v189
	v_fmac_f32_e32 v146, v100, v194
	v_fmac_f32_e32 v146, v101, v195
	v_fmac_f32_e32 v146, v102, v196
	v_fmac_f32_e32 v146, v103, v197
	v_fmac_f32_e32 v147, v100, v198
	v_fmac_f32_e32 v147, v101, v199
	v_fmac_f32_e32 v147, v102, v200
	v_fmac_f32_e32 v147, v103, v201
	ds_read_b128 v[148:151], v152 offset:33856
	ds_read_b128 v[186:189], v152 offset:42064
	ds_read_b128 v[194:197], v152 offset:50272
	ds_read_b128 v[198:201], v152 offset:58480
	s_waitcnt lgkmcnt(4)
	v_fmac_f32_e32 v132, v104, v168
	v_fmac_f32_e32 v132, v105, v169
	v_fmac_f32_e32 v132, v106, v170
	v_fmac_f32_e32 v132, v107, v171
	v_fmac_f32_e32 v133, v104, v172
	v_fmac_f32_e32 v133, v105, v173
	v_fmac_f32_e32 v133, v106, v174
	v_fmac_f32_e32 v133, v107, v175
	v_fmac_f32_e32 v134, v104, v176
	v_fmac_f32_e32 v134, v105, v177
	v_fmac_f32_e32 v134, v106, v178
	v_fmac_f32_e32 v134, v107, v179
	v_fmac_f32_e32 v135, v104, v180
	v_fmac_f32_e32 v135, v105, v181
	v_fmac_f32_e32 v135, v106, v182
	v_fmac_f32_e32 v135, v107, v183
	ds_read_b128 v[168:171], v153 offset:1024
	ds_read_b128 v[172:175], v153 offset:9232
	ds_read_b128 v[176:179], v153 offset:17440
	ds_read_b128 v[180:183], v153 offset:25648
	s_waitcnt lgkmcnt(4)
	v_fmac_f32_e32 v136, v104, v148
	v_fmac_f32_e32 v136, v105, v149
	v_fmac_f32_e32 v136, v106, v150
	v_fmac_f32_e32 v136, v107, v151
	v_fmac_f32_e32 v137, v104, v186
	v_fmac_f32_e32 v137, v105, v187
	v_fmac_f32_e32 v137, v106, v188
	v_fmac_f32_e32 v137, v107, v189
	v_fmac_f32_e32 v138, v104, v194
	v_fmac_f32_e32 v138, v105, v195
	v_fmac_f32_e32 v138, v106, v196
	v_fmac_f32_e32 v138, v107, v197
	v_fmac_f32_e32 v139, v104, v198
	v_fmac_f32_e32 v139, v105, v199
	v_fmac_f32_e32 v139, v106, v200
	v_fmac_f32_e32 v139, v107, v201
	ds_read_b128 v[148:151], v153 offset:33856
	ds_read_b128 v[186:189], v153 offset:42064
	ds_read_b128 v[194:197], v153 offset:50272
	ds_read_b128 v[198:201], v153 offset:58480
	s_waitcnt lgkmcnt(4)
	v_fmac_f32_e32 v140, v104, v168
	v_fmac_f32_e32 v140, v105, v169
	v_fmac_f32_e32 v140, v106, v170
	v_fmac_f32_e32 v140, v107, v171
	v_fmac_f32_e32 v141, v104, v172
	v_fmac_f32_e32 v141, v105, v173
	v_fmac_f32_e32 v141, v106, v174
	v_fmac_f32_e32 v141, v107, v175
	v_fmac_f32_e32 v142, v104, v176
	v_fmac_f32_e32 v142, v105, v177
	v_fmac_f32_e32 v142, v106, v178
	v_fmac_f32_e32 v142, v107, v179
	v_fmac_f32_e32 v143, v104, v180
	v_fmac_f32_e32 v143, v105, v181
	v_fmac_f32_e32 v143, v106, v182
	v_fmac_f32_e32 v143, v107, v183
	ds_read_b128 v[168:171], v152 offset:2048
	ds_read_b128 v[172:175], v152 offset:10256
	ds_read_b128 v[176:179], v152 offset:18464
	ds_read_b128 v[180:183], v152 offset:26672
	s_waitcnt lgkmcnt(4)
	v_fmac_f32_e32 v144, v104, v148
	v_fmac_f32_e32 v144, v105, v149
	v_fmac_f32_e32 v144, v106, v150
	v_fmac_f32_e32 v144, v107, v151
	v_fmac_f32_e32 v145, v104, v186
	v_fmac_f32_e32 v145, v105, v187
	v_fmac_f32_e32 v145, v106, v188
	v_fmac_f32_e32 v145, v107, v189
	v_fmac_f32_e32 v146, v104, v194
	v_fmac_f32_e32 v146, v105, v195
	v_fmac_f32_e32 v146, v106, v196
	v_fmac_f32_e32 v146, v107, v197
	v_fmac_f32_e32 v147, v104, v198
	v_fmac_f32_e32 v147, v105, v199
	v_fmac_f32_e32 v147, v106, v200
	v_fmac_f32_e32 v147, v107, v201
	ds_read_b128 v[148:151], v152 offset:34880
	ds_read_b128 v[186:189], v152 offset:43088
	ds_read_b128 v[194:197], v152 offset:51296
	ds_read_b128 v[198:201], v152 offset:59504
	s_waitcnt lgkmcnt(4)
	v_fmac_f32_e32 v132, v108, v168
	v_fmac_f32_e32 v132, v109, v169
	v_fmac_f32_e32 v132, v110, v170
	v_fmac_f32_e32 v132, v111, v171
	v_fmac_f32_e32 v133, v108, v172
	v_fmac_f32_e32 v133, v109, v173
	v_fmac_f32_e32 v133, v110, v174
	v_fmac_f32_e32 v133, v111, v175
	v_fmac_f32_e32 v134, v108, v176
	v_fmac_f32_e32 v134, v109, v177
	v_fmac_f32_e32 v134, v110, v178
	v_fmac_f32_e32 v134, v111, v179
	v_fmac_f32_e32 v135, v108, v180
	v_fmac_f32_e32 v135, v109, v181
	v_fmac_f32_e32 v135, v110, v182
	v_fmac_f32_e32 v135, v111, v183
	ds_read_b128 v[168:171], v153 offset:2048
	ds_read_b128 v[172:175], v153 offset:10256
	ds_read_b128 v[176:179], v153 offset:18464
	ds_read_b128 v[180:183], v153 offset:26672
	s_waitcnt lgkmcnt(4)
	v_fmac_f32_e32 v136, v108, v148
	v_fmac_f32_e32 v136, v109, v149
	v_fmac_f32_e32 v136, v110, v150
	v_fmac_f32_e32 v136, v111, v151
	v_fmac_f32_e32 v137, v108, v186
	v_fmac_f32_e32 v137, v109, v187
	v_fmac_f32_e32 v137, v110, v188
	v_fmac_f32_e32 v137, v111, v189
	v_fmac_f32_e32 v138, v108, v194
	v_fmac_f32_e32 v138, v109, v195
	v_fmac_f32_e32 v138, v110, v196
	v_fmac_f32_e32 v138, v111, v197
	v_fmac_f32_e32 v139, v108, v198
	v_fmac_f32_e32 v139, v109, v199
	v_fmac_f32_e32 v139, v110, v200
	v_fmac_f32_e32 v139, v111, v201
	ds_read_b128 v[148:151], v153 offset:34880
	ds_read_b128 v[186:189], v153 offset:43088
	ds_read_b128 v[194:197], v153 offset:51296
	ds_read_b128 v[198:201], v153 offset:59504
	s_waitcnt lgkmcnt(4)
	v_fmac_f32_e32 v140, v108, v168
	v_fmac_f32_e32 v140, v109, v169
	v_fmac_f32_e32 v140, v110, v170
	v_fmac_f32_e32 v140, v111, v171
	v_fmac_f32_e32 v141, v108, v172
	v_fmac_f32_e32 v141, v109, v173
	v_fmac_f32_e32 v141, v110, v174
	v_fmac_f32_e32 v141, v111, v175
	v_fmac_f32_e32 v142, v108, v176
	v_fmac_f32_e32 v142, v109, v177
	v_fmac_f32_e32 v142, v110, v178
	v_fmac_f32_e32 v142, v111, v179
	v_fmac_f32_e32 v143, v108, v180
	v_fmac_f32_e32 v143, v109, v181
	v_fmac_f32_e32 v143, v110, v182
	v_fmac_f32_e32 v143, v111, v183
	ds_read_b128 v[168:171], v152 offset:3072
	ds_read_b128 v[172:175], v152 offset:11280
	ds_read_b128 v[176:179], v152 offset:19488
	ds_read_b128 v[180:183], v152 offset:27696
	s_waitcnt lgkmcnt(4)
	v_fmac_f32_e32 v144, v108, v148
	v_fmac_f32_e32 v144, v109, v149
	v_fmac_f32_e32 v144, v110, v150
	v_fmac_f32_e32 v144, v111, v151
	v_fmac_f32_e32 v145, v108, v186
	v_fmac_f32_e32 v145, v109, v187
	v_fmac_f32_e32 v145, v110, v188
	v_fmac_f32_e32 v145, v111, v189
	v_fmac_f32_e32 v146, v108, v194
	v_fmac_f32_e32 v146, v109, v195
	v_fmac_f32_e32 v146, v110, v196
	v_fmac_f32_e32 v146, v111, v197
	v_fmac_f32_e32 v147, v108, v198
	v_fmac_f32_e32 v147, v109, v199
	v_fmac_f32_e32 v147, v110, v200
	v_fmac_f32_e32 v147, v111, v201
	ds_read_b128 v[148:151], v152 offset:35904
	ds_read_b128 v[186:189], v152 offset:44112
	ds_read_b128 v[194:197], v152 offset:52320
	ds_read_b128 v[198:201], v152 offset:60528
	s_waitcnt lgkmcnt(4)
	v_fmac_f32_e32 v132, v112, v168
	v_fmac_f32_e32 v132, v113, v169
	v_fmac_f32_e32 v132, v114, v170
	v_fmac_f32_e32 v132, v115, v171
	v_fmac_f32_e32 v133, v112, v172
	v_fmac_f32_e32 v133, v113, v173
	v_fmac_f32_e32 v133, v114, v174
	v_fmac_f32_e32 v133, v115, v175
	v_fmac_f32_e32 v134, v112, v176
	v_fmac_f32_e32 v134, v113, v177
	v_fmac_f32_e32 v134, v114, v178
	v_fmac_f32_e32 v134, v115, v179
	v_fmac_f32_e32 v135, v112, v180
	v_fmac_f32_e32 v135, v113, v181
	v_fmac_f32_e32 v135, v114, v182
	v_fmac_f32_e32 v135, v115, v183
	ds_read_b128 v[168:171], v153 offset:3072
	ds_read_b128 v[172:175], v153 offset:11280
	ds_read_b128 v[176:179], v153 offset:19488
	ds_read_b128 v[180:183], v153 offset:27696
	s_waitcnt lgkmcnt(4)
	v_fmac_f32_e32 v136, v112, v148
	v_fmac_f32_e32 v136, v113, v149
	v_fmac_f32_e32 v136, v114, v150
	v_fmac_f32_e32 v136, v115, v151
	v_fmac_f32_e32 v137, v112, v186
	v_fmac_f32_e32 v137, v113, v187
	v_fmac_f32_e32 v137, v114, v188
	v_fmac_f32_e32 v137, v115, v189
	v_fmac_f32_e32 v138, v112, v194
	v_fmac_f32_e32 v138, v113, v195
	v_fmac_f32_e32 v138, v114, v196
	v_fmac_f32_e32 v138, v115, v197
	v_fmac_f32_e32 v139, v112, v198
	v_fmac_f32_e32 v139, v113, v199
	v_fmac_f32_e32 v139, v114, v200
	v_fmac_f32_e32 v139, v115, v201
	ds_read_b128 v[148:151], v153 offset:35904
	ds_read_b128 v[186:189], v153 offset:44112
	ds_read_b128 v[194:197], v153 offset:52320
	ds_read_b128 v[198:201], v153 offset:60528
	s_waitcnt lgkmcnt(4)
	v_fmac_f32_e32 v140, v112, v168
	v_fmac_f32_e32 v140, v113, v169
	v_fmac_f32_e32 v140, v114, v170
	v_fmac_f32_e32 v140, v115, v171
	v_fmac_f32_e32 v141, v112, v172
	v_fmac_f32_e32 v141, v113, v173
	v_fmac_f32_e32 v141, v114, v174
	v_fmac_f32_e32 v141, v115, v175
	v_fmac_f32_e32 v142, v112, v176
	v_fmac_f32_e32 v142, v113, v177
	v_fmac_f32_e32 v142, v114, v178
	v_fmac_f32_e32 v142, v115, v179
	v_fmac_f32_e32 v143, v112, v180
	v_fmac_f32_e32 v143, v113, v181
	v_fmac_f32_e32 v143, v114, v182
	v_fmac_f32_e32 v143, v115, v183
	ds_read_b128 v[168:171], v152 offset:4096
	ds_read_b128 v[172:175], v152 offset:12304
	ds_read_b128 v[176:179], v152 offset:20512
	ds_read_b128 v[180:183], v152 offset:28720
	s_waitcnt lgkmcnt(4)
	v_fmac_f32_e32 v144, v112, v148
	v_fmac_f32_e32 v144, v113, v149
	v_fmac_f32_e32 v144, v114, v150
	v_fmac_f32_e32 v144, v115, v151
	v_fmac_f32_e32 v145, v112, v186
	v_fmac_f32_e32 v145, v113, v187
	v_fmac_f32_e32 v145, v114, v188
	v_fmac_f32_e32 v145, v115, v189
	v_fmac_f32_e32 v146, v112, v194
	v_fmac_f32_e32 v146, v113, v195
	v_fmac_f32_e32 v146, v114, v196
	v_fmac_f32_e32 v146, v115, v197
	v_fmac_f32_e32 v147, v112, v198
	v_fmac_f32_e32 v147, v113, v199
	v_fmac_f32_e32 v147, v114, v200
	v_fmac_f32_e32 v147, v115, v201
	ds_read_b128 v[148:151], v152 offset:36928
	ds_read_b128 v[186:189], v152 offset:45136
	ds_read_b128 v[194:197], v152 offset:53344
	ds_read_b128 v[198:201], v152 offset:61552
	s_waitcnt lgkmcnt(4)
	v_fmac_f32_e32 v132, v116, v168
	v_fmac_f32_e32 v132, v117, v169
	v_fmac_f32_e32 v132, v118, v170
	v_fmac_f32_e32 v132, v119, v171
	v_fmac_f32_e32 v133, v116, v172
	v_fmac_f32_e32 v133, v117, v173
	v_fmac_f32_e32 v133, v118, v174
	v_fmac_f32_e32 v133, v119, v175
	v_fmac_f32_e32 v134, v116, v176
	v_fmac_f32_e32 v134, v117, v177
	v_fmac_f32_e32 v134, v118, v178
	v_fmac_f32_e32 v134, v119, v179
	v_fmac_f32_e32 v135, v116, v180
	v_fmac_f32_e32 v135, v117, v181
	v_fmac_f32_e32 v135, v118, v182
	v_fmac_f32_e32 v135, v119, v183
	ds_read_b128 v[168:171], v153 offset:4096
	ds_read_b128 v[172:175], v153 offset:12304
	ds_read_b128 v[176:179], v153 offset:20512
	ds_read_b128 v[180:183], v153 offset:28720
	s_waitcnt lgkmcnt(4)
	v_fmac_f32_e32 v136, v116, v148
	v_fmac_f32_e32 v136, v117, v149
	v_fmac_f32_e32 v136, v118, v150
	v_fmac_f32_e32 v136, v119, v151
	v_fmac_f32_e32 v137, v116, v186
	v_fmac_f32_e32 v137, v117, v187
	v_fmac_f32_e32 v137, v118, v188
	v_fmac_f32_e32 v137, v119, v189
	v_fmac_f32_e32 v138, v116, v194
	v_fmac_f32_e32 v138, v117, v195
	v_fmac_f32_e32 v138, v118, v196
	v_fmac_f32_e32 v138, v119, v197
	v_fmac_f32_e32 v139, v116, v198
	v_fmac_f32_e32 v139, v117, v199
	v_fmac_f32_e32 v139, v118, v200
	v_fmac_f32_e32 v139, v119, v201
	ds_read_b128 v[148:151], v153 offset:36928
	ds_read_b128 v[186:189], v153 offset:45136
	ds_read_b128 v[194:197], v153 offset:53344
	ds_read_b128 v[198:201], v153 offset:61552
	s_waitcnt lgkmcnt(4)
	v_fmac_f32_e32 v140, v116, v168
	v_fmac_f32_e32 v140, v117, v169
	v_fmac_f32_e32 v140, v118, v170
	v_fmac_f32_e32 v140, v119, v171
	v_fmac_f32_e32 v141, v116, v172
	v_fmac_f32_e32 v141, v117, v173
	v_fmac_f32_e32 v141, v118, v174
	v_fmac_f32_e32 v141, v119, v175
	v_fmac_f32_e32 v142, v116, v176
	v_fmac_f32_e32 v142, v117, v177
	v_fmac_f32_e32 v142, v118, v178
	v_fmac_f32_e32 v142, v119, v179
	v_fmac_f32_e32 v143, v116, v180
	v_fmac_f32_e32 v143, v117, v181
	v_fmac_f32_e32 v143, v118, v182
	v_fmac_f32_e32 v143, v119, v183
	ds_read_b128 v[168:171], v152 offset:5120
	ds_read_b128 v[172:175], v152 offset:13328
	ds_read_b128 v[176:179], v152 offset:21536
	ds_read_b128 v[180:183], v152 offset:29744
	s_waitcnt lgkmcnt(4)
	v_fmac_f32_e32 v144, v116, v148
	v_fmac_f32_e32 v144, v117, v149
	v_fmac_f32_e32 v144, v118, v150
	v_fmac_f32_e32 v144, v119, v151
	v_fmac_f32_e32 v145, v116, v186
	v_fmac_f32_e32 v145, v117, v187
	v_fmac_f32_e32 v145, v118, v188
	v_fmac_f32_e32 v145, v119, v189
	v_fmac_f32_e32 v146, v116, v194
	v_fmac_f32_e32 v146, v117, v195
	v_fmac_f32_e32 v146, v118, v196
	v_fmac_f32_e32 v146, v119, v197
	v_fmac_f32_e32 v147, v116, v198
	v_fmac_f32_e32 v147, v117, v199
	v_fmac_f32_e32 v147, v118, v200
	v_fmac_f32_e32 v147, v119, v201
	ds_read_b128 v[148:151], v152 offset:37952
	ds_read_b128 v[186:189], v152 offset:46160
	ds_read_b128 v[194:197], v152 offset:54368
	ds_read_b128 v[198:201], v152 offset:62576
	s_waitcnt lgkmcnt(4)
	v_fmac_f32_e32 v132, v120, v168
	v_fmac_f32_e32 v132, v121, v169
	v_fmac_f32_e32 v132, v122, v170
	v_fmac_f32_e32 v132, v123, v171
	v_fmac_f32_e32 v133, v120, v172
	v_fmac_f32_e32 v133, v121, v173
	v_fmac_f32_e32 v133, v122, v174
	v_fmac_f32_e32 v133, v123, v175
	v_fmac_f32_e32 v134, v120, v176
	v_fmac_f32_e32 v134, v121, v177
	v_fmac_f32_e32 v134, v122, v178
	v_fmac_f32_e32 v134, v123, v179
	v_fmac_f32_e32 v135, v120, v180
	v_fmac_f32_e32 v135, v121, v181
	v_fmac_f32_e32 v135, v122, v182
	v_fmac_f32_e32 v135, v123, v183
	ds_read_b128 v[168:171], v153 offset:5120
	ds_read_b128 v[172:175], v153 offset:13328
	ds_read_b128 v[176:179], v153 offset:21536
	ds_read_b128 v[180:183], v153 offset:29744
	s_waitcnt lgkmcnt(4)
	v_fmac_f32_e32 v136, v120, v148
	v_fmac_f32_e32 v136, v121, v149
	v_fmac_f32_e32 v136, v122, v150
	v_fmac_f32_e32 v136, v123, v151
	v_fmac_f32_e32 v137, v120, v186
	v_fmac_f32_e32 v137, v121, v187
	v_fmac_f32_e32 v137, v122, v188
	v_fmac_f32_e32 v137, v123, v189
	v_fmac_f32_e32 v138, v120, v194
	v_fmac_f32_e32 v138, v121, v195
	v_fmac_f32_e32 v138, v122, v196
	v_fmac_f32_e32 v138, v123, v197
	v_fmac_f32_e32 v139, v120, v198
	v_fmac_f32_e32 v139, v121, v199
	v_fmac_f32_e32 v139, v122, v200
	v_fmac_f32_e32 v139, v123, v201
	ds_read_b128 v[148:151], v153 offset:37952
	ds_read_b128 v[186:189], v153 offset:46160
	ds_read_b128 v[194:197], v153 offset:54368
	ds_read_b128 v[198:201], v153 offset:62576
	s_waitcnt lgkmcnt(4)
	v_fmac_f32_e32 v140, v120, v168
	v_fmac_f32_e32 v140, v121, v169
	v_fmac_f32_e32 v140, v122, v170
	v_fmac_f32_e32 v140, v123, v171
	v_fmac_f32_e32 v141, v120, v172
	v_fmac_f32_e32 v141, v121, v173
	v_fmac_f32_e32 v141, v122, v174
	v_fmac_f32_e32 v141, v123, v175
	v_fmac_f32_e32 v142, v120, v176
	v_fmac_f32_e32 v142, v121, v177
	v_fmac_f32_e32 v142, v122, v178
	v_fmac_f32_e32 v142, v123, v179
	v_fmac_f32_e32 v143, v120, v180
	v_fmac_f32_e32 v143, v121, v181
	v_fmac_f32_e32 v143, v122, v182
	v_fmac_f32_e32 v143, v123, v183
	ds_read_b128 v[168:171], v152 offset:6144
	ds_read_b128 v[172:175], v152 offset:14352
	ds_read_b128 v[176:179], v152 offset:22560
	ds_read_b128 v[180:183], v152 offset:30768
	s_waitcnt lgkmcnt(4)
	v_fmac_f32_e32 v144, v120, v148
	v_fmac_f32_e32 v144, v121, v149
	v_fmac_f32_e32 v144, v122, v150
	v_fmac_f32_e32 v144, v123, v151
	v_fmac_f32_e32 v145, v120, v186
	v_fmac_f32_e32 v145, v121, v187
	v_fmac_f32_e32 v145, v122, v188
	v_fmac_f32_e32 v145, v123, v189
	v_fmac_f32_e32 v146, v120, v194
	v_fmac_f32_e32 v146, v121, v195
	v_fmac_f32_e32 v146, v122, v196
	v_fmac_f32_e32 v146, v123, v197
	v_fmac_f32_e32 v147, v120, v198
	v_fmac_f32_e32 v147, v121, v199
	v_fmac_f32_e32 v147, v122, v200
	v_fmac_f32_e32 v147, v123, v201
	ds_read_b128 v[148:151], v152 offset:38976
	ds_read_b128 v[186:189], v152 offset:47184
	ds_read_b128 v[194:197], v152 offset:55392
	ds_read_b128 v[198:201], v152 offset:63600
	s_waitcnt lgkmcnt(4)
	v_fmac_f32_e32 v132, v124, v168
	v_fmac_f32_e32 v132, v125, v169
	v_fmac_f32_e32 v132, v126, v170
	v_fmac_f32_e32 v132, v127, v171
	v_fmac_f32_e32 v133, v124, v172
	v_fmac_f32_e32 v133, v125, v173
	v_fmac_f32_e32 v133, v126, v174
	v_fmac_f32_e32 v133, v127, v175
	v_fmac_f32_e32 v134, v124, v176
	v_fmac_f32_e32 v134, v125, v177
	v_fmac_f32_e32 v134, v126, v178
	v_fmac_f32_e32 v134, v127, v179
	v_fmac_f32_e32 v135, v124, v180
	v_fmac_f32_e32 v135, v125, v181
	v_fmac_f32_e32 v135, v126, v182
	v_fmac_f32_e32 v135, v127, v183
	ds_read_b128 v[168:171], v153 offset:6144
	ds_read_b128 v[172:175], v153 offset:14352
	ds_read_b128 v[176:179], v153 offset:22560
	ds_read_b128 v[180:183], v153 offset:30768
	s_waitcnt lgkmcnt(4)
	v_fmac_f32_e32 v136, v124, v148
	v_fmac_f32_e32 v136, v125, v149
	v_fmac_f32_e32 v136, v126, v150
	v_fmac_f32_e32 v136, v127, v151
	v_fmac_f32_e32 v137, v124, v186
	v_fmac_f32_e32 v137, v125, v187
	v_fmac_f32_e32 v137, v126, v188
	v_fmac_f32_e32 v137, v127, v189
	v_fmac_f32_e32 v138, v124, v194
	v_fmac_f32_e32 v138, v125, v195
	v_fmac_f32_e32 v138, v126, v196
	v_fmac_f32_e32 v138, v127, v197
	v_fmac_f32_e32 v139, v124, v198
	v_fmac_f32_e32 v139, v125, v199
	v_fmac_f32_e32 v139, v126, v200
	v_fmac_f32_e32 v139, v127, v201
	ds_read_b128 v[148:151], v153 offset:38976
	ds_read_b128 v[186:189], v153 offset:47184
	ds_read_b128 v[194:197], v153 offset:55392
	ds_read_b128 v[198:201], v153 offset:63600
	s_waitcnt lgkmcnt(4)
	v_fmac_f32_e32 v140, v124, v168
	v_fmac_f32_e32 v140, v125, v169
	v_fmac_f32_e32 v140, v126, v170
	v_fmac_f32_e32 v140, v127, v171
	v_fmac_f32_e32 v141, v124, v172
	v_fmac_f32_e32 v141, v125, v173
	v_fmac_f32_e32 v141, v126, v174
	v_fmac_f32_e32 v141, v127, v175
	v_fmac_f32_e32 v142, v124, v176
	v_fmac_f32_e32 v142, v125, v177
	v_fmac_f32_e32 v142, v126, v178
	v_fmac_f32_e32 v142, v127, v179
	v_fmac_f32_e32 v143, v124, v180
	v_fmac_f32_e32 v143, v125, v181
	v_fmac_f32_e32 v143, v126, v182
	v_fmac_f32_e32 v143, v127, v183
	ds_read_b128 v[168:171], v152 offset:7168
	ds_read_b128 v[172:175], v152 offset:15376
	ds_read_b128 v[176:179], v152 offset:23584
	ds_read_b128 v[180:183], v152 offset:31792
	s_waitcnt lgkmcnt(4)
	v_fmac_f32_e32 v144, v124, v148
	v_fmac_f32_e32 v144, v125, v149
	v_fmac_f32_e32 v144, v126, v150
	v_fmac_f32_e32 v144, v127, v151
	v_fmac_f32_e32 v145, v124, v186
	v_fmac_f32_e32 v145, v125, v187
	v_fmac_f32_e32 v145, v126, v188
	v_fmac_f32_e32 v145, v127, v189
	v_fmac_f32_e32 v146, v124, v194
	v_fmac_f32_e32 v146, v125, v195
	v_fmac_f32_e32 v146, v126, v196
	v_fmac_f32_e32 v146, v127, v197
	v_fmac_f32_e32 v147, v124, v198
	v_fmac_f32_e32 v147, v125, v199
	v_fmac_f32_e32 v147, v126, v200
	v_fmac_f32_e32 v147, v127, v201
	ds_read_b128 v[148:151], v152 offset:40000
	ds_read_b128 v[186:189], v152 offset:48208
	ds_read_b128 v[194:197], v152 offset:56416
	ds_read_b128 v[198:201], v152 offset:64624
	s_waitcnt lgkmcnt(4)
	v_fmac_f32_e32 v132, v128, v168
	v_fmac_f32_e32 v132, v129, v169
	v_fmac_f32_e32 v132, v130, v170
	v_fmac_f32_e32 v132, v131, v171
	v_fmac_f32_e32 v133, v128, v172
	v_fmac_f32_e32 v133, v129, v173
	v_fmac_f32_e32 v133, v130, v174
	v_fmac_f32_e32 v133, v131, v175
	v_fmac_f32_e32 v134, v128, v176
	v_fmac_f32_e32 v134, v129, v177
	v_fmac_f32_e32 v134, v130, v178
	v_fmac_f32_e32 v134, v131, v179
	v_fmac_f32_e32 v135, v128, v180
	v_fmac_f32_e32 v135, v129, v181
	v_fmac_f32_e32 v135, v130, v182
	v_fmac_f32_e32 v135, v131, v183
	ds_read_b128 v[168:171], v153 offset:7168
	ds_read_b128 v[172:175], v153 offset:15376
	ds_read_b128 v[176:179], v153 offset:23584
	ds_read_b128 v[180:183], v153 offset:31792
	s_waitcnt lgkmcnt(4)
	v_fmac_f32_e32 v136, v128, v148
	v_fmac_f32_e32 v136, v129, v149
	v_fmac_f32_e32 v136, v130, v150
	v_fmac_f32_e32 v136, v131, v151
	v_fmac_f32_e32 v137, v128, v186
	v_fmac_f32_e32 v137, v129, v187
	v_fmac_f32_e32 v137, v130, v188
	v_fmac_f32_e32 v137, v131, v189
	v_fmac_f32_e32 v138, v128, v194
	v_fmac_f32_e32 v138, v129, v195
	v_fmac_f32_e32 v138, v130, v196
	v_fmac_f32_e32 v138, v131, v197
	v_fmac_f32_e32 v139, v128, v198
	v_fmac_f32_e32 v139, v129, v199
	v_fmac_f32_e32 v139, v130, v200
	v_fmac_f32_e32 v139, v131, v201
	ds_read_b128 v[148:151], v153 offset:40000
	ds_read_b128 v[186:189], v153 offset:48208
	ds_read_b128 v[194:197], v153 offset:56416
	ds_read_b128 v[198:201], v153 offset:64624
	s_waitcnt lgkmcnt(4)
	v_fmac_f32_e32 v140, v128, v168
	v_fmac_f32_e32 v140, v129, v169
	v_fmac_f32_e32 v140, v130, v170
	v_fmac_f32_e32 v140, v131, v171
	v_fmac_f32_e32 v141, v128, v172
	v_fmac_f32_e32 v141, v129, v173
	v_fmac_f32_e32 v141, v130, v174
	v_fmac_f32_e32 v141, v131, v175
	v_fmac_f32_e32 v142, v128, v176
	v_fmac_f32_e32 v142, v129, v177
	v_fmac_f32_e32 v142, v130, v178
	v_fmac_f32_e32 v142, v131, v179
	v_fmac_f32_e32 v143, v128, v180
	v_fmac_f32_e32 v143, v129, v181
	v_fmac_f32_e32 v143, v130, v182
	v_fmac_f32_e32 v143, v131, v183
	s_waitcnt lgkmcnt(0)
	v_fmac_f32_e32 v144, v128, v148
	v_fmac_f32_e32 v144, v129, v149
	v_fmac_f32_e32 v144, v130, v150
	v_fmac_f32_e32 v144, v131, v151
	v_fmac_f32_e32 v145, v128, v186
	v_fmac_f32_e32 v145, v129, v187
	v_fmac_f32_e32 v145, v130, v188
	v_fmac_f32_e32 v145, v131, v189
	v_fmac_f32_e32 v146, v128, v194
	v_fmac_f32_e32 v146, v129, v195
	v_fmac_f32_e32 v146, v130, v196
	v_fmac_f32_e32 v146, v131, v197
	v_fmac_f32_e32 v147, v128, v198
	v_fmac_f32_e32 v147, v129, v199
	v_fmac_f32_e32 v147, v130, v200
	v_fmac_f32_e32 v147, v131, v201
	s_add_i32 s11, s10, 0x4000
	s_lshr_b32 s0, s11, 8
	s_mul_i32 s0, s0, 57
	s_lshr_b32 s0, s0, 9
	s_mul_i32 s1, s0, 0x900
	s_sub_i32 s43, s11, s1
	s_lshl_b32 s1, s11, 13
	s_add_u32 s12, s48, s1
	s_addc_u32 s13, s49, 0
	s_add_u32 s14, s12, 0x1000
	s_addc_u32 s15, s13, 0
	global_load_dwordx4 v[100:103], v1, s[12:13]
	global_load_dwordx4 v[104:107], v1, s[12:13] offset:1024
	global_load_dwordx4 v[108:111], v1, s[12:13] offset:2048
	global_load_dwordx4 v[112:115], v1, s[12:13] offset:3072
	global_load_dwordx4 v[116:119], v1, s[14:15]
	global_load_dwordx4 v[120:123], v1, s[14:15] offset:1024
	global_load_dwordx4 v[124:127], v1, s[14:15] offset:2048
	global_load_dwordx4 v[128:131], v1, s[14:15] offset:3072
	v_cndmask_b32_e64 v242, v133, v132, s[62:63]
	v_cndmask_b32_e64 v132, v132, v133, s[62:63]
	v_cndmask_b32_e64 v243, v135, v134, s[62:63]
	v_cndmask_b32_e64 v134, v134, v135, s[62:63]
	v_cndmask_b32_e64 v244, v137, v136, s[62:63]
	v_cndmask_b32_e64 v136, v136, v137, s[62:63]
	v_cndmask_b32_e64 v245, v139, v138, s[62:63]
	v_cndmask_b32_e64 v138, v138, v139, s[62:63]
	v_cndmask_b32_e64 v246, v141, v140, s[62:63]
	v_cndmask_b32_e64 v140, v140, v141, s[62:63]
	v_cndmask_b32_e64 v248, v143, v142, s[62:63]
	v_cndmask_b32_e64 v142, v142, v143, s[62:63]
	v_cndmask_b32_e64 v249, v145, v144, s[62:63]
	v_cndmask_b32_e64 v144, v144, v145, s[62:63]
	v_cndmask_b32_e64 v250, v147, v146, s[62:63]
	v_cndmask_b32_e64 v146, v146, v147, s[62:63]
	v_add_f32_dpp v132, v242, v132 quad_perm:[1,0,3,2] row_mask:0xf bank_mask:0xf
	v_add_f32_dpp v134, v243, v134 quad_perm:[1,0,3,2] row_mask:0xf bank_mask:0xf
	v_add_f32_dpp v136, v244, v136 quad_perm:[1,0,3,2] row_mask:0xf bank_mask:0xf
	v_add_f32_dpp v138, v245, v138 quad_perm:[1,0,3,2] row_mask:0xf bank_mask:0xf
	v_add_f32_dpp v140, v246, v140 quad_perm:[1,0,3,2] row_mask:0xf bank_mask:0xf
	v_add_f32_dpp v142, v248, v142 quad_perm:[1,0,3,2] row_mask:0xf bank_mask:0xf
	v_add_f32_dpp v144, v249, v144 quad_perm:[1,0,3,2] row_mask:0xf bank_mask:0xf
	v_add_f32_dpp v146, v250, v146 quad_perm:[1,0,3,2] row_mask:0xf bank_mask:0xf
	v_cndmask_b32_e64 v242, v134, v132, s[64:65]
	v_cndmask_b32_e64 v132, v132, v134, s[64:65]
	v_cndmask_b32_e64 v243, v138, v136, s[64:65]
	v_cndmask_b32_e64 v136, v136, v138, s[64:65]
	v_cndmask_b32_e64 v244, v142, v140, s[64:65]
	v_cndmask_b32_e64 v140, v140, v142, s[64:65]
	v_cndmask_b32_e64 v245, v146, v144, s[64:65]
	v_cndmask_b32_e64 v144, v144, v146, s[64:65]
	s_nop 0
	v_add_f32_dpp v132, v242, v132 quad_perm:[2,3,0,1] row_mask:0xf bank_mask:0xf
	v_add_f32_dpp v136, v243, v136 quad_perm:[2,3,0,1] row_mask:0xf bank_mask:0xf
	v_add_f32_dpp v140, v244, v140 quad_perm:[2,3,0,1] row_mask:0xf bank_mask:0xf
	v_add_f32_dpp v144, v245, v144 quad_perm:[2,3,0,1] row_mask:0xf bank_mask:0xf
	v_cndmask_b32_e64 v242, v136, v132, s[66:67]
	v_cndmask_b32_e64 v132, v132, v136, s[66:67]
	v_cndmask_b32_e64 v243, v144, v140, s[66:67]
	v_cndmask_b32_e64 v140, v140, v144, s[66:67]
	s_nop 1
	v_add_f32_dpp v246, v242, v132 row_shl:4 row_mask:0xf bank_mask:0x5
	v_add_f32_dpp v246, v242, v132 row_shr:4 row_mask:0xf bank_mask:0xa
	v_add_f32_dpp v248, v243, v140 row_shl:4 row_mask:0xf bank_mask:0x5
	v_add_f32_dpp v248, v243, v140 row_shr:4 row_mask:0xf bank_mask:0xa
	v_cndmask_b32_e64 v242, v248, v246, s[68:69]
	v_cndmask_b32_e64 v243, v246, v248, s[68:69]
	s_nop 1
	v_add_f32_dpp v191, v242, v243 row_ror:8 row_mask:0xf bank_mask:0xf
	s_nop 0
	ds_bpermute_b32 v193, v165, v191
	s_waitcnt lgkmcnt(0)
	v_add_f32_e32 v191, v191, v193
	ds_bpermute_b32 v193, v166, v191
	s_waitcnt lgkmcnt(0)
	v_add_f32_e32 v191, v191, v193
	v_mov_b32_e32 v193, v191
	s_nop 1
	v_max_f32_dpp v193, v193, v193 quad_perm:[1,0,3,2] row_mask:0xf bank_mask:0xf
	s_nop 1
	v_max_f32_dpp v193, v193, v193 quad_perm:[2,3,0,1] row_mask:0xf bank_mask:0xf
	s_nop 1
	v_max_f32_dpp v193, v193, v193 row_half_mirror row_mask:0xf bank_mask:0xf
	s_nop 1
	v_max_f32_dpp v193, v193, v193 row_mirror row_mask:0xf bank_mask:0xf
	v_sub_f32_e32 v191, v191, v193
	v_mul_f32_e32 v191, 0x3fb8aa3b, v191
	v_exp_f32_e32 v191, v191
	s_nop 0
	v_mov_b32_e32 v193, v191
	s_nop 1
	v_add_f32_dpp v193, v193, v193 quad_perm:[1,0,3,2] row_mask:0xf bank_mask:0xf
	s_nop 1
	v_add_f32_dpp v193, v193, v193 quad_perm:[2,3,0,1] row_mask:0xf bank_mask:0xf
	s_nop 1
	v_add_f32_dpp v193, v193, v193 row_half_mirror row_mask:0xf bank_mask:0xf
	s_nop 1
	v_add_f32_dpp v193, v193, v193 row_mirror row_mask:0xf bank_mask:0xf
	v_rcp_f32_e32 v193, v193
	s_nop 0
	v_mul_f32_e32 v191, v191, v193
	s_mov_b64 exec, 0xffff
	global_store_dword v164, v191, s[34:35]
	s_mov_b64 exec, -1
	s_waitcnt vmcnt(9)
	s_add_i32 s11, s10, 0x3800
	s_lshr_b32 s0, s11, 8
	s_mul_i32 s0, s0, 57
	s_lshr_b32 s0, s0, 9
	s_mul_i32 s1, s0, 0x900
	s_sub_i32 s43, s11, s1
	s_lshl_b32 s1, s11, 12
	s_add_u32 s16, s50, s1
	s_addc_u32 s17, s51, 0
	s_mul_i32 s1, s0, 0x24000
	s_lshl_b32 s2, s43, 2
	s_add_i32 s1, s1, s2
	s_add_u32 s34, s54, s1
	s_addc_u32 s35, s55, 0
	v_mul_f32_e32 v184, v204, v204
	v_fmac_f32_e32 v184, v205, v205
	v_fmac_f32_e32 v184, v206, v206
	v_fmac_f32_e32 v184, v207, v207
	v_fmac_f32_e32 v184, v208, v208
	v_fmac_f32_e32 v184, v209, v209
	v_fmac_f32_e32 v184, v210, v210
	v_fmac_f32_e32 v184, v211, v211
	v_fmac_f32_e32 v184, v212, v212
	v_fmac_f32_e32 v184, v213, v213
	v_fmac_f32_e32 v184, v214, v214
	v_fmac_f32_e32 v184, v215, v215
	v_fmac_f32_e32 v184, v216, v216
	v_fmac_f32_e32 v184, v217, v217
	v_fmac_f32_e32 v184, v218, v218
	v_fmac_f32_e32 v184, v219, v219
	v_fmac_f32_e32 v184, v226, v226
	v_fmac_f32_e32 v184, v227, v227
	v_fmac_f32_e32 v184, v228, v228
	v_fmac_f32_e32 v184, v229, v229
	v_fmac_f32_e32 v184, v230, v230
	v_fmac_f32_e32 v184, v231, v231
	v_fmac_f32_e32 v184, v232, v232
	v_fmac_f32_e32 v184, v233, v233
	v_fmac_f32_e32 v184, v234, v234
	v_fmac_f32_e32 v184, v235, v235
	v_fmac_f32_e32 v184, v236, v236
	v_fmac_f32_e32 v184, v237, v237
	v_fmac_f32_e32 v184, v238, v238
	v_fmac_f32_e32 v184, v239, v239
	v_fmac_f32_e32 v184, v240, v240
	v_fmac_f32_e32 v184, v241, v241
	ds_read_b128 v[168:171], v152 offset:0
	ds_read_b128 v[172:175], v152 offset:8208
	ds_read_b128 v[176:179], v152 offset:16416
	ds_read_b128 v[180:183], v152 offset:24624
	s_nop 0
	v_add_f32_dpp v184, v184, v184 quad_perm:[1,0,3,2] row_mask:0xf bank_mask:0xf
	s_nop 1
	v_add_f32_dpp v184, v184, v184 quad_perm:[2,3,0,1] row_mask:0xf bank_mask:0xf
	s_nop 1
	v_add_f32_dpp v184, v184, v184 row_half_mirror row_mask:0xf bank_mask:0xf
	s_nop 1
	v_add_f32_dpp v184, v184, v184 row_mirror row_mask:0xf bank_mask:0xf
	s_nop 1
	v_readlane_b32 s0, v184, 0
	v_readlane_b32 s1, v184, 16
	v_readlane_b32 s2, v184, 32
	v_readlane_b32 s3, v184, 48
	v_fma_f32 v4, v4, v36, v4
	v_fma_f32 v5, v5, v37, v5
	v_fma_f32 v6, v6, v38, v6
	v_fma_f32 v7, v7, v39, v7
	v_fma_f32 v8, v8, v40, v8
	v_fma_f32 v9, v9, v41, v9
	v_fma_f32 v10, v10, v42, v10
	v_fma_f32 v11, v11, v43, v11
	v_fma_f32 v12, v12, v44, v12
	v_fma_f32 v13, v13, v45, v13
	v_fma_f32 v14, v14, v46, v14
	v_fma_f32 v15, v15, v47, v15
	v_fma_f32 v16, v16, v48, v16
	v_fma_f32 v17, v17, v49, v17
	v_fma_f32 v18, v18, v50, v18
	v_fma_f32 v19, v19, v51, v19
	v_fma_f32 v20, v20, v52, v20
	v_fma_f32 v21, v21, v53, v21
	v_fma_f32 v22, v22, v54, v22
	v_fma_f32 v23, v23, v55, v23
	v_fma_f32 v24, v24, v56, v24
	v_fma_f32 v25, v25, v57, v25
	v_fma_f32 v26, v26, v58, v26
	v_fma_f32 v27, v27, v59, v27
	v_fma_f32 v28, v28, v60, v28
	v_fma_f32 v29, v29, v61, v29
	v_fma_f32 v30, v30, v62, v30
	v_fma_f32 v31, v31, v63, v31
	v_fma_f32 v32, v32, v64, v32
	v_fma_f32 v33, v33, v65, v33
	v_fma_f32 v34, v34, v66, v34
	v_fma_f32 v35, v35, v67, v35
	v_mov_b32_e32 v190, s0
	v_add_f32_e32 v190, s1, v190
	v_add_f32_e32 v190, s2, v190
	v_add_f32_e32 v190, s3, v190
	v_mul_f32_e32 v190, 0x3a000000, v190
	v_add_f32_e32 v190, 0x358637bd, v190
	v_rsq_f32_e32 v190, v190
	s_nop 0
	v_mul_f32_e32 v4, v4, v190
	v_mul_f32_e32 v5, v5, v190
	v_mul_f32_e32 v6, v6, v190
	v_mul_f32_e32 v7, v7, v190
	v_mul_f32_e32 v8, v8, v190
	v_mul_f32_e32 v9, v9, v190
	v_mul_f32_e32 v10, v10, v190
	v_mul_f32_e32 v11, v11, v190
	v_mul_f32_e32 v12, v12, v190
	v_mul_f32_e32 v13, v13, v190
	v_mul_f32_e32 v14, v14, v190
	v_mul_f32_e32 v15, v15, v190
	v_mul_f32_e32 v16, v16, v190
	v_mul_f32_e32 v17, v17, v190
	v_mul_f32_e32 v18, v18, v190
	v_mul_f32_e32 v19, v19, v190
	v_mul_f32_e32 v20, v20, v190
	v_mul_f32_e32 v21, v21, v190
	v_mul_f32_e32 v22, v22, v190
	v_mul_f32_e32 v23, v23, v190
	v_mul_f32_e32 v24, v24, v190
	v_mul_f32_e32 v25, v25, v190
	v_mul_f32_e32 v26, v26, v190
	v_mul_f32_e32 v27, v27, v190
	v_mul_f32_e32 v28, v28, v190
	v_mul_f32_e32 v29, v29, v190
	v_mul_f32_e32 v30, v30, v190
	v_mul_f32_e32 v31, v31, v190
	v_mul_f32_e32 v32, v32, v190
	v_mul_f32_e32 v33, v33, v190
	v_mul_f32_e32 v34, v34, v190
	v_mul_f32_e32 v35, v35, v190
	v_fma_f32 v204, v204, v4, v68
	v_fma_f32 v205, v205, v5, v69
	v_fma_f32 v206, v206, v6, v70
	v_fma_f32 v207, v207, v7, v71
	v_fma_f32 v208, v208, v8, v72
	v_fma_f32 v209, v209, v9, v73
	v_fma_f32 v210, v210, v10, v74
	v_fma_f32 v211, v211, v11, v75
	v_fma_f32 v212, v212, v12, v76
	v_fma_f32 v213, v213, v13, v77
	v_fma_f32 v214, v214, v14, v78
	v_fma_f32 v215, v215, v15, v79
	v_fma_f32 v216, v216, v16, v80
	v_fma_f32 v217, v217, v17, v81
	v_fma_f32 v218, v218, v18, v82
	v_fma_f32 v219, v219, v19, v83
	v_fma_f32 v226, v226, v20, v84
	v_fma_f32 v227, v227, v21, v85
	v_fma_f32 v228, v228, v22, v86
	v_fma_f32 v229, v229, v23, v87
	v_fma_f32 v230, v230, v24, v88
	v_fma_f32 v231, v231, v25, v89
	v_fma_f32 v232, v232, v26, v90
	v_fma_f32 v233, v233, v27, v91
	v_fma_f32 v234, v234, v28, v92
	v_fma_f32 v235, v235, v29, v93
	v_fma_f32 v236, v236, v30, v94
	v_fma_f32 v237, v237, v31, v95
	v_fma_f32 v238, v238, v32, v96
	v_fma_f32 v239, v239, v33, v97
	v_fma_f32 v240, v240, v34, v98
	v_fma_f32 v241, v241, v35, v99
	v_cvt_pk_bf16_f32 v242, v204, v205
	v_cvt_pk_bf16_f32 v243, v206, v207
	global_store_dwordx2 v2, v[242:243], s[16:17]
	v_cvt_pk_bf16_f32 v244, v208, v209
	v_cvt_pk_bf16_f32 v245, v210, v211
	global_store_dwordx2 v2, v[244:245], s[16:17] offset:512
	v_cvt_pk_bf16_f32 v242, v212, v213
	v_cvt_pk_bf16_f32 v243, v214, v215
	global_store_dwordx2 v2, v[242:243], s[16:17] offset:1024
	v_cvt_pk_bf16_f32 v244, v216, v217
	v_cvt_pk_bf16_f32 v245, v218, v219
	global_store_dwordx2 v2, v[244:245], s[16:17] offset:1536
	v_cvt_pk_bf16_f32 v242, v226, v227
	v_cvt_pk_bf16_f32 v243, v228, v229
	global_store_dwordx2 v2, v[242:243], s[16:17] offset:2048
	v_cvt_pk_bf16_f32 v244, v230, v231
	v_cvt_pk_bf16_f32 v245, v232, v233
	global_store_dwordx2 v2, v[244:245], s[16:17] offset:2560
	v_cvt_pk_bf16_f32 v242, v234, v235
	v_cvt_pk_bf16_f32 v243, v236, v237
	global_store_dwordx2 v2, v[242:243], s[16:17] offset:3072
	v_cvt_pk_bf16_f32 v244, v238, v239
	v_cvt_pk_bf16_f32 v245, v240, v241
	global_store_dwordx2 v2, v[244:245], s[16:17] offset:3584
	s_add_i32 s11, s10, 0x4000
	s_lshr_b32 s0, s11, 8
	s_mul_i32 s0, s0, 57
	s_lshr_b32 s0, s0, 9
	s_mul_i32 s1, s0, 0x900
	s_sub_i32 s43, s11, s1
	s_cmpk_lt_u32 s43, 0x100
	s_cselect_b32 s0, 8, s0
	s_mul_i32 s1, s0, 0xc000
	s_add_u32 s18, s52, s1
	s_addc_u32 s19, s53, 0
	s_add_u32 s18, s18, 0x6000
	s_addc_u32 s19, s19, 0
	s_add_u32 s22, s18, 0x1000
	s_addc_u32 s23, s19, 0
	s_add_u32 s28, s18, 0x2000
	s_addc_u32 s29, s19, 0
	s_add_u32 s30, s18, 0x3000
	s_addc_u32 s31, s19, 0
	global_load_dwordx4 v[4:7], v1, s[56:57]
	global_load_dwordx4 v[36:39], v1, s[28:29]
	global_load_dwordx4 v[68:71], v1, s[18:19]
	global_load_dwordx4 v[8:11], v1, s[56:57] offset:1024
	global_load_dwordx4 v[40:43], v1, s[28:29] offset:1024
	global_load_dwordx4 v[72:75], v1, s[18:19] offset:1024
	global_load_dwordx4 v[12:15], v1, s[56:57] offset:2048
	global_load_dwordx4 v[44:47], v1, s[28:29] offset:2048
	global_load_dwordx4 v[76:79], v1, s[18:19] offset:2048
	global_load_dwordx4 v[16:19], v1, s[56:57] offset:3072
	global_load_dwordx4 v[48:51], v1, s[28:29] offset:3072
	global_load_dwordx4 v[80:83], v1, s[18:19] offset:3072
	global_load_dwordx4 v[20:23], v1, s[58:59]
	global_load_dwordx4 v[52:55], v1, s[30:31]
	global_load_dwordx4 v[84:87], v1, s[22:23]
	global_load_dwordx4 v[24:27], v1, s[58:59] offset:1024
	global_load_dwordx4 v[56:59], v1, s[30:31] offset:1024
	global_load_dwordx4 v[88:91], v1, s[22:23] offset:1024
	global_load_dwordx4 v[28:31], v1, s[58:59] offset:2048
	global_load_dwordx4 v[60:63], v1, s[30:31] offset:2048
	global_load_dwordx4 v[92:95], v1, s[22:23] offset:2048
	global_load_dwordx4 v[32:35], v1, s[58:59] offset:3072
	global_load_dwordx4 v[64:67], v1, s[30:31] offset:3072
	global_load_dwordx4 v[96:99], v1, s[22:23] offset:3072
	v_mov_b32_e32 v132, 0
	v_mov_b32_e32 v133, 0
	v_mov_b32_e32 v134, 0
	v_mov_b32_e32 v135, 0
	v_mov_b32_e32 v136, 0
	v_mov_b32_e32 v137, 0
	v_mov_b32_e32 v138, 0
	v_mov_b32_e32 v139, 0
	v_mov_b32_e32 v140, 0
	v_mov_b32_e32 v141, 0
	v_mov_b32_e32 v142, 0
	v_mov_b32_e32 v143, 0
	v_mov_b32_e32 v144, 0
	v_mov_b32_e32 v145, 0
	v_mov_b32_e32 v146, 0
	v_mov_b32_e32 v147, 0
	ds_read_b128 v[148:151], v152 offset:32832
	ds_read_b128 v[186:189], v152 offset:41040
	ds_read_b128 v[194:197], v152 offset:49248
	ds_read_b128 v[198:201], v152 offset:57456
	s_waitcnt lgkmcnt(4)
	v_fmac_f32_e32 v132, v204, v168
	v_fmac_f32_e32 v132, v205, v169
	v_fmac_f32_e32 v132, v206, v170
	v_fmac_f32_e32 v132, v207, v171
	v_fmac_f32_e32 v133, v204, v172
	v_fmac_f32_e32 v133, v205, v173
	v_fmac_f32_e32 v133, v206, v174
	v_fmac_f32_e32 v133, v207, v175
	v_fmac_f32_e32 v134, v204, v176
	v_fmac_f32_e32 v134, v205, v177
	v_fmac_f32_e32 v134, v206, v178
	v_fmac_f32_e32 v134, v207, v179
	v_fmac_f32_e32 v135, v204, v180
	v_fmac_f32_e32 v135, v205, v181
	v_fmac_f32_e32 v135, v206, v182
	v_fmac_f32_e32 v135, v207, v183
	ds_read_b128 v[168:171], v153 offset:0
	ds_read_b128 v[172:175], v153 offset:8208
	ds_read_b128 v[176:179], v153 offset:16416
	ds_read_b128 v[180:183], v153 offset:24624
	s_waitcnt lgkmcnt(4)
	v_fmac_f32_e32 v136, v204, v148
	v_fmac_f32_e32 v136, v205, v149
	v_fmac_f32_e32 v136, v206, v150
	v_fmac_f32_e32 v136, v207, v151
	v_fmac_f32_e32 v137, v204, v186
	v_fmac_f32_e32 v137, v205, v187
	v_fmac_f32_e32 v137, v206, v188
	v_fmac_f32_e32 v137, v207, v189
	v_fmac_f32_e32 v138, v204, v194
	v_fmac_f32_e32 v138, v205, v195
	v_fmac_f32_e32 v138, v206, v196
	v_fmac_f32_e32 v138, v207, v197
	v_fmac_f32_e32 v139, v204, v198
	v_fmac_f32_e32 v139, v205, v199
	v_fmac_f32_e32 v139, v206, v200
	v_fmac_f32_e32 v139, v207, v201
	ds_read_b128 v[148:151], v153 offset:32832
	ds_read_b128 v[186:189], v153 offset:41040
	ds_read_b128 v[194:197], v153 offset:49248
	ds_read_b128 v[198:201], v153 offset:57456
	s_waitcnt lgkmcnt(4)
	v_fmac_f32_e32 v140, v204, v168
	v_fmac_f32_e32 v140, v205, v169
	v_fmac_f32_e32 v140, v206, v170
	v_fmac_f32_e32 v140, v207, v171
	v_fmac_f32_e32 v141, v204, v172
	v_fmac_f32_e32 v141, v205, v173
	v_fmac_f32_e32 v141, v206, v174
	v_fmac_f32_e32 v141, v207, v175
	v_fmac_f32_e32 v142, v204, v176
	v_fmac_f32_e32 v142, v205, v177
	v_fmac_f32_e32 v142, v206, v178
	v_fmac_f32_e32 v142, v207, v179
	v_fmac_f32_e32 v143, v204, v180
	v_fmac_f32_e32 v143, v205, v181
	v_fmac_f32_e32 v143, v206, v182
	v_fmac_f32_e32 v143, v207, v183
	ds_read_b128 v[168:171], v152 offset:1024
	ds_read_b128 v[172:175], v152 offset:9232
	ds_read_b128 v[176:179], v152 offset:17440
	ds_read_b128 v[180:183], v152 offset:25648
	s_waitcnt lgkmcnt(4)
	v_fmac_f32_e32 v144, v204, v148
	v_fmac_f32_e32 v144, v205, v149
	v_fmac_f32_e32 v144, v206, v150
	v_fmac_f32_e32 v144, v207, v151
	v_fmac_f32_e32 v145, v204, v186
	v_fmac_f32_e32 v145, v205, v187
	v_fmac_f32_e32 v145, v206, v188
	v_fmac_f32_e32 v145, v207, v189
	v_fmac_f32_e32 v146, v204, v194
	v_fmac_f32_e32 v146, v205, v195
	v_fmac_f32_e32 v146, v206, v196
	v_fmac_f32_e32 v146, v207, v197
	v_fmac_f32_e32 v147, v204, v198
	v_fmac_f32_e32 v147, v205, v199
	v_fmac_f32_e32 v147, v206, v200
	v_fmac_f32_e32 v147, v207, v201
	ds_read_b128 v[148:151], v152 offset:33856
	ds_read_b128 v[186:189], v152 offset:42064
	ds_read_b128 v[194:197], v152 offset:50272
	ds_read_b128 v[198:201], v152 offset:58480
	s_waitcnt lgkmcnt(4)
	v_fmac_f32_e32 v132, v208, v168
	v_fmac_f32_e32 v132, v209, v169
	v_fmac_f32_e32 v132, v210, v170
	v_fmac_f32_e32 v132, v211, v171
	v_fmac_f32_e32 v133, v208, v172
	v_fmac_f32_e32 v133, v209, v173
	v_fmac_f32_e32 v133, v210, v174
	v_fmac_f32_e32 v133, v211, v175
	v_fmac_f32_e32 v134, v208, v176
	v_fmac_f32_e32 v134, v209, v177
	v_fmac_f32_e32 v134, v210, v178
	v_fmac_f32_e32 v134, v211, v179
	v_fmac_f32_e32 v135, v208, v180
	v_fmac_f32_e32 v135, v209, v181
	v_fmac_f32_e32 v135, v210, v182
	v_fmac_f32_e32 v135, v211, v183
	ds_read_b128 v[168:171], v153 offset:1024
	ds_read_b128 v[172:175], v153 offset:9232
	ds_read_b128 v[176:179], v153 offset:17440
	ds_read_b128 v[180:183], v153 offset:25648
	s_waitcnt lgkmcnt(4)
	v_fmac_f32_e32 v136, v208, v148
	v_fmac_f32_e32 v136, v209, v149
	v_fmac_f32_e32 v136, v210, v150
	v_fmac_f32_e32 v136, v211, v151
	v_fmac_f32_e32 v137, v208, v186
	v_fmac_f32_e32 v137, v209, v187
	v_fmac_f32_e32 v137, v210, v188
	v_fmac_f32_e32 v137, v211, v189
	v_fmac_f32_e32 v138, v208, v194
	v_fmac_f32_e32 v138, v209, v195
	v_fmac_f32_e32 v138, v210, v196
	v_fmac_f32_e32 v138, v211, v197
	v_fmac_f32_e32 v139, v208, v198
	v_fmac_f32_e32 v139, v209, v199
	v_fmac_f32_e32 v139, v210, v200
	v_fmac_f32_e32 v139, v211, v201
	ds_read_b128 v[148:151], v153 offset:33856
	ds_read_b128 v[186:189], v153 offset:42064
	ds_read_b128 v[194:197], v153 offset:50272
	ds_read_b128 v[198:201], v153 offset:58480
	s_waitcnt lgkmcnt(4)
	v_fmac_f32_e32 v140, v208, v168
	v_fmac_f32_e32 v140, v209, v169
	v_fmac_f32_e32 v140, v210, v170
	v_fmac_f32_e32 v140, v211, v171
	v_fmac_f32_e32 v141, v208, v172
	v_fmac_f32_e32 v141, v209, v173
	v_fmac_f32_e32 v141, v210, v174
	v_fmac_f32_e32 v141, v211, v175
	v_fmac_f32_e32 v142, v208, v176
	v_fmac_f32_e32 v142, v209, v177
	v_fmac_f32_e32 v142, v210, v178
	v_fmac_f32_e32 v142, v211, v179
	v_fmac_f32_e32 v143, v208, v180
	v_fmac_f32_e32 v143, v209, v181
	v_fmac_f32_e32 v143, v210, v182
	v_fmac_f32_e32 v143, v211, v183
	ds_read_b128 v[168:171], v152 offset:2048
	ds_read_b128 v[172:175], v152 offset:10256
	ds_read_b128 v[176:179], v152 offset:18464
	ds_read_b128 v[180:183], v152 offset:26672
	s_waitcnt lgkmcnt(4)
	v_fmac_f32_e32 v144, v208, v148
	v_fmac_f32_e32 v144, v209, v149
	v_fmac_f32_e32 v144, v210, v150
	v_fmac_f32_e32 v144, v211, v151
	v_fmac_f32_e32 v145, v208, v186
	v_fmac_f32_e32 v145, v209, v187
	v_fmac_f32_e32 v145, v210, v188
	v_fmac_f32_e32 v145, v211, v189
	v_fmac_f32_e32 v146, v208, v194
	v_fmac_f32_e32 v146, v209, v195
	v_fmac_f32_e32 v146, v210, v196
	v_fmac_f32_e32 v146, v211, v197
	v_fmac_f32_e32 v147, v208, v198
	v_fmac_f32_e32 v147, v209, v199
	v_fmac_f32_e32 v147, v210, v200
	v_fmac_f32_e32 v147, v211, v201
	ds_read_b128 v[148:151], v152 offset:34880
	ds_read_b128 v[186:189], v152 offset:43088
	ds_read_b128 v[194:197], v152 offset:51296
	ds_read_b128 v[198:201], v152 offset:59504
	s_waitcnt lgkmcnt(4)
	v_fmac_f32_e32 v132, v212, v168
	v_fmac_f32_e32 v132, v213, v169
	v_fmac_f32_e32 v132, v214, v170
	v_fmac_f32_e32 v132, v215, v171
	v_fmac_f32_e32 v133, v212, v172
	v_fmac_f32_e32 v133, v213, v173
	v_fmac_f32_e32 v133, v214, v174
	v_fmac_f32_e32 v133, v215, v175
	v_fmac_f32_e32 v134, v212, v176
	v_fmac_f32_e32 v134, v213, v177
	v_fmac_f32_e32 v134, v214, v178
	v_fmac_f32_e32 v134, v215, v179
	v_fmac_f32_e32 v135, v212, v180
	v_fmac_f32_e32 v135, v213, v181
	v_fmac_f32_e32 v135, v214, v182
	v_fmac_f32_e32 v135, v215, v183
	ds_read_b128 v[168:171], v153 offset:2048
	ds_read_b128 v[172:175], v153 offset:10256
	ds_read_b128 v[176:179], v153 offset:18464
	ds_read_b128 v[180:183], v153 offset:26672
	s_waitcnt lgkmcnt(4)
	v_fmac_f32_e32 v136, v212, v148
	v_fmac_f32_e32 v136, v213, v149
	v_fmac_f32_e32 v136, v214, v150
	v_fmac_f32_e32 v136, v215, v151
	v_fmac_f32_e32 v137, v212, v186
	v_fmac_f32_e32 v137, v213, v187
	v_fmac_f32_e32 v137, v214, v188
	v_fmac_f32_e32 v137, v215, v189
	v_fmac_f32_e32 v138, v212, v194
	v_fmac_f32_e32 v138, v213, v195
	v_fmac_f32_e32 v138, v214, v196
	v_fmac_f32_e32 v138, v215, v197
	v_fmac_f32_e32 v139, v212, v198
	v_fmac_f32_e32 v139, v213, v199
	v_fmac_f32_e32 v139, v214, v200
	v_fmac_f32_e32 v139, v215, v201
	ds_read_b128 v[148:151], v153 offset:34880
	ds_read_b128 v[186:189], v153 offset:43088
	ds_read_b128 v[194:197], v153 offset:51296
	ds_read_b128 v[198:201], v153 offset:59504
	s_waitcnt lgkmcnt(4)
	v_fmac_f32_e32 v140, v212, v168
	v_fmac_f32_e32 v140, v213, v169
	v_fmac_f32_e32 v140, v214, v170
	v_fmac_f32_e32 v140, v215, v171
	v_fmac_f32_e32 v141, v212, v172
	v_fmac_f32_e32 v141, v213, v173
	v_fmac_f32_e32 v141, v214, v174
	v_fmac_f32_e32 v141, v215, v175
	v_fmac_f32_e32 v142, v212, v176
	v_fmac_f32_e32 v142, v213, v177
	v_fmac_f32_e32 v142, v214, v178
	v_fmac_f32_e32 v142, v215, v179
	v_fmac_f32_e32 v143, v212, v180
	v_fmac_f32_e32 v143, v213, v181
	v_fmac_f32_e32 v143, v214, v182
	v_fmac_f32_e32 v143, v215, v183
	ds_read_b128 v[168:171], v152 offset:3072
	ds_read_b128 v[172:175], v152 offset:11280
	ds_read_b128 v[176:179], v152 offset:19488
	ds_read_b128 v[180:183], v152 offset:27696
	s_waitcnt lgkmcnt(4)
	v_fmac_f32_e32 v144, v212, v148
	v_fmac_f32_e32 v144, v213, v149
	v_fmac_f32_e32 v144, v214, v150
	v_fmac_f32_e32 v144, v215, v151
	v_fmac_f32_e32 v145, v212, v186
	v_fmac_f32_e32 v145, v213, v187
	v_fmac_f32_e32 v145, v214, v188
	v_fmac_f32_e32 v145, v215, v189
	v_fmac_f32_e32 v146, v212, v194
	v_fmac_f32_e32 v146, v213, v195
	v_fmac_f32_e32 v146, v214, v196
	v_fmac_f32_e32 v146, v215, v197
	v_fmac_f32_e32 v147, v212, v198
	v_fmac_f32_e32 v147, v213, v199
	v_fmac_f32_e32 v147, v214, v200
	v_fmac_f32_e32 v147, v215, v201
	ds_read_b128 v[148:151], v152 offset:35904
	ds_read_b128 v[186:189], v152 offset:44112
	ds_read_b128 v[194:197], v152 offset:52320
	ds_read_b128 v[198:201], v152 offset:60528
	s_waitcnt lgkmcnt(4)
	v_fmac_f32_e32 v132, v216, v168
	v_fmac_f32_e32 v132, v217, v169
	v_fmac_f32_e32 v132, v218, v170
	v_fmac_f32_e32 v132, v219, v171
	v_fmac_f32_e32 v133, v216, v172
	v_fmac_f32_e32 v133, v217, v173
	v_fmac_f32_e32 v133, v218, v174
	v_fmac_f32_e32 v133, v219, v175
	v_fmac_f32_e32 v134, v216, v176
	v_fmac_f32_e32 v134, v217, v177
	v_fmac_f32_e32 v134, v218, v178
	v_fmac_f32_e32 v134, v219, v179
	v_fmac_f32_e32 v135, v216, v180
	v_fmac_f32_e32 v135, v217, v181
	v_fmac_f32_e32 v135, v218, v182
	v_fmac_f32_e32 v135, v219, v183
	ds_read_b128 v[168:171], v153 offset:3072
	ds_read_b128 v[172:175], v153 offset:11280
	ds_read_b128 v[176:179], v153 offset:19488
	ds_read_b128 v[180:183], v153 offset:27696
	s_waitcnt lgkmcnt(4)
	v_fmac_f32_e32 v136, v216, v148
	v_fmac_f32_e32 v136, v217, v149
	v_fmac_f32_e32 v136, v218, v150
	v_fmac_f32_e32 v136, v219, v151
	v_fmac_f32_e32 v137, v216, v186
	v_fmac_f32_e32 v137, v217, v187
	v_fmac_f32_e32 v137, v218, v188
	v_fmac_f32_e32 v137, v219, v189
	v_fmac_f32_e32 v138, v216, v194
	v_fmac_f32_e32 v138, v217, v195
	v_fmac_f32_e32 v138, v218, v196
	v_fmac_f32_e32 v138, v219, v197
	v_fmac_f32_e32 v139, v216, v198
	v_fmac_f32_e32 v139, v217, v199
	v_fmac_f32_e32 v139, v218, v200
	v_fmac_f32_e32 v139, v219, v201
	ds_read_b128 v[148:151], v153 offset:35904
	ds_read_b128 v[186:189], v153 offset:44112
	ds_read_b128 v[194:197], v153 offset:52320
	ds_read_b128 v[198:201], v153 offset:60528
	s_waitcnt lgkmcnt(4)
	v_fmac_f32_e32 v140, v216, v168
	v_fmac_f32_e32 v140, v217, v169
	v_fmac_f32_e32 v140, v218, v170
	v_fmac_f32_e32 v140, v219, v171
	v_fmac_f32_e32 v141, v216, v172
	v_fmac_f32_e32 v141, v217, v173
	v_fmac_f32_e32 v141, v218, v174
	v_fmac_f32_e32 v141, v219, v175
	v_fmac_f32_e32 v142, v216, v176
	v_fmac_f32_e32 v142, v217, v177
	v_fmac_f32_e32 v142, v218, v178
	v_fmac_f32_e32 v142, v219, v179
	v_fmac_f32_e32 v143, v216, v180
	v_fmac_f32_e32 v143, v217, v181
	v_fmac_f32_e32 v143, v218, v182
	v_fmac_f32_e32 v143, v219, v183
	ds_read_b128 v[168:171], v152 offset:4096
	ds_read_b128 v[172:175], v152 offset:12304
	ds_read_b128 v[176:179], v152 offset:20512
	ds_read_b128 v[180:183], v152 offset:28720
	s_waitcnt lgkmcnt(4)
	v_fmac_f32_e32 v144, v216, v148
	v_fmac_f32_e32 v144, v217, v149
	v_fmac_f32_e32 v144, v218, v150
	v_fmac_f32_e32 v144, v219, v151
	v_fmac_f32_e32 v145, v216, v186
	v_fmac_f32_e32 v145, v217, v187
	v_fmac_f32_e32 v145, v218, v188
	v_fmac_f32_e32 v145, v219, v189
	v_fmac_f32_e32 v146, v216, v194
	v_fmac_f32_e32 v146, v217, v195
	v_fmac_f32_e32 v146, v218, v196
	v_fmac_f32_e32 v146, v219, v197
	v_fmac_f32_e32 v147, v216, v198
	v_fmac_f32_e32 v147, v217, v199
	v_fmac_f32_e32 v147, v218, v200
	v_fmac_f32_e32 v147, v219, v201
	ds_read_b128 v[148:151], v152 offset:36928
	ds_read_b128 v[186:189], v152 offset:45136
	ds_read_b128 v[194:197], v152 offset:53344
	ds_read_b128 v[198:201], v152 offset:61552
	s_waitcnt lgkmcnt(4)
	v_fmac_f32_e32 v132, v226, v168
	v_fmac_f32_e32 v132, v227, v169
	v_fmac_f32_e32 v132, v228, v170
	v_fmac_f32_e32 v132, v229, v171
	v_fmac_f32_e32 v133, v226, v172
	v_fmac_f32_e32 v133, v227, v173
	v_fmac_f32_e32 v133, v228, v174
	v_fmac_f32_e32 v133, v229, v175
	v_fmac_f32_e32 v134, v226, v176
	v_fmac_f32_e32 v134, v227, v177
	v_fmac_f32_e32 v134, v228, v178
	v_fmac_f32_e32 v134, v229, v179
	v_fmac_f32_e32 v135, v226, v180
	v_fmac_f32_e32 v135, v227, v181
	v_fmac_f32_e32 v135, v228, v182
	v_fmac_f32_e32 v135, v229, v183
	ds_read_b128 v[168:171], v153 offset:4096
	ds_read_b128 v[172:175], v153 offset:12304
	ds_read_b128 v[176:179], v153 offset:20512
	ds_read_b128 v[180:183], v153 offset:28720
	s_waitcnt lgkmcnt(4)
	v_fmac_f32_e32 v136, v226, v148
	v_fmac_f32_e32 v136, v227, v149
	v_fmac_f32_e32 v136, v228, v150
	v_fmac_f32_e32 v136, v229, v151
	v_fmac_f32_e32 v137, v226, v186
	v_fmac_f32_e32 v137, v227, v187
	v_fmac_f32_e32 v137, v228, v188
	v_fmac_f32_e32 v137, v229, v189
	v_fmac_f32_e32 v138, v226, v194
	v_fmac_f32_e32 v138, v227, v195
	v_fmac_f32_e32 v138, v228, v196
	v_fmac_f32_e32 v138, v229, v197
	v_fmac_f32_e32 v139, v226, v198
	v_fmac_f32_e32 v139, v227, v199
	v_fmac_f32_e32 v139, v228, v200
	v_fmac_f32_e32 v139, v229, v201
	ds_read_b128 v[148:151], v153 offset:36928
	ds_read_b128 v[186:189], v153 offset:45136
	ds_read_b128 v[194:197], v153 offset:53344
	ds_read_b128 v[198:201], v153 offset:61552
	s_waitcnt lgkmcnt(4)
	v_fmac_f32_e32 v140, v226, v168
	v_fmac_f32_e32 v140, v227, v169
	v_fmac_f32_e32 v140, v228, v170
	v_fmac_f32_e32 v140, v229, v171
	v_fmac_f32_e32 v141, v226, v172
	v_fmac_f32_e32 v141, v227, v173
	v_fmac_f32_e32 v141, v228, v174
	v_fmac_f32_e32 v141, v229, v175
	v_fmac_f32_e32 v142, v226, v176
	v_fmac_f32_e32 v142, v227, v177
	v_fmac_f32_e32 v142, v228, v178
	v_fmac_f32_e32 v142, v229, v179
	v_fmac_f32_e32 v143, v226, v180
	v_fmac_f32_e32 v143, v227, v181
	v_fmac_f32_e32 v143, v228, v182
	v_fmac_f32_e32 v143, v229, v183
	ds_read_b128 v[168:171], v152 offset:5120
	ds_read_b128 v[172:175], v152 offset:13328
	ds_read_b128 v[176:179], v152 offset:21536
	ds_read_b128 v[180:183], v152 offset:29744
	s_waitcnt lgkmcnt(4)
	v_fmac_f32_e32 v144, v226, v148
	v_fmac_f32_e32 v144, v227, v149
	v_fmac_f32_e32 v144, v228, v150
	v_fmac_f32_e32 v144, v229, v151
	v_fmac_f32_e32 v145, v226, v186
	v_fmac_f32_e32 v145, v227, v187
	v_fmac_f32_e32 v145, v228, v188
	v_fmac_f32_e32 v145, v229, v189
	v_fmac_f32_e32 v146, v226, v194
	v_fmac_f32_e32 v146, v227, v195
	v_fmac_f32_e32 v146, v228, v196
	v_fmac_f32_e32 v146, v229, v197
	v_fmac_f32_e32 v147, v226, v198
	v_fmac_f32_e32 v147, v227, v199
	v_fmac_f32_e32 v147, v228, v200
	v_fmac_f32_e32 v147, v229, v201
	ds_read_b128 v[148:151], v152 offset:37952
	ds_read_b128 v[186:189], v152 offset:46160
	ds_read_b128 v[194:197], v152 offset:54368
	ds_read_b128 v[198:201], v152 offset:62576
	s_waitcnt lgkmcnt(4)
	v_fmac_f32_e32 v132, v230, v168
	v_fmac_f32_e32 v132, v231, v169
	v_fmac_f32_e32 v132, v232, v170
	v_fmac_f32_e32 v132, v233, v171
	v_fmac_f32_e32 v133, v230, v172
	v_fmac_f32_e32 v133, v231, v173
	v_fmac_f32_e32 v133, v232, v174
	v_fmac_f32_e32 v133, v233, v175
	v_fmac_f32_e32 v134, v230, v176
	v_fmac_f32_e32 v134, v231, v177
	v_fmac_f32_e32 v134, v232, v178
	v_fmac_f32_e32 v134, v233, v179
	v_fmac_f32_e32 v135, v230, v180
	v_fmac_f32_e32 v135, v231, v181
	v_fmac_f32_e32 v135, v232, v182
	v_fmac_f32_e32 v135, v233, v183
	ds_read_b128 v[168:171], v153 offset:5120
	ds_read_b128 v[172:175], v153 offset:13328
	ds_read_b128 v[176:179], v153 offset:21536
	ds_read_b128 v[180:183], v153 offset:29744
	s_waitcnt lgkmcnt(4)
	v_fmac_f32_e32 v136, v230, v148
	v_fmac_f32_e32 v136, v231, v149
	v_fmac_f32_e32 v136, v232, v150
	v_fmac_f32_e32 v136, v233, v151
	v_fmac_f32_e32 v137, v230, v186
	v_fmac_f32_e32 v137, v231, v187
	v_fmac_f32_e32 v137, v232, v188
	v_fmac_f32_e32 v137, v233, v189
	v_fmac_f32_e32 v138, v230, v194
	v_fmac_f32_e32 v138, v231, v195
	v_fmac_f32_e32 v138, v232, v196
	v_fmac_f32_e32 v138, v233, v197
	v_fmac_f32_e32 v139, v230, v198
	v_fmac_f32_e32 v139, v231, v199
	v_fmac_f32_e32 v139, v232, v200
	v_fmac_f32_e32 v139, v233, v201
	ds_read_b128 v[148:151], v153 offset:37952
	ds_read_b128 v[186:189], v153 offset:46160
	ds_read_b128 v[194:197], v153 offset:54368
	ds_read_b128 v[198:201], v153 offset:62576
	s_waitcnt lgkmcnt(4)
	v_fmac_f32_e32 v140, v230, v168
	v_fmac_f32_e32 v140, v231, v169
	v_fmac_f32_e32 v140, v232, v170
	v_fmac_f32_e32 v140, v233, v171
	v_fmac_f32_e32 v141, v230, v172
	v_fmac_f32_e32 v141, v231, v173
	v_fmac_f32_e32 v141, v232, v174
	v_fmac_f32_e32 v141, v233, v175
	v_fmac_f32_e32 v142, v230, v176
	v_fmac_f32_e32 v142, v231, v177
	v_fmac_f32_e32 v142, v232, v178
	v_fmac_f32_e32 v142, v233, v179
	v_fmac_f32_e32 v143, v230, v180
	v_fmac_f32_e32 v143, v231, v181
	v_fmac_f32_e32 v143, v232, v182
	v_fmac_f32_e32 v143, v233, v183
	ds_read_b128 v[168:171], v152 offset:6144
	ds_read_b128 v[172:175], v152 offset:14352
	ds_read_b128 v[176:179], v152 offset:22560
	ds_read_b128 v[180:183], v152 offset:30768
	s_waitcnt lgkmcnt(4)
	v_fmac_f32_e32 v144, v230, v148
	v_fmac_f32_e32 v144, v231, v149
	v_fmac_f32_e32 v144, v232, v150
	v_fmac_f32_e32 v144, v233, v151
	v_fmac_f32_e32 v145, v230, v186
	v_fmac_f32_e32 v145, v231, v187
	v_fmac_f32_e32 v145, v232, v188
	v_fmac_f32_e32 v145, v233, v189
	v_fmac_f32_e32 v146, v230, v194
	v_fmac_f32_e32 v146, v231, v195
	v_fmac_f32_e32 v146, v232, v196
	v_fmac_f32_e32 v146, v233, v197
	v_fmac_f32_e32 v147, v230, v198
	v_fmac_f32_e32 v147, v231, v199
	v_fmac_f32_e32 v147, v232, v200
	v_fmac_f32_e32 v147, v233, v201
	ds_read_b128 v[148:151], v152 offset:38976
	ds_read_b128 v[186:189], v152 offset:47184
	ds_read_b128 v[194:197], v152 offset:55392
	ds_read_b128 v[198:201], v152 offset:63600
	s_waitcnt lgkmcnt(4)
	v_fmac_f32_e32 v132, v234, v168
	v_fmac_f32_e32 v132, v235, v169
	v_fmac_f32_e32 v132, v236, v170
	v_fmac_f32_e32 v132, v237, v171
	v_fmac_f32_e32 v133, v234, v172
	v_fmac_f32_e32 v133, v235, v173
	v_fmac_f32_e32 v133, v236, v174
	v_fmac_f32_e32 v133, v237, v175
	v_fmac_f32_e32 v134, v234, v176
	v_fmac_f32_e32 v134, v235, v177
	v_fmac_f32_e32 v134, v236, v178
	v_fmac_f32_e32 v134, v237, v179
	v_fmac_f32_e32 v135, v234, v180
	v_fmac_f32_e32 v135, v235, v181
	v_fmac_f32_e32 v135, v236, v182
	v_fmac_f32_e32 v135, v237, v183
	ds_read_b128 v[168:171], v153 offset:6144
	ds_read_b128 v[172:175], v153 offset:14352
	ds_read_b128 v[176:179], v153 offset:22560
	ds_read_b128 v[180:183], v153 offset:30768
	s_waitcnt lgkmcnt(4)
	v_fmac_f32_e32 v136, v234, v148
	v_fmac_f32_e32 v136, v235, v149
	v_fmac_f32_e32 v136, v236, v150
	v_fmac_f32_e32 v136, v237, v151
	v_fmac_f32_e32 v137, v234, v186
	v_fmac_f32_e32 v137, v235, v187
	v_fmac_f32_e32 v137, v236, v188
	v_fmac_f32_e32 v137, v237, v189
	v_fmac_f32_e32 v138, v234, v194
	v_fmac_f32_e32 v138, v235, v195
	v_fmac_f32_e32 v138, v236, v196
	v_fmac_f32_e32 v138, v237, v197
	v_fmac_f32_e32 v139, v234, v198
	v_fmac_f32_e32 v139, v235, v199
	v_fmac_f32_e32 v139, v236, v200
	v_fmac_f32_e32 v139, v237, v201
	ds_read_b128 v[148:151], v153 offset:38976
	ds_read_b128 v[186:189], v153 offset:47184
	ds_read_b128 v[194:197], v153 offset:55392
	ds_read_b128 v[198:201], v153 offset:63600
	s_waitcnt lgkmcnt(4)
	v_fmac_f32_e32 v140, v234, v168
	v_fmac_f32_e32 v140, v235, v169
	v_fmac_f32_e32 v140, v236, v170
	v_fmac_f32_e32 v140, v237, v171
	v_fmac_f32_e32 v141, v234, v172
	v_fmac_f32_e32 v141, v235, v173
	v_fmac_f32_e32 v141, v236, v174
	v_fmac_f32_e32 v141, v237, v175
	v_fmac_f32_e32 v142, v234, v176
	v_fmac_f32_e32 v142, v235, v177
	v_fmac_f32_e32 v142, v236, v178
	v_fmac_f32_e32 v142, v237, v179
	v_fmac_f32_e32 v143, v234, v180
	v_fmac_f32_e32 v143, v235, v181
	v_fmac_f32_e32 v143, v236, v182
	v_fmac_f32_e32 v143, v237, v183
	ds_read_b128 v[168:171], v152 offset:7168
	ds_read_b128 v[172:175], v152 offset:15376
	ds_read_b128 v[176:179], v152 offset:23584
	ds_read_b128 v[180:183], v152 offset:31792
	s_waitcnt lgkmcnt(4)
	v_fmac_f32_e32 v144, v234, v148
	v_fmac_f32_e32 v144, v235, v149
	v_fmac_f32_e32 v144, v236, v150
	v_fmac_f32_e32 v144, v237, v151
	v_fmac_f32_e32 v145, v234, v186
	v_fmac_f32_e32 v145, v235, v187
	v_fmac_f32_e32 v145, v236, v188
	v_fmac_f32_e32 v145, v237, v189
	v_fmac_f32_e32 v146, v234, v194
	v_fmac_f32_e32 v146, v235, v195
	v_fmac_f32_e32 v146, v236, v196
	v_fmac_f32_e32 v146, v237, v197
	v_fmac_f32_e32 v147, v234, v198
	v_fmac_f32_e32 v147, v235, v199
	v_fmac_f32_e32 v147, v236, v200
	v_fmac_f32_e32 v147, v237, v201
	ds_read_b128 v[148:151], v152 offset:40000
	ds_read_b128 v[186:189], v152 offset:48208
	ds_read_b128 v[194:197], v152 offset:56416
	ds_read_b128 v[198:201], v152 offset:64624
	s_waitcnt lgkmcnt(4)
	v_fmac_f32_e32 v132, v238, v168
	v_fmac_f32_e32 v132, v239, v169
	v_fmac_f32_e32 v132, v240, v170
	v_fmac_f32_e32 v132, v241, v171
	v_fmac_f32_e32 v133, v238, v172
	v_fmac_f32_e32 v133, v239, v173
	v_fmac_f32_e32 v133, v240, v174
	v_fmac_f32_e32 v133, v241, v175
	v_fmac_f32_e32 v134, v238, v176
	v_fmac_f32_e32 v134, v239, v177
	v_fmac_f32_e32 v134, v240, v178
	v_fmac_f32_e32 v134, v241, v179
	v_fmac_f32_e32 v135, v238, v180
	v_fmac_f32_e32 v135, v239, v181
	v_fmac_f32_e32 v135, v240, v182
	v_fmac_f32_e32 v135, v241, v183
	ds_read_b128 v[168:171], v153 offset:7168
	ds_read_b128 v[172:175], v153 offset:15376
	ds_read_b128 v[176:179], v153 offset:23584
	ds_read_b128 v[180:183], v153 offset:31792
	s_waitcnt lgkmcnt(4)
	v_fmac_f32_e32 v136, v238, v148
	v_fmac_f32_e32 v136, v239, v149
	v_fmac_f32_e32 v136, v240, v150
	v_fmac_f32_e32 v136, v241, v151
	v_fmac_f32_e32 v137, v238, v186
	v_fmac_f32_e32 v137, v239, v187
	v_fmac_f32_e32 v137, v240, v188
	v_fmac_f32_e32 v137, v241, v189
	v_fmac_f32_e32 v138, v238, v194
	v_fmac_f32_e32 v138, v239, v195
	v_fmac_f32_e32 v138, v240, v196
	v_fmac_f32_e32 v138, v241, v197
	v_fmac_f32_e32 v139, v238, v198
	v_fmac_f32_e32 v139, v239, v199
	v_fmac_f32_e32 v139, v240, v200
	v_fmac_f32_e32 v139, v241, v201
	ds_read_b128 v[148:151], v153 offset:40000
	ds_read_b128 v[186:189], v153 offset:48208
	ds_read_b128 v[194:197], v153 offset:56416
	ds_read_b128 v[198:201], v153 offset:64624
	s_waitcnt lgkmcnt(4)
	v_fmac_f32_e32 v140, v238, v168
	v_fmac_f32_e32 v140, v239, v169
	v_fmac_f32_e32 v140, v240, v170
	v_fmac_f32_e32 v140, v241, v171
	v_fmac_f32_e32 v141, v238, v172
	v_fmac_f32_e32 v141, v239, v173
	v_fmac_f32_e32 v141, v240, v174
	v_fmac_f32_e32 v141, v241, v175
	v_fmac_f32_e32 v142, v238, v176
	v_fmac_f32_e32 v142, v239, v177
	v_fmac_f32_e32 v142, v240, v178
	v_fmac_f32_e32 v142, v241, v179
	v_fmac_f32_e32 v143, v238, v180
	v_fmac_f32_e32 v143, v239, v181
	v_fmac_f32_e32 v143, v240, v182
	v_fmac_f32_e32 v143, v241, v183
	s_waitcnt lgkmcnt(0)
	v_fmac_f32_e32 v144, v238, v148
	v_fmac_f32_e32 v144, v239, v149
	v_fmac_f32_e32 v144, v240, v150
	v_fmac_f32_e32 v144, v241, v151
	v_fmac_f32_e32 v145, v238, v186
	v_fmac_f32_e32 v145, v239, v187
	v_fmac_f32_e32 v145, v240, v188
	v_fmac_f32_e32 v145, v241, v189
	v_fmac_f32_e32 v146, v238, v194
	v_fmac_f32_e32 v146, v239, v195
	v_fmac_f32_e32 v146, v240, v196
	v_fmac_f32_e32 v146, v241, v197
	v_fmac_f32_e32 v147, v238, v198
	v_fmac_f32_e32 v147, v239, v199
	v_fmac_f32_e32 v147, v240, v200
	v_fmac_f32_e32 v147, v241, v201
	v_cndmask_b32_e64 v242, v133, v132, s[62:63]
	v_cndmask_b32_e64 v132, v132, v133, s[62:63]
	v_cndmask_b32_e64 v243, v135, v134, s[62:63]
	v_cndmask_b32_e64 v134, v134, v135, s[62:63]
	v_cndmask_b32_e64 v244, v137, v136, s[62:63]
	v_cndmask_b32_e64 v136, v136, v137, s[62:63]
	v_cndmask_b32_e64 v245, v139, v138, s[62:63]
	v_cndmask_b32_e64 v138, v138, v139, s[62:63]
	v_cndmask_b32_e64 v246, v141, v140, s[62:63]
	v_cndmask_b32_e64 v140, v140, v141, s[62:63]
	v_cndmask_b32_e64 v248, v143, v142, s[62:63]
	v_cndmask_b32_e64 v142, v142, v143, s[62:63]
	v_cndmask_b32_e64 v249, v145, v144, s[62:63]
	v_cndmask_b32_e64 v144, v144, v145, s[62:63]
	v_cndmask_b32_e64 v250, v147, v146, s[62:63]
	v_cndmask_b32_e64 v146, v146, v147, s[62:63]
	v_add_f32_dpp v132, v242, v132 quad_perm:[1,0,3,2] row_mask:0xf bank_mask:0xf
	v_add_f32_dpp v134, v243, v134 quad_perm:[1,0,3,2] row_mask:0xf bank_mask:0xf
	v_add_f32_dpp v136, v244, v136 quad_perm:[1,0,3,2] row_mask:0xf bank_mask:0xf
	v_add_f32_dpp v138, v245, v138 quad_perm:[1,0,3,2] row_mask:0xf bank_mask:0xf
	v_add_f32_dpp v140, v246, v140 quad_perm:[1,0,3,2] row_mask:0xf bank_mask:0xf
	v_add_f32_dpp v142, v248, v142 quad_perm:[1,0,3,2] row_mask:0xf bank_mask:0xf
	v_add_f32_dpp v144, v249, v144 quad_perm:[1,0,3,2] row_mask:0xf bank_mask:0xf
	v_add_f32_dpp v146, v250, v146 quad_perm:[1,0,3,2] row_mask:0xf bank_mask:0xf
	v_cndmask_b32_e64 v242, v134, v132, s[64:65]
	v_cndmask_b32_e64 v132, v132, v134, s[64:65]
	v_cndmask_b32_e64 v243, v138, v136, s[64:65]
	v_cndmask_b32_e64 v136, v136, v138, s[64:65]
	v_cndmask_b32_e64 v244, v142, v140, s[64:65]
	v_cndmask_b32_e64 v140, v140, v142, s[64:65]
	v_cndmask_b32_e64 v245, v146, v144, s[64:65]
	v_cndmask_b32_e64 v144, v144, v146, s[64:65]
	s_nop 0
	v_add_f32_dpp v132, v242, v132 quad_perm:[2,3,0,1] row_mask:0xf bank_mask:0xf
	v_add_f32_dpp v136, v243, v136 quad_perm:[2,3,0,1] row_mask:0xf bank_mask:0xf
	v_add_f32_dpp v140, v244, v140 quad_perm:[2,3,0,1] row_mask:0xf bank_mask:0xf
	v_add_f32_dpp v144, v245, v144 quad_perm:[2,3,0,1] row_mask:0xf bank_mask:0xf
	v_cndmask_b32_e64 v242, v136, v132, s[66:67]
	v_cndmask_b32_e64 v132, v132, v136, s[66:67]
	v_cndmask_b32_e64 v243, v144, v140, s[66:67]
	v_cndmask_b32_e64 v140, v140, v144, s[66:67]
	s_nop 1
	v_add_f32_dpp v246, v242, v132 row_shl:4 row_mask:0xf bank_mask:0x5
	v_add_f32_dpp v246, v242, v132 row_shr:4 row_mask:0xf bank_mask:0xa
	v_add_f32_dpp v248, v243, v140 row_shl:4 row_mask:0xf bank_mask:0x5
	v_add_f32_dpp v248, v243, v140 row_shr:4 row_mask:0xf bank_mask:0xa
	v_cndmask_b32_e64 v242, v248, v246, s[68:69]
	v_cndmask_b32_e64 v243, v246, v248, s[68:69]
	s_nop 1
	v_add_f32_dpp v191, v242, v243 row_ror:8 row_mask:0xf bank_mask:0xf
	s_nop 0
	ds_bpermute_b32 v193, v165, v191
	s_waitcnt lgkmcnt(0)
	v_add_f32_e32 v191, v191, v193
	ds_bpermute_b32 v193, v166, v191
	s_waitcnt lgkmcnt(0)
	v_add_f32_e32 v191, v191, v193
	v_mov_b32_e32 v193, v191
	s_nop 1
	v_max_f32_dpp v193, v193, v193 quad_perm:[1,0,3,2] row_mask:0xf bank_mask:0xf
	s_nop 1
	v_max_f32_dpp v193, v193, v193 quad_perm:[2,3,0,1] row_mask:0xf bank_mask:0xf
	s_nop 1
	v_max_f32_dpp v193, v193, v193 row_half_mirror row_mask:0xf bank_mask:0xf
	s_nop 1
	v_max_f32_dpp v193, v193, v193 row_mirror row_mask:0xf bank_mask:0xf
	v_sub_f32_e32 v191, v191, v193
	v_mul_f32_e32 v191, 0x3fb8aa3b, v191
	v_exp_f32_e32 v191, v191
	s_nop 0
	v_mov_b32_e32 v193, v191
	s_nop 1
	v_add_f32_dpp v193, v193, v193 quad_perm:[1,0,3,2] row_mask:0xf bank_mask:0xf
	s_nop 1
	v_add_f32_dpp v193, v193, v193 quad_perm:[2,3,0,1] row_mask:0xf bank_mask:0xf
	s_nop 1
	v_add_f32_dpp v193, v193, v193 row_half_mirror row_mask:0xf bank_mask:0xf
	s_nop 1
	v_add_f32_dpp v193, v193, v193 row_mirror row_mask:0xf bank_mask:0xf
	v_rcp_f32_e32 v193, v193
	s_nop 0
	v_mul_f32_e32 v191, v191, v193
	s_mov_b64 exec, 0xffff
	global_store_dword v164, v191, s[34:35]
	s_mov_b64 exec, -1
	s_waitcnt vmcnt(1)
	s_add_i32 s11, s10, 0x4000
	s_lshr_b32 s0, s11, 8
	s_mul_i32 s0, s0, 57
	s_lshr_b32 s0, s0, 9
	s_mul_i32 s1, s0, 0x900
	s_sub_i32 s43, s11, s1
	s_lshl_b32 s1, s11, 12
	s_add_u32 s16, s50, s1
	s_addc_u32 s17, s51, 0
	s_mul_i32 s1, s0, 0x24000
	s_lshl_b32 s2, s43, 2
	s_add_i32 s1, s1, s2
	s_add_u32 s34, s54, s1
	s_addc_u32 s35, s55, 0
	v_mul_f32_e32 v184, v100, v100
	v_fmac_f32_e32 v184, v101, v101
	v_fmac_f32_e32 v184, v102, v102
	v_fmac_f32_e32 v184, v103, v103
	v_fmac_f32_e32 v184, v104, v104
	v_fmac_f32_e32 v184, v105, v105
	v_fmac_f32_e32 v184, v106, v106
	v_fmac_f32_e32 v184, v107, v107
	v_fmac_f32_e32 v184, v108, v108
	v_fmac_f32_e32 v184, v109, v109
	v_fmac_f32_e32 v184, v110, v110
	v_fmac_f32_e32 v184, v111, v111
	v_fmac_f32_e32 v184, v112, v112
	v_fmac_f32_e32 v184, v113, v113
	v_fmac_f32_e32 v184, v114, v114
	v_fmac_f32_e32 v184, v115, v115
	v_fmac_f32_e32 v184, v116, v116
	v_fmac_f32_e32 v184, v117, v117
	v_fmac_f32_e32 v184, v118, v118
	v_fmac_f32_e32 v184, v119, v119
	v_fmac_f32_e32 v184, v120, v120
	v_fmac_f32_e32 v184, v121, v121
	v_fmac_f32_e32 v184, v122, v122
	v_fmac_f32_e32 v184, v123, v123
	v_fmac_f32_e32 v184, v124, v124
	v_fmac_f32_e32 v184, v125, v125
	v_fmac_f32_e32 v184, v126, v126
	v_fmac_f32_e32 v184, v127, v127
	v_fmac_f32_e32 v184, v128, v128
	v_fmac_f32_e32 v184, v129, v129
	v_fmac_f32_e32 v184, v130, v130
	v_fmac_f32_e32 v184, v131, v131
	ds_read_b128 v[168:171], v152 offset:0
	ds_read_b128 v[172:175], v152 offset:8208
	ds_read_b128 v[176:179], v152 offset:16416
	ds_read_b128 v[180:183], v152 offset:24624
	s_nop 0
	v_add_f32_dpp v184, v184, v184 quad_perm:[1,0,3,2] row_mask:0xf bank_mask:0xf
	s_nop 1
	v_add_f32_dpp v184, v184, v184 quad_perm:[2,3,0,1] row_mask:0xf bank_mask:0xf
	s_nop 1
	v_add_f32_dpp v184, v184, v184 row_half_mirror row_mask:0xf bank_mask:0xf
	s_nop 1
	v_add_f32_dpp v184, v184, v184 row_mirror row_mask:0xf bank_mask:0xf
	s_nop 1
	v_readlane_b32 s0, v184, 0
	v_readlane_b32 s1, v184, 16
	v_readlane_b32 s2, v184, 32
	v_readlane_b32 s3, v184, 48
	v_fma_f32 v4, v4, v36, v4
	v_fma_f32 v5, v5, v37, v5
	v_fma_f32 v6, v6, v38, v6
	v_fma_f32 v7, v7, v39, v7
	v_fma_f32 v8, v8, v40, v8
	v_fma_f32 v9, v9, v41, v9
	v_fma_f32 v10, v10, v42, v10
	v_fma_f32 v11, v11, v43, v11
	v_fma_f32 v12, v12, v44, v12
	v_fma_f32 v13, v13, v45, v13
	v_fma_f32 v14, v14, v46, v14
	v_fma_f32 v15, v15, v47, v15
	v_fma_f32 v16, v16, v48, v16
	v_fma_f32 v17, v17, v49, v17
	v_fma_f32 v18, v18, v50, v18
	v_fma_f32 v19, v19, v51, v19
	v_fma_f32 v20, v20, v52, v20
	v_fma_f32 v21, v21, v53, v21
	v_fma_f32 v22, v22, v54, v22
	v_fma_f32 v23, v23, v55, v23
	v_fma_f32 v24, v24, v56, v24
	v_fma_f32 v25, v25, v57, v25
	v_fma_f32 v26, v26, v58, v26
	v_fma_f32 v27, v27, v59, v27
	v_fma_f32 v28, v28, v60, v28
	v_fma_f32 v29, v29, v61, v29
	v_fma_f32 v30, v30, v62, v30
	v_fma_f32 v31, v31, v63, v31
	v_fma_f32 v32, v32, v64, v32
	v_fma_f32 v33, v33, v65, v33
	v_fma_f32 v34, v34, v66, v34
	v_fma_f32 v35, v35, v67, v35
	v_mov_b32_e32 v190, s0
	v_add_f32_e32 v190, s1, v190
	v_add_f32_e32 v190, s2, v190
	v_add_f32_e32 v190, s3, v190
	v_mul_f32_e32 v190, 0x3a000000, v190
	v_add_f32_e32 v190, 0x358637bd, v190
	v_rsq_f32_e32 v190, v190
	s_nop 0
	v_mul_f32_e32 v4, v4, v190
	v_mul_f32_e32 v5, v5, v190
	v_mul_f32_e32 v6, v6, v190
	v_mul_f32_e32 v7, v7, v190
	v_mul_f32_e32 v8, v8, v190
	v_mul_f32_e32 v9, v9, v190
	v_mul_f32_e32 v10, v10, v190
	v_mul_f32_e32 v11, v11, v190
	v_mul_f32_e32 v12, v12, v190
	v_mul_f32_e32 v13, v13, v190
	v_mul_f32_e32 v14, v14, v190
	v_mul_f32_e32 v15, v15, v190
	v_mul_f32_e32 v16, v16, v190
	v_mul_f32_e32 v17, v17, v190
	v_mul_f32_e32 v18, v18, v190
	v_mul_f32_e32 v19, v19, v190
	v_mul_f32_e32 v20, v20, v190
	v_mul_f32_e32 v21, v21, v190
	v_mul_f32_e32 v22, v22, v190
	v_mul_f32_e32 v23, v23, v190
	v_mul_f32_e32 v24, v24, v190
	v_mul_f32_e32 v25, v25, v190
	v_mul_f32_e32 v26, v26, v190
	v_mul_f32_e32 v27, v27, v190
	v_mul_f32_e32 v28, v28, v190
	v_mul_f32_e32 v29, v29, v190
	v_mul_f32_e32 v30, v30, v190
	v_mul_f32_e32 v31, v31, v190
	v_mul_f32_e32 v32, v32, v190
	v_mul_f32_e32 v33, v33, v190
	v_mul_f32_e32 v34, v34, v190
	v_mul_f32_e32 v35, v35, v190
	v_fma_f32 v100, v100, v4, v68
	v_fma_f32 v101, v101, v5, v69
	v_fma_f32 v102, v102, v6, v70
	v_fma_f32 v103, v103, v7, v71
	v_fma_f32 v104, v104, v8, v72
	v_fma_f32 v105, v105, v9, v73
	v_fma_f32 v106, v106, v10, v74
	v_fma_f32 v107, v107, v11, v75
	v_fma_f32 v108, v108, v12, v76
	v_fma_f32 v109, v109, v13, v77
	v_fma_f32 v110, v110, v14, v78
	v_fma_f32 v111, v111, v15, v79
	v_fma_f32 v112, v112, v16, v80
	v_fma_f32 v113, v113, v17, v81
	v_fma_f32 v114, v114, v18, v82
	v_fma_f32 v115, v115, v19, v83
	v_fma_f32 v116, v116, v20, v84
	v_fma_f32 v117, v117, v21, v85
	v_fma_f32 v118, v118, v22, v86
	v_fma_f32 v119, v119, v23, v87
	v_fma_f32 v120, v120, v24, v88
	v_fma_f32 v121, v121, v25, v89
	v_fma_f32 v122, v122, v26, v90
	v_fma_f32 v123, v123, v27, v91
	v_fma_f32 v124, v124, v28, v92
	v_fma_f32 v125, v125, v29, v93
	v_fma_f32 v126, v126, v30, v94
	v_fma_f32 v127, v127, v31, v95
	v_fma_f32 v128, v128, v32, v96
	v_fma_f32 v129, v129, v33, v97
	v_fma_f32 v130, v130, v34, v98
	v_fma_f32 v131, v131, v35, v99
	v_cvt_pk_bf16_f32 v242, v100, v101
	v_cvt_pk_bf16_f32 v243, v102, v103
	global_store_dwordx2 v2, v[242:243], s[16:17]
	v_cvt_pk_bf16_f32 v244, v104, v105
	v_cvt_pk_bf16_f32 v245, v106, v107
	global_store_dwordx2 v2, v[244:245], s[16:17] offset:512
	v_cvt_pk_bf16_f32 v242, v108, v109
	v_cvt_pk_bf16_f32 v243, v110, v111
	global_store_dwordx2 v2, v[242:243], s[16:17] offset:1024
	v_cvt_pk_bf16_f32 v244, v112, v113
	v_cvt_pk_bf16_f32 v245, v114, v115
	global_store_dwordx2 v2, v[244:245], s[16:17] offset:1536
	v_cvt_pk_bf16_f32 v242, v116, v117
	v_cvt_pk_bf16_f32 v243, v118, v119
	global_store_dwordx2 v2, v[242:243], s[16:17] offset:2048
	v_cvt_pk_bf16_f32 v244, v120, v121
	v_cvt_pk_bf16_f32 v245, v122, v123
	global_store_dwordx2 v2, v[244:245], s[16:17] offset:2560
	v_cvt_pk_bf16_f32 v242, v124, v125
	v_cvt_pk_bf16_f32 v243, v126, v127
	global_store_dwordx2 v2, v[242:243], s[16:17] offset:3072
	v_cvt_pk_bf16_f32 v244, v128, v129
	v_cvt_pk_bf16_f32 v245, v130, v131
	global_store_dwordx2 v2, v[244:245], s[16:17] offset:3584
	v_mov_b32_e32 v132, 0
	v_mov_b32_e32 v133, 0
	v_mov_b32_e32 v134, 0
	v_mov_b32_e32 v135, 0
	v_mov_b32_e32 v136, 0
	v_mov_b32_e32 v137, 0
	v_mov_b32_e32 v138, 0
	v_mov_b32_e32 v139, 0
	v_mov_b32_e32 v140, 0
	v_mov_b32_e32 v141, 0
	v_mov_b32_e32 v142, 0
	v_mov_b32_e32 v143, 0
	v_mov_b32_e32 v144, 0
	v_mov_b32_e32 v145, 0
	v_mov_b32_e32 v146, 0
	v_mov_b32_e32 v147, 0
	ds_read_b128 v[148:151], v152 offset:32832
	ds_read_b128 v[186:189], v152 offset:41040
	ds_read_b128 v[194:197], v152 offset:49248
	ds_read_b128 v[198:201], v152 offset:57456
	s_waitcnt lgkmcnt(4)
	v_fmac_f32_e32 v132, v100, v168
	v_fmac_f32_e32 v132, v101, v169
	v_fmac_f32_e32 v132, v102, v170
	v_fmac_f32_e32 v132, v103, v171
	v_fmac_f32_e32 v133, v100, v172
	v_fmac_f32_e32 v133, v101, v173
	v_fmac_f32_e32 v133, v102, v174
	v_fmac_f32_e32 v133, v103, v175
	v_fmac_f32_e32 v134, v100, v176
	v_fmac_f32_e32 v134, v101, v177
	v_fmac_f32_e32 v134, v102, v178
	v_fmac_f32_e32 v134, v103, v179
	v_fmac_f32_e32 v135, v100, v180
	v_fmac_f32_e32 v135, v101, v181
	v_fmac_f32_e32 v135, v102, v182
	v_fmac_f32_e32 v135, v103, v183
	ds_read_b128 v[168:171], v153 offset:0
	ds_read_b128 v[172:175], v153 offset:8208
	ds_read_b128 v[176:179], v153 offset:16416
	ds_read_b128 v[180:183], v153 offset:24624
	s_waitcnt lgkmcnt(4)
	v_fmac_f32_e32 v136, v100, v148
	v_fmac_f32_e32 v136, v101, v149
	v_fmac_f32_e32 v136, v102, v150
	v_fmac_f32_e32 v136, v103, v151
	v_fmac_f32_e32 v137, v100, v186
	v_fmac_f32_e32 v137, v101, v187
	v_fmac_f32_e32 v137, v102, v188
	v_fmac_f32_e32 v137, v103, v189
	v_fmac_f32_e32 v138, v100, v194
	v_fmac_f32_e32 v138, v101, v195
	v_fmac_f32_e32 v138, v102, v196
	v_fmac_f32_e32 v138, v103, v197
	v_fmac_f32_e32 v139, v100, v198
	v_fmac_f32_e32 v139, v101, v199
	v_fmac_f32_e32 v139, v102, v200
	v_fmac_f32_e32 v139, v103, v201
	ds_read_b128 v[148:151], v153 offset:32832
	ds_read_b128 v[186:189], v153 offset:41040
	ds_read_b128 v[194:197], v153 offset:49248
	ds_read_b128 v[198:201], v153 offset:57456
	s_waitcnt lgkmcnt(4)
	v_fmac_f32_e32 v140, v100, v168
	v_fmac_f32_e32 v140, v101, v169
	v_fmac_f32_e32 v140, v102, v170
	v_fmac_f32_e32 v140, v103, v171
	v_fmac_f32_e32 v141, v100, v172
	v_fmac_f32_e32 v141, v101, v173
	v_fmac_f32_e32 v141, v102, v174
	v_fmac_f32_e32 v141, v103, v175
	v_fmac_f32_e32 v142, v100, v176
	v_fmac_f32_e32 v142, v101, v177
	v_fmac_f32_e32 v142, v102, v178
	v_fmac_f32_e32 v142, v103, v179
	v_fmac_f32_e32 v143, v100, v180
	v_fmac_f32_e32 v143, v101, v181
	v_fmac_f32_e32 v143, v102, v182
	v_fmac_f32_e32 v143, v103, v183
	ds_read_b128 v[168:171], v152 offset:1024
	ds_read_b128 v[172:175], v152 offset:9232
	ds_read_b128 v[176:179], v152 offset:17440
	ds_read_b128 v[180:183], v152 offset:25648
	s_waitcnt lgkmcnt(4)
	v_fmac_f32_e32 v144, v100, v148
	v_fmac_f32_e32 v144, v101, v149
	v_fmac_f32_e32 v144, v102, v150
	v_fmac_f32_e32 v144, v103, v151
	v_fmac_f32_e32 v145, v100, v186
	v_fmac_f32_e32 v145, v101, v187
	v_fmac_f32_e32 v145, v102, v188
	v_fmac_f32_e32 v145, v103, v189
	v_fmac_f32_e32 v146, v100, v194
	v_fmac_f32_e32 v146, v101, v195
	v_fmac_f32_e32 v146, v102, v196
	v_fmac_f32_e32 v146, v103, v197
	v_fmac_f32_e32 v147, v100, v198
	v_fmac_f32_e32 v147, v101, v199
	v_fmac_f32_e32 v147, v102, v200
	v_fmac_f32_e32 v147, v103, v201
	ds_read_b128 v[148:151], v152 offset:33856
	ds_read_b128 v[186:189], v152 offset:42064
	ds_read_b128 v[194:197], v152 offset:50272
	ds_read_b128 v[198:201], v152 offset:58480
	s_waitcnt lgkmcnt(4)
	v_fmac_f32_e32 v132, v104, v168
	v_fmac_f32_e32 v132, v105, v169
	v_fmac_f32_e32 v132, v106, v170
	v_fmac_f32_e32 v132, v107, v171
	v_fmac_f32_e32 v133, v104, v172
	v_fmac_f32_e32 v133, v105, v173
	v_fmac_f32_e32 v133, v106, v174
	v_fmac_f32_e32 v133, v107, v175
	v_fmac_f32_e32 v134, v104, v176
	v_fmac_f32_e32 v134, v105, v177
	v_fmac_f32_e32 v134, v106, v178
	v_fmac_f32_e32 v134, v107, v179
	v_fmac_f32_e32 v135, v104, v180
	v_fmac_f32_e32 v135, v105, v181
	v_fmac_f32_e32 v135, v106, v182
	v_fmac_f32_e32 v135, v107, v183
	ds_read_b128 v[168:171], v153 offset:1024
	ds_read_b128 v[172:175], v153 offset:9232
	ds_read_b128 v[176:179], v153 offset:17440
	ds_read_b128 v[180:183], v153 offset:25648
	s_waitcnt lgkmcnt(4)
	v_fmac_f32_e32 v136, v104, v148
	v_fmac_f32_e32 v136, v105, v149
	v_fmac_f32_e32 v136, v106, v150
	v_fmac_f32_e32 v136, v107, v151
	v_fmac_f32_e32 v137, v104, v186
	v_fmac_f32_e32 v137, v105, v187
	v_fmac_f32_e32 v137, v106, v188
	v_fmac_f32_e32 v137, v107, v189
	v_fmac_f32_e32 v138, v104, v194
	v_fmac_f32_e32 v138, v105, v195
	v_fmac_f32_e32 v138, v106, v196
	v_fmac_f32_e32 v138, v107, v197
	v_fmac_f32_e32 v139, v104, v198
	v_fmac_f32_e32 v139, v105, v199
	v_fmac_f32_e32 v139, v106, v200
	v_fmac_f32_e32 v139, v107, v201
	ds_read_b128 v[148:151], v153 offset:33856
	ds_read_b128 v[186:189], v153 offset:42064
	ds_read_b128 v[194:197], v153 offset:50272
	ds_read_b128 v[198:201], v153 offset:58480
	s_waitcnt lgkmcnt(4)
	v_fmac_f32_e32 v140, v104, v168
	v_fmac_f32_e32 v140, v105, v169
	v_fmac_f32_e32 v140, v106, v170
	v_fmac_f32_e32 v140, v107, v171
	v_fmac_f32_e32 v141, v104, v172
	v_fmac_f32_e32 v141, v105, v173
	v_fmac_f32_e32 v141, v106, v174
	v_fmac_f32_e32 v141, v107, v175
	v_fmac_f32_e32 v142, v104, v176
	v_fmac_f32_e32 v142, v105, v177
	v_fmac_f32_e32 v142, v106, v178
	v_fmac_f32_e32 v142, v107, v179
	v_fmac_f32_e32 v143, v104, v180
	v_fmac_f32_e32 v143, v105, v181
	v_fmac_f32_e32 v143, v106, v182
	v_fmac_f32_e32 v143, v107, v183
	ds_read_b128 v[168:171], v152 offset:2048
	ds_read_b128 v[172:175], v152 offset:10256
	ds_read_b128 v[176:179], v152 offset:18464
	ds_read_b128 v[180:183], v152 offset:26672
	s_waitcnt lgkmcnt(4)
	v_fmac_f32_e32 v144, v104, v148
	v_fmac_f32_e32 v144, v105, v149
	v_fmac_f32_e32 v144, v106, v150
	v_fmac_f32_e32 v144, v107, v151
	v_fmac_f32_e32 v145, v104, v186
	v_fmac_f32_e32 v145, v105, v187
	v_fmac_f32_e32 v145, v106, v188
	v_fmac_f32_e32 v145, v107, v189
	v_fmac_f32_e32 v146, v104, v194
	v_fmac_f32_e32 v146, v105, v195
	v_fmac_f32_e32 v146, v106, v196
	v_fmac_f32_e32 v146, v107, v197
	v_fmac_f32_e32 v147, v104, v198
	v_fmac_f32_e32 v147, v105, v199
	v_fmac_f32_e32 v147, v106, v200
	v_fmac_f32_e32 v147, v107, v201
	ds_read_b128 v[148:151], v152 offset:34880
	ds_read_b128 v[186:189], v152 offset:43088
	ds_read_b128 v[194:197], v152 offset:51296
	ds_read_b128 v[198:201], v152 offset:59504
	s_waitcnt lgkmcnt(4)
	v_fmac_f32_e32 v132, v108, v168
	v_fmac_f32_e32 v132, v109, v169
	v_fmac_f32_e32 v132, v110, v170
	v_fmac_f32_e32 v132, v111, v171
	v_fmac_f32_e32 v133, v108, v172
	v_fmac_f32_e32 v133, v109, v173
	v_fmac_f32_e32 v133, v110, v174
	v_fmac_f32_e32 v133, v111, v175
	v_fmac_f32_e32 v134, v108, v176
	v_fmac_f32_e32 v134, v109, v177
	v_fmac_f32_e32 v134, v110, v178
	v_fmac_f32_e32 v134, v111, v179
	v_fmac_f32_e32 v135, v108, v180
	v_fmac_f32_e32 v135, v109, v181
	v_fmac_f32_e32 v135, v110, v182
	v_fmac_f32_e32 v135, v111, v183
	ds_read_b128 v[168:171], v153 offset:2048
	ds_read_b128 v[172:175], v153 offset:10256
	ds_read_b128 v[176:179], v153 offset:18464
	ds_read_b128 v[180:183], v153 offset:26672
	s_waitcnt lgkmcnt(4)
	v_fmac_f32_e32 v136, v108, v148
	v_fmac_f32_e32 v136, v109, v149
	v_fmac_f32_e32 v136, v110, v150
	v_fmac_f32_e32 v136, v111, v151
	v_fmac_f32_e32 v137, v108, v186
	v_fmac_f32_e32 v137, v109, v187
	v_fmac_f32_e32 v137, v110, v188
	v_fmac_f32_e32 v137, v111, v189
	v_fmac_f32_e32 v138, v108, v194
	v_fmac_f32_e32 v138, v109, v195
	v_fmac_f32_e32 v138, v110, v196
	v_fmac_f32_e32 v138, v111, v197
	v_fmac_f32_e32 v139, v108, v198
	v_fmac_f32_e32 v139, v109, v199
	v_fmac_f32_e32 v139, v110, v200
	v_fmac_f32_e32 v139, v111, v201
	ds_read_b128 v[148:151], v153 offset:34880
	ds_read_b128 v[186:189], v153 offset:43088
	ds_read_b128 v[194:197], v153 offset:51296
	ds_read_b128 v[198:201], v153 offset:59504
	s_waitcnt lgkmcnt(4)
	v_fmac_f32_e32 v140, v108, v168
	v_fmac_f32_e32 v140, v109, v169
	v_fmac_f32_e32 v140, v110, v170
	v_fmac_f32_e32 v140, v111, v171
	v_fmac_f32_e32 v141, v108, v172
	v_fmac_f32_e32 v141, v109, v173
	v_fmac_f32_e32 v141, v110, v174
	v_fmac_f32_e32 v141, v111, v175
	v_fmac_f32_e32 v142, v108, v176
	v_fmac_f32_e32 v142, v109, v177
	v_fmac_f32_e32 v142, v110, v178
	v_fmac_f32_e32 v142, v111, v179
	v_fmac_f32_e32 v143, v108, v180
	v_fmac_f32_e32 v143, v109, v181
	v_fmac_f32_e32 v143, v110, v182
	v_fmac_f32_e32 v143, v111, v183
	ds_read_b128 v[168:171], v152 offset:3072
	ds_read_b128 v[172:175], v152 offset:11280
	ds_read_b128 v[176:179], v152 offset:19488
	ds_read_b128 v[180:183], v152 offset:27696
	s_waitcnt lgkmcnt(4)
	v_fmac_f32_e32 v144, v108, v148
	v_fmac_f32_e32 v144, v109, v149
	v_fmac_f32_e32 v144, v110, v150
	v_fmac_f32_e32 v144, v111, v151
	v_fmac_f32_e32 v145, v108, v186
	v_fmac_f32_e32 v145, v109, v187
	v_fmac_f32_e32 v145, v110, v188
	v_fmac_f32_e32 v145, v111, v189
	v_fmac_f32_e32 v146, v108, v194
	v_fmac_f32_e32 v146, v109, v195
	v_fmac_f32_e32 v146, v110, v196
	v_fmac_f32_e32 v146, v111, v197
	v_fmac_f32_e32 v147, v108, v198
	v_fmac_f32_e32 v147, v109, v199
	v_fmac_f32_e32 v147, v110, v200
	v_fmac_f32_e32 v147, v111, v201
	ds_read_b128 v[148:151], v152 offset:35904
	ds_read_b128 v[186:189], v152 offset:44112
	ds_read_b128 v[194:197], v152 offset:52320
	ds_read_b128 v[198:201], v152 offset:60528
	s_waitcnt lgkmcnt(4)
	v_fmac_f32_e32 v132, v112, v168
	v_fmac_f32_e32 v132, v113, v169
	v_fmac_f32_e32 v132, v114, v170
	v_fmac_f32_e32 v132, v115, v171
	v_fmac_f32_e32 v133, v112, v172
	v_fmac_f32_e32 v133, v113, v173
	v_fmac_f32_e32 v133, v114, v174
	v_fmac_f32_e32 v133, v115, v175
	v_fmac_f32_e32 v134, v112, v176
	v_fmac_f32_e32 v134, v113, v177
	v_fmac_f32_e32 v134, v114, v178
	v_fmac_f32_e32 v134, v115, v179
	v_fmac_f32_e32 v135, v112, v180
	v_fmac_f32_e32 v135, v113, v181
	v_fmac_f32_e32 v135, v114, v182
	v_fmac_f32_e32 v135, v115, v183
	ds_read_b128 v[168:171], v153 offset:3072
	ds_read_b128 v[172:175], v153 offset:11280
	ds_read_b128 v[176:179], v153 offset:19488
	ds_read_b128 v[180:183], v153 offset:27696
	s_waitcnt lgkmcnt(4)
	v_fmac_f32_e32 v136, v112, v148
	v_fmac_f32_e32 v136, v113, v149
	v_fmac_f32_e32 v136, v114, v150
	v_fmac_f32_e32 v136, v115, v151
	v_fmac_f32_e32 v137, v112, v186
	v_fmac_f32_e32 v137, v113, v187
	v_fmac_f32_e32 v137, v114, v188
	v_fmac_f32_e32 v137, v115, v189
	v_fmac_f32_e32 v138, v112, v194
	v_fmac_f32_e32 v138, v113, v195
	v_fmac_f32_e32 v138, v114, v196
	v_fmac_f32_e32 v138, v115, v197
	v_fmac_f32_e32 v139, v112, v198
	v_fmac_f32_e32 v139, v113, v199
	v_fmac_f32_e32 v139, v114, v200
	v_fmac_f32_e32 v139, v115, v201
	ds_read_b128 v[148:151], v153 offset:35904
	ds_read_b128 v[186:189], v153 offset:44112
	ds_read_b128 v[194:197], v153 offset:52320
	ds_read_b128 v[198:201], v153 offset:60528
	s_waitcnt lgkmcnt(4)
	v_fmac_f32_e32 v140, v112, v168
	v_fmac_f32_e32 v140, v113, v169
	v_fmac_f32_e32 v140, v114, v170
	v_fmac_f32_e32 v140, v115, v171
	v_fmac_f32_e32 v141, v112, v172
	v_fmac_f32_e32 v141, v113, v173
	v_fmac_f32_e32 v141, v114, v174
	v_fmac_f32_e32 v141, v115, v175
	v_fmac_f32_e32 v142, v112, v176
	v_fmac_f32_e32 v142, v113, v177
	v_fmac_f32_e32 v142, v114, v178
	v_fmac_f32_e32 v142, v115, v179
	v_fmac_f32_e32 v143, v112, v180
	v_fmac_f32_e32 v143, v113, v181
	v_fmac_f32_e32 v143, v114, v182
	v_fmac_f32_e32 v143, v115, v183
	ds_read_b128 v[168:171], v152 offset:4096
	ds_read_b128 v[172:175], v152 offset:12304
	ds_read_b128 v[176:179], v152 offset:20512
	ds_read_b128 v[180:183], v152 offset:28720
	s_waitcnt lgkmcnt(4)
	v_fmac_f32_e32 v144, v112, v148
	v_fmac_f32_e32 v144, v113, v149
	v_fmac_f32_e32 v144, v114, v150
	v_fmac_f32_e32 v144, v115, v151
	v_fmac_f32_e32 v145, v112, v186
	v_fmac_f32_e32 v145, v113, v187
	v_fmac_f32_e32 v145, v114, v188
	v_fmac_f32_e32 v145, v115, v189
	v_fmac_f32_e32 v146, v112, v194
	v_fmac_f32_e32 v146, v113, v195
	v_fmac_f32_e32 v146, v114, v196
	v_fmac_f32_e32 v146, v115, v197
	v_fmac_f32_e32 v147, v112, v198
	v_fmac_f32_e32 v147, v113, v199
	v_fmac_f32_e32 v147, v114, v200
	v_fmac_f32_e32 v147, v115, v201
	ds_read_b128 v[148:151], v152 offset:36928
	ds_read_b128 v[186:189], v152 offset:45136
	ds_read_b128 v[194:197], v152 offset:53344
	ds_read_b128 v[198:201], v152 offset:61552
	s_waitcnt lgkmcnt(4)
	v_fmac_f32_e32 v132, v116, v168
	v_fmac_f32_e32 v132, v117, v169
	v_fmac_f32_e32 v132, v118, v170
	v_fmac_f32_e32 v132, v119, v171
	v_fmac_f32_e32 v133, v116, v172
	v_fmac_f32_e32 v133, v117, v173
	v_fmac_f32_e32 v133, v118, v174
	v_fmac_f32_e32 v133, v119, v175
	v_fmac_f32_e32 v134, v116, v176
	v_fmac_f32_e32 v134, v117, v177
	v_fmac_f32_e32 v134, v118, v178
	v_fmac_f32_e32 v134, v119, v179
	v_fmac_f32_e32 v135, v116, v180
	v_fmac_f32_e32 v135, v117, v181
	v_fmac_f32_e32 v135, v118, v182
	v_fmac_f32_e32 v135, v119, v183
	ds_read_b128 v[168:171], v153 offset:4096
	ds_read_b128 v[172:175], v153 offset:12304
	ds_read_b128 v[176:179], v153 offset:20512
	ds_read_b128 v[180:183], v153 offset:28720
	s_waitcnt lgkmcnt(4)
	v_fmac_f32_e32 v136, v116, v148
	v_fmac_f32_e32 v136, v117, v149
	v_fmac_f32_e32 v136, v118, v150
	v_fmac_f32_e32 v136, v119, v151
	v_fmac_f32_e32 v137, v116, v186
	v_fmac_f32_e32 v137, v117, v187
	v_fmac_f32_e32 v137, v118, v188
	v_fmac_f32_e32 v137, v119, v189
	v_fmac_f32_e32 v138, v116, v194
	v_fmac_f32_e32 v138, v117, v195
	v_fmac_f32_e32 v138, v118, v196
	v_fmac_f32_e32 v138, v119, v197
	v_fmac_f32_e32 v139, v116, v198
	v_fmac_f32_e32 v139, v117, v199
	v_fmac_f32_e32 v139, v118, v200
	v_fmac_f32_e32 v139, v119, v201
	ds_read_b128 v[148:151], v153 offset:36928
	ds_read_b128 v[186:189], v153 offset:45136
	ds_read_b128 v[194:197], v153 offset:53344
	ds_read_b128 v[198:201], v153 offset:61552
	s_waitcnt lgkmcnt(4)
	v_fmac_f32_e32 v140, v116, v168
	v_fmac_f32_e32 v140, v117, v169
	v_fmac_f32_e32 v140, v118, v170
	v_fmac_f32_e32 v140, v119, v171
	v_fmac_f32_e32 v141, v116, v172
	v_fmac_f32_e32 v141, v117, v173
	v_fmac_f32_e32 v141, v118, v174
	v_fmac_f32_e32 v141, v119, v175
	v_fmac_f32_e32 v142, v116, v176
	v_fmac_f32_e32 v142, v117, v177
	v_fmac_f32_e32 v142, v118, v178
	v_fmac_f32_e32 v142, v119, v179
	v_fmac_f32_e32 v143, v116, v180
	v_fmac_f32_e32 v143, v117, v181
	v_fmac_f32_e32 v143, v118, v182
	v_fmac_f32_e32 v143, v119, v183
	ds_read_b128 v[168:171], v152 offset:5120
	ds_read_b128 v[172:175], v152 offset:13328
	ds_read_b128 v[176:179], v152 offset:21536
	ds_read_b128 v[180:183], v152 offset:29744
	s_waitcnt lgkmcnt(4)
	v_fmac_f32_e32 v144, v116, v148
	v_fmac_f32_e32 v144, v117, v149
	v_fmac_f32_e32 v144, v118, v150
	v_fmac_f32_e32 v144, v119, v151
	v_fmac_f32_e32 v145, v116, v186
	v_fmac_f32_e32 v145, v117, v187
	v_fmac_f32_e32 v145, v118, v188
	v_fmac_f32_e32 v145, v119, v189
	v_fmac_f32_e32 v146, v116, v194
	v_fmac_f32_e32 v146, v117, v195
	v_fmac_f32_e32 v146, v118, v196
	v_fmac_f32_e32 v146, v119, v197
	v_fmac_f32_e32 v147, v116, v198
	v_fmac_f32_e32 v147, v117, v199
	v_fmac_f32_e32 v147, v118, v200
	v_fmac_f32_e32 v147, v119, v201
	ds_read_b128 v[148:151], v152 offset:37952
	ds_read_b128 v[186:189], v152 offset:46160
	ds_read_b128 v[194:197], v152 offset:54368
	ds_read_b128 v[198:201], v152 offset:62576
	s_waitcnt lgkmcnt(4)
	v_fmac_f32_e32 v132, v120, v168
	v_fmac_f32_e32 v132, v121, v169
	v_fmac_f32_e32 v132, v122, v170
	v_fmac_f32_e32 v132, v123, v171
	v_fmac_f32_e32 v133, v120, v172
	v_fmac_f32_e32 v133, v121, v173
	v_fmac_f32_e32 v133, v122, v174
	v_fmac_f32_e32 v133, v123, v175
	v_fmac_f32_e32 v134, v120, v176
	v_fmac_f32_e32 v134, v121, v177
	v_fmac_f32_e32 v134, v122, v178
	v_fmac_f32_e32 v134, v123, v179
	v_fmac_f32_e32 v135, v120, v180
	v_fmac_f32_e32 v135, v121, v181
	v_fmac_f32_e32 v135, v122, v182
	v_fmac_f32_e32 v135, v123, v183
	ds_read_b128 v[168:171], v153 offset:5120
	ds_read_b128 v[172:175], v153 offset:13328
	ds_read_b128 v[176:179], v153 offset:21536
	ds_read_b128 v[180:183], v153 offset:29744
	s_waitcnt lgkmcnt(4)
	v_fmac_f32_e32 v136, v120, v148
	v_fmac_f32_e32 v136, v121, v149
	v_fmac_f32_e32 v136, v122, v150
	v_fmac_f32_e32 v136, v123, v151
	v_fmac_f32_e32 v137, v120, v186
	v_fmac_f32_e32 v137, v121, v187
	v_fmac_f32_e32 v137, v122, v188
	v_fmac_f32_e32 v137, v123, v189
	v_fmac_f32_e32 v138, v120, v194
	v_fmac_f32_e32 v138, v121, v195
	v_fmac_f32_e32 v138, v122, v196
	v_fmac_f32_e32 v138, v123, v197
	v_fmac_f32_e32 v139, v120, v198
	v_fmac_f32_e32 v139, v121, v199
	v_fmac_f32_e32 v139, v122, v200
	v_fmac_f32_e32 v139, v123, v201
	ds_read_b128 v[148:151], v153 offset:37952
	ds_read_b128 v[186:189], v153 offset:46160
	ds_read_b128 v[194:197], v153 offset:54368
	ds_read_b128 v[198:201], v153 offset:62576
	s_waitcnt lgkmcnt(4)
	v_fmac_f32_e32 v140, v120, v168
	v_fmac_f32_e32 v140, v121, v169
	v_fmac_f32_e32 v140, v122, v170
	v_fmac_f32_e32 v140, v123, v171
	v_fmac_f32_e32 v141, v120, v172
	v_fmac_f32_e32 v141, v121, v173
	v_fmac_f32_e32 v141, v122, v174
	v_fmac_f32_e32 v141, v123, v175
	v_fmac_f32_e32 v142, v120, v176
	v_fmac_f32_e32 v142, v121, v177
	v_fmac_f32_e32 v142, v122, v178
	v_fmac_f32_e32 v142, v123, v179
	v_fmac_f32_e32 v143, v120, v180
	v_fmac_f32_e32 v143, v121, v181
	v_fmac_f32_e32 v143, v122, v182
	v_fmac_f32_e32 v143, v123, v183
	ds_read_b128 v[168:171], v152 offset:6144
	ds_read_b128 v[172:175], v152 offset:14352
	ds_read_b128 v[176:179], v152 offset:22560
	ds_read_b128 v[180:183], v152 offset:30768
	s_waitcnt lgkmcnt(4)
	v_fmac_f32_e32 v144, v120, v148
	v_fmac_f32_e32 v144, v121, v149
	v_fmac_f32_e32 v144, v122, v150
	v_fmac_f32_e32 v144, v123, v151
	v_fmac_f32_e32 v145, v120, v186
	v_fmac_f32_e32 v145, v121, v187
	v_fmac_f32_e32 v145, v122, v188
	v_fmac_f32_e32 v145, v123, v189
	v_fmac_f32_e32 v146, v120, v194
	v_fmac_f32_e32 v146, v121, v195
	v_fmac_f32_e32 v146, v122, v196
	v_fmac_f32_e32 v146, v123, v197
	v_fmac_f32_e32 v147, v120, v198
	v_fmac_f32_e32 v147, v121, v199
	v_fmac_f32_e32 v147, v122, v200
	v_fmac_f32_e32 v147, v123, v201
	ds_read_b128 v[148:151], v152 offset:38976
	ds_read_b128 v[186:189], v152 offset:47184
	ds_read_b128 v[194:197], v152 offset:55392
	ds_read_b128 v[198:201], v152 offset:63600
	s_waitcnt lgkmcnt(4)
	v_fmac_f32_e32 v132, v124, v168
	v_fmac_f32_e32 v132, v125, v169
	v_fmac_f32_e32 v132, v126, v170
	v_fmac_f32_e32 v132, v127, v171
	v_fmac_f32_e32 v133, v124, v172
	v_fmac_f32_e32 v133, v125, v173
	v_fmac_f32_e32 v133, v126, v174
	v_fmac_f32_e32 v133, v127, v175
	v_fmac_f32_e32 v134, v124, v176
	v_fmac_f32_e32 v134, v125, v177
	v_fmac_f32_e32 v134, v126, v178
	v_fmac_f32_e32 v134, v127, v179
	v_fmac_f32_e32 v135, v124, v180
	v_fmac_f32_e32 v135, v125, v181
	v_fmac_f32_e32 v135, v126, v182
	v_fmac_f32_e32 v135, v127, v183
	ds_read_b128 v[168:171], v153 offset:6144
	ds_read_b128 v[172:175], v153 offset:14352
	ds_read_b128 v[176:179], v153 offset:22560
	ds_read_b128 v[180:183], v153 offset:30768
	s_waitcnt lgkmcnt(4)
	v_fmac_f32_e32 v136, v124, v148
	v_fmac_f32_e32 v136, v125, v149
	v_fmac_f32_e32 v136, v126, v150
	v_fmac_f32_e32 v136, v127, v151
	v_fmac_f32_e32 v137, v124, v186
	v_fmac_f32_e32 v137, v125, v187
	v_fmac_f32_e32 v137, v126, v188
	v_fmac_f32_e32 v137, v127, v189
	v_fmac_f32_e32 v138, v124, v194
	v_fmac_f32_e32 v138, v125, v195
	v_fmac_f32_e32 v138, v126, v196
	v_fmac_f32_e32 v138, v127, v197
	v_fmac_f32_e32 v139, v124, v198
	v_fmac_f32_e32 v139, v125, v199
	v_fmac_f32_e32 v139, v126, v200
	v_fmac_f32_e32 v139, v127, v201
	ds_read_b128 v[148:151], v153 offset:38976
	ds_read_b128 v[186:189], v153 offset:47184
	ds_read_b128 v[194:197], v153 offset:55392
	ds_read_b128 v[198:201], v153 offset:63600
	s_waitcnt lgkmcnt(4)
	v_fmac_f32_e32 v140, v124, v168
	v_fmac_f32_e32 v140, v125, v169
	v_fmac_f32_e32 v140, v126, v170
	v_fmac_f32_e32 v140, v127, v171
	v_fmac_f32_e32 v141, v124, v172
	v_fmac_f32_e32 v141, v125, v173
	v_fmac_f32_e32 v141, v126, v174
	v_fmac_f32_e32 v141, v127, v175
	v_fmac_f32_e32 v142, v124, v176
	v_fmac_f32_e32 v142, v125, v177
	v_fmac_f32_e32 v142, v126, v178
	v_fmac_f32_e32 v142, v127, v179
	v_fmac_f32_e32 v143, v124, v180
	v_fmac_f32_e32 v143, v125, v181
	v_fmac_f32_e32 v143, v126, v182
	v_fmac_f32_e32 v143, v127, v183
	ds_read_b128 v[168:171], v152 offset:7168
	ds_read_b128 v[172:175], v152 offset:15376
	ds_read_b128 v[176:179], v152 offset:23584
	ds_read_b128 v[180:183], v152 offset:31792
	s_waitcnt lgkmcnt(4)
	v_fmac_f32_e32 v144, v124, v148
	v_fmac_f32_e32 v144, v125, v149
	v_fmac_f32_e32 v144, v126, v150
	v_fmac_f32_e32 v144, v127, v151
	v_fmac_f32_e32 v145, v124, v186
	v_fmac_f32_e32 v145, v125, v187
	v_fmac_f32_e32 v145, v126, v188
	v_fmac_f32_e32 v145, v127, v189
	v_fmac_f32_e32 v146, v124, v194
	v_fmac_f32_e32 v146, v125, v195
	v_fmac_f32_e32 v146, v126, v196
	v_fmac_f32_e32 v146, v127, v197
	v_fmac_f32_e32 v147, v124, v198
	v_fmac_f32_e32 v147, v125, v199
	v_fmac_f32_e32 v147, v126, v200
	v_fmac_f32_e32 v147, v127, v201
	ds_read_b128 v[148:151], v152 offset:40000
	ds_read_b128 v[186:189], v152 offset:48208
	ds_read_b128 v[194:197], v152 offset:56416
	ds_read_b128 v[198:201], v152 offset:64624
	s_waitcnt lgkmcnt(4)
	v_fmac_f32_e32 v132, v128, v168
	v_fmac_f32_e32 v132, v129, v169
	v_fmac_f32_e32 v132, v130, v170
	v_fmac_f32_e32 v132, v131, v171
	v_fmac_f32_e32 v133, v128, v172
	v_fmac_f32_e32 v133, v129, v173
	v_fmac_f32_e32 v133, v130, v174
	v_fmac_f32_e32 v133, v131, v175
	v_fmac_f32_e32 v134, v128, v176
	v_fmac_f32_e32 v134, v129, v177
	v_fmac_f32_e32 v134, v130, v178
	v_fmac_f32_e32 v134, v131, v179
	v_fmac_f32_e32 v135, v128, v180
	v_fmac_f32_e32 v135, v129, v181
	v_fmac_f32_e32 v135, v130, v182
	v_fmac_f32_e32 v135, v131, v183
	ds_read_b128 v[168:171], v153 offset:7168
	ds_read_b128 v[172:175], v153 offset:15376
	ds_read_b128 v[176:179], v153 offset:23584
	ds_read_b128 v[180:183], v153 offset:31792
	s_waitcnt lgkmcnt(4)
	v_fmac_f32_e32 v136, v128, v148
	v_fmac_f32_e32 v136, v129, v149
	v_fmac_f32_e32 v136, v130, v150
	v_fmac_f32_e32 v136, v131, v151
	v_fmac_f32_e32 v137, v128, v186
	v_fmac_f32_e32 v137, v129, v187
	v_fmac_f32_e32 v137, v130, v188
	v_fmac_f32_e32 v137, v131, v189
	v_fmac_f32_e32 v138, v128, v194
	v_fmac_f32_e32 v138, v129, v195
	v_fmac_f32_e32 v138, v130, v196
	v_fmac_f32_e32 v138, v131, v197
	v_fmac_f32_e32 v139, v128, v198
	v_fmac_f32_e32 v139, v129, v199
	v_fmac_f32_e32 v139, v130, v200
	v_fmac_f32_e32 v139, v131, v201
	ds_read_b128 v[148:151], v153 offset:40000
	ds_read_b128 v[186:189], v153 offset:48208
	ds_read_b128 v[194:197], v153 offset:56416
	ds_read_b128 v[198:201], v153 offset:64624
	s_waitcnt lgkmcnt(4)
	v_fmac_f32_e32 v140, v128, v168
	v_fmac_f32_e32 v140, v129, v169
	v_fmac_f32_e32 v140, v130, v170
	v_fmac_f32_e32 v140, v131, v171
	v_fmac_f32_e32 v141, v128, v172
	v_fmac_f32_e32 v141, v129, v173
	v_fmac_f32_e32 v141, v130, v174
	v_fmac_f32_e32 v141, v131, v175
	v_fmac_f32_e32 v142, v128, v176
	v_fmac_f32_e32 v142, v129, v177
	v_fmac_f32_e32 v142, v130, v178
	v_fmac_f32_e32 v142, v131, v179
	v_fmac_f32_e32 v143, v128, v180
	v_fmac_f32_e32 v143, v129, v181
	v_fmac_f32_e32 v143, v130, v182
	v_fmac_f32_e32 v143, v131, v183
	s_waitcnt lgkmcnt(0)
	v_fmac_f32_e32 v144, v128, v148
	v_fmac_f32_e32 v144, v129, v149
	v_fmac_f32_e32 v144, v130, v150
	v_fmac_f32_e32 v144, v131, v151
	v_fmac_f32_e32 v145, v128, v186
	v_fmac_f32_e32 v145, v129, v187
	v_fmac_f32_e32 v145, v130, v188
	v_fmac_f32_e32 v145, v131, v189
	v_fmac_f32_e32 v146, v128, v194
	v_fmac_f32_e32 v146, v129, v195
	v_fmac_f32_e32 v146, v130, v196
	v_fmac_f32_e32 v146, v131, v197
	v_fmac_f32_e32 v147, v128, v198
	v_fmac_f32_e32 v147, v129, v199
	v_fmac_f32_e32 v147, v130, v200
	v_fmac_f32_e32 v147, v131, v201
	v_cndmask_b32_e64 v242, v133, v132, s[62:63]
	v_cndmask_b32_e64 v132, v132, v133, s[62:63]
	v_cndmask_b32_e64 v243, v135, v134, s[62:63]
	v_cndmask_b32_e64 v134, v134, v135, s[62:63]
	v_cndmask_b32_e64 v244, v137, v136, s[62:63]
	v_cndmask_b32_e64 v136, v136, v137, s[62:63]
	v_cndmask_b32_e64 v245, v139, v138, s[62:63]
	v_cndmask_b32_e64 v138, v138, v139, s[62:63]
	v_cndmask_b32_e64 v246, v141, v140, s[62:63]
	v_cndmask_b32_e64 v140, v140, v141, s[62:63]
	v_cndmask_b32_e64 v248, v143, v142, s[62:63]
	v_cndmask_b32_e64 v142, v142, v143, s[62:63]
	v_cndmask_b32_e64 v249, v145, v144, s[62:63]
	v_cndmask_b32_e64 v144, v144, v145, s[62:63]
	v_cndmask_b32_e64 v250, v147, v146, s[62:63]
	v_cndmask_b32_e64 v146, v146, v147, s[62:63]
	v_add_f32_dpp v132, v242, v132 quad_perm:[1,0,3,2] row_mask:0xf bank_mask:0xf
	v_add_f32_dpp v134, v243, v134 quad_perm:[1,0,3,2] row_mask:0xf bank_mask:0xf
	v_add_f32_dpp v136, v244, v136 quad_perm:[1,0,3,2] row_mask:0xf bank_mask:0xf
	v_add_f32_dpp v138, v245, v138 quad_perm:[1,0,3,2] row_mask:0xf bank_mask:0xf
	v_add_f32_dpp v140, v246, v140 quad_perm:[1,0,3,2] row_mask:0xf bank_mask:0xf
	v_add_f32_dpp v142, v248, v142 quad_perm:[1,0,3,2] row_mask:0xf bank_mask:0xf
	v_add_f32_dpp v144, v249, v144 quad_perm:[1,0,3,2] row_mask:0xf bank_mask:0xf
	v_add_f32_dpp v146, v250, v146 quad_perm:[1,0,3,2] row_mask:0xf bank_mask:0xf
	v_cndmask_b32_e64 v242, v134, v132, s[64:65]
	v_cndmask_b32_e64 v132, v132, v134, s[64:65]
	v_cndmask_b32_e64 v243, v138, v136, s[64:65]
	v_cndmask_b32_e64 v136, v136, v138, s[64:65]
	v_cndmask_b32_e64 v244, v142, v140, s[64:65]
	v_cndmask_b32_e64 v140, v140, v142, s[64:65]
	v_cndmask_b32_e64 v245, v146, v144, s[64:65]
	v_cndmask_b32_e64 v144, v144, v146, s[64:65]
	s_nop 0
	v_add_f32_dpp v132, v242, v132 quad_perm:[2,3,0,1] row_mask:0xf bank_mask:0xf
	v_add_f32_dpp v136, v243, v136 quad_perm:[2,3,0,1] row_mask:0xf bank_mask:0xf
	v_add_f32_dpp v140, v244, v140 quad_perm:[2,3,0,1] row_mask:0xf bank_mask:0xf
	v_add_f32_dpp v144, v245, v144 quad_perm:[2,3,0,1] row_mask:0xf bank_mask:0xf
	v_cndmask_b32_e64 v242, v136, v132, s[66:67]
	v_cndmask_b32_e64 v132, v132, v136, s[66:67]
	v_cndmask_b32_e64 v243, v144, v140, s[66:67]
	v_cndmask_b32_e64 v140, v140, v144, s[66:67]
	s_nop 1
	v_add_f32_dpp v246, v242, v132 row_shl:4 row_mask:0xf bank_mask:0x5
	v_add_f32_dpp v246, v242, v132 row_shr:4 row_mask:0xf bank_mask:0xa
	v_add_f32_dpp v248, v243, v140 row_shl:4 row_mask:0xf bank_mask:0x5
	v_add_f32_dpp v248, v243, v140 row_shr:4 row_mask:0xf bank_mask:0xa
	v_cndmask_b32_e64 v242, v248, v246, s[68:69]
	v_cndmask_b32_e64 v243, v246, v248, s[68:69]
	s_nop 1
	v_add_f32_dpp v191, v242, v243 row_ror:8 row_mask:0xf bank_mask:0xf
	s_nop 0
	ds_bpermute_b32 v193, v165, v191
	s_waitcnt lgkmcnt(0)
	v_add_f32_e32 v191, v191, v193
	ds_bpermute_b32 v193, v166, v191
	s_waitcnt lgkmcnt(0)
	v_add_f32_e32 v191, v191, v193
	v_mov_b32_e32 v193, v191
	s_nop 1
	v_max_f32_dpp v193, v193, v193 quad_perm:[1,0,3,2] row_mask:0xf bank_mask:0xf
	s_nop 1
	v_max_f32_dpp v193, v193, v193 quad_perm:[2,3,0,1] row_mask:0xf bank_mask:0xf
	s_nop 1
	v_max_f32_dpp v193, v193, v193 row_half_mirror row_mask:0xf bank_mask:0xf
	s_nop 1
	v_max_f32_dpp v193, v193, v193 row_mirror row_mask:0xf bank_mask:0xf
	v_sub_f32_e32 v191, v191, v193
	v_mul_f32_e32 v191, 0x3fb8aa3b, v191
	v_exp_f32_e32 v191, v191
	s_nop 0
	v_mov_b32_e32 v193, v191
	s_nop 1
	v_add_f32_dpp v193, v193, v193 quad_perm:[1,0,3,2] row_mask:0xf bank_mask:0xf
	s_nop 1
	v_add_f32_dpp v193, v193, v193 quad_perm:[2,3,0,1] row_mask:0xf bank_mask:0xf
	s_nop 1
	v_add_f32_dpp v193, v193, v193 row_half_mirror row_mask:0xf bank_mask:0xf
	s_nop 1
	v_add_f32_dpp v193, v193, v193 row_mirror row_mask:0xf bank_mask:0xf
	v_rcp_f32_e32 v193, v193
	s_nop 0
	v_mul_f32_e32 v191, v191, v193
	s_mov_b64 exec, 0xffff
	global_store_dword v164, v191, s[34:35]
	s_mov_b64 exec, -1
